# router logits on the f32 matrix core (v_mfma_f32_32x32x2_f32) instead of VALU FMAs; plus shorter grid-barrier tail
# speedup vs baseline: 1.0171x; 1.0075x over previous
.LBB0_651:
	s_waitcnt vmcnt(0)
	s_barrier
	s_waitcnt vmcnt(0)
	buffer_inv sc1
	s_waitcnt vmcnt(0)
	v_readlane_b32 s98, v253, 20
	v_mbcnt_lo_u32_b32 v216, -1, 0
	v_mbcnt_hi_u32_b32 v216, -1, v216
	s_lshr_b32 s99, s98, 1
	s_and_b32 s100, s98, 1
	v_lshrrev_b32_e32 v217, 5, v216
	v_and_b32_e32 v216, 31, v216
	s_lshl_b32 s101, s99, 4
	v_add_u32_e32 v218, s101, v217
	v_lshlrev_b32_e32 v219, 7, v218
	v_lshl_add_u32 v219, v216, 2, v219
	v_add_u32_e32 v219, 0xa400, v219
	v_mul_u32_u24_e32 v218, 0x110, v218
	s_lshl_b32 s101, s100, 7
	v_add_u32_e32 v218, s101, v218
	v_lshl_add_u32 v218, v216, 2, v218
	v_add_u32_e32 v218, 0x6000, v218
	s_lshl_b32 s101, s99, 13
	s_lshl_b32 s100, s100, 12
	s_add_i32 s101, s101, s100
	v_lshlrev_b32_e32 v217, 9, v217
	v_add_u32_e32 v217, s101, v217
	v_lshl_add_u32 v217, v216, 2, v217
	s_and_saveexec_b64 s[16:17], s[4:5]
	ds_write_b32 v103, v45 offset:58624
	s_or_b64 exec, exec, s[16:17]
	v_add_u32_e32 v0, s62, v42
	v_ashrrev_i32_e32 v1, 31, v0
	v_lshlrev_b64 v[0:1], 11, v[0:1]
	v_lshl_add_u64 v[94:95], v[46:47], 0, v[0:1]
	global_load_dwordx4 v[30:33], v[94:95], off
	global_load_dwordx4 v[34:37], v[48:49], off
	global_load_dwordx4 v[20:23], v[52:53], off
	global_load_dwordx4 v[24:27], v[94:95], off offset:128
	ds_read_b64 v[38:39], v115 offset:20480
	ds_read_b128 v[98:101], v43 offset:12288
	ds_read_b128 v[122:125], v43 offset:12304
	ds_read_b128 v[126:129], v43 offset:16384
	ds_read_b128 v[130:133], v43 offset:16400
	v_add_u32_e32 v96, 0x6000, v105
	v_mov_b32_e32 v4, 0
	s_waitcnt lgkmcnt(4)
	v_mov_b32_e32 v0, v38
	v_mov_b32_e32 v1, v38
	v_mov_b32_e32 v2, v38
	v_mov_b32_e32 v3, v38
	v_mov_b32_e32 v90, v39
	v_mov_b32_e32 v91, v39
	v_mov_b32_e32 v92, v39
	v_mov_b32_e32 v93, v39
	v_add_u32_e32 v44, 0x6400, v105
	s_mov_b32 s16, 0
	v_mov_b32_e32 v28, v112
	v_mov_b32_e32 v5, v4
	v_mov_b32_e32 v6, v4
	v_mov_b32_e32 v7, v4
	v_mov_b32_e32 v8, v4
	v_mov_b32_e32 v9, v4
	v_mov_b32_e32 v10, v4
	v_mov_b32_e32 v11, v4
	v_mov_b32_e32 v12, v4
	v_mov_b32_e32 v13, v4
	v_mov_b32_e32 v14, v4
	v_mov_b32_e32 v15, v4
	v_mov_b32_e32 v16, v4
	v_mov_b32_e32 v17, v4
	v_mov_b32_e32 v18, v4
	s_waitcnt vmcnt(3)
	v_cvt_f32_f16_sdwa v19, v31 dst_sel:DWORD dst_unused:UNUSED_PAD src0_sel:WORD_1
	v_cvt_f32_f16_e32 v29, v31
	v_cvt_f32_f16_sdwa v31, v30 dst_sel:DWORD dst_unused:UNUSED_PAD src0_sel:WORD_1
	v_cvt_f32_f16_e32 v30, v30
	v_cvt_f32_f16_sdwa v97, v33 dst_sel:DWORD dst_unused:UNUSED_PAD src0_sel:WORD_1
	v_cvt_f32_f16_e32 v136, v33
	v_cvt_f32_f16_sdwa v135, v32 dst_sel:DWORD dst_unused:UNUSED_PAD src0_sel:WORD_1
	v_cvt_f32_f16_e32 v134, v32
	v_sub_f32_e32 v30, v30, v38
	v_sub_f32_e32 v31, v31, v38
	v_sub_f32_e32 v32, v29, v38
	v_sub_f32_e32 v33, v19, v38
	v_sub_f32_e32 v134, v134, v38
	v_sub_f32_e32 v135, v135, v38
	v_sub_f32_e32 v136, v136, v38
	v_sub_f32_e32 v137, v97, v38
	v_pk_mul_f32 v[30:31], v[38:39], v[30:31] op_sel:[1,0]
	v_pk_mul_f32 v[32:33], v[38:39], v[32:33] op_sel:[1,0]
	v_pk_mul_f32 v[136:137], v[38:39], v[136:137] op_sel:[1,0]
	v_pk_mul_f32 v[38:39], v[38:39], v[134:135] op_sel:[1,0]
	s_waitcnt lgkmcnt(1)
	v_fma_f32 v19, v98, v30, v126
	v_fma_f32 v30, v99, v31, v127
	s_waitcnt lgkmcnt(0)
	v_fma_f32 v29, v122, v38, v130
	v_fma_f32 v31, v123, v39, v131
	v_fma_f32 v32, v100, v32, v128
	v_fma_f32 v38, v124, v136, v132
	v_fmac_f32_e32 v129, v101, v33
	v_fmac_f32_e32 v133, v125, v137
	ds_write2_b32 v96, v19, v30 offset1:68
	ds_write2_b32 v44, v29, v31 offset0:16 offset1:84
	ds_write2_b32 v96, v32, v129 offset0:136 offset1:204
	ds_write2_b32 v44, v38, v133 offset0:152 offset1:220
	s_waitcnt vmcnt(2)
	ds_write_b128 v104, v[34:37] offset:41984
	v_mov_b32_e32 v19, v4
	s_waitcnt lgkmcnt(0)
	s_barrier
	ds_read_b32 v200, v218
	ds_read_b32 v208, v219
	ds_read_b32 v201, v218 offset:544
	ds_read_b32 v209, v219 offset:256
	ds_read_b32 v202, v218 offset:1088
	ds_read_b32 v210, v219 offset:512
	ds_read_b32 v203, v218 offset:1632
	ds_read_b32 v211, v219 offset:768
	ds_read_b32 v204, v218 offset:2176
	ds_read_b32 v212, v219 offset:1024
	ds_read_b32 v205, v218 offset:2720
	ds_read_b32 v213, v219 offset:1280
	ds_read_b32 v206, v218 offset:3264
	ds_read_b32 v214, v219 offset:1536
	s_waitcnt lgkmcnt(12)
	v_mfma_f32_32x32x2_f32 v[4:19], v200, v208, v[4:19]
	ds_read_b32 v207, v218 offset:3808
	ds_read_b32 v215, v219 offset:1792
	s_waitcnt lgkmcnt(12)
	v_mfma_f32_32x32x2_f32 v[4:19], v201, v209, v[4:19]
	s_waitcnt lgkmcnt(10)
	v_mfma_f32_32x32x2_f32 v[4:19], v202, v210, v[4:19]
	s_waitcnt lgkmcnt(8)
	v_mfma_f32_32x32x2_f32 v[4:19], v203, v211, v[4:19]
	s_waitcnt lgkmcnt(6)
	v_mfma_f32_32x32x2_f32 v[4:19], v204, v212, v[4:19]
	s_waitcnt lgkmcnt(4)
	v_mfma_f32_32x32x2_f32 v[4:19], v205, v213, v[4:19]
	s_waitcnt lgkmcnt(2)
	v_mfma_f32_32x32x2_f32 v[4:19], v206, v214, v[4:19]
	s_waitcnt lgkmcnt(0)
	v_mfma_f32_32x32x2_f32 v[4:19], v207, v215, v[4:19]
	s_barrier
	global_load_dwordx4 v[32:35], v[94:95], off offset:256
	global_load_dwordx4 v[28:31], v[54:55], off
	s_waitcnt vmcnt(2)
	v_cvt_f32_f16_sdwa v130, v24 dst_sel:DWORD dst_unused:UNUSED_PAD src0_sel:WORD_1
	v_cvt_f32_f16_e32 v24, v24
	v_cvt_f32_f16_e32 v131, v25
	v_cvt_f32_f16_sdwa v132, v26 dst_sel:DWORD dst_unused:UNUSED_PAD src0_sel:WORD_1
	v_cvt_f32_f16_e32 v135, v26
	ds_read_b128 v[36:39], v43 offset:12544
	ds_read_b128 v[98:101], v43 offset:12560
	ds_read_b128 v[122:125], v43 offset:16640
	ds_read_b128 v[126:129], v43 offset:16656
	v_cvt_f32_f16_sdwa v97, v25 dst_sel:DWORD dst_unused:UNUSED_PAD src0_sel:WORD_1
	v_cvt_f32_f16_sdwa v133, v27 dst_sel:DWORD dst_unused:UNUSED_PAD src0_sel:WORD_1
	v_cvt_f32_f16_e32 v134, v27
	v_sub_f32_e32 v24, v24, v0
	v_sub_f32_e32 v25, v130, v1
	v_sub_f32_e32 v26, v131, v2
	v_pk_mul_f32 v[24:25], v[90:91], v[24:25]
	v_sub_f32_e32 v130, v135, v0
	v_sub_f32_e32 v131, v132, v1
	v_sub_f32_e32 v27, v97, v3
	v_sub_f32_e32 v132, v134, v2
	v_sub_f32_e32 v133, v133, v3
	v_pk_mul_f32 v[130:131], v[90:91], v[130:131]
	s_waitcnt lgkmcnt(1)
	v_fma_f32 v24, v36, v24, v122
	v_fma_f32 v25, v37, v25, v123
	v_pk_mul_f32 v[26:27], v[92:93], v[26:27]
	v_pk_mul_f32 v[132:133], v[92:93], v[132:133]
	s_waitcnt lgkmcnt(0)
	v_fma_f32 v36, v98, v130, v126
	ds_write2_b32 v96, v24, v25 offset1:68
	v_fma_f32 v24, v99, v131, v127
	ds_write2_b32 v44, v36, v24 offset0:16 offset1:84
	v_fma_f32 v24, v38, v26, v124
	v_fma_f32 v25, v100, v132, v128
	v_fmac_f32_e32 v125, v39, v27
	v_fmac_f32_e32 v129, v101, v133
	ds_write2_b32 v96, v24, v125 offset0:136 offset1:204
	ds_write2_b32 v44, v25, v129 offset0:152 offset1:220
	ds_write_b128 v104, v[20:23] offset:41984
	s_mov_b32 s16, 0
	v_mov_b32_e32 v20, v112
	s_waitcnt lgkmcnt(0)
	s_barrier
	ds_read_b32 v200, v218
	ds_read_b32 v208, v219
	ds_read_b32 v201, v218 offset:544
	ds_read_b32 v209, v219 offset:256
	ds_read_b32 v202, v218 offset:1088
	ds_read_b32 v210, v219 offset:512
	ds_read_b32 v203, v218 offset:1632
	ds_read_b32 v211, v219 offset:768
	ds_read_b32 v204, v218 offset:2176
	ds_read_b32 v212, v219 offset:1024
	ds_read_b32 v205, v218 offset:2720
	ds_read_b32 v213, v219 offset:1280
	ds_read_b32 v206, v218 offset:3264
	ds_read_b32 v214, v219 offset:1536
	s_waitcnt lgkmcnt(12)
	v_mfma_f32_32x32x2_f32 v[4:19], v200, v208, v[4:19]
	ds_read_b32 v207, v218 offset:3808
	ds_read_b32 v215, v219 offset:1792
	s_waitcnt lgkmcnt(12)
	v_mfma_f32_32x32x2_f32 v[4:19], v201, v209, v[4:19]
	s_waitcnt lgkmcnt(10)
	v_mfma_f32_32x32x2_f32 v[4:19], v202, v210, v[4:19]
	s_waitcnt lgkmcnt(8)
	v_mfma_f32_32x32x2_f32 v[4:19], v203, v211, v[4:19]
	s_waitcnt lgkmcnt(6)
	v_mfma_f32_32x32x2_f32 v[4:19], v204, v212, v[4:19]
	s_waitcnt lgkmcnt(4)
	v_mfma_f32_32x32x2_f32 v[4:19], v205, v213, v[4:19]
	s_waitcnt lgkmcnt(2)
	v_mfma_f32_32x32x2_f32 v[4:19], v206, v214, v[4:19]
	s_waitcnt lgkmcnt(0)
	v_mfma_f32_32x32x2_f32 v[4:19], v207, v215, v[4:19]
	s_barrier
	global_load_dwordx4 v[36:39], v[94:95], off offset:384
	global_load_dwordx4 v[20:23], v[56:57], off
	s_waitcnt vmcnt(3)
	v_cvt_f32_f16_sdwa v130, v32 dst_sel:DWORD dst_unused:UNUSED_PAD src0_sel:WORD_1
	v_cvt_f32_f16_e32 v32, v32
	v_cvt_f32_f16_e32 v131, v33
	v_cvt_f32_f16_sdwa v132, v34 dst_sel:DWORD dst_unused:UNUSED_PAD src0_sel:WORD_1
	v_cvt_f32_f16_e32 v135, v34
	ds_read_b128 v[24:27], v43 offset:12800
	ds_read_b128 v[98:101], v43 offset:12816
	ds_read_b128 v[122:125], v43 offset:16896
	ds_read_b128 v[126:129], v43 offset:16912
	v_cvt_f32_f16_sdwa v97, v33 dst_sel:DWORD dst_unused:UNUSED_PAD src0_sel:WORD_1
	v_cvt_f32_f16_sdwa v133, v35 dst_sel:DWORD dst_unused:UNUSED_PAD src0_sel:WORD_1
	v_cvt_f32_f16_e32 v134, v35
	v_sub_f32_e32 v32, v32, v0
	v_sub_f32_e32 v33, v130, v1
	v_sub_f32_e32 v34, v131, v2
	v_pk_mul_f32 v[32:33], v[90:91], v[32:33]
	v_sub_f32_e32 v130, v135, v0
	v_sub_f32_e32 v131, v132, v1
	v_sub_f32_e32 v35, v97, v3
	v_pk_mul_f32 v[130:131], v[90:91], v[130:131]
	s_waitcnt lgkmcnt(1)
	v_fma_f32 v24, v24, v32, v122
	v_fma_f32 v25, v25, v33, v123
	v_pk_mul_f32 v[34:35], v[92:93], v[34:35]
	v_sub_f32_e32 v132, v134, v2
	v_sub_f32_e32 v133, v133, v3
	s_waitcnt lgkmcnt(0)
	v_fma_f32 v32, v98, v130, v126
	ds_write2_b32 v96, v24, v25 offset1:68
	v_fma_f32 v24, v99, v131, v127
	v_pk_mul_f32 v[132:133], v[92:93], v[132:133]
	ds_write2_b32 v44, v32, v24 offset0:16 offset1:84
	v_fma_f32 v24, v26, v34, v124
	v_fmac_f32_e32 v125, v27, v35
	v_fma_f32 v25, v100, v132, v128
	ds_write2_b32 v96, v24, v125 offset0:136 offset1:204
	v_fmac_f32_e32 v129, v101, v133
	s_mov_b32 s16, 0
	v_mov_b32_e32 v24, v112
	ds_write2_b32 v44, v25, v129 offset0:152 offset1:220
	s_waitcnt vmcnt(2)
	ds_write_b128 v104, v[28:31] offset:41984
	s_waitcnt lgkmcnt(0)
	s_barrier
	ds_read_b32 v200, v218
	ds_read_b32 v208, v219
	ds_read_b32 v201, v218 offset:544
	ds_read_b32 v209, v219 offset:256
	ds_read_b32 v202, v218 offset:1088
	ds_read_b32 v210, v219 offset:512
	ds_read_b32 v203, v218 offset:1632
	ds_read_b32 v211, v219 offset:768
	ds_read_b32 v204, v218 offset:2176
	ds_read_b32 v212, v219 offset:1024
	ds_read_b32 v205, v218 offset:2720
	ds_read_b32 v213, v219 offset:1280
	ds_read_b32 v206, v218 offset:3264
	ds_read_b32 v214, v219 offset:1536
	s_waitcnt lgkmcnt(12)
	v_mfma_f32_32x32x2_f32 v[4:19], v200, v208, v[4:19]
	ds_read_b32 v207, v218 offset:3808
	ds_read_b32 v215, v219 offset:1792
	s_waitcnt lgkmcnt(12)
	v_mfma_f32_32x32x2_f32 v[4:19], v201, v209, v[4:19]
	s_waitcnt lgkmcnt(10)
	v_mfma_f32_32x32x2_f32 v[4:19], v202, v210, v[4:19]
	s_waitcnt lgkmcnt(8)
	v_mfma_f32_32x32x2_f32 v[4:19], v203, v211, v[4:19]
	s_waitcnt lgkmcnt(6)
	v_mfma_f32_32x32x2_f32 v[4:19], v204, v212, v[4:19]
	s_waitcnt lgkmcnt(4)
	v_mfma_f32_32x32x2_f32 v[4:19], v205, v213, v[4:19]
	s_waitcnt lgkmcnt(2)
	v_mfma_f32_32x32x2_f32 v[4:19], v206, v214, v[4:19]
	s_waitcnt lgkmcnt(0)
	v_mfma_f32_32x32x2_f32 v[4:19], v207, v215, v[4:19]
	s_barrier
	global_load_dwordx4 v[28:31], v[94:95], off offset:512
	global_load_dwordx4 v[24:27], v[58:59], off
	s_waitcnt vmcnt(3)
	v_cvt_f32_f16_sdwa v130, v36 dst_sel:DWORD dst_unused:UNUSED_PAD src0_sel:WORD_1
	v_cvt_f32_f16_e32 v36, v36
	v_cvt_f32_f16_e32 v131, v37
	v_cvt_f32_f16_sdwa v132, v38 dst_sel:DWORD dst_unused:UNUSED_PAD src0_sel:WORD_1
	v_cvt_f32_f16_e32 v135, v38
	ds_read_b128 v[32:35], v43 offset:13056
	ds_read_b128 v[98:101], v43 offset:13072
	ds_read_b128 v[122:125], v43 offset:17152
	ds_read_b128 v[126:129], v43 offset:17168
	v_cvt_f32_f16_sdwa v97, v37 dst_sel:DWORD dst_unused:UNUSED_PAD src0_sel:WORD_1
	v_cvt_f32_f16_sdwa v133, v39 dst_sel:DWORD dst_unused:UNUSED_PAD src0_sel:WORD_1
	v_cvt_f32_f16_e32 v134, v39
	v_sub_f32_e32 v36, v36, v0
	v_sub_f32_e32 v37, v130, v1
	v_sub_f32_e32 v38, v131, v2
	v_pk_mul_f32 v[36:37], v[90:91], v[36:37]
	v_sub_f32_e32 v130, v135, v0
	v_sub_f32_e32 v131, v132, v1
	v_sub_f32_e32 v39, v97, v3
	v_sub_f32_e32 v132, v134, v2
	v_sub_f32_e32 v133, v133, v3
	v_pk_mul_f32 v[130:131], v[90:91], v[130:131]
	s_waitcnt lgkmcnt(1)
	v_fma_f32 v32, v32, v36, v122
	v_fma_f32 v33, v33, v37, v123
	v_pk_mul_f32 v[38:39], v[92:93], v[38:39]
	v_pk_mul_f32 v[132:133], v[92:93], v[132:133]
	s_waitcnt lgkmcnt(0)
	v_fma_f32 v36, v98, v130, v126
	ds_write2_b32 v96, v32, v33 offset1:68
	v_fma_f32 v32, v99, v131, v127
	ds_write2_b32 v44, v36, v32 offset0:16 offset1:84
	v_fma_f32 v32, v34, v38, v124
	v_fma_f32 v33, v100, v132, v128
	v_fmac_f32_e32 v125, v35, v39
	v_fmac_f32_e32 v129, v101, v133
	ds_write2_b32 v96, v32, v125 offset0:136 offset1:204
	ds_write2_b32 v44, v33, v129 offset0:152 offset1:220
	s_waitcnt vmcnt(2)
	ds_write_b128 v104, v[20:23] offset:41984
	s_mov_b32 s16, 0
	v_mov_b32_e32 v20, v112
	s_waitcnt lgkmcnt(0)
	s_barrier
	ds_read_b32 v200, v218
	ds_read_b32 v208, v219
	ds_read_b32 v201, v218 offset:544
	ds_read_b32 v209, v219 offset:256
	ds_read_b32 v202, v218 offset:1088
	ds_read_b32 v210, v219 offset:512
	ds_read_b32 v203, v218 offset:1632
	ds_read_b32 v211, v219 offset:768
	ds_read_b32 v204, v218 offset:2176
	ds_read_b32 v212, v219 offset:1024
	ds_read_b32 v205, v218 offset:2720
	ds_read_b32 v213, v219 offset:1280
	ds_read_b32 v206, v218 offset:3264
	ds_read_b32 v214, v219 offset:1536
	s_waitcnt lgkmcnt(12)
	v_mfma_f32_32x32x2_f32 v[4:19], v200, v208, v[4:19]
	ds_read_b32 v207, v218 offset:3808
	ds_read_b32 v215, v219 offset:1792
	s_waitcnt lgkmcnt(12)
	v_mfma_f32_32x32x2_f32 v[4:19], v201, v209, v[4:19]
	s_waitcnt lgkmcnt(10)
	v_mfma_f32_32x32x2_f32 v[4:19], v202, v210, v[4:19]
	s_waitcnt lgkmcnt(8)
	v_mfma_f32_32x32x2_f32 v[4:19], v203, v211, v[4:19]
	s_waitcnt lgkmcnt(6)
	v_mfma_f32_32x32x2_f32 v[4:19], v204, v212, v[4:19]
	s_waitcnt lgkmcnt(4)
	v_mfma_f32_32x32x2_f32 v[4:19], v205, v213, v[4:19]
	s_waitcnt lgkmcnt(2)
	v_mfma_f32_32x32x2_f32 v[4:19], v206, v214, v[4:19]
	s_waitcnt lgkmcnt(0)
	v_mfma_f32_32x32x2_f32 v[4:19], v207, v215, v[4:19]
	s_barrier
	global_load_dwordx4 v[32:35], v[94:95], off offset:640
	global_load_dwordx4 v[20:23], v[60:61], off
	s_waitcnt vmcnt(3)
	v_cvt_f32_f16_sdwa v130, v28 dst_sel:DWORD dst_unused:UNUSED_PAD src0_sel:WORD_1
	v_cvt_f32_f16_e32 v28, v28
	v_cvt_f32_f16_e32 v131, v29
	v_cvt_f32_f16_sdwa v132, v30 dst_sel:DWORD dst_unused:UNUSED_PAD src0_sel:WORD_1
	v_cvt_f32_f16_e32 v135, v30
	ds_read_b128 v[36:39], v43 offset:13312
	ds_read_b128 v[98:101], v43 offset:13328
	ds_read_b128 v[122:125], v43 offset:17408
	ds_read_b128 v[126:129], v43 offset:17424
	v_cvt_f32_f16_sdwa v97, v29 dst_sel:DWORD dst_unused:UNUSED_PAD src0_sel:WORD_1
	v_cvt_f32_f16_sdwa v133, v31 dst_sel:DWORD dst_unused:UNUSED_PAD src0_sel:WORD_1
	v_cvt_f32_f16_e32 v134, v31
	v_sub_f32_e32 v28, v28, v0
	v_sub_f32_e32 v29, v130, v1
	v_sub_f32_e32 v30, v131, v2
	v_pk_mul_f32 v[28:29], v[90:91], v[28:29]
	v_sub_f32_e32 v130, v135, v0
	v_sub_f32_e32 v131, v132, v1
	v_sub_f32_e32 v31, v97, v3
	v_sub_f32_e32 v132, v134, v2
	v_sub_f32_e32 v133, v133, v3
	v_pk_mul_f32 v[130:131], v[90:91], v[130:131]
	s_waitcnt lgkmcnt(1)
	v_fma_f32 v28, v36, v28, v122
	v_fma_f32 v29, v37, v29, v123
	v_pk_mul_f32 v[30:31], v[92:93], v[30:31]
	v_pk_mul_f32 v[132:133], v[92:93], v[132:133]
	s_waitcnt lgkmcnt(0)
	v_fma_f32 v36, v98, v130, v126
	ds_write2_b32 v96, v28, v29 offset1:68
	v_fma_f32 v28, v99, v131, v127
	ds_write2_b32 v44, v36, v28 offset0:16 offset1:84
	v_fma_f32 v28, v38, v30, v124
	v_fma_f32 v29, v100, v132, v128
	v_fmac_f32_e32 v125, v39, v31
	v_fmac_f32_e32 v129, v101, v133
	ds_write2_b32 v96, v28, v125 offset0:136 offset1:204
	ds_write2_b32 v44, v29, v129 offset0:152 offset1:220
	s_waitcnt vmcnt(2)
	ds_write_b128 v104, v[24:27] offset:41984
	s_mov_b32 s16, 0
	v_mov_b32_e32 v24, v112
	s_waitcnt lgkmcnt(0)
	s_barrier
	ds_read_b32 v200, v218
	ds_read_b32 v208, v219
	ds_read_b32 v201, v218 offset:544
	ds_read_b32 v209, v219 offset:256
	ds_read_b32 v202, v218 offset:1088
	ds_read_b32 v210, v219 offset:512
	ds_read_b32 v203, v218 offset:1632
	ds_read_b32 v211, v219 offset:768
	ds_read_b32 v204, v218 offset:2176
	ds_read_b32 v212, v219 offset:1024
	ds_read_b32 v205, v218 offset:2720
	ds_read_b32 v213, v219 offset:1280
	ds_read_b32 v206, v218 offset:3264
	ds_read_b32 v214, v219 offset:1536
	s_waitcnt lgkmcnt(12)
	v_mfma_f32_32x32x2_f32 v[4:19], v200, v208, v[4:19]
	ds_read_b32 v207, v218 offset:3808
	ds_read_b32 v215, v219 offset:1792
	s_waitcnt lgkmcnt(12)
	v_mfma_f32_32x32x2_f32 v[4:19], v201, v209, v[4:19]
	s_waitcnt lgkmcnt(10)
	v_mfma_f32_32x32x2_f32 v[4:19], v202, v210, v[4:19]
	s_waitcnt lgkmcnt(8)
	v_mfma_f32_32x32x2_f32 v[4:19], v203, v211, v[4:19]
	s_waitcnt lgkmcnt(6)
	v_mfma_f32_32x32x2_f32 v[4:19], v204, v212, v[4:19]
	s_waitcnt lgkmcnt(4)
	v_mfma_f32_32x32x2_f32 v[4:19], v205, v213, v[4:19]
	s_waitcnt lgkmcnt(2)
	v_mfma_f32_32x32x2_f32 v[4:19], v206, v214, v[4:19]
	s_waitcnt lgkmcnt(0)
	v_mfma_f32_32x32x2_f32 v[4:19], v207, v215, v[4:19]
	s_barrier
	global_load_dwordx4 v[28:31], v[94:95], off offset:768
	global_load_dwordx4 v[24:27], v[62:63], off
	s_waitcnt vmcnt(3)
	v_cvt_f32_f16_sdwa v130, v32 dst_sel:DWORD dst_unused:UNUSED_PAD src0_sel:WORD_1
	v_cvt_f32_f16_e32 v32, v32
	v_cvt_f32_f16_e32 v131, v33
	v_cvt_f32_f16_sdwa v132, v34 dst_sel:DWORD dst_unused:UNUSED_PAD src0_sel:WORD_1
	v_cvt_f32_f16_e32 v135, v34
	ds_read_b128 v[36:39], v43 offset:13568
	ds_read_b128 v[98:101], v43 offset:13584
	ds_read_b128 v[122:125], v43 offset:17664
	ds_read_b128 v[126:129], v43 offset:17680
	v_cvt_f32_f16_sdwa v97, v33 dst_sel:DWORD dst_unused:UNUSED_PAD src0_sel:WORD_1
	v_cvt_f32_f16_sdwa v133, v35 dst_sel:DWORD dst_unused:UNUSED_PAD src0_sel:WORD_1
	v_cvt_f32_f16_e32 v134, v35
	v_sub_f32_e32 v32, v32, v0
	v_sub_f32_e32 v33, v130, v1
	v_sub_f32_e32 v34, v131, v2
	v_pk_mul_f32 v[32:33], v[90:91], v[32:33]
	v_sub_f32_e32 v130, v135, v0
	v_sub_f32_e32 v131, v132, v1
	v_sub_f32_e32 v35, v97, v3
	v_sub_f32_e32 v132, v134, v2
	v_sub_f32_e32 v133, v133, v3
	v_pk_mul_f32 v[130:131], v[90:91], v[130:131]
	s_waitcnt lgkmcnt(1)
	v_fma_f32 v32, v36, v32, v122
	v_fma_f32 v33, v37, v33, v123
	v_pk_mul_f32 v[34:35], v[92:93], v[34:35]
	v_pk_mul_f32 v[132:133], v[92:93], v[132:133]
	s_waitcnt lgkmcnt(0)
	v_fma_f32 v36, v98, v130, v126
	ds_write2_b32 v96, v32, v33 offset1:68
	v_fma_f32 v32, v99, v131, v127
	ds_write2_b32 v44, v36, v32 offset0:16 offset1:84
	v_fma_f32 v32, v38, v34, v124
	v_fma_f32 v33, v100, v132, v128
	v_fmac_f32_e32 v125, v39, v35
	v_fmac_f32_e32 v129, v101, v133
	ds_write2_b32 v96, v32, v125 offset0:136 offset1:204
	ds_write2_b32 v44, v33, v129 offset0:152 offset1:220
	s_waitcnt vmcnt(2)
	ds_write_b128 v104, v[20:23] offset:41984
	s_mov_b32 s16, 0
	v_mov_b32_e32 v20, v112
	s_waitcnt lgkmcnt(0)
	s_barrier
	ds_read_b32 v200, v218
	ds_read_b32 v208, v219
	ds_read_b32 v201, v218 offset:544
	ds_read_b32 v209, v219 offset:256
	ds_read_b32 v202, v218 offset:1088
	ds_read_b32 v210, v219 offset:512
	ds_read_b32 v203, v218 offset:1632
	ds_read_b32 v211, v219 offset:768
	ds_read_b32 v204, v218 offset:2176
	ds_read_b32 v212, v219 offset:1024
	ds_read_b32 v205, v218 offset:2720
	ds_read_b32 v213, v219 offset:1280
	ds_read_b32 v206, v218 offset:3264
	ds_read_b32 v214, v219 offset:1536
	s_waitcnt lgkmcnt(12)
	v_mfma_f32_32x32x2_f32 v[4:19], v200, v208, v[4:19]
	ds_read_b32 v207, v218 offset:3808
	ds_read_b32 v215, v219 offset:1792
	s_waitcnt lgkmcnt(12)
	v_mfma_f32_32x32x2_f32 v[4:19], v201, v209, v[4:19]
	s_waitcnt lgkmcnt(10)
	v_mfma_f32_32x32x2_f32 v[4:19], v202, v210, v[4:19]
	s_waitcnt lgkmcnt(8)
	v_mfma_f32_32x32x2_f32 v[4:19], v203, v211, v[4:19]
	s_waitcnt lgkmcnt(6)
	v_mfma_f32_32x32x2_f32 v[4:19], v204, v212, v[4:19]
	s_waitcnt lgkmcnt(4)
	v_mfma_f32_32x32x2_f32 v[4:19], v205, v213, v[4:19]
	s_waitcnt lgkmcnt(2)
	v_mfma_f32_32x32x2_f32 v[4:19], v206, v214, v[4:19]
	s_waitcnt lgkmcnt(0)
	v_mfma_f32_32x32x2_f32 v[4:19], v207, v215, v[4:19]
	s_barrier
	global_load_dwordx4 v[32:35], v[94:95], off offset:896
	global_load_dwordx4 v[20:23], v[64:65], off
	s_waitcnt vmcnt(3)
	v_cvt_f32_f16_sdwa v130, v28 dst_sel:DWORD dst_unused:UNUSED_PAD src0_sel:WORD_1
	v_cvt_f32_f16_e32 v28, v28
	v_cvt_f32_f16_e32 v131, v29
	v_cvt_f32_f16_sdwa v132, v30 dst_sel:DWORD dst_unused:UNUSED_PAD src0_sel:WORD_1
	v_cvt_f32_f16_e32 v135, v30
	ds_read_b128 v[36:39], v43 offset:13824
	ds_read_b128 v[98:101], v43 offset:13840
	ds_read_b128 v[122:125], v43 offset:17920
	ds_read_b128 v[126:129], v43 offset:17936
	v_cvt_f32_f16_sdwa v97, v29 dst_sel:DWORD dst_unused:UNUSED_PAD src0_sel:WORD_1
	v_cvt_f32_f16_sdwa v133, v31 dst_sel:DWORD dst_unused:UNUSED_PAD src0_sel:WORD_1
	v_cvt_f32_f16_e32 v134, v31
	v_sub_f32_e32 v28, v28, v0
	v_sub_f32_e32 v29, v130, v1
	v_sub_f32_e32 v30, v131, v2
	v_pk_mul_f32 v[28:29], v[90:91], v[28:29]
	v_sub_f32_e32 v130, v135, v0
	v_sub_f32_e32 v131, v132, v1
	v_sub_f32_e32 v31, v97, v3
	v_sub_f32_e32 v132, v134, v2
	v_sub_f32_e32 v133, v133, v3
	v_pk_mul_f32 v[130:131], v[90:91], v[130:131]
	s_waitcnt lgkmcnt(1)
	v_fma_f32 v28, v36, v28, v122
	v_fma_f32 v29, v37, v29, v123
	v_pk_mul_f32 v[30:31], v[92:93], v[30:31]
	v_pk_mul_f32 v[132:133], v[92:93], v[132:133]
	s_waitcnt lgkmcnt(0)
	v_fma_f32 v36, v98, v130, v126
	ds_write2_b32 v96, v28, v29 offset1:68
	v_fma_f32 v28, v99, v131, v127
	ds_write2_b32 v44, v36, v28 offset0:16 offset1:84
	v_fma_f32 v28, v38, v30, v124
	v_fma_f32 v29, v100, v132, v128
	v_fmac_f32_e32 v125, v39, v31
	v_fmac_f32_e32 v129, v101, v133
	ds_write2_b32 v96, v28, v125 offset0:136 offset1:204
	ds_write2_b32 v44, v29, v129 offset0:152 offset1:220
	s_waitcnt vmcnt(2)
	ds_write_b128 v104, v[24:27] offset:41984
	s_mov_b32 s16, 0
	v_mov_b32_e32 v24, v112
	s_waitcnt lgkmcnt(0)
	s_barrier
	ds_read_b32 v200, v218
	ds_read_b32 v208, v219
	ds_read_b32 v201, v218 offset:544
	ds_read_b32 v209, v219 offset:256
	ds_read_b32 v202, v218 offset:1088
	ds_read_b32 v210, v219 offset:512
	ds_read_b32 v203, v218 offset:1632
	ds_read_b32 v211, v219 offset:768
	ds_read_b32 v204, v218 offset:2176
	ds_read_b32 v212, v219 offset:1024
	ds_read_b32 v205, v218 offset:2720
	ds_read_b32 v213, v219 offset:1280
	ds_read_b32 v206, v218 offset:3264
	ds_read_b32 v214, v219 offset:1536
	s_waitcnt lgkmcnt(12)
	v_mfma_f32_32x32x2_f32 v[4:19], v200, v208, v[4:19]
	ds_read_b32 v207, v218 offset:3808
	ds_read_b32 v215, v219 offset:1792
	s_waitcnt lgkmcnt(12)
	v_mfma_f32_32x32x2_f32 v[4:19], v201, v209, v[4:19]
	s_waitcnt lgkmcnt(10)
	v_mfma_f32_32x32x2_f32 v[4:19], v202, v210, v[4:19]
	s_waitcnt lgkmcnt(8)
	v_mfma_f32_32x32x2_f32 v[4:19], v203, v211, v[4:19]
	s_waitcnt lgkmcnt(6)
	v_mfma_f32_32x32x2_f32 v[4:19], v204, v212, v[4:19]
	s_waitcnt lgkmcnt(4)
	v_mfma_f32_32x32x2_f32 v[4:19], v205, v213, v[4:19]
	s_waitcnt lgkmcnt(2)
	v_mfma_f32_32x32x2_f32 v[4:19], v206, v214, v[4:19]
	s_waitcnt lgkmcnt(0)
	v_mfma_f32_32x32x2_f32 v[4:19], v207, v215, v[4:19]
	s_barrier
	global_load_dwordx4 v[28:31], v[94:95], off offset:1024
	global_load_dwordx4 v[24:27], v[66:67], off
	s_waitcnt vmcnt(3)
	v_cvt_f32_f16_sdwa v130, v32 dst_sel:DWORD dst_unused:UNUSED_PAD src0_sel:WORD_1
	v_cvt_f32_f16_e32 v32, v32
	v_cvt_f32_f16_e32 v131, v33
	v_cvt_f32_f16_sdwa v132, v34 dst_sel:DWORD dst_unused:UNUSED_PAD src0_sel:WORD_1
	v_cvt_f32_f16_e32 v135, v34
	ds_read_b128 v[36:39], v43 offset:14080
	ds_read_b128 v[98:101], v43 offset:14096
	ds_read_b128 v[122:125], v43 offset:18176
	ds_read_b128 v[126:129], v43 offset:18192
	v_cvt_f32_f16_sdwa v97, v33 dst_sel:DWORD dst_unused:UNUSED_PAD src0_sel:WORD_1
	v_cvt_f32_f16_sdwa v133, v35 dst_sel:DWORD dst_unused:UNUSED_PAD src0_sel:WORD_1
	v_cvt_f32_f16_e32 v134, v35
	v_sub_f32_e32 v32, v32, v0
	v_sub_f32_e32 v33, v130, v1
	v_sub_f32_e32 v34, v131, v2
	v_pk_mul_f32 v[32:33], v[90:91], v[32:33]
	v_sub_f32_e32 v130, v135, v0
	v_sub_f32_e32 v131, v132, v1
	v_sub_f32_e32 v35, v97, v3
	v_sub_f32_e32 v132, v134, v2
	v_sub_f32_e32 v133, v133, v3
	v_pk_mul_f32 v[130:131], v[90:91], v[130:131]
	s_waitcnt lgkmcnt(1)
	v_fma_f32 v32, v36, v32, v122
	v_fma_f32 v33, v37, v33, v123
	v_pk_mul_f32 v[34:35], v[92:93], v[34:35]
	v_pk_mul_f32 v[132:133], v[92:93], v[132:133]
	s_waitcnt lgkmcnt(0)
	v_fma_f32 v36, v98, v130, v126
	ds_write2_b32 v96, v32, v33 offset1:68
	v_fma_f32 v32, v99, v131, v127
	ds_write2_b32 v44, v36, v32 offset0:16 offset1:84
	v_fma_f32 v32, v38, v34, v124
	v_fma_f32 v33, v100, v132, v128
	v_fmac_f32_e32 v125, v39, v35
	v_fmac_f32_e32 v129, v101, v133
	ds_write2_b32 v96, v32, v125 offset0:136 offset1:204
	ds_write2_b32 v44, v33, v129 offset0:152 offset1:220
	s_waitcnt vmcnt(2)
	ds_write_b128 v104, v[20:23] offset:41984
	s_mov_b32 s16, 0
	v_mov_b32_e32 v20, v112
	s_waitcnt lgkmcnt(0)
	s_barrier
	ds_read_b32 v200, v218
	ds_read_b32 v208, v219
	ds_read_b32 v201, v218 offset:544
	ds_read_b32 v209, v219 offset:256
	ds_read_b32 v202, v218 offset:1088
	ds_read_b32 v210, v219 offset:512
	ds_read_b32 v203, v218 offset:1632
	ds_read_b32 v211, v219 offset:768
	ds_read_b32 v204, v218 offset:2176
	ds_read_b32 v212, v219 offset:1024
	ds_read_b32 v205, v218 offset:2720
	ds_read_b32 v213, v219 offset:1280
	ds_read_b32 v206, v218 offset:3264
	ds_read_b32 v214, v219 offset:1536
	s_waitcnt lgkmcnt(12)
	v_mfma_f32_32x32x2_f32 v[4:19], v200, v208, v[4:19]
	ds_read_b32 v207, v218 offset:3808
	ds_read_b32 v215, v219 offset:1792
	s_waitcnt lgkmcnt(12)
	v_mfma_f32_32x32x2_f32 v[4:19], v201, v209, v[4:19]
	s_waitcnt lgkmcnt(10)
	v_mfma_f32_32x32x2_f32 v[4:19], v202, v210, v[4:19]
	s_waitcnt lgkmcnt(8)
	v_mfma_f32_32x32x2_f32 v[4:19], v203, v211, v[4:19]
	s_waitcnt lgkmcnt(6)
	v_mfma_f32_32x32x2_f32 v[4:19], v204, v212, v[4:19]
	s_waitcnt lgkmcnt(4)
	v_mfma_f32_32x32x2_f32 v[4:19], v205, v213, v[4:19]
	s_waitcnt lgkmcnt(2)
	v_mfma_f32_32x32x2_f32 v[4:19], v206, v214, v[4:19]
	s_waitcnt lgkmcnt(0)
	v_mfma_f32_32x32x2_f32 v[4:19], v207, v215, v[4:19]
	s_barrier
	global_load_dwordx4 v[32:35], v[94:95], off offset:1152
	global_load_dwordx4 v[20:23], v[68:69], off
	s_waitcnt vmcnt(3)
	v_cvt_f32_f16_sdwa v130, v28 dst_sel:DWORD dst_unused:UNUSED_PAD src0_sel:WORD_1
	v_cvt_f32_f16_e32 v28, v28
	v_cvt_f32_f16_e32 v131, v29
	v_cvt_f32_f16_sdwa v132, v30 dst_sel:DWORD dst_unused:UNUSED_PAD src0_sel:WORD_1
	v_cvt_f32_f16_e32 v135, v30
	ds_read_b128 v[36:39], v43 offset:14336
	ds_read_b128 v[98:101], v43 offset:14352
	ds_read_b128 v[122:125], v43 offset:18432
	ds_read_b128 v[126:129], v43 offset:18448
	v_cvt_f32_f16_sdwa v97, v29 dst_sel:DWORD dst_unused:UNUSED_PAD src0_sel:WORD_1
	v_cvt_f32_f16_sdwa v133, v31 dst_sel:DWORD dst_unused:UNUSED_PAD src0_sel:WORD_1
	v_cvt_f32_f16_e32 v134, v31
	v_sub_f32_e32 v28, v28, v0
	v_sub_f32_e32 v29, v130, v1
	v_sub_f32_e32 v30, v131, v2
	v_pk_mul_f32 v[28:29], v[90:91], v[28:29]
	v_sub_f32_e32 v130, v135, v0
	v_sub_f32_e32 v131, v132, v1
	v_sub_f32_e32 v31, v97, v3
	v_sub_f32_e32 v132, v134, v2
	v_sub_f32_e32 v133, v133, v3
	v_pk_mul_f32 v[130:131], v[90:91], v[130:131]
	s_waitcnt lgkmcnt(1)
	v_fma_f32 v28, v36, v28, v122
	v_fma_f32 v29, v37, v29, v123
	v_pk_mul_f32 v[30:31], v[92:93], v[30:31]
	v_pk_mul_f32 v[132:133], v[92:93], v[132:133]
	s_waitcnt lgkmcnt(0)
	v_fma_f32 v36, v98, v130, v126
	ds_write2_b32 v96, v28, v29 offset1:68
	v_fma_f32 v28, v99, v131, v127
	ds_write2_b32 v44, v36, v28 offset0:16 offset1:84
	v_fma_f32 v28, v38, v30, v124
	v_fma_f32 v29, v100, v132, v128
	v_fmac_f32_e32 v125, v39, v31
	v_fmac_f32_e32 v129, v101, v133
	ds_write2_b32 v96, v28, v125 offset0:136 offset1:204
	ds_write2_b32 v44, v29, v129 offset0:152 offset1:220
	s_waitcnt vmcnt(2)
	ds_write_b128 v104, v[24:27] offset:41984
	s_mov_b32 s16, 0
	v_mov_b32_e32 v24, v112
	s_waitcnt lgkmcnt(0)
	s_barrier
	ds_read_b32 v200, v218
	ds_read_b32 v208, v219
	ds_read_b32 v201, v218 offset:544
	ds_read_b32 v209, v219 offset:256
	ds_read_b32 v202, v218 offset:1088
	ds_read_b32 v210, v219 offset:512
	ds_read_b32 v203, v218 offset:1632
	ds_read_b32 v211, v219 offset:768
	ds_read_b32 v204, v218 offset:2176
	ds_read_b32 v212, v219 offset:1024
	ds_read_b32 v205, v218 offset:2720
	ds_read_b32 v213, v219 offset:1280
	ds_read_b32 v206, v218 offset:3264
	ds_read_b32 v214, v219 offset:1536
	s_waitcnt lgkmcnt(12)
	v_mfma_f32_32x32x2_f32 v[4:19], v200, v208, v[4:19]
	ds_read_b32 v207, v218 offset:3808
	ds_read_b32 v215, v219 offset:1792
	s_waitcnt lgkmcnt(12)
	v_mfma_f32_32x32x2_f32 v[4:19], v201, v209, v[4:19]
	s_waitcnt lgkmcnt(10)
	v_mfma_f32_32x32x2_f32 v[4:19], v202, v210, v[4:19]
	s_waitcnt lgkmcnt(8)
	v_mfma_f32_32x32x2_f32 v[4:19], v203, v211, v[4:19]
	s_waitcnt lgkmcnt(6)
	v_mfma_f32_32x32x2_f32 v[4:19], v204, v212, v[4:19]
	s_waitcnt lgkmcnt(4)
	v_mfma_f32_32x32x2_f32 v[4:19], v205, v213, v[4:19]
	s_waitcnt lgkmcnt(2)
	v_mfma_f32_32x32x2_f32 v[4:19], v206, v214, v[4:19]
	s_waitcnt lgkmcnt(0)
	v_mfma_f32_32x32x2_f32 v[4:19], v207, v215, v[4:19]
	s_barrier
	global_load_dwordx4 v[28:31], v[94:95], off offset:1280
	global_load_dwordx4 v[24:27], v[70:71], off
	s_waitcnt vmcnt(3)
	v_cvt_f32_f16_sdwa v130, v32 dst_sel:DWORD dst_unused:UNUSED_PAD src0_sel:WORD_1
	v_cvt_f32_f16_e32 v32, v32
	v_cvt_f32_f16_e32 v131, v33
	v_cvt_f32_f16_sdwa v132, v34 dst_sel:DWORD dst_unused:UNUSED_PAD src0_sel:WORD_1
	v_cvt_f32_f16_e32 v135, v34
	ds_read_b128 v[36:39], v43 offset:14592
	ds_read_b128 v[98:101], v43 offset:14608
	ds_read_b128 v[122:125], v43 offset:18688
	ds_read_b128 v[126:129], v43 offset:18704
	v_cvt_f32_f16_sdwa v97, v33 dst_sel:DWORD dst_unused:UNUSED_PAD src0_sel:WORD_1
	v_cvt_f32_f16_sdwa v133, v35 dst_sel:DWORD dst_unused:UNUSED_PAD src0_sel:WORD_1
	v_cvt_f32_f16_e32 v134, v35
	v_sub_f32_e32 v32, v32, v0
	v_sub_f32_e32 v33, v130, v1
	v_sub_f32_e32 v34, v131, v2
	v_pk_mul_f32 v[32:33], v[90:91], v[32:33]
	v_sub_f32_e32 v130, v135, v0
	v_sub_f32_e32 v131, v132, v1
	v_sub_f32_e32 v35, v97, v3
	v_sub_f32_e32 v132, v134, v2
	v_sub_f32_e32 v133, v133, v3
	v_pk_mul_f32 v[130:131], v[90:91], v[130:131]
	s_waitcnt lgkmcnt(1)
	v_fma_f32 v32, v36, v32, v122
	v_fma_f32 v33, v37, v33, v123
	v_pk_mul_f32 v[34:35], v[92:93], v[34:35]
	v_pk_mul_f32 v[132:133], v[92:93], v[132:133]
	s_waitcnt lgkmcnt(0)
	v_fma_f32 v36, v98, v130, v126
	ds_write2_b32 v96, v32, v33 offset1:68
	v_fma_f32 v32, v99, v131, v127
	ds_write2_b32 v44, v36, v32 offset0:16 offset1:84
	v_fma_f32 v32, v38, v34, v124
	v_fma_f32 v33, v100, v132, v128
	v_fmac_f32_e32 v125, v39, v35
	v_fmac_f32_e32 v129, v101, v133
	ds_write2_b32 v96, v32, v125 offset0:136 offset1:204
	ds_write2_b32 v44, v33, v129 offset0:152 offset1:220
	s_waitcnt vmcnt(2)
	ds_write_b128 v104, v[20:23] offset:41984
	s_mov_b32 s16, 0
	v_mov_b32_e32 v20, v112
	s_waitcnt lgkmcnt(0)
	s_barrier
	ds_read_b32 v200, v218
	ds_read_b32 v208, v219
	ds_read_b32 v201, v218 offset:544
	ds_read_b32 v209, v219 offset:256
	ds_read_b32 v202, v218 offset:1088
	ds_read_b32 v210, v219 offset:512
	ds_read_b32 v203, v218 offset:1632
	ds_read_b32 v211, v219 offset:768
	ds_read_b32 v204, v218 offset:2176
	ds_read_b32 v212, v219 offset:1024
	ds_read_b32 v205, v218 offset:2720
	ds_read_b32 v213, v219 offset:1280
	ds_read_b32 v206, v218 offset:3264
	ds_read_b32 v214, v219 offset:1536
	s_waitcnt lgkmcnt(12)
	v_mfma_f32_32x32x2_f32 v[4:19], v200, v208, v[4:19]
	ds_read_b32 v207, v218 offset:3808
	ds_read_b32 v215, v219 offset:1792
	s_waitcnt lgkmcnt(12)
	v_mfma_f32_32x32x2_f32 v[4:19], v201, v209, v[4:19]
	s_waitcnt lgkmcnt(10)
	v_mfma_f32_32x32x2_f32 v[4:19], v202, v210, v[4:19]
	s_waitcnt lgkmcnt(8)
	v_mfma_f32_32x32x2_f32 v[4:19], v203, v211, v[4:19]
	s_waitcnt lgkmcnt(6)
	v_mfma_f32_32x32x2_f32 v[4:19], v204, v212, v[4:19]
	s_waitcnt lgkmcnt(4)
	v_mfma_f32_32x32x2_f32 v[4:19], v205, v213, v[4:19]
	s_waitcnt lgkmcnt(2)
	v_mfma_f32_32x32x2_f32 v[4:19], v206, v214, v[4:19]
	s_waitcnt lgkmcnt(0)
	v_mfma_f32_32x32x2_f32 v[4:19], v207, v215, v[4:19]
	s_barrier
	global_load_dwordx4 v[32:35], v[94:95], off offset:1408
	global_load_dwordx4 v[20:23], v[72:73], off
	s_waitcnt vmcnt(3)
	v_cvt_f32_f16_sdwa v130, v28 dst_sel:DWORD dst_unused:UNUSED_PAD src0_sel:WORD_1
	v_cvt_f32_f16_e32 v28, v28
	v_cvt_f32_f16_e32 v131, v29
	v_cvt_f32_f16_sdwa v132, v30 dst_sel:DWORD dst_unused:UNUSED_PAD src0_sel:WORD_1
	v_cvt_f32_f16_e32 v135, v30
	ds_read_b128 v[36:39], v43 offset:14848
	ds_read_b128 v[98:101], v43 offset:14864
	ds_read_b128 v[122:125], v43 offset:18944
	ds_read_b128 v[126:129], v43 offset:18960
	v_cvt_f32_f16_sdwa v97, v29 dst_sel:DWORD dst_unused:UNUSED_PAD src0_sel:WORD_1
	v_cvt_f32_f16_sdwa v133, v31 dst_sel:DWORD dst_unused:UNUSED_PAD src0_sel:WORD_1
	v_cvt_f32_f16_e32 v134, v31
	v_sub_f32_e32 v28, v28, v0
	v_sub_f32_e32 v29, v130, v1
	v_sub_f32_e32 v30, v131, v2
	v_pk_mul_f32 v[28:29], v[90:91], v[28:29]
	v_sub_f32_e32 v130, v135, v0
	v_sub_f32_e32 v131, v132, v1
	v_sub_f32_e32 v31, v97, v3
	v_sub_f32_e32 v132, v134, v2
	v_sub_f32_e32 v133, v133, v3
	v_pk_mul_f32 v[130:131], v[90:91], v[130:131]
	s_waitcnt lgkmcnt(1)
	v_fma_f32 v28, v36, v28, v122
	v_fma_f32 v29, v37, v29, v123
	v_pk_mul_f32 v[30:31], v[92:93], v[30:31]
	v_pk_mul_f32 v[132:133], v[92:93], v[132:133]
	s_waitcnt lgkmcnt(0)
	v_fma_f32 v36, v98, v130, v126
	ds_write2_b32 v96, v28, v29 offset1:68
	v_fma_f32 v28, v99, v131, v127
	ds_write2_b32 v44, v36, v28 offset0:16 offset1:84
	v_fma_f32 v28, v38, v30, v124
	v_fma_f32 v29, v100, v132, v128
	v_fmac_f32_e32 v125, v39, v31
	v_fmac_f32_e32 v129, v101, v133
	ds_write2_b32 v96, v28, v125 offset0:136 offset1:204
	ds_write2_b32 v44, v29, v129 offset0:152 offset1:220
	s_waitcnt vmcnt(2)
	ds_write_b128 v104, v[24:27] offset:41984
	s_mov_b32 s16, 0
	v_mov_b32_e32 v24, v112
	s_waitcnt lgkmcnt(0)
	s_barrier
	ds_read_b32 v200, v218
	ds_read_b32 v208, v219
	ds_read_b32 v201, v218 offset:544
	ds_read_b32 v209, v219 offset:256
	ds_read_b32 v202, v218 offset:1088
	ds_read_b32 v210, v219 offset:512
	ds_read_b32 v203, v218 offset:1632
	ds_read_b32 v211, v219 offset:768
	ds_read_b32 v204, v218 offset:2176
	ds_read_b32 v212, v219 offset:1024
	ds_read_b32 v205, v218 offset:2720
	ds_read_b32 v213, v219 offset:1280
	ds_read_b32 v206, v218 offset:3264
	ds_read_b32 v214, v219 offset:1536
	s_waitcnt lgkmcnt(12)
	v_mfma_f32_32x32x2_f32 v[4:19], v200, v208, v[4:19]
	ds_read_b32 v207, v218 offset:3808
	ds_read_b32 v215, v219 offset:1792
	s_waitcnt lgkmcnt(12)
	v_mfma_f32_32x32x2_f32 v[4:19], v201, v209, v[4:19]
	s_waitcnt lgkmcnt(10)
	v_mfma_f32_32x32x2_f32 v[4:19], v202, v210, v[4:19]
	s_waitcnt lgkmcnt(8)
	v_mfma_f32_32x32x2_f32 v[4:19], v203, v211, v[4:19]
	s_waitcnt lgkmcnt(6)
	v_mfma_f32_32x32x2_f32 v[4:19], v204, v212, v[4:19]
	s_waitcnt lgkmcnt(4)
	v_mfma_f32_32x32x2_f32 v[4:19], v205, v213, v[4:19]
	s_waitcnt lgkmcnt(2)
	v_mfma_f32_32x32x2_f32 v[4:19], v206, v214, v[4:19]
	s_waitcnt lgkmcnt(0)
	v_mfma_f32_32x32x2_f32 v[4:19], v207, v215, v[4:19]
	s_barrier
	global_load_dwordx4 v[28:31], v[94:95], off offset:1536
	global_load_dwordx4 v[24:27], v[74:75], off
	s_waitcnt vmcnt(3)
	v_cvt_f32_f16_sdwa v130, v32 dst_sel:DWORD dst_unused:UNUSED_PAD src0_sel:WORD_1
	v_cvt_f32_f16_e32 v32, v32
	v_cvt_f32_f16_e32 v131, v33
	v_cvt_f32_f16_sdwa v132, v34 dst_sel:DWORD dst_unused:UNUSED_PAD src0_sel:WORD_1
	v_cvt_f32_f16_e32 v135, v34
	ds_read_b128 v[36:39], v43 offset:15104
	ds_read_b128 v[98:101], v43 offset:15120
	ds_read_b128 v[122:125], v43 offset:19200
	ds_read_b128 v[126:129], v43 offset:19216
	v_cvt_f32_f16_sdwa v97, v33 dst_sel:DWORD dst_unused:UNUSED_PAD src0_sel:WORD_1
	v_cvt_f32_f16_sdwa v133, v35 dst_sel:DWORD dst_unused:UNUSED_PAD src0_sel:WORD_1
	v_cvt_f32_f16_e32 v134, v35
	v_sub_f32_e32 v32, v32, v0
	v_sub_f32_e32 v33, v130, v1
	v_sub_f32_e32 v34, v131, v2
	v_pk_mul_f32 v[32:33], v[90:91], v[32:33]
	v_sub_f32_e32 v130, v135, v0
	v_sub_f32_e32 v131, v132, v1
	v_sub_f32_e32 v35, v97, v3
	v_sub_f32_e32 v132, v134, v2
	v_sub_f32_e32 v133, v133, v3
	v_pk_mul_f32 v[130:131], v[90:91], v[130:131]
	s_waitcnt lgkmcnt(1)
	v_fma_f32 v32, v36, v32, v122
	v_fma_f32 v33, v37, v33, v123
	v_pk_mul_f32 v[34:35], v[92:93], v[34:35]
	v_pk_mul_f32 v[132:133], v[92:93], v[132:133]
	s_waitcnt lgkmcnt(0)
	v_fma_f32 v36, v98, v130, v126
	ds_write2_b32 v96, v32, v33 offset1:68
	v_fma_f32 v32, v99, v131, v127
	ds_write2_b32 v44, v36, v32 offset0:16 offset1:84
	v_fma_f32 v32, v38, v34, v124
	v_fma_f32 v33, v100, v132, v128
	v_fmac_f32_e32 v125, v39, v35
	v_fmac_f32_e32 v129, v101, v133
	ds_write2_b32 v96, v32, v125 offset0:136 offset1:204
	ds_write2_b32 v44, v33, v129 offset0:152 offset1:220
	s_waitcnt vmcnt(2)
	ds_write_b128 v104, v[20:23] offset:41984
	s_mov_b32 s16, 0
	v_mov_b32_e32 v20, v112
	s_waitcnt lgkmcnt(0)
	s_barrier
	ds_read_b32 v200, v218
	ds_read_b32 v208, v219
	ds_read_b32 v201, v218 offset:544
	ds_read_b32 v209, v219 offset:256
	ds_read_b32 v202, v218 offset:1088
	ds_read_b32 v210, v219 offset:512
	ds_read_b32 v203, v218 offset:1632
	ds_read_b32 v211, v219 offset:768
	ds_read_b32 v204, v218 offset:2176
	ds_read_b32 v212, v219 offset:1024
	ds_read_b32 v205, v218 offset:2720
	ds_read_b32 v213, v219 offset:1280
	ds_read_b32 v206, v218 offset:3264
	ds_read_b32 v214, v219 offset:1536
	s_waitcnt lgkmcnt(12)
	v_mfma_f32_32x32x2_f32 v[4:19], v200, v208, v[4:19]
	ds_read_b32 v207, v218 offset:3808
	ds_read_b32 v215, v219 offset:1792
	s_waitcnt lgkmcnt(12)
	v_mfma_f32_32x32x2_f32 v[4:19], v201, v209, v[4:19]
	s_waitcnt lgkmcnt(10)
	v_mfma_f32_32x32x2_f32 v[4:19], v202, v210, v[4:19]
	s_waitcnt lgkmcnt(8)
	v_mfma_f32_32x32x2_f32 v[4:19], v203, v211, v[4:19]
	s_waitcnt lgkmcnt(6)
	v_mfma_f32_32x32x2_f32 v[4:19], v204, v212, v[4:19]
	s_waitcnt lgkmcnt(4)
	v_mfma_f32_32x32x2_f32 v[4:19], v205, v213, v[4:19]
	s_waitcnt lgkmcnt(2)
	v_mfma_f32_32x32x2_f32 v[4:19], v206, v214, v[4:19]
	s_waitcnt lgkmcnt(0)
	v_mfma_f32_32x32x2_f32 v[4:19], v207, v215, v[4:19]
	s_barrier
	global_load_dwordx4 v[32:35], v[94:95], off offset:1664
	global_load_dwordx4 v[20:23], v[76:77], off
	s_waitcnt vmcnt(3)
	v_cvt_f32_f16_sdwa v130, v28 dst_sel:DWORD dst_unused:UNUSED_PAD src0_sel:WORD_1
	v_cvt_f32_f16_e32 v28, v28
	v_cvt_f32_f16_e32 v131, v29
	v_cvt_f32_f16_sdwa v132, v30 dst_sel:DWORD dst_unused:UNUSED_PAD src0_sel:WORD_1
	v_cvt_f32_f16_e32 v135, v30
	ds_read_b128 v[36:39], v43 offset:15360
	ds_read_b128 v[98:101], v43 offset:15376
	ds_read_b128 v[122:125], v43 offset:19456
	ds_read_b128 v[126:129], v43 offset:19472
	v_cvt_f32_f16_sdwa v97, v29 dst_sel:DWORD dst_unused:UNUSED_PAD src0_sel:WORD_1
	v_cvt_f32_f16_sdwa v133, v31 dst_sel:DWORD dst_unused:UNUSED_PAD src0_sel:WORD_1
	v_cvt_f32_f16_e32 v134, v31
	v_sub_f32_e32 v28, v28, v0
	v_sub_f32_e32 v29, v130, v1
	v_sub_f32_e32 v30, v131, v2
	v_pk_mul_f32 v[28:29], v[90:91], v[28:29]
	v_sub_f32_e32 v130, v135, v0
	v_sub_f32_e32 v131, v132, v1
	v_sub_f32_e32 v31, v97, v3
	v_sub_f32_e32 v132, v134, v2
	v_sub_f32_e32 v133, v133, v3
	v_pk_mul_f32 v[130:131], v[90:91], v[130:131]
	s_waitcnt lgkmcnt(1)
	v_fma_f32 v28, v36, v28, v122
	v_fma_f32 v29, v37, v29, v123
	v_pk_mul_f32 v[30:31], v[92:93], v[30:31]
	v_pk_mul_f32 v[132:133], v[92:93], v[132:133]
	s_waitcnt lgkmcnt(0)
	v_fma_f32 v36, v98, v130, v126
	ds_write2_b32 v96, v28, v29 offset1:68
	v_fma_f32 v28, v99, v131, v127
	ds_write2_b32 v44, v36, v28 offset0:16 offset1:84
	v_fma_f32 v28, v38, v30, v124
	v_fma_f32 v29, v100, v132, v128
	v_fmac_f32_e32 v125, v39, v31
	v_fmac_f32_e32 v129, v101, v133
	ds_write2_b32 v96, v28, v125 offset0:136 offset1:204
	ds_write2_b32 v44, v29, v129 offset0:152 offset1:220
	s_waitcnt vmcnt(2)
	ds_write_b128 v104, v[24:27] offset:41984
	s_mov_b32 s16, 0
	v_mov_b32_e32 v24, v112
	s_waitcnt lgkmcnt(0)
	s_barrier
	ds_read_b32 v200, v218
	ds_read_b32 v208, v219
	ds_read_b32 v201, v218 offset:544
	ds_read_b32 v209, v219 offset:256
	ds_read_b32 v202, v218 offset:1088
	ds_read_b32 v210, v219 offset:512
	ds_read_b32 v203, v218 offset:1632
	ds_read_b32 v211, v219 offset:768
	ds_read_b32 v204, v218 offset:2176
	ds_read_b32 v212, v219 offset:1024
	ds_read_b32 v205, v218 offset:2720
	ds_read_b32 v213, v219 offset:1280
	ds_read_b32 v206, v218 offset:3264
	ds_read_b32 v214, v219 offset:1536
	s_waitcnt lgkmcnt(12)
	v_mfma_f32_32x32x2_f32 v[4:19], v200, v208, v[4:19]
	ds_read_b32 v207, v218 offset:3808
	ds_read_b32 v215, v219 offset:1792
	s_waitcnt lgkmcnt(12)
	v_mfma_f32_32x32x2_f32 v[4:19], v201, v209, v[4:19]
	s_waitcnt lgkmcnt(10)
	v_mfma_f32_32x32x2_f32 v[4:19], v202, v210, v[4:19]
	s_waitcnt lgkmcnt(8)
	v_mfma_f32_32x32x2_f32 v[4:19], v203, v211, v[4:19]
	s_waitcnt lgkmcnt(6)
	v_mfma_f32_32x32x2_f32 v[4:19], v204, v212, v[4:19]
	s_waitcnt lgkmcnt(4)
	v_mfma_f32_32x32x2_f32 v[4:19], v205, v213, v[4:19]
	s_waitcnt lgkmcnt(2)
	v_mfma_f32_32x32x2_f32 v[4:19], v206, v214, v[4:19]
	s_waitcnt lgkmcnt(0)
	v_mfma_f32_32x32x2_f32 v[4:19], v207, v215, v[4:19]
	s_barrier
	global_load_dwordx4 v[28:31], v[94:95], off offset:1792
	global_load_dwordx4 v[24:27], v[78:79], off
	s_waitcnt vmcnt(3)
	v_cvt_f32_f16_sdwa v130, v32 dst_sel:DWORD dst_unused:UNUSED_PAD src0_sel:WORD_1
	v_cvt_f32_f16_e32 v32, v32
	v_cvt_f32_f16_e32 v131, v33
	v_cvt_f32_f16_sdwa v132, v34 dst_sel:DWORD dst_unused:UNUSED_PAD src0_sel:WORD_1
	v_cvt_f32_f16_e32 v135, v34
	ds_read_b128 v[36:39], v43 offset:15616
	ds_read_b128 v[98:101], v43 offset:15632
	ds_read_b128 v[122:125], v43 offset:19712
	ds_read_b128 v[126:129], v43 offset:19728
	v_cvt_f32_f16_sdwa v97, v33 dst_sel:DWORD dst_unused:UNUSED_PAD src0_sel:WORD_1
	v_cvt_f32_f16_sdwa v133, v35 dst_sel:DWORD dst_unused:UNUSED_PAD src0_sel:WORD_1
	v_cvt_f32_f16_e32 v134, v35
	v_sub_f32_e32 v32, v32, v0
	v_sub_f32_e32 v33, v130, v1
	v_sub_f32_e32 v34, v131, v2
	v_pk_mul_f32 v[32:33], v[90:91], v[32:33]
	v_sub_f32_e32 v130, v135, v0
	v_sub_f32_e32 v131, v132, v1
	v_sub_f32_e32 v35, v97, v3
	v_sub_f32_e32 v132, v134, v2
	v_sub_f32_e32 v133, v133, v3
	v_pk_mul_f32 v[130:131], v[90:91], v[130:131]
	s_waitcnt lgkmcnt(1)
	v_fma_f32 v32, v36, v32, v122
	v_fma_f32 v33, v37, v33, v123
	v_pk_mul_f32 v[34:35], v[92:93], v[34:35]
	v_pk_mul_f32 v[132:133], v[92:93], v[132:133]
	s_waitcnt lgkmcnt(0)
	v_fma_f32 v36, v98, v130, v126
	ds_write2_b32 v96, v32, v33 offset1:68
	v_fma_f32 v32, v99, v131, v127
	ds_write2_b32 v44, v36, v32 offset0:16 offset1:84
	v_fma_f32 v32, v38, v34, v124
	v_fma_f32 v33, v100, v132, v128
	v_fmac_f32_e32 v125, v39, v35
	v_fmac_f32_e32 v129, v101, v133
	ds_write2_b32 v96, v32, v125 offset0:136 offset1:204
	ds_write2_b32 v44, v33, v129 offset0:152 offset1:220
	s_waitcnt vmcnt(2)
	ds_write_b128 v104, v[20:23] offset:41984
	s_mov_b32 s16, 0
	v_mov_b32_e32 v20, v112
	s_waitcnt lgkmcnt(0)
	s_barrier
	ds_read_b32 v200, v218
	ds_read_b32 v208, v219
	ds_read_b32 v201, v218 offset:544
	ds_read_b32 v209, v219 offset:256
	ds_read_b32 v202, v218 offset:1088
	ds_read_b32 v210, v219 offset:512
	ds_read_b32 v203, v218 offset:1632
	ds_read_b32 v211, v219 offset:768
	ds_read_b32 v204, v218 offset:2176
	ds_read_b32 v212, v219 offset:1024
	ds_read_b32 v205, v218 offset:2720
	ds_read_b32 v213, v219 offset:1280
	ds_read_b32 v206, v218 offset:3264
	ds_read_b32 v214, v219 offset:1536
	s_waitcnt lgkmcnt(12)
	v_mfma_f32_32x32x2_f32 v[4:19], v200, v208, v[4:19]
	ds_read_b32 v207, v218 offset:3808
	ds_read_b32 v215, v219 offset:1792
	s_waitcnt lgkmcnt(12)
	v_mfma_f32_32x32x2_f32 v[4:19], v201, v209, v[4:19]
	s_waitcnt lgkmcnt(10)
	v_mfma_f32_32x32x2_f32 v[4:19], v202, v210, v[4:19]
	s_waitcnt lgkmcnt(8)
	v_mfma_f32_32x32x2_f32 v[4:19], v203, v211, v[4:19]
	s_waitcnt lgkmcnt(6)
	v_mfma_f32_32x32x2_f32 v[4:19], v204, v212, v[4:19]
	s_waitcnt lgkmcnt(4)
	v_mfma_f32_32x32x2_f32 v[4:19], v205, v213, v[4:19]
	s_waitcnt lgkmcnt(2)
	v_mfma_f32_32x32x2_f32 v[4:19], v206, v214, v[4:19]
	s_waitcnt lgkmcnt(0)
	v_mfma_f32_32x32x2_f32 v[4:19], v207, v215, v[4:19]
	s_barrier
	global_load_dwordx4 v[32:35], v[94:95], off offset:1920
	global_load_dwordx4 v[20:23], v[80:81], off
	s_waitcnt vmcnt(3)
	v_cvt_f32_f16_sdwa v95, v28 dst_sel:DWORD dst_unused:UNUSED_PAD src0_sel:WORD_1
	v_cvt_f32_f16_e32 v28, v28
	v_cvt_f32_f16_sdwa v94, v29 dst_sel:DWORD dst_unused:UNUSED_PAD src0_sel:WORD_1
	v_cvt_f32_f16_sdwa v130, v30 dst_sel:DWORD dst_unused:UNUSED_PAD src0_sel:WORD_1
	v_cvt_f32_f16_e32 v133, v30
	ds_read_b128 v[36:39], v43 offset:15872
	ds_read_b128 v[98:101], v43 offset:15888
	ds_read_b128 v[122:125], v43 offset:19968
	ds_read_b128 v[126:129], v43 offset:19984
	v_cvt_f32_f16_e32 v97, v29
	v_cvt_f32_f16_sdwa v131, v31 dst_sel:DWORD dst_unused:UNUSED_PAD src0_sel:WORD_1
	v_cvt_f32_f16_e32 v132, v31
	v_sub_f32_e32 v28, v28, v0
	v_sub_f32_e32 v29, v95, v1
	v_sub_f32_e32 v31, v94, v3
	v_pk_mul_f32 v[28:29], v[90:91], v[28:29]
	v_sub_f32_e32 v94, v133, v0
	v_sub_f32_e32 v95, v130, v1
	v_sub_f32_e32 v30, v97, v2
	v_sub_f32_e32 v130, v132, v2
	v_sub_f32_e32 v131, v131, v3
	v_pk_mul_f32 v[94:95], v[90:91], v[94:95]
	s_waitcnt lgkmcnt(1)
	v_fma_f32 v28, v36, v28, v122
	v_fma_f32 v29, v37, v29, v123
	v_pk_mul_f32 v[30:31], v[92:93], v[30:31]
	v_pk_mul_f32 v[130:131], v[92:93], v[130:131]
	s_waitcnt lgkmcnt(0)
	v_fma_f32 v36, v98, v94, v126
	ds_write2_b32 v96, v28, v29 offset1:68
	v_fma_f32 v28, v99, v95, v127
	ds_write2_b32 v44, v36, v28 offset0:16 offset1:84
	v_fma_f32 v28, v38, v30, v124
	v_fma_f32 v29, v100, v130, v128
	v_fmac_f32_e32 v125, v39, v31
	v_fmac_f32_e32 v129, v101, v131
	ds_write2_b32 v96, v28, v125 offset0:136 offset1:204
	ds_write2_b32 v44, v29, v129 offset0:152 offset1:220
	s_waitcnt vmcnt(2)
	ds_write_b128 v104, v[24:27] offset:41984
	s_mov_b32 s16, 0
	v_mov_b32_e32 v24, v112
	s_waitcnt lgkmcnt(0)
	s_barrier
	ds_read_b32 v200, v218
	ds_read_b32 v208, v219
	ds_read_b32 v201, v218 offset:544
	ds_read_b32 v209, v219 offset:256
	ds_read_b32 v202, v218 offset:1088
	ds_read_b32 v210, v219 offset:512
	ds_read_b32 v203, v218 offset:1632
	ds_read_b32 v211, v219 offset:768
	ds_read_b32 v204, v218 offset:2176
	ds_read_b32 v212, v219 offset:1024
	ds_read_b32 v205, v218 offset:2720
	ds_read_b32 v213, v219 offset:1280
	ds_read_b32 v206, v218 offset:3264
	ds_read_b32 v214, v219 offset:1536
	s_waitcnt lgkmcnt(12)
	v_mfma_f32_32x32x2_f32 v[4:19], v200, v208, v[4:19]
	ds_read_b32 v207, v218 offset:3808
	ds_read_b32 v215, v219 offset:1792
	s_waitcnt lgkmcnt(12)
	v_mfma_f32_32x32x2_f32 v[4:19], v201, v209, v[4:19]
	s_waitcnt lgkmcnt(10)
	v_mfma_f32_32x32x2_f32 v[4:19], v202, v210, v[4:19]
	s_waitcnt lgkmcnt(8)
	v_mfma_f32_32x32x2_f32 v[4:19], v203, v211, v[4:19]
	s_waitcnt lgkmcnt(6)
	v_mfma_f32_32x32x2_f32 v[4:19], v204, v212, v[4:19]
	s_waitcnt lgkmcnt(4)
	v_mfma_f32_32x32x2_f32 v[4:19], v205, v213, v[4:19]
	s_waitcnt lgkmcnt(2)
	v_mfma_f32_32x32x2_f32 v[4:19], v206, v214, v[4:19]
	s_waitcnt lgkmcnt(0)
	v_mfma_f32_32x32x2_f32 v[4:19], v207, v215, v[4:19]
	s_waitcnt vmcnt(1)
	v_cvt_f32_f16_sdwa v95, v32 dst_sel:DWORD dst_unused:UNUSED_PAD src0_sel:WORD_1
	v_cvt_f32_f16_e32 v32, v32
	v_cvt_f32_f16_sdwa v123, v34 dst_sel:DWORD dst_unused:UNUSED_PAD src0_sel:WORD_1
	v_cvt_f32_f16_e32 v125, v34
	s_barrier
	ds_read_b128 v[24:27], v43 offset:16128
	ds_read_b128 v[28:31], v43 offset:16144
	ds_read_b128 v[36:39], v43 offset:20224
	ds_read_b128 v[98:101], v43 offset:20240
	v_cvt_f32_f16_sdwa v94, v33 dst_sel:DWORD dst_unused:UNUSED_PAD src0_sel:WORD_1
	v_cvt_f32_f16_e32 v97, v33
	v_cvt_f32_f16_sdwa v122, v35 dst_sel:DWORD dst_unused:UNUSED_PAD src0_sel:WORD_1
	v_cvt_f32_f16_e32 v124, v35
	v_sub_f32_e32 v32, v32, v0
	v_sub_f32_e32 v33, v95, v1
	v_sub_f32_e32 v0, v125, v0
	v_sub_f32_e32 v1, v123, v1
	v_sub_f32_e32 v34, v97, v2
	v_sub_f32_e32 v35, v94, v3
	v_pk_mul_f32 v[0:1], v[90:91], v[0:1]
	v_pk_mul_f32 v[34:35], v[92:93], v[34:35]
	v_sub_f32_e32 v2, v124, v2
	v_sub_f32_e32 v3, v122, v3
	s_waitcnt lgkmcnt(0)
	v_fma_f32 v0, v28, v0, v98
	v_fma_f32 v1, v29, v1, v99
	v_pk_mul_f32 v[32:33], v[90:91], v[32:33]
	v_pk_mul_f32 v[2:3], v[92:93], v[2:3]
	ds_write2_b32 v44, v0, v1 offset0:16 offset1:84
	v_fma_f32 v0, v26, v34, v38
	v_fmac_f32_e32 v39, v27, v35
	v_fma_f32 v24, v24, v32, v36
	v_fma_f32 v25, v25, v33, v37
	v_fma_f32 v1, v30, v2, v100
	ds_write2_b32 v96, v0, v39 offset0:136 offset1:204
	v_fmac_f32_e32 v101, v31, v3
	s_mov_b32 s16, 0
	v_mov_b32_e32 v0, v112
	ds_write2_b32 v96, v24, v25 offset1:68
	ds_write2_b32 v44, v1, v101 offset0:152 offset1:220
	s_waitcnt vmcnt(0)
	ds_write_b128 v104, v[20:23] offset:41984
	s_waitcnt lgkmcnt(0)
	s_barrier
	ds_read_b32 v200, v218
	ds_read_b32 v208, v219
	ds_read_b32 v201, v218 offset:544
	ds_read_b32 v209, v219 offset:256
	ds_read_b32 v202, v218 offset:1088
	ds_read_b32 v210, v219 offset:512
	ds_read_b32 v203, v218 offset:1632
	ds_read_b32 v211, v219 offset:768
	ds_read_b32 v204, v218 offset:2176
	ds_read_b32 v212, v219 offset:1024
	ds_read_b32 v205, v218 offset:2720
	ds_read_b32 v213, v219 offset:1280
	ds_read_b32 v206, v218 offset:3264
	ds_read_b32 v214, v219 offset:1536
	s_waitcnt lgkmcnt(12)
	v_mfma_f32_32x32x2_f32 v[4:19], v200, v208, v[4:19]
	ds_read_b32 v207, v218 offset:3808
	ds_read_b32 v215, v219 offset:1792
	s_waitcnt lgkmcnt(12)
	v_mfma_f32_32x32x2_f32 v[4:19], v201, v209, v[4:19]
	s_waitcnt lgkmcnt(10)
	v_mfma_f32_32x32x2_f32 v[4:19], v202, v210, v[4:19]
	s_waitcnt lgkmcnt(8)
	v_mfma_f32_32x32x2_f32 v[4:19], v203, v211, v[4:19]
	s_waitcnt lgkmcnt(6)
	v_mfma_f32_32x32x2_f32 v[4:19], v204, v212, v[4:19]
	s_waitcnt lgkmcnt(4)
	v_mfma_f32_32x32x2_f32 v[4:19], v205, v213, v[4:19]
	s_waitcnt lgkmcnt(2)
	v_mfma_f32_32x32x2_f32 v[4:19], v206, v214, v[4:19]
	s_waitcnt lgkmcnt(0)
	v_mfma_f32_32x32x2_f32 v[4:19], v207, v215, v[4:19]
	s_barrier
	s_nop 15
	s_nop 3
	ds_write_b32 v217, v4 offset:58752
	ds_write_b32 v217, v5 offset:58880
	ds_write_b32 v217, v6 offset:59008
	ds_write_b32 v217, v7 offset:59136
	ds_write_b32 v217, v8 offset:59776
	ds_write_b32 v217, v9 offset:59904
	ds_write_b32 v217, v10 offset:60032
	ds_write_b32 v217, v11 offset:60160
	ds_write_b32 v217, v12 offset:60800
	ds_write_b32 v217, v13 offset:60928
	ds_write_b32 v217, v14 offset:61056
	ds_write_b32 v217, v15 offset:61184
	ds_write_b32 v217, v16 offset:61824
	ds_write_b32 v217, v17 offset:61952
	ds_write_b32 v217, v18 offset:62080
	ds_write_b32 v217, v19 offset:62208
	s_waitcnt lgkmcnt(0)
	s_barrier
	global_load_dwordx4 v[0:3], v[50:51], off
	ds_read_b128 v[4:7], v106 offset:58752
	ds_read_b128 v[8:11], v107 offset:8192
	ds_read_b128 v[12:15], v107 offset:16384
	ds_read_b128 v[16:19], v107 offset:24576
	v_add_u32_e32 v20, 0xc400, v108
	v_add_u32_e32 v21, 0xc408, v108
	s_waitcnt lgkmcnt(2)
	v_pk_add_f32 v[4:5], v[4:5], v[8:9]
	v_pk_add_f32 v[6:7], v[6:7], v[10:11]
	s_waitcnt lgkmcnt(1)
	v_pk_add_f32 v[4:5], v[12:13], v[4:5]
	v_pk_add_f32 v[6:7], v[14:15], v[6:7]
	s_waitcnt lgkmcnt(0)
	v_pk_add_f32 v[4:5], v[16:17], v[4:5]
	v_pk_add_f32 v[6:7], v[18:19], v[6:7]
	s_waitcnt vmcnt(0)
	v_pk_add_f32 v[0:1], v[0:1], v[4:5]
	v_pk_add_f32 v[2:3], v[6:7], v[2:3]
	ds_write2_b32 v20, v0, v1 offset1:1
	ds_write2_b32 v21, v2, v3 offset1:1
	s_waitcnt lgkmcnt(0)
	s_barrier
	s_and_saveexec_b64 s[28:29], s[6:7]
	s_cbranch_execz .LBB0_687
	v_add_u32_e32 v0, 0xc400, v117
	v_add_u32_e32 v1, 0xc408, v117
	v_add_u32_e32 v2, 0xc410, v117
	v_add_u32_e32 v3, 0xc418, v117
	ds_read2_b32 v[34:35], v0 offset1:1
	ds_read2_b32 v[30:31], v1 offset1:1
	ds_read2_b32 v[22:23], v2 offset1:1
	ds_read2_b32 v[10:11], v3 offset1:1
	s_mov_b32 s16, 0xff61b1e6
	s_waitcnt lgkmcnt(3)
	v_max_f32_e32 v0, v34, v34
	v_max_f32_e32 v0, 0xff61b1e6, v0
	v_cmp_lt_f32_e32 vcc, s16, v34
	v_cmp_gt_f32_e64 s[16:17], v35, v0
	v_add_u32_e32 v2, 0xc420, v117
	ds_read2_b32 v[24:25], v2 offset1:1
	v_cndmask_b32_e64 v0, v0, v35, s[16:17]
	v_cndmask_b32_e64 v1, 0, 1, s[16:17]
	s_waitcnt lgkmcnt(3)
	v_cmp_gt_f32_e64 s[16:17], v30, v0
	v_add_u32_e32 v2, 0xc428, v117
	v_add_u32_e32 v3, 0xc430, v117
	v_cndmask_b32_e64 v0, v0, v30, s[16:17]
	v_cndmask_b32_e64 v1, v1, 2, s[16:17]
	v_cmp_gt_f32_e64 s[16:17], v31, v0
	v_add_u32_e32 v4, 0xc438, v117
	ds_read2_b32 v[32:33], v2 offset1:1
	ds_read2_b32 v[20:21], v3 offset1:1
	ds_read2_b32 v[6:7], v4 offset1:1
	v_cndmask_b32_e64 v0, v0, v31, s[16:17]
	v_cndmask_b32_e64 v1, v1, 3, s[16:17]
	s_waitcnt lgkmcnt(5)
	v_cmp_gt_f32_e64 s[16:17], v22, v0
	v_add_u32_e32 v2, 0xc440, v117
	ds_read2_b32 v[18:19], v2 offset1:1
	v_cndmask_b32_e64 v0, v0, v22, s[16:17]
	v_cndmask_b32_e64 v1, v1, 4, s[16:17]
	v_cmp_gt_f32_e64 s[16:17], v23, v0
	v_add_u32_e32 v2, 0xc448, v117
	v_add_u32_e32 v4, 0xc458, v117
	v_cndmask_b32_e64 v0, v0, v23, s[16:17]
	v_cndmask_b32_e64 v1, v1, 5, s[16:17]
	s_waitcnt lgkmcnt(5)
	v_cmp_gt_f32_e64 s[16:17], v10, v0
	v_add_u32_e32 v3, 0xc450, v117
	ds_read2_b32 v[26:27], v2 offset1:1
	ds_read2_b32 v[12:13], v3 offset1:1
	ds_read2_b32 v[4:5], v4 offset1:1
	v_cndmask_b32_e64 v0, v0, v10, s[16:17]
	v_cndmask_b32_e64 v1, v1, 6, s[16:17]
	v_cmp_gt_f32_e64 s[16:17], v11, v0
	v_add_u32_e32 v2, 0xc460, v117
	ds_read2_b32 v[14:15], v2 offset1:1
	v_cndmask_b32_e64 v0, v0, v11, s[16:17]
	v_cndmask_b32_e64 v1, v1, 7, s[16:17]
	s_waitcnt lgkmcnt(8)
	v_cmp_gt_f32_e64 s[16:17], v24, v0
	v_add_u32_e32 v2, 0xc468, v117
	v_add_u32_e32 v8, 0xc478, v117
	v_cndmask_b32_e64 v0, v0, v24, s[16:17]
	v_cndmask_b32_e64 v1, v1, 8, s[16:17]
	v_cmp_gt_f32_e64 s[16:17], v25, v0
	v_add_u32_e32 v3, 0xc470, v117
	ds_read2_b32 v[28:29], v2 offset1:1
	ds_read2_b32 v[16:17], v3 offset1:1
	ds_read2_b32 v[8:9], v8 offset1:1
	v_cndmask_b32_e64 v0, v0, v25, s[16:17]
	v_cndmask_b32_e64 v1, v1, 9, s[16:17]
	s_waitcnt lgkmcnt(10)
	v_cmp_gt_f32_e64 s[16:17], v32, v0
	s_nop 1
	v_cndmask_b32_e64 v0, v0, v32, s[16:17]
	v_cndmask_b32_e64 v1, v1, 10, s[16:17]
	v_cmp_gt_f32_e64 s[16:17], v33, v0
	s_nop 1
	v_cndmask_b32_e64 v0, v0, v33, s[16:17]
	v_cndmask_b32_e64 v1, v1, 11, s[16:17]
	s_waitcnt lgkmcnt(9)
	v_cmp_gt_f32_e64 s[16:17], v20, v0
	s_nop 1
	v_cndmask_b32_e64 v0, v0, v20, s[16:17]
	v_cndmask_b32_e64 v1, v1, 12, s[16:17]
	v_cmp_gt_f32_e64 s[16:17], v21, v0
	s_nop 1
	v_cndmask_b32_e64 v0, v0, v21, s[16:17]
	v_cndmask_b32_e64 v1, v1, 13, s[16:17]
	s_waitcnt lgkmcnt(8)
	v_cmp_gt_f32_e64 s[16:17], v6, v0
	s_nop 1
	v_cndmask_b32_e64 v0, v0, v6, s[16:17]
	v_cndmask_b32_e64 v1, v1, 14, s[16:17]
	v_cmp_gt_f32_e64 s[16:17], v7, v0
	s_nop 1
	v_cndmask_b32_e64 v0, v0, v7, s[16:17]
	v_cndmask_b32_e64 v1, v1, 15, s[16:17]
	s_waitcnt lgkmcnt(7)
	v_cmp_gt_f32_e64 s[16:17], v18, v0
	s_nop 1
	v_cndmask_b32_e64 v0, v0, v18, s[16:17]
	v_cndmask_b32_e64 v1, v1, 16, s[16:17]
	v_cmp_gt_f32_e64 s[16:17], v19, v0
	s_nop 1
	v_cndmask_b32_e64 v0, v0, v19, s[16:17]
	v_cndmask_b32_e64 v1, v1, 17, s[16:17]
	s_waitcnt lgkmcnt(6)
	v_cmp_gt_f32_e64 s[16:17], v26, v0
	s_nop 1
	v_cndmask_b32_e64 v0, v0, v26, s[16:17]
	v_cndmask_b32_e64 v1, v1, 18, s[16:17]
	v_cmp_gt_f32_e64 s[16:17], v27, v0
	s_nop 1
	v_cndmask_b32_e64 v0, v0, v27, s[16:17]
	v_cndmask_b32_e64 v1, v1, 19, s[16:17]
	s_waitcnt lgkmcnt(5)
	v_cmp_gt_f32_e64 s[16:17], v12, v0
	s_nop 1
	v_cndmask_b32_e64 v0, v0, v12, s[16:17]
	v_cndmask_b32_e64 v1, v1, 20, s[16:17]
	v_cmp_gt_f32_e64 s[16:17], v13, v0
	s_nop 1
	v_cndmask_b32_e64 v0, v0, v13, s[16:17]
	v_cndmask_b32_e64 v1, v1, 21, s[16:17]
	s_waitcnt lgkmcnt(4)
	v_cmp_gt_f32_e64 s[16:17], v4, v0
	s_nop 1
	v_cndmask_b32_e64 v0, v0, v4, s[16:17]
	v_cndmask_b32_e64 v1, v1, 22, s[16:17]
	v_cmp_gt_f32_e64 s[16:17], v5, v0
	s_nop 1
	v_cndmask_b32_e64 v0, v0, v5, s[16:17]
	v_cndmask_b32_e64 v1, v1, 23, s[16:17]
	s_waitcnt lgkmcnt(3)
	v_cmp_gt_f32_e64 s[16:17], v14, v0
	s_nop 1
	v_cndmask_b32_e64 v0, v0, v14, s[16:17]
	v_cndmask_b32_e64 v1, v1, 24, s[16:17]
	v_cmp_gt_f32_e64 s[16:17], v15, v0
	s_nop 1
	v_cndmask_b32_e64 v0, v0, v15, s[16:17]
	v_cndmask_b32_e64 v1, v1, 25, s[16:17]
	s_waitcnt lgkmcnt(2)
	v_cmp_gt_f32_e64 s[16:17], v28, v0
	s_nop 1
	v_cndmask_b32_e64 v0, v0, v28, s[16:17]
	v_cndmask_b32_e64 v1, v1, 26, s[16:17]
	v_cmp_gt_f32_e64 s[16:17], v29, v0
	s_nop 1
	v_cndmask_b32_e64 v0, v0, v29, s[16:17]
	v_cndmask_b32_e64 v1, v1, 27, s[16:17]
	s_waitcnt lgkmcnt(1)
	v_cmp_gt_f32_e64 s[16:17], v16, v0
	s_nop 1
	v_cndmask_b32_e64 v0, v0, v16, s[16:17]
	v_cndmask_b32_e64 v1, v1, 28, s[16:17]
	v_cmp_gt_f32_e64 s[16:17], v17, v0
	s_nop 1
	v_cndmask_b32_e64 v0, v0, v17, s[16:17]
	v_cndmask_b32_e64 v1, v1, 29, s[16:17]
	s_waitcnt lgkmcnt(0)
	v_cmp_gt_f32_e64 s[16:17], v8, v0
	s_nop 1
	v_cndmask_b32_e64 v0, v0, v8, s[16:17]
	v_cndmask_b32_e64 v1, v1, 30, s[16:17]
	v_cmp_gt_f32_e64 s[16:17], v9, v0
	s_nop 1
	v_cndmask_b32_e64 v36, v0, v9, s[16:17]
	v_cndmask_b32_e64 v0, v1, 31, s[16:17]
	v_cmp_ne_u32_e64 s[16:17], 0, v0
	v_lshlrev_b32_e64 v2, v0, 1
	s_and_b64 s[16:17], s[16:17], vcc
	v_cndmask_b32_e64 v1, v121, v34, s[16:17]
	v_and_b32_e32 v3, 2, v2
	v_cmp_eq_u32_e64 s[16:17], 0, v3
	v_cmp_gt_f32_e64 s[18:19], v35, v1
	s_and_b64 s[16:17], s[16:17], s[18:19]
	v_cndmask_b32_e64 v1, v1, v35, s[16:17]
	v_and_b32_e32 v37, 4, v2
	v_cndmask_b32_e64 v3, 0, 1, s[16:17]
	v_cmp_eq_u32_e64 s[16:17], 0, v37
	v_cmp_gt_f32_e64 s[18:19], v30, v1
	s_and_b64 s[16:17], s[16:17], s[18:19]
	v_cndmask_b32_e64 v1, v1, v30, s[16:17]
	v_and_b32_e32 v37, 8, v2
	v_cndmask_b32_e64 v3, v3, 2, s[16:17]
	v_cmp_eq_u32_e64 s[16:17], 0, v37
	v_cmp_gt_f32_e64 s[18:19], v31, v1
	s_and_b64 s[16:17], s[16:17], s[18:19]
	v_cndmask_b32_e64 v1, v1, v31, s[16:17]
	v_and_b32_e32 v37, 16, v2
	v_cndmask_b32_e64 v3, v3, 3, s[16:17]
	v_cmp_eq_u32_e64 s[16:17], 0, v37
	v_cmp_gt_f32_e64 s[18:19], v22, v1
	s_and_b64 s[16:17], s[16:17], s[18:19]
	v_cndmask_b32_e64 v1, v1, v22, s[16:17]
	v_and_b32_e32 v37, 32, v2
	v_cndmask_b32_e64 v3, v3, 4, s[16:17]
	v_cmp_eq_u32_e64 s[16:17], 0, v37
	v_cmp_gt_f32_e64 s[18:19], v23, v1
	s_and_b64 s[16:17], s[16:17], s[18:19]
	v_cndmask_b32_e64 v1, v1, v23, s[16:17]
	v_and_b32_e32 v37, 64, v2
	v_cndmask_b32_e64 v3, v3, 5, s[16:17]
	v_cmp_eq_u32_e64 s[16:17], 0, v37
	v_cmp_gt_f32_e64 s[18:19], v10, v1
	s_and_b64 s[16:17], s[16:17], s[18:19]
	v_cndmask_b32_e64 v1, v1, v10, s[16:17]
	v_and_b32_e32 v37, 0x80, v2
	v_cndmask_b32_e64 v3, v3, 6, s[16:17]
	v_cmp_eq_u32_e64 s[16:17], 0, v37
	v_cmp_gt_f32_e64 s[18:19], v11, v1
	s_and_b64 s[16:17], s[16:17], s[18:19]
	v_cndmask_b32_e64 v1, v1, v11, s[16:17]
	v_and_b32_e32 v37, 0x100, v2
	v_cndmask_b32_e64 v3, v3, 7, s[16:17]
	v_cmp_eq_u32_e64 s[16:17], 0, v37
	v_cmp_gt_f32_e64 s[18:19], v24, v1
	s_and_b64 s[16:17], s[16:17], s[18:19]
	v_cndmask_b32_e64 v1, v1, v24, s[16:17]
	v_and_b32_e32 v37, 0x200, v2
	v_cndmask_b32_e64 v3, v3, 8, s[16:17]
	v_cmp_eq_u32_e64 s[16:17], 0, v37
	v_cmp_gt_f32_e64 s[18:19], v25, v1
	s_and_b64 s[16:17], s[16:17], s[18:19]
	v_cndmask_b32_e64 v1, v1, v25, s[16:17]
	v_and_b32_e32 v37, 0x400, v2
	v_cndmask_b32_e64 v3, v3, 9, s[16:17]
	v_cmp_eq_u32_e64 s[16:17], 0, v37
	v_cmp_gt_f32_e64 s[18:19], v32, v1
	s_and_b64 s[16:17], s[16:17], s[18:19]
	v_cndmask_b32_e64 v1, v1, v32, s[16:17]
	v_and_b32_e32 v37, 0x800, v2
	v_cndmask_b32_e64 v3, v3, 10, s[16:17]
	v_cmp_eq_u32_e64 s[16:17], 0, v37
	v_cmp_gt_f32_e64 s[18:19], v33, v1
	s_and_b64 s[16:17], s[16:17], s[18:19]
	v_cndmask_b32_e64 v1, v1, v33, s[16:17]
	v_and_b32_e32 v37, 0x1000, v2
	v_cndmask_b32_e64 v3, v3, 11, s[16:17]
	v_cmp_eq_u32_e64 s[16:17], 0, v37
	v_cmp_gt_f32_e64 s[18:19], v20, v1
	s_and_b64 s[16:17], s[16:17], s[18:19]
	v_cndmask_b32_e64 v1, v1, v20, s[16:17]
	v_and_b32_e32 v37, 0x2000, v2
	v_cndmask_b32_e64 v3, v3, 12, s[16:17]
	v_cmp_eq_u32_e64 s[16:17], 0, v37
	v_cmp_gt_f32_e64 s[18:19], v21, v1
	s_and_b64 s[16:17], s[16:17], s[18:19]
	v_cndmask_b32_e64 v1, v1, v21, s[16:17]
	v_and_b32_e32 v37, 0x4000, v2
	v_cndmask_b32_e64 v3, v3, 13, s[16:17]
	v_cmp_eq_u32_e64 s[16:17], 0, v37
	v_cmp_gt_f32_e64 s[18:19], v6, v1
	s_and_b64 s[16:17], s[16:17], s[18:19]
	v_cndmask_b32_e64 v1, v1, v6, s[16:17]
	v_and_b32_e32 v37, 0x8000, v2
	v_cndmask_b32_e64 v3, v3, 14, s[16:17]
	v_cmp_eq_u32_e64 s[16:17], 0, v37
	v_cmp_gt_f32_e64 s[18:19], v7, v1
	s_and_b64 s[16:17], s[16:17], s[18:19]
	v_cndmask_b32_e64 v1, v1, v7, s[16:17]
	v_and_b32_e32 v37, 0x10000, v2
	v_cndmask_b32_e64 v3, v3, 15, s[16:17]
	v_cmp_eq_u32_e64 s[16:17], 0, v37
	v_cmp_gt_f32_e64 s[18:19], v18, v1
	s_and_b64 s[16:17], s[16:17], s[18:19]
	v_cndmask_b32_e64 v1, v1, v18, s[16:17]
	v_and_b32_e32 v37, 0x20000, v2
	v_cndmask_b32_e64 v3, v3, 16, s[16:17]
	v_cmp_eq_u32_e64 s[16:17], 0, v37
	v_cmp_gt_f32_e64 s[18:19], v19, v1
	s_and_b64 s[16:17], s[16:17], s[18:19]
	v_cndmask_b32_e64 v1, v1, v19, s[16:17]
	v_and_b32_e32 v37, 0x40000, v2
	v_cndmask_b32_e64 v3, v3, 17, s[16:17]
	v_cmp_eq_u32_e64 s[16:17], 0, v37
	v_cmp_gt_f32_e64 s[18:19], v26, v1
	s_and_b64 s[16:17], s[16:17], s[18:19]
	v_cndmask_b32_e64 v1, v1, v26, s[16:17]
	v_and_b32_e32 v37, 0x80000, v2
	v_cndmask_b32_e64 v3, v3, 18, s[16:17]
	v_cmp_eq_u32_e64 s[16:17], 0, v37
	v_cmp_gt_f32_e64 s[18:19], v27, v1
	s_and_b64 s[16:17], s[16:17], s[18:19]
	v_cndmask_b32_e64 v1, v1, v27, s[16:17]
	v_and_b32_e32 v37, 0x100000, v2
	v_cndmask_b32_e64 v3, v3, 19, s[16:17]
	v_cmp_eq_u32_e64 s[16:17], 0, v37
	v_cmp_gt_f32_e64 s[18:19], v12, v1
	s_and_b64 s[16:17], s[16:17], s[18:19]
	v_cndmask_b32_e64 v1, v1, v12, s[16:17]
	v_and_b32_e32 v37, 0x200000, v2
	v_cndmask_b32_e64 v3, v3, 20, s[16:17]
	v_cmp_eq_u32_e64 s[16:17], 0, v37
	v_cmp_gt_f32_e64 s[18:19], v13, v1
	s_and_b64 s[16:17], s[16:17], s[18:19]
	v_cndmask_b32_e64 v1, v1, v13, s[16:17]
	v_and_b32_e32 v37, 0x400000, v2
	v_cndmask_b32_e64 v3, v3, 21, s[16:17]
	v_cmp_eq_u32_e64 s[16:17], 0, v37
	v_cmp_gt_f32_e64 s[18:19], v4, v1
	s_and_b64 s[16:17], s[16:17], s[18:19]
	v_cndmask_b32_e64 v1, v1, v4, s[16:17]
	v_and_b32_e32 v37, 0x800000, v2
	v_cndmask_b32_e64 v3, v3, 22, s[16:17]
	v_cmp_eq_u32_e64 s[16:17], 0, v37
	v_cmp_gt_f32_e64 s[18:19], v5, v1
	s_and_b64 s[16:17], s[16:17], s[18:19]
	v_cndmask_b32_e64 v1, v1, v5, s[16:17]
	v_and_b32_e32 v37, 0x1000000, v2
	v_cndmask_b32_e64 v3, v3, 23, s[16:17]
	v_cmp_eq_u32_e64 s[16:17], 0, v37
	v_cmp_gt_f32_e64 s[18:19], v14, v1
	s_and_b64 s[16:17], s[16:17], s[18:19]
	v_cndmask_b32_e64 v1, v1, v14, s[16:17]
	v_and_b32_e32 v37, 0x2000000, v2
	v_cndmask_b32_e64 v3, v3, 24, s[16:17]
	v_cmp_eq_u32_e64 s[16:17], 0, v37
	v_cmp_gt_f32_e64 s[18:19], v15, v1
	s_and_b64 s[16:17], s[16:17], s[18:19]
	v_cndmask_b32_e64 v1, v1, v15, s[16:17]
	v_and_b32_e32 v37, 0x4000000, v2
	v_cndmask_b32_e64 v3, v3, 25, s[16:17]
	v_cmp_eq_u32_e64 s[16:17], 0, v37
	v_cmp_gt_f32_e64 s[18:19], v28, v1
	s_and_b64 s[16:17], s[16:17], s[18:19]
	v_cndmask_b32_e64 v1, v1, v28, s[16:17]
	v_and_b32_e32 v37, 0x8000000, v2
	v_cndmask_b32_e64 v3, v3, 26, s[16:17]
	v_cmp_eq_u32_e64 s[16:17], 0, v37
	v_cmp_gt_f32_e64 s[18:19], v29, v1
	s_and_b64 s[16:17], s[16:17], s[18:19]
	v_cndmask_b32_e64 v1, v1, v29, s[16:17]
	v_and_b32_e32 v37, 0x10000000, v2
	v_cndmask_b32_e64 v3, v3, 27, s[16:17]
	v_cmp_eq_u32_e64 s[16:17], 0, v37
	v_cmp_gt_f32_e64 s[18:19], v16, v1
	s_and_b64 s[16:17], s[16:17], s[18:19]
	v_cndmask_b32_e64 v1, v1, v16, s[16:17]
	v_and_b32_e32 v37, 0x20000000, v2
	v_cndmask_b32_e64 v3, v3, 28, s[16:17]
	v_cmp_eq_u32_e64 s[16:17], 0, v37
	v_cmp_gt_f32_e64 s[18:19], v17, v1
	s_and_b64 s[16:17], s[16:17], s[18:19]
	v_cndmask_b32_e64 v1, v1, v17, s[16:17]
	v_and_b32_e32 v37, 2.0, v2
	v_cndmask_b32_e64 v3, v3, 29, s[16:17]
	v_cmp_eq_u32_e64 s[16:17], 0, v37
	v_cmp_gt_f32_e64 s[18:19], v8, v1
	s_and_b64 s[16:17], s[16:17], s[18:19]
	v_cndmask_b32_e64 v1, v1, v8, s[16:17]
	v_cndmask_b32_e64 v3, v3, 30, s[16:17]
	v_cmp_ne_u32_e64 s[16:17], 31, v0
	v_cmp_gt_f32_e64 s[18:19], v9, v1
	s_and_b64 s[16:17], s[16:17], s[18:19]
	v_cndmask_b32_e64 v37, v1, v9, s[16:17]
	v_cndmask_b32_e64 v1, v3, 31, s[16:17]
	v_lshl_or_b32 v3, 1, v1, v2
	v_and_b32_e32 v2, 1, v3
	v_cmp_eq_u32_e64 s[16:17], 0, v2
	s_and_b64 s[16:17], s[16:17], vcc
	v_and_b32_e32 v38, 2, v3
	v_cndmask_b32_e64 v2, v121, v34, s[16:17]
	v_cmp_eq_u32_e64 s[16:17], 0, v38
	v_cmp_gt_f32_e64 s[18:19], v35, v2
	s_and_b64 s[16:17], s[16:17], s[18:19]
	v_cndmask_b32_e64 v2, v2, v35, s[16:17]
	v_and_b32_e32 v39, 4, v3
	v_cndmask_b32_e64 v38, 0, 1, s[16:17]
	v_cmp_eq_u32_e64 s[16:17], 0, v39
	v_cmp_gt_f32_e64 s[18:19], v30, v2
	s_and_b64 s[16:17], s[16:17], s[18:19]
	v_cndmask_b32_e64 v2, v2, v30, s[16:17]
	v_and_b32_e32 v39, 8, v3
	v_cndmask_b32_e64 v38, v38, 2, s[16:17]
	v_cmp_eq_u32_e64 s[16:17], 0, v39
	v_cmp_gt_f32_e64 s[18:19], v31, v2
	s_and_b64 s[16:17], s[16:17], s[18:19]
	v_cndmask_b32_e64 v2, v2, v31, s[16:17]
	v_and_b32_e32 v39, 16, v3
	v_cndmask_b32_e64 v38, v38, 3, s[16:17]
	v_cmp_eq_u32_e64 s[16:17], 0, v39
	v_cmp_gt_f32_e64 s[18:19], v22, v2
	s_and_b64 s[16:17], s[16:17], s[18:19]
	v_cndmask_b32_e64 v2, v2, v22, s[16:17]
	v_and_b32_e32 v39, 32, v3
	v_cndmask_b32_e64 v38, v38, 4, s[16:17]
	v_cmp_eq_u32_e64 s[16:17], 0, v39
	v_cmp_gt_f32_e64 s[18:19], v23, v2
	s_and_b64 s[16:17], s[16:17], s[18:19]
	v_cndmask_b32_e64 v2, v2, v23, s[16:17]
	v_and_b32_e32 v39, 64, v3
	v_cndmask_b32_e64 v38, v38, 5, s[16:17]
	v_cmp_eq_u32_e64 s[16:17], 0, v39
	v_cmp_gt_f32_e64 s[18:19], v10, v2
	s_and_b64 s[16:17], s[16:17], s[18:19]
	v_cndmask_b32_e64 v2, v2, v10, s[16:17]
	v_and_b32_e32 v39, 0x80, v3
	v_cndmask_b32_e64 v38, v38, 6, s[16:17]
	v_cmp_eq_u32_e64 s[16:17], 0, v39
	v_cmp_gt_f32_e64 s[18:19], v11, v2
	s_and_b64 s[16:17], s[16:17], s[18:19]
	v_cndmask_b32_e64 v2, v2, v11, s[16:17]
	v_and_b32_e32 v39, 0x100, v3
	v_cndmask_b32_e64 v38, v38, 7, s[16:17]
	v_cmp_eq_u32_e64 s[16:17], 0, v39
	v_cmp_gt_f32_e64 s[18:19], v24, v2
	s_and_b64 s[16:17], s[16:17], s[18:19]
	v_cndmask_b32_e64 v2, v2, v24, s[16:17]
	v_and_b32_e32 v39, 0x200, v3
	v_cndmask_b32_e64 v38, v38, 8, s[16:17]
	v_cmp_eq_u32_e64 s[16:17], 0, v39
	v_cmp_gt_f32_e64 s[18:19], v25, v2
	s_and_b64 s[16:17], s[16:17], s[18:19]
	v_cndmask_b32_e64 v2, v2, v25, s[16:17]
	v_and_b32_e32 v39, 0x400, v3
	v_cndmask_b32_e64 v38, v38, 9, s[16:17]
	v_cmp_eq_u32_e64 s[16:17], 0, v39
	v_cmp_gt_f32_e64 s[18:19], v32, v2
	s_and_b64 s[16:17], s[16:17], s[18:19]
	v_cndmask_b32_e64 v2, v2, v32, s[16:17]
	v_and_b32_e32 v39, 0x800, v3
	v_cndmask_b32_e64 v38, v38, 10, s[16:17]
	v_cmp_eq_u32_e64 s[16:17], 0, v39
	v_cmp_gt_f32_e64 s[18:19], v33, v2
	s_and_b64 s[16:17], s[16:17], s[18:19]
	v_cndmask_b32_e64 v2, v2, v33, s[16:17]
	v_and_b32_e32 v39, 0x1000, v3
	v_cndmask_b32_e64 v38, v38, 11, s[16:17]
	v_cmp_eq_u32_e64 s[16:17], 0, v39
	v_cmp_gt_f32_e64 s[18:19], v20, v2
	s_and_b64 s[16:17], s[16:17], s[18:19]
	v_cndmask_b32_e64 v2, v2, v20, s[16:17]
	v_and_b32_e32 v39, 0x2000, v3
	v_cndmask_b32_e64 v38, v38, 12, s[16:17]
	v_cmp_eq_u32_e64 s[16:17], 0, v39
	v_cmp_gt_f32_e64 s[18:19], v21, v2
	s_and_b64 s[16:17], s[16:17], s[18:19]
	v_cndmask_b32_e64 v2, v2, v21, s[16:17]
	v_and_b32_e32 v39, 0x4000, v3
	v_cndmask_b32_e64 v38, v38, 13, s[16:17]
	v_cmp_eq_u32_e64 s[16:17], 0, v39
	v_cmp_gt_f32_e64 s[18:19], v6, v2
	s_and_b64 s[16:17], s[16:17], s[18:19]
	v_cndmask_b32_e64 v2, v2, v6, s[16:17]
	v_and_b32_e32 v39, 0x8000, v3
	v_cndmask_b32_e64 v38, v38, 14, s[16:17]
	v_cmp_eq_u32_e64 s[16:17], 0, v39
	v_cmp_gt_f32_e64 s[18:19], v7, v2
	s_and_b64 s[16:17], s[16:17], s[18:19]
	v_cndmask_b32_e64 v2, v2, v7, s[16:17]
	v_and_b32_e32 v39, 0x10000, v3
	v_cndmask_b32_e64 v38, v38, 15, s[16:17]
	v_cmp_eq_u32_e64 s[16:17], 0, v39
	v_cmp_gt_f32_e64 s[18:19], v18, v2
	s_and_b64 s[16:17], s[16:17], s[18:19]
	v_cndmask_b32_e64 v2, v2, v18, s[16:17]
	v_and_b32_e32 v39, 0x20000, v3
	v_cndmask_b32_e64 v38, v38, 16, s[16:17]
	v_cmp_eq_u32_e64 s[16:17], 0, v39
	v_cmp_gt_f32_e64 s[18:19], v19, v2
	s_and_b64 s[16:17], s[16:17], s[18:19]
	v_cndmask_b32_e64 v2, v2, v19, s[16:17]
	v_and_b32_e32 v39, 0x40000, v3
	v_cndmask_b32_e64 v38, v38, 17, s[16:17]
	v_cmp_eq_u32_e64 s[16:17], 0, v39
	v_cmp_gt_f32_e64 s[18:19], v26, v2
	s_and_b64 s[16:17], s[16:17], s[18:19]
	v_cndmask_b32_e64 v2, v2, v26, s[16:17]
	v_and_b32_e32 v39, 0x80000, v3
	v_cndmask_b32_e64 v38, v38, 18, s[16:17]
	v_cmp_eq_u32_e64 s[16:17], 0, v39
	v_cmp_gt_f32_e64 s[18:19], v27, v2
	s_and_b64 s[16:17], s[16:17], s[18:19]
	v_cndmask_b32_e64 v2, v2, v27, s[16:17]
	v_and_b32_e32 v39, 0x100000, v3
	v_cndmask_b32_e64 v38, v38, 19, s[16:17]
	v_cmp_eq_u32_e64 s[16:17], 0, v39
	v_cmp_gt_f32_e64 s[18:19], v12, v2
	s_and_b64 s[16:17], s[16:17], s[18:19]
	v_cndmask_b32_e64 v2, v2, v12, s[16:17]
	v_and_b32_e32 v39, 0x200000, v3
	v_cndmask_b32_e64 v38, v38, 20, s[16:17]
	v_cmp_eq_u32_e64 s[16:17], 0, v39
	v_cmp_gt_f32_e64 s[18:19], v13, v2
	s_and_b64 s[16:17], s[16:17], s[18:19]
	v_cndmask_b32_e64 v2, v2, v13, s[16:17]
	v_and_b32_e32 v39, 0x400000, v3
	v_cndmask_b32_e64 v38, v38, 21, s[16:17]
	v_cmp_eq_u32_e64 s[16:17], 0, v39
	v_cmp_gt_f32_e64 s[18:19], v4, v2
	s_and_b64 s[16:17], s[16:17], s[18:19]
	v_cndmask_b32_e64 v2, v2, v4, s[16:17]
	v_and_b32_e32 v39, 0x800000, v3
	v_cndmask_b32_e64 v38, v38, 22, s[16:17]
	v_cmp_eq_u32_e64 s[16:17], 0, v39
	v_cmp_gt_f32_e64 s[18:19], v5, v2
	s_and_b64 s[16:17], s[16:17], s[18:19]
	v_cndmask_b32_e64 v2, v2, v5, s[16:17]
	v_and_b32_e32 v39, 0x1000000, v3
	v_cndmask_b32_e64 v38, v38, 23, s[16:17]
	v_cmp_eq_u32_e64 s[16:17], 0, v39
	v_cmp_gt_f32_e64 s[18:19], v14, v2
	s_and_b64 s[16:17], s[16:17], s[18:19]
	v_cndmask_b32_e64 v2, v2, v14, s[16:17]
	v_and_b32_e32 v39, 0x2000000, v3
	v_cndmask_b32_e64 v38, v38, 24, s[16:17]
	v_cmp_eq_u32_e64 s[16:17], 0, v39
	v_cmp_gt_f32_e64 s[18:19], v15, v2
	s_and_b64 s[16:17], s[16:17], s[18:19]
	v_cndmask_b32_e64 v2, v2, v15, s[16:17]
	v_and_b32_e32 v39, 0x4000000, v3
	v_cndmask_b32_e64 v38, v38, 25, s[16:17]
	v_cmp_eq_u32_e64 s[16:17], 0, v39
	v_cmp_gt_f32_e64 s[18:19], v28, v2
	s_and_b64 s[16:17], s[16:17], s[18:19]
	v_cndmask_b32_e64 v2, v2, v28, s[16:17]
	v_and_b32_e32 v39, 0x8000000, v3
	v_cndmask_b32_e64 v38, v38, 26, s[16:17]
	v_cmp_eq_u32_e64 s[16:17], 0, v39
	v_cmp_gt_f32_e64 s[18:19], v29, v2
	s_and_b64 s[16:17], s[16:17], s[18:19]
	v_cndmask_b32_e64 v2, v2, v29, s[16:17]
	v_and_b32_e32 v39, 0x10000000, v3
	v_cndmask_b32_e64 v38, v38, 27, s[16:17]
	v_cmp_eq_u32_e64 s[16:17], 0, v39
	v_cmp_gt_f32_e64 s[18:19], v16, v2
	s_and_b64 s[16:17], s[16:17], s[18:19]
	v_cndmask_b32_e64 v2, v2, v16, s[16:17]
	v_and_b32_e32 v39, 0x20000000, v3
	v_cndmask_b32_e64 v38, v38, 28, s[16:17]
	v_cmp_eq_u32_e64 s[16:17], 0, v39
	v_cmp_gt_f32_e64 s[18:19], v17, v2
	s_and_b64 s[16:17], s[16:17], s[18:19]
	v_cndmask_b32_e64 v2, v2, v17, s[16:17]
	v_and_b32_e32 v39, 2.0, v3
	v_cndmask_b32_e64 v38, v38, 29, s[16:17]
	v_cmp_eq_u32_e64 s[16:17], 0, v39
	v_cmp_gt_f32_e64 s[18:19], v8, v2
	s_and_b64 s[16:17], s[16:17], s[18:19]
	v_cndmask_b32_e64 v2, v2, v8, s[16:17]
	v_cndmask_b32_e64 v38, v38, 30, s[16:17]
	v_cmp_lt_i32_e64 s[16:17], -1, v3
	v_cmp_gt_f32_e64 s[18:19], v9, v2
	s_and_b64 s[16:17], s[16:17], s[18:19]
	v_cndmask_b32_e64 v39, v2, v9, s[16:17]
	v_cndmask_b32_e64 v2, v38, 31, s[16:17]
	v_lshlrev_b32_e64 v38, v2, 1
	v_bitop3_b32 v90, v38, 1, v3 bitop3:0xc8
	v_cmp_eq_u32_e64 s[16:17], 0, v90
	s_and_b64 vcc, s[16:17], vcc
	v_cndmask_b32_e32 v34, v121, v34, vcc
	v_bitop3_b32 v90, v38, 2, v3 bitop3:0xc8
	v_cmp_eq_u32_e32 vcc, 0, v90
	v_cmp_gt_f32_e64 s[16:17], v35, v34
	s_and_b64 vcc, vcc, s[16:17]
	v_cndmask_b32_e32 v34, v34, v35, vcc
	v_bitop3_b32 v90, v38, 4, v3 bitop3:0xc8
	v_cndmask_b32_e64 v35, 0, 1, vcc
	v_cmp_eq_u32_e32 vcc, 0, v90
	v_cmp_gt_f32_e64 s[16:17], v30, v34
	s_and_b64 vcc, vcc, s[16:17]
	v_cndmask_b32_e32 v30, v34, v30, vcc
	v_cndmask_b32_e64 v34, v35, 2, vcc
	v_bitop3_b32 v35, v38, 8, v3 bitop3:0xc8
	v_cmp_eq_u32_e32 vcc, 0, v35
	v_cmp_gt_f32_e64 s[16:17], v31, v30
	s_and_b64 vcc, vcc, s[16:17]
	v_cndmask_b32_e32 v30, v30, v31, vcc
	v_cndmask_b32_e64 v31, v34, 3, vcc
	v_bitop3_b32 v34, v38, 16, v3 bitop3:0xc8
	v_cmp_eq_u32_e32 vcc, 0, v34
	v_cmp_gt_f32_e64 s[16:17], v22, v30
	s_and_b64 vcc, vcc, s[16:17]
	v_cndmask_b32_e32 v22, v30, v22, vcc
	v_cndmask_b32_e64 v30, v31, 4, vcc
	v_bitop3_b32 v31, v38, 32, v3 bitop3:0xc8
	v_cmp_eq_u32_e32 vcc, 0, v31
	v_cmp_gt_f32_e64 s[16:17], v23, v22
	s_and_b64 vcc, vcc, s[16:17]
	v_cndmask_b32_e32 v22, v22, v23, vcc
	v_cndmask_b32_e64 v23, v30, 5, vcc
	v_bitop3_b32 v30, v38, 64, v3 bitop3:0xc8
	v_cmp_eq_u32_e32 vcc, 0, v30
	v_cmp_gt_f32_e64 s[16:17], v10, v22
	s_and_b64 vcc, vcc, s[16:17]
	s_movk_i32 s16, 0x80
	v_cndmask_b32_e32 v10, v22, v10, vcc
	v_cndmask_b32_e64 v22, v23, 6, vcc
	v_bitop3_b32 v23, v38, s16, v3 bitop3:0xc8
	v_cmp_eq_u32_e32 vcc, 0, v23
	v_cmp_gt_f32_e64 s[16:17], v11, v10
	s_and_b64 vcc, vcc, s[16:17]
	s_movk_i32 s16, 0x100
	v_cndmask_b32_e32 v10, v10, v11, vcc
	v_cndmask_b32_e64 v11, v22, 7, vcc
	v_bitop3_b32 v22, v38, s16, v3 bitop3:0xc8
	v_cmp_eq_u32_e32 vcc, 0, v22
	v_cmp_gt_f32_e64 s[16:17], v24, v10
	s_and_b64 vcc, vcc, s[16:17]
	s_movk_i32 s16, 0x200
	v_cndmask_b32_e32 v10, v10, v24, vcc
	v_bitop3_b32 v22, v38, s16, v3 bitop3:0xc8
	v_cndmask_b32_e64 v11, v11, 8, vcc
	v_cmp_eq_u32_e32 vcc, 0, v22
	v_cmp_gt_f32_e64 s[16:17], v25, v10
	s_and_b64 vcc, vcc, s[16:17]
	v_cndmask_b32_e32 v10, v10, v25, vcc
	v_bitop3_b32 v22, v38, s46, v3 bitop3:0xc8
	v_cndmask_b32_e64 v11, v11, 9, vcc
	v_cmp_eq_u32_e32 vcc, 0, v22
	v_cmp_gt_f32_e64 s[16:17], v32, v10
	s_and_b64 vcc, vcc, s[16:17]
	s_movk_i32 s16, 0x800
	v_cndmask_b32_e32 v10, v10, v32, vcc
	v_bitop3_b32 v22, v38, s16, v3 bitop3:0xc8
	v_cndmask_b32_e64 v11, v11, 10, vcc
	v_cmp_eq_u32_e32 vcc, 0, v22
	v_cmp_gt_f32_e64 s[16:17], v33, v10
	s_and_b64 vcc, vcc, s[16:17]
	s_movk_i32 s16, 0x1000
	v_cndmask_b32_e32 v10, v10, v33, vcc
	v_bitop3_b32 v22, v38, s16, v3 bitop3:0xc8
	v_cndmask_b32_e64 v11, v11, 11, vcc
	v_cmp_eq_u32_e32 vcc, 0, v22
	v_cmp_gt_f32_e64 s[16:17], v20, v10
	s_and_b64 vcc, vcc, s[16:17]
	s_movk_i32 s16, 0x2000
	v_cndmask_b32_e32 v10, v10, v20, vcc
	v_bitop3_b32 v20, v38, s16, v3 bitop3:0xc8
	v_cndmask_b32_e64 v11, v11, 12, vcc
	v_cmp_eq_u32_e32 vcc, 0, v20
	v_cmp_gt_f32_e64 s[16:17], v21, v10
	s_and_b64 vcc, vcc, s[16:17]
	s_movk_i32 s16, 0x4000
	v_cndmask_b32_e32 v10, v10, v21, vcc
	v_bitop3_b32 v20, v38, s16, v3 bitop3:0xc8
	v_cndmask_b32_e64 v11, v11, 13, vcc
	v_cmp_eq_u32_e32 vcc, 0, v20
	v_cmp_gt_f32_e64 s[16:17], v6, v10
	s_and_b64 vcc, vcc, s[16:17]
	s_mov_b32 s16, 0x8000
	v_cndmask_b32_e32 v6, v10, v6, vcc
	v_cndmask_b32_e64 v10, v11, 14, vcc
	v_bitop3_b32 v11, v38, s16, v3 bitop3:0xc8
	v_cmp_eq_u32_e32 vcc, 0, v11
	v_cmp_gt_f32_e64 s[16:17], v7, v6
	s_and_b64 vcc, vcc, s[16:17]
	s_mov_b32 s16, 0x10000
	v_cndmask_b32_e32 v6, v6, v7, vcc
	v_cndmask_b32_e64 v7, v10, 15, vcc
	v_bitop3_b32 v10, v38, s16, v3 bitop3:0xc8
	v_cmp_eq_u32_e32 vcc, 0, v10
	v_cmp_gt_f32_e64 s[16:17], v18, v6
	s_and_b64 vcc, vcc, s[16:17]
	s_mov_b32 s16, 0x20000
	v_cndmask_b32_e32 v6, v6, v18, vcc
	v_bitop3_b32 v10, v38, s16, v3 bitop3:0xc8
	v_cndmask_b32_e64 v7, v7, 16, vcc
	v_cmp_eq_u32_e32 vcc, 0, v10
	v_cmp_gt_f32_e64 s[16:17], v19, v6
	s_and_b64 vcc, vcc, s[16:17]
	s_mov_b32 s16, 0x40000
	v_cndmask_b32_e32 v6, v6, v19, vcc
	v_bitop3_b32 v10, v38, s16, v3 bitop3:0xc8
	v_cndmask_b32_e64 v7, v7, 17, vcc
	v_cmp_eq_u32_e32 vcc, 0, v10
	v_cmp_gt_f32_e64 s[16:17], v26, v6
	s_and_b64 vcc, vcc, s[16:17]
	s_mov_b32 s16, 0x80000
	v_cndmask_b32_e32 v6, v6, v26, vcc
	v_bitop3_b32 v10, v38, s16, v3 bitop3:0xc8
	v_cndmask_b32_e64 v7, v7, 18, vcc
	v_cmp_eq_u32_e32 vcc, 0, v10
	v_cmp_gt_f32_e64 s[16:17], v27, v6
	s_and_b64 vcc, vcc, s[16:17]
	s_mov_b32 s16, 0x100000
	v_cndmask_b32_e32 v6, v6, v27, vcc
	v_bitop3_b32 v10, v38, s16, v3 bitop3:0xc8
	v_cndmask_b32_e64 v7, v7, 19, vcc
	v_cmp_eq_u32_e32 vcc, 0, v10
	v_cmp_gt_f32_e64 s[16:17], v12, v6
	s_and_b64 vcc, vcc, s[16:17]
	s_mov_b32 s16, 0x200000
	v_cndmask_b32_e32 v6, v6, v12, vcc
	v_bitop3_b32 v10, v38, s16, v3 bitop3:0xc8
	v_cndmask_b32_e64 v7, v7, 20, vcc
	v_cmp_eq_u32_e32 vcc, 0, v10
	v_cmp_gt_f32_e64 s[16:17], v13, v6
	s_and_b64 vcc, vcc, s[16:17]
	s_mov_b32 s16, 0x400000
	v_cndmask_b32_e32 v6, v6, v13, vcc
	v_bitop3_b32 v10, v38, s16, v3 bitop3:0xc8
	v_cndmask_b32_e64 v7, v7, 21, vcc
	v_cmp_eq_u32_e32 vcc, 0, v10
	v_cmp_gt_f32_e64 s[16:17], v4, v6
	s_and_b64 vcc, vcc, s[16:17]
	s_mov_b32 s16, 0x800000
	v_cndmask_b32_e32 v4, v6, v4, vcc
	v_cndmask_b32_e64 v6, v7, 22, vcc
	v_bitop3_b32 v7, v38, s16, v3 bitop3:0xc8
	v_cmp_eq_u32_e32 vcc, 0, v7
	v_cmp_gt_f32_e64 s[16:17], v5, v4
	s_and_b64 vcc, vcc, s[16:17]
	v_cndmask_b32_e32 v4, v4, v5, vcc
	v_cndmask_b32_e64 v5, v6, 23, vcc
	v_bitop3_b32 v6, v38, s55, v3 bitop3:0xc8
	v_cmp_eq_u32_e32 vcc, 0, v6
	v_cmp_gt_f32_e64 s[16:17], v14, v4
	s_and_b64 vcc, vcc, s[16:17]
	v_cndmask_b32_e32 v4, v4, v14, vcc
	v_bitop3_b32 v6, v38, s56, v3 bitop3:0xc8
	v_cndmask_b32_e64 v5, v5, 24, vcc
	v_cmp_eq_u32_e32 vcc, 0, v6
	v_cmp_gt_f32_e64 s[16:17], v15, v4
	s_and_b64 vcc, vcc, s[16:17]
	v_cndmask_b32_e32 v4, v4, v15, vcc
	v_bitop3_b32 v6, v38, s57, v3 bitop3:0xc8
	v_cndmask_b32_e64 v5, v5, 25, vcc
	v_cmp_eq_u32_e32 vcc, 0, v6
	v_cmp_gt_f32_e64 s[16:17], v28, v4
	s_and_b64 vcc, vcc, s[16:17]
	v_cndmask_b32_e32 v4, v4, v28, vcc
	v_bitop3_b32 v6, v38, s58, v3 bitop3:0xc8
	v_cndmask_b32_e64 v5, v5, 26, vcc
	v_cmp_eq_u32_e32 vcc, 0, v6
	v_cmp_gt_f32_e64 s[16:17], v29, v4
	s_and_b64 vcc, vcc, s[16:17]
	v_cndmask_b32_e32 v4, v4, v29, vcc
	v_bitop3_b32 v6, v38, s59, v3 bitop3:0xc8
	v_cndmask_b32_e64 v5, v5, 27, vcc
	v_cmp_eq_u32_e32 vcc, 0, v6
	v_cmp_gt_f32_e64 s[16:17], v16, v4
	s_and_b64 vcc, vcc, s[16:17]
	v_cndmask_b32_e32 v4, v4, v16, vcc
	v_bitop3_b32 v6, v38, s60, v3 bitop3:0xc8
	v_cndmask_b32_e64 v5, v5, 28, vcc
	v_cmp_eq_u32_e32 vcc, 0, v6
	v_cmp_gt_f32_e64 s[16:17], v17, v4
	s_and_b64 vcc, vcc, s[16:17]
	v_or_b32_e32 v44, v38, v3
	v_cndmask_b32_e32 v4, v4, v17, vcc
	v_bitop3_b32 v3, v38, 2.0, v3 bitop3:0xc8
	v_cndmask_b32_e64 v5, v5, 29, vcc
	v_cmp_eq_u32_e32 vcc, 0, v3
	v_cmp_gt_f32_e64 s[16:17], v8, v4
	s_and_b64 vcc, vcc, s[16:17]
	v_cndmask_b32_e32 v3, v4, v8, vcc
	v_cndmask_b32_e64 v4, v5, 30, vcc
	v_cmp_lt_i32_e32 vcc, -1, v44
	v_cmp_gt_f32_e64 s[16:17], v9, v3
	s_and_b64 vcc, vcc, s[16:17]
	v_cndmask_b32_e32 v5, v3, v9, vcc
	v_cndmask_b32_e64 v3, v4, 31, vcc
	v_sub_f32_e32 v4, v36, v36
	v_mul_f32_e32 v4, 0x3fb8aa3b, v4
	v_exp_f32_e32 v10, v4
	v_sub_f32_e32 v4, v37, v36
	v_mul_f32_e32 v4, 0x3fb8aa3b, v4
	v_exp_f32_e32 v11, v4
	v_sub_f32_e32 v4, v39, v36
	v_mul_f32_e32 v4, 0x3fb8aa3b, v4
	v_exp_f32_e32 v12, v4
	v_sub_f32_e32 v4, v5, v36
	v_mul_f32_e32 v4, 0x3fb8aa3b, v4
	v_exp_f32_e32 v13, v4
	v_add_f32_e32 v4, 0, v10
	v_add_f32_e32 v4, v4, v11
	v_add_f32_e32 v4, v4, v12
	v_add_f32_e32 v14, v4, v13
	v_div_scale_f32 v15, s[16:17], v14, v14, v10
	v_rcp_f32_e32 v16, v15
	v_lshl_add_u32 v4, s61, 8, v102
	v_ashrrev_i32_e32 v5, 31, v4
	v_lshlrev_b64 v[6:7], 2, v[4:5]
	v_fma_f32 v5, -v15, v16, 1.0
	v_fmac_f32_e32 v16, v5, v16
	v_div_scale_f32 v5, vcc, v10, v14, v10
	v_mul_f32_e32 v17, v5, v16
	v_fma_f32 v18, -v15, v17, v5
	v_fmac_f32_e32 v17, v18, v16
	v_fma_f32 v5, -v15, v17, v5
	v_div_fmas_f32 v5, v5, v16, v17
	v_div_fixup_f32 v5, v5, v14, v10
	v_div_scale_f32 v10, s[16:17], v14, v14, v11
	v_rcp_f32_e32 v15, v10
	v_lshl_add_u64 v[8:9], s[20:21], 0, v[6:7]
	v_lshl_add_u64 v[6:7], s[22:23], 0, v[6:7]
	global_store_dword v[6:7], v5, off
	v_or_b32_e32 v6, 1, v4
	v_fma_f32 v4, -v10, v15, 1.0
	v_lshl_add_u32 v5, v0, 2, 0
	v_fmac_f32_e32 v15, v4, v15
	v_div_scale_f32 v4, vcc, v11, v14, v11
	ds_add_u32 v5, v118 offset:58624
	v_mul_f32_e32 v5, v4, v15
	v_fma_f32 v16, -v10, v5, v4
	v_fmac_f32_e32 v5, v16, v15
	v_fma_f32 v4, -v10, v5, v4
	v_div_fmas_f32 v4, v4, v15, v5
	v_div_scale_f32 v5, s[16:17], v14, v14, v12
	v_rcp_f32_e32 v15, v5
	v_ashrrev_i32_e32 v7, 31, v6
	v_div_fixup_f32 v4, v4, v14, v11
	v_lshl_add_u64 v[10:11], v[6:7], 2, s[22:23]
	v_lshl_add_u32 v6, v1, 2, 0
	ds_add_u32 v6, v118 offset:58624
	v_fma_f32 v6, -v5, v15, 1.0
	v_fmac_f32_e32 v15, v6, v15
	v_div_scale_f32 v6, vcc, v12, v14, v12
	v_mul_f32_e32 v7, v6, v15
	v_fma_f32 v16, -v5, v7, v6
	v_fmac_f32_e32 v7, v16, v15
	v_fma_f32 v5, -v5, v7, v6
	v_div_scale_f32 v6, s[16:17], v14, v14, v13
	v_div_fmas_f32 v5, v5, v15, v7
	v_rcp_f32_e32 v7, v6
	v_div_fixup_f32 v5, v5, v14, v12
	v_lshl_add_u32 v12, v2, 2, 0
	ds_add_u32 v12, v118 offset:58624
	global_store_dwordx4 v[8:9], v[0:3], off
	s_nop 1
	v_fma_f32 v0, -v6, v7, 1.0
	v_fmac_f32_e32 v7, v0, v7
	v_div_scale_f32 v0, vcc, v13, v14, v13
	v_mul_f32_e32 v1, v0, v7
	v_fma_f32 v2, -v6, v1, v0
	v_fmac_f32_e32 v1, v2, v7
	v_fma_f32 v0, -v6, v1, v0
	v_div_fmas_f32 v0, v0, v7, v1
	v_div_fixup_f32 v6, v0, v14, v13
	global_store_dwordx3 v[10:11], v[4:6], off
	v_lshl_add_u32 v0, v3, 2, 0
	ds_add_u32 v0, v118 offset:58624

.LBB0_1474:
	s_waitcnt vmcnt(0)
	s_barrier
	s_waitcnt vmcnt(0)
	buffer_inv sc1
	s_waitcnt vmcnt(0)
	v_readlane_b32 s98, v253, 20
	v_mbcnt_lo_u32_b32 v216, -1, 0
	v_mbcnt_hi_u32_b32 v216, -1, v216
	s_lshr_b32 s99, s98, 1
	s_and_b32 s100, s98, 1
	v_lshrrev_b32_e32 v217, 5, v216
	v_and_b32_e32 v216, 31, v216
	s_lshl_b32 s101, s99, 4
	v_add_u32_e32 v218, s101, v217
	v_lshlrev_b32_e32 v219, 7, v218
	v_lshl_add_u32 v219, v216, 2, v219
	v_add_u32_e32 v219, 0xa400, v219
	v_mul_u32_u24_e32 v218, 0x110, v218
	s_lshl_b32 s101, s100, 7
	v_add_u32_e32 v218, s101, v218
	v_lshl_add_u32 v218, v216, 2, v218
	v_add_u32_e32 v218, 0x6000, v218
	s_lshl_b32 s101, s99, 13
	s_lshl_b32 s100, s100, 12
	s_add_i32 s101, s101, s100
	v_lshlrev_b32_e32 v217, 9, v217
	v_add_u32_e32 v217, s101, v217
	v_lshl_add_u32 v217, v216, 2, v217
	s_and_saveexec_b64 s[16:17], s[4:5]
	ds_write_b32 v95, v45 offset:58624
	s_or_b64 exec, exec, s[16:17]
	v_add_u32_e32 v0, s67, v42
	v_ashrrev_i32_e32 v1, 31, v0
	v_lshlrev_b64 v[0:1], 11, v[0:1]
	v_lshl_add_u64 v[92:93], v[46:47], 0, v[0:1]
	global_load_dwordx4 v[30:33], v[92:93], off
	global_load_dwordx4 v[34:37], v[48:49], off
	global_load_dwordx4 v[20:23], v[52:53], off
	global_load_dwordx4 v[24:27], v[92:93], off offset:128
	ds_read_b64 v[38:39], v106 offset:20480
	ds_read_b128 v[116:119], v43 offset:12288
	ds_read_b128 v[120:123], v43 offset:12304
	ds_read_b128 v[124:127], v43 offset:16384
	ds_read_b128 v[128:131], v43 offset:16400
	v_add_u32_e32 v114, 0x6000, v97
	v_mov_b32_e32 v4, 0
	s_waitcnt lgkmcnt(4)
	v_mov_b32_e32 v0, v38
	v_mov_b32_e32 v1, v38
	v_mov_b32_e32 v2, v38
	v_mov_b32_e32 v3, v38
	v_mov_b32_e32 v88, v39
	v_mov_b32_e32 v89, v39
	v_mov_b32_e32 v90, v39
	v_mov_b32_e32 v91, v39
	v_add_u32_e32 v113, 0x6400, v97
	s_mov_b32 s16, 0
	v_mov_b32_e32 v28, v103
	v_mov_b32_e32 v5, v4
	v_mov_b32_e32 v6, v4
	v_mov_b32_e32 v7, v4
	v_mov_b32_e32 v8, v4
	v_mov_b32_e32 v9, v4
	v_mov_b32_e32 v10, v4
	v_mov_b32_e32 v11, v4
	v_mov_b32_e32 v12, v4
	v_mov_b32_e32 v13, v4
	v_mov_b32_e32 v14, v4
	v_mov_b32_e32 v15, v4
	v_mov_b32_e32 v16, v4
	v_mov_b32_e32 v17, v4
	v_mov_b32_e32 v18, v4
	s_waitcnt vmcnt(3)
	v_cvt_f32_f16_sdwa v19, v31 dst_sel:DWORD dst_unused:UNUSED_PAD src0_sel:WORD_1
	v_cvt_f32_f16_e32 v29, v31
	v_cvt_f32_f16_sdwa v31, v30 dst_sel:DWORD dst_unused:UNUSED_PAD src0_sel:WORD_1
	v_cvt_f32_f16_e32 v30, v30
	v_cvt_f32_f16_sdwa v115, v33 dst_sel:DWORD dst_unused:UNUSED_PAD src0_sel:WORD_1
	v_cvt_f32_f16_e32 v134, v33
	v_cvt_f32_f16_sdwa v133, v32 dst_sel:DWORD dst_unused:UNUSED_PAD src0_sel:WORD_1
	v_cvt_f32_f16_e32 v132, v32
	v_sub_f32_e32 v30, v30, v38
	v_sub_f32_e32 v31, v31, v38
	v_sub_f32_e32 v32, v29, v38
	v_sub_f32_e32 v33, v19, v38
	v_sub_f32_e32 v132, v132, v38
	v_sub_f32_e32 v133, v133, v38
	v_sub_f32_e32 v134, v134, v38
	v_sub_f32_e32 v135, v115, v38
	v_pk_mul_f32 v[30:31], v[38:39], v[30:31] op_sel:[1,0]
	v_pk_mul_f32 v[32:33], v[38:39], v[32:33] op_sel:[1,0]
	v_pk_mul_f32 v[134:135], v[38:39], v[134:135] op_sel:[1,0]
	v_pk_mul_f32 v[38:39], v[38:39], v[132:133] op_sel:[1,0]
	s_waitcnt lgkmcnt(1)
	v_fma_f32 v19, v116, v30, v124
	v_fma_f32 v30, v117, v31, v125
	s_waitcnt lgkmcnt(0)
	v_fma_f32 v29, v120, v38, v128
	v_fma_f32 v31, v121, v39, v129
	v_fma_f32 v32, v118, v32, v126
	v_fma_f32 v38, v122, v134, v130
	v_fmac_f32_e32 v127, v119, v33
	v_fmac_f32_e32 v131, v123, v135
	ds_write2_b32 v114, v19, v30 offset1:68
	ds_write2_b32 v113, v29, v31 offset0:16 offset1:84
	ds_write2_b32 v114, v32, v127 offset0:136 offset1:204
	ds_write2_b32 v113, v38, v131 offset0:152 offset1:220
	s_waitcnt vmcnt(2)
	ds_write_b128 v96, v[34:37] offset:41984
	v_mov_b32_e32 v19, v4
	s_waitcnt lgkmcnt(0)
	s_barrier
	ds_read_b32 v200, v218
	ds_read_b32 v208, v219
	ds_read_b32 v201, v218 offset:544
	ds_read_b32 v209, v219 offset:256
	ds_read_b32 v202, v218 offset:1088
	ds_read_b32 v210, v219 offset:512
	ds_read_b32 v203, v218 offset:1632
	ds_read_b32 v211, v219 offset:768
	ds_read_b32 v204, v218 offset:2176
	ds_read_b32 v212, v219 offset:1024
	ds_read_b32 v205, v218 offset:2720
	ds_read_b32 v213, v219 offset:1280
	ds_read_b32 v206, v218 offset:3264
	ds_read_b32 v214, v219 offset:1536
	s_waitcnt lgkmcnt(12)
	v_mfma_f32_32x32x2_f32 v[4:19], v200, v208, v[4:19]
	ds_read_b32 v207, v218 offset:3808
	ds_read_b32 v215, v219 offset:1792
	s_waitcnt lgkmcnt(12)
	v_mfma_f32_32x32x2_f32 v[4:19], v201, v209, v[4:19]
	s_waitcnt lgkmcnt(10)
	v_mfma_f32_32x32x2_f32 v[4:19], v202, v210, v[4:19]
	s_waitcnt lgkmcnt(8)
	v_mfma_f32_32x32x2_f32 v[4:19], v203, v211, v[4:19]
	s_waitcnt lgkmcnt(6)
	v_mfma_f32_32x32x2_f32 v[4:19], v204, v212, v[4:19]
	s_waitcnt lgkmcnt(4)
	v_mfma_f32_32x32x2_f32 v[4:19], v205, v213, v[4:19]
	s_waitcnt lgkmcnt(2)
	v_mfma_f32_32x32x2_f32 v[4:19], v206, v214, v[4:19]
	s_waitcnt lgkmcnt(0)
	v_mfma_f32_32x32x2_f32 v[4:19], v207, v215, v[4:19]
	s_barrier
	global_load_dwordx4 v[32:35], v[92:93], off offset:256
	global_load_dwordx4 v[28:31], v[54:55], off
	s_waitcnt vmcnt(2)
	v_cvt_f32_f16_sdwa v128, v24 dst_sel:DWORD dst_unused:UNUSED_PAD src0_sel:WORD_1
	v_cvt_f32_f16_e32 v24, v24
	v_cvt_f32_f16_e32 v129, v25
	v_cvt_f32_f16_sdwa v130, v26 dst_sel:DWORD dst_unused:UNUSED_PAD src0_sel:WORD_1
	v_cvt_f32_f16_e32 v133, v26
	ds_read_b128 v[36:39], v43 offset:12544
	ds_read_b128 v[116:119], v43 offset:12560
	ds_read_b128 v[120:123], v43 offset:16640
	ds_read_b128 v[124:127], v43 offset:16656
	v_cvt_f32_f16_sdwa v115, v25 dst_sel:DWORD dst_unused:UNUSED_PAD src0_sel:WORD_1
	v_cvt_f32_f16_sdwa v131, v27 dst_sel:DWORD dst_unused:UNUSED_PAD src0_sel:WORD_1
	v_cvt_f32_f16_e32 v132, v27
	v_sub_f32_e32 v24, v24, v0
	v_sub_f32_e32 v25, v128, v1
	v_sub_f32_e32 v26, v129, v2
	v_pk_mul_f32 v[24:25], v[88:89], v[24:25]
	v_sub_f32_e32 v128, v133, v0
	v_sub_f32_e32 v129, v130, v1
	v_sub_f32_e32 v27, v115, v3
	v_sub_f32_e32 v130, v132, v2
	v_sub_f32_e32 v131, v131, v3
	v_pk_mul_f32 v[128:129], v[88:89], v[128:129]
	s_waitcnt lgkmcnt(1)
	v_fma_f32 v24, v36, v24, v120
	v_fma_f32 v25, v37, v25, v121
	v_pk_mul_f32 v[26:27], v[90:91], v[26:27]
	v_pk_mul_f32 v[130:131], v[90:91], v[130:131]
	s_waitcnt lgkmcnt(0)
	v_fma_f32 v36, v116, v128, v124
	ds_write2_b32 v114, v24, v25 offset1:68
	v_fma_f32 v24, v117, v129, v125
	ds_write2_b32 v113, v36, v24 offset0:16 offset1:84
	v_fma_f32 v24, v38, v26, v122
	v_fma_f32 v25, v118, v130, v126
	v_fmac_f32_e32 v123, v39, v27
	v_fmac_f32_e32 v127, v119, v131
	ds_write2_b32 v114, v24, v123 offset0:136 offset1:204
	ds_write2_b32 v113, v25, v127 offset0:152 offset1:220
	ds_write_b128 v96, v[20:23] offset:41984
	s_mov_b32 s16, 0
	v_mov_b32_e32 v20, v103
	s_waitcnt lgkmcnt(0)
	s_barrier
	ds_read_b32 v200, v218
	ds_read_b32 v208, v219
	ds_read_b32 v201, v218 offset:544
	ds_read_b32 v209, v219 offset:256
	ds_read_b32 v202, v218 offset:1088
	ds_read_b32 v210, v219 offset:512
	ds_read_b32 v203, v218 offset:1632
	ds_read_b32 v211, v219 offset:768
	ds_read_b32 v204, v218 offset:2176
	ds_read_b32 v212, v219 offset:1024
	ds_read_b32 v205, v218 offset:2720
	ds_read_b32 v213, v219 offset:1280
	ds_read_b32 v206, v218 offset:3264
	ds_read_b32 v214, v219 offset:1536
	s_waitcnt lgkmcnt(12)
	v_mfma_f32_32x32x2_f32 v[4:19], v200, v208, v[4:19]
	ds_read_b32 v207, v218 offset:3808
	ds_read_b32 v215, v219 offset:1792
	s_waitcnt lgkmcnt(12)
	v_mfma_f32_32x32x2_f32 v[4:19], v201, v209, v[4:19]
	s_waitcnt lgkmcnt(10)
	v_mfma_f32_32x32x2_f32 v[4:19], v202, v210, v[4:19]
	s_waitcnt lgkmcnt(8)
	v_mfma_f32_32x32x2_f32 v[4:19], v203, v211, v[4:19]
	s_waitcnt lgkmcnt(6)
	v_mfma_f32_32x32x2_f32 v[4:19], v204, v212, v[4:19]
	s_waitcnt lgkmcnt(4)
	v_mfma_f32_32x32x2_f32 v[4:19], v205, v213, v[4:19]
	s_waitcnt lgkmcnt(2)
	v_mfma_f32_32x32x2_f32 v[4:19], v206, v214, v[4:19]
	s_waitcnt lgkmcnt(0)
	v_mfma_f32_32x32x2_f32 v[4:19], v207, v215, v[4:19]
	s_barrier
	global_load_dwordx4 v[36:39], v[92:93], off offset:384
	global_load_dwordx4 v[20:23], v[56:57], off
	s_waitcnt vmcnt(3)
	v_cvt_f32_f16_sdwa v128, v32 dst_sel:DWORD dst_unused:UNUSED_PAD src0_sel:WORD_1
	v_cvt_f32_f16_e32 v32, v32
	v_cvt_f32_f16_e32 v129, v33
	v_cvt_f32_f16_sdwa v130, v34 dst_sel:DWORD dst_unused:UNUSED_PAD src0_sel:WORD_1
	v_cvt_f32_f16_e32 v133, v34
	ds_read_b128 v[24:27], v43 offset:12800
	ds_read_b128 v[116:119], v43 offset:12816
	ds_read_b128 v[120:123], v43 offset:16896
	ds_read_b128 v[124:127], v43 offset:16912
	v_cvt_f32_f16_sdwa v115, v33 dst_sel:DWORD dst_unused:UNUSED_PAD src0_sel:WORD_1
	v_cvt_f32_f16_sdwa v131, v35 dst_sel:DWORD dst_unused:UNUSED_PAD src0_sel:WORD_1
	v_cvt_f32_f16_e32 v132, v35
	v_sub_f32_e32 v32, v32, v0
	v_sub_f32_e32 v33, v128, v1
	v_sub_f32_e32 v34, v129, v2
	v_pk_mul_f32 v[32:33], v[88:89], v[32:33]
	v_sub_f32_e32 v128, v133, v0
	v_sub_f32_e32 v129, v130, v1
	v_sub_f32_e32 v35, v115, v3
	v_pk_mul_f32 v[128:129], v[88:89], v[128:129]
	s_waitcnt lgkmcnt(1)
	v_fma_f32 v24, v24, v32, v120
	v_fma_f32 v25, v25, v33, v121
	v_pk_mul_f32 v[34:35], v[90:91], v[34:35]
	v_sub_f32_e32 v130, v132, v2
	v_sub_f32_e32 v131, v131, v3
	s_waitcnt lgkmcnt(0)
	v_fma_f32 v32, v116, v128, v124
	ds_write2_b32 v114, v24, v25 offset1:68
	v_fma_f32 v24, v117, v129, v125
	v_pk_mul_f32 v[130:131], v[90:91], v[130:131]
	ds_write2_b32 v113, v32, v24 offset0:16 offset1:84
	v_fma_f32 v24, v26, v34, v122
	v_fmac_f32_e32 v123, v27, v35
	v_fma_f32 v25, v118, v130, v126
	ds_write2_b32 v114, v24, v123 offset0:136 offset1:204
	v_fmac_f32_e32 v127, v119, v131
	s_mov_b32 s16, 0
	v_mov_b32_e32 v24, v103
	ds_write2_b32 v113, v25, v127 offset0:152 offset1:220
	s_waitcnt vmcnt(2)
	ds_write_b128 v96, v[28:31] offset:41984
	s_waitcnt lgkmcnt(0)
	s_barrier
	ds_read_b32 v200, v218
	ds_read_b32 v208, v219
	ds_read_b32 v201, v218 offset:544
	ds_read_b32 v209, v219 offset:256
	ds_read_b32 v202, v218 offset:1088
	ds_read_b32 v210, v219 offset:512
	ds_read_b32 v203, v218 offset:1632
	ds_read_b32 v211, v219 offset:768
	ds_read_b32 v204, v218 offset:2176
	ds_read_b32 v212, v219 offset:1024
	ds_read_b32 v205, v218 offset:2720
	ds_read_b32 v213, v219 offset:1280
	ds_read_b32 v206, v218 offset:3264
	ds_read_b32 v214, v219 offset:1536
	s_waitcnt lgkmcnt(12)
	v_mfma_f32_32x32x2_f32 v[4:19], v200, v208, v[4:19]
	ds_read_b32 v207, v218 offset:3808
	ds_read_b32 v215, v219 offset:1792
	s_waitcnt lgkmcnt(12)
	v_mfma_f32_32x32x2_f32 v[4:19], v201, v209, v[4:19]
	s_waitcnt lgkmcnt(10)
	v_mfma_f32_32x32x2_f32 v[4:19], v202, v210, v[4:19]
	s_waitcnt lgkmcnt(8)
	v_mfma_f32_32x32x2_f32 v[4:19], v203, v211, v[4:19]
	s_waitcnt lgkmcnt(6)
	v_mfma_f32_32x32x2_f32 v[4:19], v204, v212, v[4:19]
	s_waitcnt lgkmcnt(4)
	v_mfma_f32_32x32x2_f32 v[4:19], v205, v213, v[4:19]
	s_waitcnt lgkmcnt(2)
	v_mfma_f32_32x32x2_f32 v[4:19], v206, v214, v[4:19]
	s_waitcnt lgkmcnt(0)
	v_mfma_f32_32x32x2_f32 v[4:19], v207, v215, v[4:19]
	s_barrier
	global_load_dwordx4 v[28:31], v[92:93], off offset:512
	global_load_dwordx4 v[24:27], v[58:59], off
	s_waitcnt vmcnt(3)
	v_cvt_f32_f16_sdwa v128, v36 dst_sel:DWORD dst_unused:UNUSED_PAD src0_sel:WORD_1
	v_cvt_f32_f16_e32 v36, v36
	v_cvt_f32_f16_e32 v129, v37
	v_cvt_f32_f16_sdwa v130, v38 dst_sel:DWORD dst_unused:UNUSED_PAD src0_sel:WORD_1
	v_cvt_f32_f16_e32 v133, v38
	ds_read_b128 v[32:35], v43 offset:13056
	ds_read_b128 v[116:119], v43 offset:13072
	ds_read_b128 v[120:123], v43 offset:17152
	ds_read_b128 v[124:127], v43 offset:17168
	v_cvt_f32_f16_sdwa v115, v37 dst_sel:DWORD dst_unused:UNUSED_PAD src0_sel:WORD_1
	v_cvt_f32_f16_sdwa v131, v39 dst_sel:DWORD dst_unused:UNUSED_PAD src0_sel:WORD_1
	v_cvt_f32_f16_e32 v132, v39
	v_sub_f32_e32 v36, v36, v0
	v_sub_f32_e32 v37, v128, v1
	v_sub_f32_e32 v38, v129, v2
	v_pk_mul_f32 v[36:37], v[88:89], v[36:37]
	v_sub_f32_e32 v128, v133, v0
	v_sub_f32_e32 v129, v130, v1
	v_sub_f32_e32 v39, v115, v3
	v_sub_f32_e32 v130, v132, v2
	v_sub_f32_e32 v131, v131, v3
	v_pk_mul_f32 v[128:129], v[88:89], v[128:129]
	s_waitcnt lgkmcnt(1)
	v_fma_f32 v32, v32, v36, v120
	v_fma_f32 v33, v33, v37, v121
	v_pk_mul_f32 v[38:39], v[90:91], v[38:39]
	v_pk_mul_f32 v[130:131], v[90:91], v[130:131]
	s_waitcnt lgkmcnt(0)
	v_fma_f32 v36, v116, v128, v124
	ds_write2_b32 v114, v32, v33 offset1:68
	v_fma_f32 v32, v117, v129, v125
	ds_write2_b32 v113, v36, v32 offset0:16 offset1:84
	v_fma_f32 v32, v34, v38, v122
	v_fma_f32 v33, v118, v130, v126
	v_fmac_f32_e32 v123, v35, v39
	v_fmac_f32_e32 v127, v119, v131
	ds_write2_b32 v114, v32, v123 offset0:136 offset1:204
	ds_write2_b32 v113, v33, v127 offset0:152 offset1:220
	s_waitcnt vmcnt(2)
	ds_write_b128 v96, v[20:23] offset:41984
	s_mov_b32 s16, 0
	v_mov_b32_e32 v20, v103
	s_waitcnt lgkmcnt(0)
	s_barrier
	ds_read_b32 v200, v218
	ds_read_b32 v208, v219
	ds_read_b32 v201, v218 offset:544
	ds_read_b32 v209, v219 offset:256
	ds_read_b32 v202, v218 offset:1088
	ds_read_b32 v210, v219 offset:512
	ds_read_b32 v203, v218 offset:1632
	ds_read_b32 v211, v219 offset:768
	ds_read_b32 v204, v218 offset:2176
	ds_read_b32 v212, v219 offset:1024
	ds_read_b32 v205, v218 offset:2720
	ds_read_b32 v213, v219 offset:1280
	ds_read_b32 v206, v218 offset:3264
	ds_read_b32 v214, v219 offset:1536
	s_waitcnt lgkmcnt(12)
	v_mfma_f32_32x32x2_f32 v[4:19], v200, v208, v[4:19]
	ds_read_b32 v207, v218 offset:3808
	ds_read_b32 v215, v219 offset:1792
	s_waitcnt lgkmcnt(12)
	v_mfma_f32_32x32x2_f32 v[4:19], v201, v209, v[4:19]
	s_waitcnt lgkmcnt(10)
	v_mfma_f32_32x32x2_f32 v[4:19], v202, v210, v[4:19]
	s_waitcnt lgkmcnt(8)
	v_mfma_f32_32x32x2_f32 v[4:19], v203, v211, v[4:19]
	s_waitcnt lgkmcnt(6)
	v_mfma_f32_32x32x2_f32 v[4:19], v204, v212, v[4:19]
	s_waitcnt lgkmcnt(4)
	v_mfma_f32_32x32x2_f32 v[4:19], v205, v213, v[4:19]
	s_waitcnt lgkmcnt(2)
	v_mfma_f32_32x32x2_f32 v[4:19], v206, v214, v[4:19]
	s_waitcnt lgkmcnt(0)
	v_mfma_f32_32x32x2_f32 v[4:19], v207, v215, v[4:19]
	s_barrier
	global_load_dwordx4 v[32:35], v[92:93], off offset:640
	global_load_dwordx4 v[20:23], v[60:61], off
	s_waitcnt vmcnt(3)
	v_cvt_f32_f16_sdwa v128, v28 dst_sel:DWORD dst_unused:UNUSED_PAD src0_sel:WORD_1
	v_cvt_f32_f16_e32 v28, v28
	v_cvt_f32_f16_e32 v129, v29
	v_cvt_f32_f16_sdwa v130, v30 dst_sel:DWORD dst_unused:UNUSED_PAD src0_sel:WORD_1
	v_cvt_f32_f16_e32 v133, v30
	ds_read_b128 v[36:39], v43 offset:13312
	ds_read_b128 v[116:119], v43 offset:13328
	ds_read_b128 v[120:123], v43 offset:17408
	ds_read_b128 v[124:127], v43 offset:17424
	v_cvt_f32_f16_sdwa v115, v29 dst_sel:DWORD dst_unused:UNUSED_PAD src0_sel:WORD_1
	v_cvt_f32_f16_sdwa v131, v31 dst_sel:DWORD dst_unused:UNUSED_PAD src0_sel:WORD_1
	v_cvt_f32_f16_e32 v132, v31
	v_sub_f32_e32 v28, v28, v0
	v_sub_f32_e32 v29, v128, v1
	v_sub_f32_e32 v30, v129, v2
	v_pk_mul_f32 v[28:29], v[88:89], v[28:29]
	v_sub_f32_e32 v128, v133, v0
	v_sub_f32_e32 v129, v130, v1
	v_sub_f32_e32 v31, v115, v3
	v_sub_f32_e32 v130, v132, v2
	v_sub_f32_e32 v131, v131, v3
	v_pk_mul_f32 v[128:129], v[88:89], v[128:129]
	s_waitcnt lgkmcnt(1)
	v_fma_f32 v28, v36, v28, v120
	v_fma_f32 v29, v37, v29, v121
	v_pk_mul_f32 v[30:31], v[90:91], v[30:31]
	v_pk_mul_f32 v[130:131], v[90:91], v[130:131]
	s_waitcnt lgkmcnt(0)
	v_fma_f32 v36, v116, v128, v124
	ds_write2_b32 v114, v28, v29 offset1:68
	v_fma_f32 v28, v117, v129, v125
	ds_write2_b32 v113, v36, v28 offset0:16 offset1:84
	v_fma_f32 v28, v38, v30, v122
	v_fma_f32 v29, v118, v130, v126
	v_fmac_f32_e32 v123, v39, v31
	v_fmac_f32_e32 v127, v119, v131
	ds_write2_b32 v114, v28, v123 offset0:136 offset1:204
	ds_write2_b32 v113, v29, v127 offset0:152 offset1:220
	s_waitcnt vmcnt(2)
	ds_write_b128 v96, v[24:27] offset:41984
	s_mov_b32 s16, 0
	v_mov_b32_e32 v24, v103
	s_waitcnt lgkmcnt(0)
	s_barrier
	ds_read_b32 v200, v218
	ds_read_b32 v208, v219
	ds_read_b32 v201, v218 offset:544
	ds_read_b32 v209, v219 offset:256
	ds_read_b32 v202, v218 offset:1088
	ds_read_b32 v210, v219 offset:512
	ds_read_b32 v203, v218 offset:1632
	ds_read_b32 v211, v219 offset:768
	ds_read_b32 v204, v218 offset:2176
	ds_read_b32 v212, v219 offset:1024
	ds_read_b32 v205, v218 offset:2720
	ds_read_b32 v213, v219 offset:1280
	ds_read_b32 v206, v218 offset:3264
	ds_read_b32 v214, v219 offset:1536
	s_waitcnt lgkmcnt(12)
	v_mfma_f32_32x32x2_f32 v[4:19], v200, v208, v[4:19]
	ds_read_b32 v207, v218 offset:3808
	ds_read_b32 v215, v219 offset:1792
	s_waitcnt lgkmcnt(12)
	v_mfma_f32_32x32x2_f32 v[4:19], v201, v209, v[4:19]
	s_waitcnt lgkmcnt(10)
	v_mfma_f32_32x32x2_f32 v[4:19], v202, v210, v[4:19]
	s_waitcnt lgkmcnt(8)
	v_mfma_f32_32x32x2_f32 v[4:19], v203, v211, v[4:19]
	s_waitcnt lgkmcnt(6)
	v_mfma_f32_32x32x2_f32 v[4:19], v204, v212, v[4:19]
	s_waitcnt lgkmcnt(4)
	v_mfma_f32_32x32x2_f32 v[4:19], v205, v213, v[4:19]
	s_waitcnt lgkmcnt(2)
	v_mfma_f32_32x32x2_f32 v[4:19], v206, v214, v[4:19]
	s_waitcnt lgkmcnt(0)
	v_mfma_f32_32x32x2_f32 v[4:19], v207, v215, v[4:19]
	s_barrier
	global_load_dwordx4 v[28:31], v[92:93], off offset:768
	global_load_dwordx4 v[24:27], v[62:63], off
	s_waitcnt vmcnt(3)
	v_cvt_f32_f16_sdwa v128, v32 dst_sel:DWORD dst_unused:UNUSED_PAD src0_sel:WORD_1
	v_cvt_f32_f16_e32 v32, v32
	v_cvt_f32_f16_e32 v129, v33
	v_cvt_f32_f16_sdwa v130, v34 dst_sel:DWORD dst_unused:UNUSED_PAD src0_sel:WORD_1
	v_cvt_f32_f16_e32 v133, v34
	ds_read_b128 v[36:39], v43 offset:13568
	ds_read_b128 v[116:119], v43 offset:13584
	ds_read_b128 v[120:123], v43 offset:17664
	ds_read_b128 v[124:127], v43 offset:17680
	v_cvt_f32_f16_sdwa v115, v33 dst_sel:DWORD dst_unused:UNUSED_PAD src0_sel:WORD_1
	v_cvt_f32_f16_sdwa v131, v35 dst_sel:DWORD dst_unused:UNUSED_PAD src0_sel:WORD_1
	v_cvt_f32_f16_e32 v132, v35
	v_sub_f32_e32 v32, v32, v0
	v_sub_f32_e32 v33, v128, v1
	v_sub_f32_e32 v34, v129, v2
	v_pk_mul_f32 v[32:33], v[88:89], v[32:33]
	v_sub_f32_e32 v128, v133, v0
	v_sub_f32_e32 v129, v130, v1
	v_sub_f32_e32 v35, v115, v3
	v_sub_f32_e32 v130, v132, v2
	v_sub_f32_e32 v131, v131, v3
	v_pk_mul_f32 v[128:129], v[88:89], v[128:129]
	s_waitcnt lgkmcnt(1)
	v_fma_f32 v32, v36, v32, v120
	v_fma_f32 v33, v37, v33, v121
	v_pk_mul_f32 v[34:35], v[90:91], v[34:35]
	v_pk_mul_f32 v[130:131], v[90:91], v[130:131]
	s_waitcnt lgkmcnt(0)
	v_fma_f32 v36, v116, v128, v124
	ds_write2_b32 v114, v32, v33 offset1:68
	v_fma_f32 v32, v117, v129, v125
	ds_write2_b32 v113, v36, v32 offset0:16 offset1:84
	v_fma_f32 v32, v38, v34, v122
	v_fma_f32 v33, v118, v130, v126
	v_fmac_f32_e32 v123, v39, v35
	v_fmac_f32_e32 v127, v119, v131
	ds_write2_b32 v114, v32, v123 offset0:136 offset1:204
	ds_write2_b32 v113, v33, v127 offset0:152 offset1:220
	s_waitcnt vmcnt(2)
	ds_write_b128 v96, v[20:23] offset:41984
	s_mov_b32 s16, 0
	v_mov_b32_e32 v20, v103
	s_waitcnt lgkmcnt(0)
	s_barrier
	ds_read_b32 v200, v218
	ds_read_b32 v208, v219
	ds_read_b32 v201, v218 offset:544
	ds_read_b32 v209, v219 offset:256
	ds_read_b32 v202, v218 offset:1088
	ds_read_b32 v210, v219 offset:512
	ds_read_b32 v203, v218 offset:1632
	ds_read_b32 v211, v219 offset:768
	ds_read_b32 v204, v218 offset:2176
	ds_read_b32 v212, v219 offset:1024
	ds_read_b32 v205, v218 offset:2720
	ds_read_b32 v213, v219 offset:1280
	ds_read_b32 v206, v218 offset:3264
	ds_read_b32 v214, v219 offset:1536
	s_waitcnt lgkmcnt(12)
	v_mfma_f32_32x32x2_f32 v[4:19], v200, v208, v[4:19]
	ds_read_b32 v207, v218 offset:3808
	ds_read_b32 v215, v219 offset:1792
	s_waitcnt lgkmcnt(12)
	v_mfma_f32_32x32x2_f32 v[4:19], v201, v209, v[4:19]
	s_waitcnt lgkmcnt(10)
	v_mfma_f32_32x32x2_f32 v[4:19], v202, v210, v[4:19]
	s_waitcnt lgkmcnt(8)
	v_mfma_f32_32x32x2_f32 v[4:19], v203, v211, v[4:19]
	s_waitcnt lgkmcnt(6)
	v_mfma_f32_32x32x2_f32 v[4:19], v204, v212, v[4:19]
	s_waitcnt lgkmcnt(4)
	v_mfma_f32_32x32x2_f32 v[4:19], v205, v213, v[4:19]
	s_waitcnt lgkmcnt(2)
	v_mfma_f32_32x32x2_f32 v[4:19], v206, v214, v[4:19]
	s_waitcnt lgkmcnt(0)
	v_mfma_f32_32x32x2_f32 v[4:19], v207, v215, v[4:19]
	s_barrier
	global_load_dwordx4 v[32:35], v[92:93], off offset:896
	global_load_dwordx4 v[20:23], v[64:65], off
	s_waitcnt vmcnt(3)
	v_cvt_f32_f16_sdwa v128, v28 dst_sel:DWORD dst_unused:UNUSED_PAD src0_sel:WORD_1
	v_cvt_f32_f16_e32 v28, v28
	v_cvt_f32_f16_e32 v129, v29
	v_cvt_f32_f16_sdwa v130, v30 dst_sel:DWORD dst_unused:UNUSED_PAD src0_sel:WORD_1
	v_cvt_f32_f16_e32 v133, v30
	ds_read_b128 v[36:39], v43 offset:13824
	ds_read_b128 v[116:119], v43 offset:13840
	ds_read_b128 v[120:123], v43 offset:17920
	ds_read_b128 v[124:127], v43 offset:17936
	v_cvt_f32_f16_sdwa v115, v29 dst_sel:DWORD dst_unused:UNUSED_PAD src0_sel:WORD_1
	v_cvt_f32_f16_sdwa v131, v31 dst_sel:DWORD dst_unused:UNUSED_PAD src0_sel:WORD_1
	v_cvt_f32_f16_e32 v132, v31
	v_sub_f32_e32 v28, v28, v0
	v_sub_f32_e32 v29, v128, v1
	v_sub_f32_e32 v30, v129, v2
	v_pk_mul_f32 v[28:29], v[88:89], v[28:29]
	v_sub_f32_e32 v128, v133, v0
	v_sub_f32_e32 v129, v130, v1
	v_sub_f32_e32 v31, v115, v3
	v_sub_f32_e32 v130, v132, v2
	v_sub_f32_e32 v131, v131, v3
	v_pk_mul_f32 v[128:129], v[88:89], v[128:129]
	s_waitcnt lgkmcnt(1)
	v_fma_f32 v28, v36, v28, v120
	v_fma_f32 v29, v37, v29, v121
	v_pk_mul_f32 v[30:31], v[90:91], v[30:31]
	v_pk_mul_f32 v[130:131], v[90:91], v[130:131]
	s_waitcnt lgkmcnt(0)
	v_fma_f32 v36, v116, v128, v124
	ds_write2_b32 v114, v28, v29 offset1:68
	v_fma_f32 v28, v117, v129, v125
	ds_write2_b32 v113, v36, v28 offset0:16 offset1:84
	v_fma_f32 v28, v38, v30, v122
	v_fma_f32 v29, v118, v130, v126
	v_fmac_f32_e32 v123, v39, v31
	v_fmac_f32_e32 v127, v119, v131
	ds_write2_b32 v114, v28, v123 offset0:136 offset1:204
	ds_write2_b32 v113, v29, v127 offset0:152 offset1:220
	s_waitcnt vmcnt(2)
	ds_write_b128 v96, v[24:27] offset:41984
	s_mov_b32 s16, 0
	v_mov_b32_e32 v24, v103
	s_waitcnt lgkmcnt(0)
	s_barrier
	ds_read_b32 v200, v218
	ds_read_b32 v208, v219
	ds_read_b32 v201, v218 offset:544
	ds_read_b32 v209, v219 offset:256
	ds_read_b32 v202, v218 offset:1088
	ds_read_b32 v210, v219 offset:512
	ds_read_b32 v203, v218 offset:1632
	ds_read_b32 v211, v219 offset:768
	ds_read_b32 v204, v218 offset:2176
	ds_read_b32 v212, v219 offset:1024
	ds_read_b32 v205, v218 offset:2720
	ds_read_b32 v213, v219 offset:1280
	ds_read_b32 v206, v218 offset:3264
	ds_read_b32 v214, v219 offset:1536
	s_waitcnt lgkmcnt(12)
	v_mfma_f32_32x32x2_f32 v[4:19], v200, v208, v[4:19]
	ds_read_b32 v207, v218 offset:3808
	ds_read_b32 v215, v219 offset:1792
	s_waitcnt lgkmcnt(12)
	v_mfma_f32_32x32x2_f32 v[4:19], v201, v209, v[4:19]
	s_waitcnt lgkmcnt(10)
	v_mfma_f32_32x32x2_f32 v[4:19], v202, v210, v[4:19]
	s_waitcnt lgkmcnt(8)
	v_mfma_f32_32x32x2_f32 v[4:19], v203, v211, v[4:19]
	s_waitcnt lgkmcnt(6)
	v_mfma_f32_32x32x2_f32 v[4:19], v204, v212, v[4:19]
	s_waitcnt lgkmcnt(4)
	v_mfma_f32_32x32x2_f32 v[4:19], v205, v213, v[4:19]
	s_waitcnt lgkmcnt(2)
	v_mfma_f32_32x32x2_f32 v[4:19], v206, v214, v[4:19]
	s_waitcnt lgkmcnt(0)
	v_mfma_f32_32x32x2_f32 v[4:19], v207, v215, v[4:19]
	s_barrier
	global_load_dwordx4 v[28:31], v[92:93], off offset:1024
	global_load_dwordx4 v[24:27], v[66:67], off
	s_waitcnt vmcnt(3)
	v_cvt_f32_f16_sdwa v128, v32 dst_sel:DWORD dst_unused:UNUSED_PAD src0_sel:WORD_1
	v_cvt_f32_f16_e32 v32, v32
	v_cvt_f32_f16_e32 v129, v33
	v_cvt_f32_f16_sdwa v130, v34 dst_sel:DWORD dst_unused:UNUSED_PAD src0_sel:WORD_1
	v_cvt_f32_f16_e32 v133, v34
	ds_read_b128 v[36:39], v43 offset:14080
	ds_read_b128 v[116:119], v43 offset:14096
	ds_read_b128 v[120:123], v43 offset:18176
	ds_read_b128 v[124:127], v43 offset:18192
	v_cvt_f32_f16_sdwa v115, v33 dst_sel:DWORD dst_unused:UNUSED_PAD src0_sel:WORD_1
	v_cvt_f32_f16_sdwa v131, v35 dst_sel:DWORD dst_unused:UNUSED_PAD src0_sel:WORD_1
	v_cvt_f32_f16_e32 v132, v35
	v_sub_f32_e32 v32, v32, v0
	v_sub_f32_e32 v33, v128, v1
	v_sub_f32_e32 v34, v129, v2
	v_pk_mul_f32 v[32:33], v[88:89], v[32:33]
	v_sub_f32_e32 v128, v133, v0
	v_sub_f32_e32 v129, v130, v1
	v_sub_f32_e32 v35, v115, v3
	v_sub_f32_e32 v130, v132, v2
	v_sub_f32_e32 v131, v131, v3
	v_pk_mul_f32 v[128:129], v[88:89], v[128:129]
	s_waitcnt lgkmcnt(1)
	v_fma_f32 v32, v36, v32, v120
	v_fma_f32 v33, v37, v33, v121
	v_pk_mul_f32 v[34:35], v[90:91], v[34:35]
	v_pk_mul_f32 v[130:131], v[90:91], v[130:131]
	s_waitcnt lgkmcnt(0)
	v_fma_f32 v36, v116, v128, v124
	ds_write2_b32 v114, v32, v33 offset1:68
	v_fma_f32 v32, v117, v129, v125
	ds_write2_b32 v113, v36, v32 offset0:16 offset1:84
	v_fma_f32 v32, v38, v34, v122
	v_fma_f32 v33, v118, v130, v126
	v_fmac_f32_e32 v123, v39, v35
	v_fmac_f32_e32 v127, v119, v131
	ds_write2_b32 v114, v32, v123 offset0:136 offset1:204
	ds_write2_b32 v113, v33, v127 offset0:152 offset1:220
	s_waitcnt vmcnt(2)
	ds_write_b128 v96, v[20:23] offset:41984
	s_mov_b32 s16, 0
	v_mov_b32_e32 v20, v103
	s_waitcnt lgkmcnt(0)
	s_barrier
	ds_read_b32 v200, v218
	ds_read_b32 v208, v219
	ds_read_b32 v201, v218 offset:544
	ds_read_b32 v209, v219 offset:256
	ds_read_b32 v202, v218 offset:1088
	ds_read_b32 v210, v219 offset:512
	ds_read_b32 v203, v218 offset:1632
	ds_read_b32 v211, v219 offset:768
	ds_read_b32 v204, v218 offset:2176
	ds_read_b32 v212, v219 offset:1024
	ds_read_b32 v205, v218 offset:2720
	ds_read_b32 v213, v219 offset:1280
	ds_read_b32 v206, v218 offset:3264
	ds_read_b32 v214, v219 offset:1536
	s_waitcnt lgkmcnt(12)
	v_mfma_f32_32x32x2_f32 v[4:19], v200, v208, v[4:19]
	ds_read_b32 v207, v218 offset:3808
	ds_read_b32 v215, v219 offset:1792
	s_waitcnt lgkmcnt(12)
	v_mfma_f32_32x32x2_f32 v[4:19], v201, v209, v[4:19]
	s_waitcnt lgkmcnt(10)
	v_mfma_f32_32x32x2_f32 v[4:19], v202, v210, v[4:19]
	s_waitcnt lgkmcnt(8)
	v_mfma_f32_32x32x2_f32 v[4:19], v203, v211, v[4:19]
	s_waitcnt lgkmcnt(6)
	v_mfma_f32_32x32x2_f32 v[4:19], v204, v212, v[4:19]
	s_waitcnt lgkmcnt(4)
	v_mfma_f32_32x32x2_f32 v[4:19], v205, v213, v[4:19]
	s_waitcnt lgkmcnt(2)
	v_mfma_f32_32x32x2_f32 v[4:19], v206, v214, v[4:19]
	s_waitcnt lgkmcnt(0)
	v_mfma_f32_32x32x2_f32 v[4:19], v207, v215, v[4:19]
	s_barrier
	global_load_dwordx4 v[32:35], v[92:93], off offset:1152
	global_load_dwordx4 v[20:23], v[68:69], off
	s_waitcnt vmcnt(3)
	v_cvt_f32_f16_sdwa v128, v28 dst_sel:DWORD dst_unused:UNUSED_PAD src0_sel:WORD_1
	v_cvt_f32_f16_e32 v28, v28
	v_cvt_f32_f16_e32 v129, v29
	v_cvt_f32_f16_sdwa v130, v30 dst_sel:DWORD dst_unused:UNUSED_PAD src0_sel:WORD_1
	v_cvt_f32_f16_e32 v133, v30
	ds_read_b128 v[36:39], v43 offset:14336
	ds_read_b128 v[116:119], v43 offset:14352
	ds_read_b128 v[120:123], v43 offset:18432
	ds_read_b128 v[124:127], v43 offset:18448
	v_cvt_f32_f16_sdwa v115, v29 dst_sel:DWORD dst_unused:UNUSED_PAD src0_sel:WORD_1
	v_cvt_f32_f16_sdwa v131, v31 dst_sel:DWORD dst_unused:UNUSED_PAD src0_sel:WORD_1
	v_cvt_f32_f16_e32 v132, v31
	v_sub_f32_e32 v28, v28, v0
	v_sub_f32_e32 v29, v128, v1
	v_sub_f32_e32 v30, v129, v2
	v_pk_mul_f32 v[28:29], v[88:89], v[28:29]
	v_sub_f32_e32 v128, v133, v0
	v_sub_f32_e32 v129, v130, v1
	v_sub_f32_e32 v31, v115, v3
	v_sub_f32_e32 v130, v132, v2
	v_sub_f32_e32 v131, v131, v3
	v_pk_mul_f32 v[128:129], v[88:89], v[128:129]
	s_waitcnt lgkmcnt(1)
	v_fma_f32 v28, v36, v28, v120
	v_fma_f32 v29, v37, v29, v121
	v_pk_mul_f32 v[30:31], v[90:91], v[30:31]
	v_pk_mul_f32 v[130:131], v[90:91], v[130:131]
	s_waitcnt lgkmcnt(0)
	v_fma_f32 v36, v116, v128, v124
	ds_write2_b32 v114, v28, v29 offset1:68
	v_fma_f32 v28, v117, v129, v125
	ds_write2_b32 v113, v36, v28 offset0:16 offset1:84
	v_fma_f32 v28, v38, v30, v122
	v_fma_f32 v29, v118, v130, v126
	v_fmac_f32_e32 v123, v39, v31
	v_fmac_f32_e32 v127, v119, v131
	ds_write2_b32 v114, v28, v123 offset0:136 offset1:204
	ds_write2_b32 v113, v29, v127 offset0:152 offset1:220
	s_waitcnt vmcnt(2)
	ds_write_b128 v96, v[24:27] offset:41984
	s_mov_b32 s16, 0
	v_mov_b32_e32 v24, v103
	s_waitcnt lgkmcnt(0)
	s_barrier
	ds_read_b32 v200, v218
	ds_read_b32 v208, v219
	ds_read_b32 v201, v218 offset:544
	ds_read_b32 v209, v219 offset:256
	ds_read_b32 v202, v218 offset:1088
	ds_read_b32 v210, v219 offset:512
	ds_read_b32 v203, v218 offset:1632
	ds_read_b32 v211, v219 offset:768
	ds_read_b32 v204, v218 offset:2176
	ds_read_b32 v212, v219 offset:1024
	ds_read_b32 v205, v218 offset:2720
	ds_read_b32 v213, v219 offset:1280
	ds_read_b32 v206, v218 offset:3264
	ds_read_b32 v214, v219 offset:1536
	s_waitcnt lgkmcnt(12)
	v_mfma_f32_32x32x2_f32 v[4:19], v200, v208, v[4:19]
	ds_read_b32 v207, v218 offset:3808
	ds_read_b32 v215, v219 offset:1792
	s_waitcnt lgkmcnt(12)
	v_mfma_f32_32x32x2_f32 v[4:19], v201, v209, v[4:19]
	s_waitcnt lgkmcnt(10)
	v_mfma_f32_32x32x2_f32 v[4:19], v202, v210, v[4:19]
	s_waitcnt lgkmcnt(8)
	v_mfma_f32_32x32x2_f32 v[4:19], v203, v211, v[4:19]
	s_waitcnt lgkmcnt(6)
	v_mfma_f32_32x32x2_f32 v[4:19], v204, v212, v[4:19]
	s_waitcnt lgkmcnt(4)
	v_mfma_f32_32x32x2_f32 v[4:19], v205, v213, v[4:19]
	s_waitcnt lgkmcnt(2)
	v_mfma_f32_32x32x2_f32 v[4:19], v206, v214, v[4:19]
	s_waitcnt lgkmcnt(0)
	v_mfma_f32_32x32x2_f32 v[4:19], v207, v215, v[4:19]
	s_barrier
	global_load_dwordx4 v[28:31], v[92:93], off offset:1280
	global_load_dwordx4 v[24:27], v[70:71], off
	s_waitcnt vmcnt(3)
	v_cvt_f32_f16_sdwa v128, v32 dst_sel:DWORD dst_unused:UNUSED_PAD src0_sel:WORD_1
	v_cvt_f32_f16_e32 v32, v32
	v_cvt_f32_f16_e32 v129, v33
	v_cvt_f32_f16_sdwa v130, v34 dst_sel:DWORD dst_unused:UNUSED_PAD src0_sel:WORD_1
	v_cvt_f32_f16_e32 v133, v34
	ds_read_b128 v[36:39], v43 offset:14592
	ds_read_b128 v[116:119], v43 offset:14608
	ds_read_b128 v[120:123], v43 offset:18688
	ds_read_b128 v[124:127], v43 offset:18704
	v_cvt_f32_f16_sdwa v115, v33 dst_sel:DWORD dst_unused:UNUSED_PAD src0_sel:WORD_1
	v_cvt_f32_f16_sdwa v131, v35 dst_sel:DWORD dst_unused:UNUSED_PAD src0_sel:WORD_1
	v_cvt_f32_f16_e32 v132, v35
	v_sub_f32_e32 v32, v32, v0
	v_sub_f32_e32 v33, v128, v1
	v_sub_f32_e32 v34, v129, v2
	v_pk_mul_f32 v[32:33], v[88:89], v[32:33]
	v_sub_f32_e32 v128, v133, v0
	v_sub_f32_e32 v129, v130, v1
	v_sub_f32_e32 v35, v115, v3
	v_sub_f32_e32 v130, v132, v2
	v_sub_f32_e32 v131, v131, v3
	v_pk_mul_f32 v[128:129], v[88:89], v[128:129]
	s_waitcnt lgkmcnt(1)
	v_fma_f32 v32, v36, v32, v120
	v_fma_f32 v33, v37, v33, v121
	v_pk_mul_f32 v[34:35], v[90:91], v[34:35]
	v_pk_mul_f32 v[130:131], v[90:91], v[130:131]
	s_waitcnt lgkmcnt(0)
	v_fma_f32 v36, v116, v128, v124
	ds_write2_b32 v114, v32, v33 offset1:68
	v_fma_f32 v32, v117, v129, v125
	ds_write2_b32 v113, v36, v32 offset0:16 offset1:84
	v_fma_f32 v32, v38, v34, v122
	v_fma_f32 v33, v118, v130, v126
	v_fmac_f32_e32 v123, v39, v35
	v_fmac_f32_e32 v127, v119, v131
	ds_write2_b32 v114, v32, v123 offset0:136 offset1:204
	ds_write2_b32 v113, v33, v127 offset0:152 offset1:220
	s_waitcnt vmcnt(2)
	ds_write_b128 v96, v[20:23] offset:41984
	s_mov_b32 s16, 0
	v_mov_b32_e32 v20, v103
	s_waitcnt lgkmcnt(0)
	s_barrier
	ds_read_b32 v200, v218
	ds_read_b32 v208, v219
	ds_read_b32 v201, v218 offset:544
	ds_read_b32 v209, v219 offset:256
	ds_read_b32 v202, v218 offset:1088
	ds_read_b32 v210, v219 offset:512
	ds_read_b32 v203, v218 offset:1632
	ds_read_b32 v211, v219 offset:768
	ds_read_b32 v204, v218 offset:2176
	ds_read_b32 v212, v219 offset:1024
	ds_read_b32 v205, v218 offset:2720
	ds_read_b32 v213, v219 offset:1280
	ds_read_b32 v206, v218 offset:3264
	ds_read_b32 v214, v219 offset:1536
	s_waitcnt lgkmcnt(12)
	v_mfma_f32_32x32x2_f32 v[4:19], v200, v208, v[4:19]
	ds_read_b32 v207, v218 offset:3808
	ds_read_b32 v215, v219 offset:1792
	s_waitcnt lgkmcnt(12)
	v_mfma_f32_32x32x2_f32 v[4:19], v201, v209, v[4:19]
	s_waitcnt lgkmcnt(10)
	v_mfma_f32_32x32x2_f32 v[4:19], v202, v210, v[4:19]
	s_waitcnt lgkmcnt(8)
	v_mfma_f32_32x32x2_f32 v[4:19], v203, v211, v[4:19]
	s_waitcnt lgkmcnt(6)
	v_mfma_f32_32x32x2_f32 v[4:19], v204, v212, v[4:19]
	s_waitcnt lgkmcnt(4)
	v_mfma_f32_32x32x2_f32 v[4:19], v205, v213, v[4:19]
	s_waitcnt lgkmcnt(2)
	v_mfma_f32_32x32x2_f32 v[4:19], v206, v214, v[4:19]
	s_waitcnt lgkmcnt(0)
	v_mfma_f32_32x32x2_f32 v[4:19], v207, v215, v[4:19]
	s_barrier
	global_load_dwordx4 v[32:35], v[92:93], off offset:1408
	global_load_dwordx4 v[20:23], v[72:73], off
	s_waitcnt vmcnt(3)
	v_cvt_f32_f16_sdwa v128, v28 dst_sel:DWORD dst_unused:UNUSED_PAD src0_sel:WORD_1
	v_cvt_f32_f16_e32 v28, v28
	v_cvt_f32_f16_e32 v129, v29
	v_cvt_f32_f16_sdwa v130, v30 dst_sel:DWORD dst_unused:UNUSED_PAD src0_sel:WORD_1
	v_cvt_f32_f16_e32 v133, v30
	ds_read_b128 v[36:39], v43 offset:14848
	ds_read_b128 v[116:119], v43 offset:14864
	ds_read_b128 v[120:123], v43 offset:18944
	ds_read_b128 v[124:127], v43 offset:18960
	v_cvt_f32_f16_sdwa v115, v29 dst_sel:DWORD dst_unused:UNUSED_PAD src0_sel:WORD_1
	v_cvt_f32_f16_sdwa v131, v31 dst_sel:DWORD dst_unused:UNUSED_PAD src0_sel:WORD_1
	v_cvt_f32_f16_e32 v132, v31
	v_sub_f32_e32 v28, v28, v0
	v_sub_f32_e32 v29, v128, v1
	v_sub_f32_e32 v30, v129, v2
	v_pk_mul_f32 v[28:29], v[88:89], v[28:29]
	v_sub_f32_e32 v128, v133, v0
	v_sub_f32_e32 v129, v130, v1
	v_sub_f32_e32 v31, v115, v3
	v_sub_f32_e32 v130, v132, v2
	v_sub_f32_e32 v131, v131, v3
	v_pk_mul_f32 v[128:129], v[88:89], v[128:129]
	s_waitcnt lgkmcnt(1)
	v_fma_f32 v28, v36, v28, v120
	v_fma_f32 v29, v37, v29, v121
	v_pk_mul_f32 v[30:31], v[90:91], v[30:31]
	v_pk_mul_f32 v[130:131], v[90:91], v[130:131]
	s_waitcnt lgkmcnt(0)
	v_fma_f32 v36, v116, v128, v124
	ds_write2_b32 v114, v28, v29 offset1:68
	v_fma_f32 v28, v117, v129, v125
	ds_write2_b32 v113, v36, v28 offset0:16 offset1:84
	v_fma_f32 v28, v38, v30, v122
	v_fma_f32 v29, v118, v130, v126
	v_fmac_f32_e32 v123, v39, v31
	v_fmac_f32_e32 v127, v119, v131
	ds_write2_b32 v114, v28, v123 offset0:136 offset1:204
	ds_write2_b32 v113, v29, v127 offset0:152 offset1:220
	s_waitcnt vmcnt(2)
	ds_write_b128 v96, v[24:27] offset:41984
	s_mov_b32 s16, 0
	v_mov_b32_e32 v24, v103
	s_waitcnt lgkmcnt(0)
	s_barrier
	ds_read_b32 v200, v218
	ds_read_b32 v208, v219
	ds_read_b32 v201, v218 offset:544
	ds_read_b32 v209, v219 offset:256
	ds_read_b32 v202, v218 offset:1088
	ds_read_b32 v210, v219 offset:512
	ds_read_b32 v203, v218 offset:1632
	ds_read_b32 v211, v219 offset:768
	ds_read_b32 v204, v218 offset:2176
	ds_read_b32 v212, v219 offset:1024
	ds_read_b32 v205, v218 offset:2720
	ds_read_b32 v213, v219 offset:1280
	ds_read_b32 v206, v218 offset:3264
	ds_read_b32 v214, v219 offset:1536
	s_waitcnt lgkmcnt(12)
	v_mfma_f32_32x32x2_f32 v[4:19], v200, v208, v[4:19]
	ds_read_b32 v207, v218 offset:3808
	ds_read_b32 v215, v219 offset:1792
	s_waitcnt lgkmcnt(12)
	v_mfma_f32_32x32x2_f32 v[4:19], v201, v209, v[4:19]
	s_waitcnt lgkmcnt(10)
	v_mfma_f32_32x32x2_f32 v[4:19], v202, v210, v[4:19]
	s_waitcnt lgkmcnt(8)
	v_mfma_f32_32x32x2_f32 v[4:19], v203, v211, v[4:19]
	s_waitcnt lgkmcnt(6)
	v_mfma_f32_32x32x2_f32 v[4:19], v204, v212, v[4:19]
	s_waitcnt lgkmcnt(4)
	v_mfma_f32_32x32x2_f32 v[4:19], v205, v213, v[4:19]
	s_waitcnt lgkmcnt(2)
	v_mfma_f32_32x32x2_f32 v[4:19], v206, v214, v[4:19]
	s_waitcnt lgkmcnt(0)
	v_mfma_f32_32x32x2_f32 v[4:19], v207, v215, v[4:19]
	s_barrier
	global_load_dwordx4 v[28:31], v[92:93], off offset:1536
	global_load_dwordx4 v[24:27], v[74:75], off
	s_waitcnt vmcnt(3)
	v_cvt_f32_f16_sdwa v128, v32 dst_sel:DWORD dst_unused:UNUSED_PAD src0_sel:WORD_1
	v_cvt_f32_f16_e32 v32, v32
	v_cvt_f32_f16_e32 v129, v33
	v_cvt_f32_f16_sdwa v130, v34 dst_sel:DWORD dst_unused:UNUSED_PAD src0_sel:WORD_1
	v_cvt_f32_f16_e32 v133, v34
	ds_read_b128 v[36:39], v43 offset:15104
	ds_read_b128 v[116:119], v43 offset:15120
	ds_read_b128 v[120:123], v43 offset:19200
	ds_read_b128 v[124:127], v43 offset:19216
	v_cvt_f32_f16_sdwa v115, v33 dst_sel:DWORD dst_unused:UNUSED_PAD src0_sel:WORD_1
	v_cvt_f32_f16_sdwa v131, v35 dst_sel:DWORD dst_unused:UNUSED_PAD src0_sel:WORD_1
	v_cvt_f32_f16_e32 v132, v35
	v_sub_f32_e32 v32, v32, v0
	v_sub_f32_e32 v33, v128, v1
	v_sub_f32_e32 v34, v129, v2
	v_pk_mul_f32 v[32:33], v[88:89], v[32:33]
	v_sub_f32_e32 v128, v133, v0
	v_sub_f32_e32 v129, v130, v1
	v_sub_f32_e32 v35, v115, v3
	v_sub_f32_e32 v130, v132, v2
	v_sub_f32_e32 v131, v131, v3
	v_pk_mul_f32 v[128:129], v[88:89], v[128:129]
	s_waitcnt lgkmcnt(1)
	v_fma_f32 v32, v36, v32, v120
	v_fma_f32 v33, v37, v33, v121
	v_pk_mul_f32 v[34:35], v[90:91], v[34:35]
	v_pk_mul_f32 v[130:131], v[90:91], v[130:131]
	s_waitcnt lgkmcnt(0)
	v_fma_f32 v36, v116, v128, v124
	ds_write2_b32 v114, v32, v33 offset1:68
	v_fma_f32 v32, v117, v129, v125
	ds_write2_b32 v113, v36, v32 offset0:16 offset1:84
	v_fma_f32 v32, v38, v34, v122
	v_fma_f32 v33, v118, v130, v126
	v_fmac_f32_e32 v123, v39, v35
	v_fmac_f32_e32 v127, v119, v131
	ds_write2_b32 v114, v32, v123 offset0:136 offset1:204
	ds_write2_b32 v113, v33, v127 offset0:152 offset1:220
	s_waitcnt vmcnt(2)
	ds_write_b128 v96, v[20:23] offset:41984
	s_mov_b32 s16, 0
	v_mov_b32_e32 v20, v103
	s_waitcnt lgkmcnt(0)
	s_barrier
	ds_read_b32 v200, v218
	ds_read_b32 v208, v219
	ds_read_b32 v201, v218 offset:544
	ds_read_b32 v209, v219 offset:256
	ds_read_b32 v202, v218 offset:1088
	ds_read_b32 v210, v219 offset:512
	ds_read_b32 v203, v218 offset:1632
	ds_read_b32 v211, v219 offset:768
	ds_read_b32 v204, v218 offset:2176
	ds_read_b32 v212, v219 offset:1024
	ds_read_b32 v205, v218 offset:2720
	ds_read_b32 v213, v219 offset:1280
	ds_read_b32 v206, v218 offset:3264
	ds_read_b32 v214, v219 offset:1536
	s_waitcnt lgkmcnt(12)
	v_mfma_f32_32x32x2_f32 v[4:19], v200, v208, v[4:19]
	ds_read_b32 v207, v218 offset:3808
	ds_read_b32 v215, v219 offset:1792
	s_waitcnt lgkmcnt(12)
	v_mfma_f32_32x32x2_f32 v[4:19], v201, v209, v[4:19]
	s_waitcnt lgkmcnt(10)
	v_mfma_f32_32x32x2_f32 v[4:19], v202, v210, v[4:19]
	s_waitcnt lgkmcnt(8)
	v_mfma_f32_32x32x2_f32 v[4:19], v203, v211, v[4:19]
	s_waitcnt lgkmcnt(6)
	v_mfma_f32_32x32x2_f32 v[4:19], v204, v212, v[4:19]
	s_waitcnt lgkmcnt(4)
	v_mfma_f32_32x32x2_f32 v[4:19], v205, v213, v[4:19]
	s_waitcnt lgkmcnt(2)
	v_mfma_f32_32x32x2_f32 v[4:19], v206, v214, v[4:19]
	s_waitcnt lgkmcnt(0)
	v_mfma_f32_32x32x2_f32 v[4:19], v207, v215, v[4:19]
	s_barrier
	global_load_dwordx4 v[32:35], v[92:93], off offset:1664
	global_load_dwordx4 v[20:23], v[76:77], off
	s_waitcnt vmcnt(3)
	v_cvt_f32_f16_sdwa v128, v28 dst_sel:DWORD dst_unused:UNUSED_PAD src0_sel:WORD_1
	v_cvt_f32_f16_e32 v28, v28
	v_cvt_f32_f16_e32 v129, v29
	v_cvt_f32_f16_sdwa v130, v30 dst_sel:DWORD dst_unused:UNUSED_PAD src0_sel:WORD_1
	v_cvt_f32_f16_e32 v133, v30
	ds_read_b128 v[36:39], v43 offset:15360
	ds_read_b128 v[116:119], v43 offset:15376
	ds_read_b128 v[120:123], v43 offset:19456
	ds_read_b128 v[124:127], v43 offset:19472
	v_cvt_f32_f16_sdwa v115, v29 dst_sel:DWORD dst_unused:UNUSED_PAD src0_sel:WORD_1
	v_cvt_f32_f16_sdwa v131, v31 dst_sel:DWORD dst_unused:UNUSED_PAD src0_sel:WORD_1
	v_cvt_f32_f16_e32 v132, v31
	v_sub_f32_e32 v28, v28, v0
	v_sub_f32_e32 v29, v128, v1
	v_sub_f32_e32 v30, v129, v2
	v_pk_mul_f32 v[28:29], v[88:89], v[28:29]
	v_sub_f32_e32 v128, v133, v0
	v_sub_f32_e32 v129, v130, v1
	v_sub_f32_e32 v31, v115, v3
	v_sub_f32_e32 v130, v132, v2
	v_sub_f32_e32 v131, v131, v3
	v_pk_mul_f32 v[128:129], v[88:89], v[128:129]
	s_waitcnt lgkmcnt(1)
	v_fma_f32 v28, v36, v28, v120
	v_fma_f32 v29, v37, v29, v121
	v_pk_mul_f32 v[30:31], v[90:91], v[30:31]
	v_pk_mul_f32 v[130:131], v[90:91], v[130:131]
	s_waitcnt lgkmcnt(0)
	v_fma_f32 v36, v116, v128, v124
	ds_write2_b32 v114, v28, v29 offset1:68
	v_fma_f32 v28, v117, v129, v125
	ds_write2_b32 v113, v36, v28 offset0:16 offset1:84
	v_fma_f32 v28, v38, v30, v122
	v_fma_f32 v29, v118, v130, v126
	v_fmac_f32_e32 v123, v39, v31
	v_fmac_f32_e32 v127, v119, v131
	ds_write2_b32 v114, v28, v123 offset0:136 offset1:204
	ds_write2_b32 v113, v29, v127 offset0:152 offset1:220
	s_waitcnt vmcnt(2)
	ds_write_b128 v96, v[24:27] offset:41984
	s_mov_b32 s16, 0
	v_mov_b32_e32 v24, v103
	s_waitcnt lgkmcnt(0)
	s_barrier
	ds_read_b32 v200, v218
	ds_read_b32 v208, v219
	ds_read_b32 v201, v218 offset:544
	ds_read_b32 v209, v219 offset:256
	ds_read_b32 v202, v218 offset:1088
	ds_read_b32 v210, v219 offset:512
	ds_read_b32 v203, v218 offset:1632
	ds_read_b32 v211, v219 offset:768
	ds_read_b32 v204, v218 offset:2176
	ds_read_b32 v212, v219 offset:1024
	ds_read_b32 v205, v218 offset:2720
	ds_read_b32 v213, v219 offset:1280
	ds_read_b32 v206, v218 offset:3264
	ds_read_b32 v214, v219 offset:1536
	s_waitcnt lgkmcnt(12)
	v_mfma_f32_32x32x2_f32 v[4:19], v200, v208, v[4:19]
	ds_read_b32 v207, v218 offset:3808
	ds_read_b32 v215, v219 offset:1792
	s_waitcnt lgkmcnt(12)
	v_mfma_f32_32x32x2_f32 v[4:19], v201, v209, v[4:19]
	s_waitcnt lgkmcnt(10)
	v_mfma_f32_32x32x2_f32 v[4:19], v202, v210, v[4:19]
	s_waitcnt lgkmcnt(8)
	v_mfma_f32_32x32x2_f32 v[4:19], v203, v211, v[4:19]
	s_waitcnt lgkmcnt(6)
	v_mfma_f32_32x32x2_f32 v[4:19], v204, v212, v[4:19]
	s_waitcnt lgkmcnt(4)
	v_mfma_f32_32x32x2_f32 v[4:19], v205, v213, v[4:19]
	s_waitcnt lgkmcnt(2)
	v_mfma_f32_32x32x2_f32 v[4:19], v206, v214, v[4:19]
	s_waitcnt lgkmcnt(0)
	v_mfma_f32_32x32x2_f32 v[4:19], v207, v215, v[4:19]
	s_barrier
	global_load_dwordx4 v[28:31], v[92:93], off offset:1792
	global_load_dwordx4 v[24:27], v[78:79], off
	s_waitcnt vmcnt(3)
	v_cvt_f32_f16_sdwa v128, v32 dst_sel:DWORD dst_unused:UNUSED_PAD src0_sel:WORD_1
	v_cvt_f32_f16_e32 v32, v32
	v_cvt_f32_f16_e32 v129, v33
	v_cvt_f32_f16_sdwa v130, v34 dst_sel:DWORD dst_unused:UNUSED_PAD src0_sel:WORD_1
	v_cvt_f32_f16_e32 v133, v34
	ds_read_b128 v[36:39], v43 offset:15616
	ds_read_b128 v[116:119], v43 offset:15632
	ds_read_b128 v[120:123], v43 offset:19712
	ds_read_b128 v[124:127], v43 offset:19728
	v_cvt_f32_f16_sdwa v115, v33 dst_sel:DWORD dst_unused:UNUSED_PAD src0_sel:WORD_1
	v_cvt_f32_f16_sdwa v131, v35 dst_sel:DWORD dst_unused:UNUSED_PAD src0_sel:WORD_1
	v_cvt_f32_f16_e32 v132, v35
	v_sub_f32_e32 v32, v32, v0
	v_sub_f32_e32 v33, v128, v1
	v_sub_f32_e32 v34, v129, v2
	v_pk_mul_f32 v[32:33], v[88:89], v[32:33]
	v_sub_f32_e32 v128, v133, v0
	v_sub_f32_e32 v129, v130, v1
	v_sub_f32_e32 v35, v115, v3
	v_sub_f32_e32 v130, v132, v2
	v_sub_f32_e32 v131, v131, v3
	v_pk_mul_f32 v[128:129], v[88:89], v[128:129]
	s_waitcnt lgkmcnt(1)
	v_fma_f32 v32, v36, v32, v120
	v_fma_f32 v33, v37, v33, v121
	v_pk_mul_f32 v[34:35], v[90:91], v[34:35]
	v_pk_mul_f32 v[130:131], v[90:91], v[130:131]
	s_waitcnt lgkmcnt(0)
	v_fma_f32 v36, v116, v128, v124
	ds_write2_b32 v114, v32, v33 offset1:68
	v_fma_f32 v32, v117, v129, v125
	ds_write2_b32 v113, v36, v32 offset0:16 offset1:84
	v_fma_f32 v32, v38, v34, v122
	v_fma_f32 v33, v118, v130, v126
	v_fmac_f32_e32 v123, v39, v35
	v_fmac_f32_e32 v127, v119, v131
	ds_write2_b32 v114, v32, v123 offset0:136 offset1:204
	ds_write2_b32 v113, v33, v127 offset0:152 offset1:220
	s_waitcnt vmcnt(2)
	ds_write_b128 v96, v[20:23] offset:41984
	s_mov_b32 s16, 0
	v_mov_b32_e32 v20, v103
	s_waitcnt lgkmcnt(0)
	s_barrier
	ds_read_b32 v200, v218
	ds_read_b32 v208, v219
	ds_read_b32 v201, v218 offset:544
	ds_read_b32 v209, v219 offset:256
	ds_read_b32 v202, v218 offset:1088
	ds_read_b32 v210, v219 offset:512
	ds_read_b32 v203, v218 offset:1632
	ds_read_b32 v211, v219 offset:768
	ds_read_b32 v204, v218 offset:2176
	ds_read_b32 v212, v219 offset:1024
	ds_read_b32 v205, v218 offset:2720
	ds_read_b32 v213, v219 offset:1280
	ds_read_b32 v206, v218 offset:3264
	ds_read_b32 v214, v219 offset:1536
	s_waitcnt lgkmcnt(12)
	v_mfma_f32_32x32x2_f32 v[4:19], v200, v208, v[4:19]
	ds_read_b32 v207, v218 offset:3808
	ds_read_b32 v215, v219 offset:1792
	s_waitcnt lgkmcnt(12)
	v_mfma_f32_32x32x2_f32 v[4:19], v201, v209, v[4:19]
	s_waitcnt lgkmcnt(10)
	v_mfma_f32_32x32x2_f32 v[4:19], v202, v210, v[4:19]
	s_waitcnt lgkmcnt(8)
	v_mfma_f32_32x32x2_f32 v[4:19], v203, v211, v[4:19]
	s_waitcnt lgkmcnt(6)
	v_mfma_f32_32x32x2_f32 v[4:19], v204, v212, v[4:19]
	s_waitcnt lgkmcnt(4)
	v_mfma_f32_32x32x2_f32 v[4:19], v205, v213, v[4:19]
	s_waitcnt lgkmcnt(2)
	v_mfma_f32_32x32x2_f32 v[4:19], v206, v214, v[4:19]
	s_waitcnt lgkmcnt(0)
	v_mfma_f32_32x32x2_f32 v[4:19], v207, v215, v[4:19]
	s_barrier
	global_load_dwordx4 v[32:35], v[92:93], off offset:1920
	global_load_dwordx4 v[20:23], v[80:81], off
	s_waitcnt vmcnt(3)
	v_cvt_f32_f16_sdwa v93, v28 dst_sel:DWORD dst_unused:UNUSED_PAD src0_sel:WORD_1
	v_cvt_f32_f16_e32 v28, v28
	v_cvt_f32_f16_sdwa v92, v29 dst_sel:DWORD dst_unused:UNUSED_PAD src0_sel:WORD_1
	v_cvt_f32_f16_sdwa v128, v30 dst_sel:DWORD dst_unused:UNUSED_PAD src0_sel:WORD_1
	v_cvt_f32_f16_e32 v131, v30
	ds_read_b128 v[36:39], v43 offset:15872
	ds_read_b128 v[116:119], v43 offset:15888
	ds_read_b128 v[120:123], v43 offset:19968
	ds_read_b128 v[124:127], v43 offset:19984
	v_cvt_f32_f16_e32 v115, v29
	v_cvt_f32_f16_sdwa v129, v31 dst_sel:DWORD dst_unused:UNUSED_PAD src0_sel:WORD_1
	v_cvt_f32_f16_e32 v130, v31
	v_sub_f32_e32 v28, v28, v0
	v_sub_f32_e32 v29, v93, v1
	v_sub_f32_e32 v31, v92, v3
	v_pk_mul_f32 v[28:29], v[88:89], v[28:29]
	v_sub_f32_e32 v92, v131, v0
	v_sub_f32_e32 v93, v128, v1
	v_sub_f32_e32 v30, v115, v2
	v_sub_f32_e32 v128, v130, v2
	v_sub_f32_e32 v129, v129, v3
	v_pk_mul_f32 v[92:93], v[88:89], v[92:93]
	s_waitcnt lgkmcnt(1)
	v_fma_f32 v28, v36, v28, v120
	v_fma_f32 v29, v37, v29, v121
	v_pk_mul_f32 v[30:31], v[90:91], v[30:31]
	v_pk_mul_f32 v[128:129], v[90:91], v[128:129]
	s_waitcnt lgkmcnt(0)
	v_fma_f32 v36, v116, v92, v124
	ds_write2_b32 v114, v28, v29 offset1:68
	v_fma_f32 v28, v117, v93, v125
	ds_write2_b32 v113, v36, v28 offset0:16 offset1:84
	v_fma_f32 v28, v38, v30, v122
	v_fma_f32 v29, v118, v128, v126
	v_fmac_f32_e32 v123, v39, v31
	v_fmac_f32_e32 v127, v119, v129
	ds_write2_b32 v114, v28, v123 offset0:136 offset1:204
	ds_write2_b32 v113, v29, v127 offset0:152 offset1:220
	s_waitcnt vmcnt(2)
	ds_write_b128 v96, v[24:27] offset:41984
	s_mov_b32 s16, 0
	v_mov_b32_e32 v24, v103
	s_waitcnt lgkmcnt(0)
	s_barrier
	ds_read_b32 v200, v218
	ds_read_b32 v208, v219
	ds_read_b32 v201, v218 offset:544
	ds_read_b32 v209, v219 offset:256
	ds_read_b32 v202, v218 offset:1088
	ds_read_b32 v210, v219 offset:512
	ds_read_b32 v203, v218 offset:1632
	ds_read_b32 v211, v219 offset:768
	ds_read_b32 v204, v218 offset:2176
	ds_read_b32 v212, v219 offset:1024
	ds_read_b32 v205, v218 offset:2720
	ds_read_b32 v213, v219 offset:1280
	ds_read_b32 v206, v218 offset:3264
	ds_read_b32 v214, v219 offset:1536
	s_waitcnt lgkmcnt(12)
	v_mfma_f32_32x32x2_f32 v[4:19], v200, v208, v[4:19]
	ds_read_b32 v207, v218 offset:3808
	ds_read_b32 v215, v219 offset:1792
	s_waitcnt lgkmcnt(12)
	v_mfma_f32_32x32x2_f32 v[4:19], v201, v209, v[4:19]
	s_waitcnt lgkmcnt(10)
	v_mfma_f32_32x32x2_f32 v[4:19], v202, v210, v[4:19]
	s_waitcnt lgkmcnt(8)
	v_mfma_f32_32x32x2_f32 v[4:19], v203, v211, v[4:19]
	s_waitcnt lgkmcnt(6)
	v_mfma_f32_32x32x2_f32 v[4:19], v204, v212, v[4:19]
	s_waitcnt lgkmcnt(4)
	v_mfma_f32_32x32x2_f32 v[4:19], v205, v213, v[4:19]
	s_waitcnt lgkmcnt(2)
	v_mfma_f32_32x32x2_f32 v[4:19], v206, v214, v[4:19]
	s_waitcnt lgkmcnt(0)
	v_mfma_f32_32x32x2_f32 v[4:19], v207, v215, v[4:19]
	s_waitcnt vmcnt(1)
	v_cvt_f32_f16_sdwa v93, v32 dst_sel:DWORD dst_unused:UNUSED_PAD src0_sel:WORD_1
	v_cvt_f32_f16_e32 v32, v32
	v_cvt_f32_f16_sdwa v121, v34 dst_sel:DWORD dst_unused:UNUSED_PAD src0_sel:WORD_1
	v_cvt_f32_f16_e32 v123, v34
	s_barrier
	ds_read_b128 v[24:27], v43 offset:16128
	ds_read_b128 v[28:31], v43 offset:16144
	ds_read_b128 v[36:39], v43 offset:20224
	ds_read_b128 v[116:119], v43 offset:20240
	v_cvt_f32_f16_sdwa v92, v33 dst_sel:DWORD dst_unused:UNUSED_PAD src0_sel:WORD_1
	v_cvt_f32_f16_e32 v115, v33
	v_cvt_f32_f16_sdwa v120, v35 dst_sel:DWORD dst_unused:UNUSED_PAD src0_sel:WORD_1
	v_cvt_f32_f16_e32 v122, v35
	v_sub_f32_e32 v32, v32, v0
	v_sub_f32_e32 v33, v93, v1
	v_sub_f32_e32 v0, v123, v0
	v_sub_f32_e32 v1, v121, v1
	v_sub_f32_e32 v34, v115, v2
	v_sub_f32_e32 v35, v92, v3
	v_pk_mul_f32 v[0:1], v[88:89], v[0:1]
	v_pk_mul_f32 v[34:35], v[90:91], v[34:35]
	v_sub_f32_e32 v2, v122, v2
	v_sub_f32_e32 v3, v120, v3
	s_waitcnt lgkmcnt(0)
	v_fma_f32 v0, v28, v0, v116
	v_fma_f32 v1, v29, v1, v117
	v_pk_mul_f32 v[32:33], v[88:89], v[32:33]
	v_pk_mul_f32 v[2:3], v[90:91], v[2:3]
	ds_write2_b32 v113, v0, v1 offset0:16 offset1:84
	v_fma_f32 v0, v26, v34, v38
	v_fmac_f32_e32 v39, v27, v35
	v_fma_f32 v24, v24, v32, v36
	v_fma_f32 v25, v25, v33, v37
	v_fma_f32 v1, v30, v2, v118
	ds_write2_b32 v114, v0, v39 offset0:136 offset1:204
	v_fmac_f32_e32 v119, v31, v3
	s_mov_b32 s16, 0
	v_mov_b32_e32 v0, v103
	ds_write2_b32 v114, v24, v25 offset1:68
	ds_write2_b32 v113, v1, v119 offset0:152 offset1:220
	s_waitcnt vmcnt(0)
	ds_write_b128 v96, v[20:23] offset:41984
	s_waitcnt lgkmcnt(0)
	s_barrier
	ds_read_b32 v200, v218
	ds_read_b32 v208, v219
	ds_read_b32 v201, v218 offset:544
	ds_read_b32 v209, v219 offset:256
	ds_read_b32 v202, v218 offset:1088
	ds_read_b32 v210, v219 offset:512
	ds_read_b32 v203, v218 offset:1632
	ds_read_b32 v211, v219 offset:768
	ds_read_b32 v204, v218 offset:2176
	ds_read_b32 v212, v219 offset:1024
	ds_read_b32 v205, v218 offset:2720
	ds_read_b32 v213, v219 offset:1280
	ds_read_b32 v206, v218 offset:3264
	ds_read_b32 v214, v219 offset:1536
	s_waitcnt lgkmcnt(12)
	v_mfma_f32_32x32x2_f32 v[4:19], v200, v208, v[4:19]
	ds_read_b32 v207, v218 offset:3808
	ds_read_b32 v215, v219 offset:1792
	s_waitcnt lgkmcnt(12)
	v_mfma_f32_32x32x2_f32 v[4:19], v201, v209, v[4:19]
	s_waitcnt lgkmcnt(10)
	v_mfma_f32_32x32x2_f32 v[4:19], v202, v210, v[4:19]
	s_waitcnt lgkmcnt(8)
	v_mfma_f32_32x32x2_f32 v[4:19], v203, v211, v[4:19]
	s_waitcnt lgkmcnt(6)
	v_mfma_f32_32x32x2_f32 v[4:19], v204, v212, v[4:19]
	s_waitcnt lgkmcnt(4)
	v_mfma_f32_32x32x2_f32 v[4:19], v205, v213, v[4:19]
	s_waitcnt lgkmcnt(2)
	v_mfma_f32_32x32x2_f32 v[4:19], v206, v214, v[4:19]
	s_waitcnt lgkmcnt(0)
	v_mfma_f32_32x32x2_f32 v[4:19], v207, v215, v[4:19]
	s_barrier
	s_nop 15
	s_nop 3
	ds_write_b32 v217, v4 offset:58752
	ds_write_b32 v217, v5 offset:58880
	ds_write_b32 v217, v6 offset:59008
	ds_write_b32 v217, v7 offset:59136
	ds_write_b32 v217, v8 offset:59776
	ds_write_b32 v217, v9 offset:59904
	ds_write_b32 v217, v10 offset:60032
	ds_write_b32 v217, v11 offset:60160
	ds_write_b32 v217, v12 offset:60800
	ds_write_b32 v217, v13 offset:60928
	ds_write_b32 v217, v14 offset:61056
	ds_write_b32 v217, v15 offset:61184
	ds_write_b32 v217, v16 offset:61824
	ds_write_b32 v217, v17 offset:61952
	ds_write_b32 v217, v18 offset:62080
	ds_write_b32 v217, v19 offset:62208
	s_waitcnt lgkmcnt(0)
	s_barrier
	global_load_dwordx4 v[0:3], v[50:51], off offset:128
	ds_read_b128 v[4:7], v98 offset:58752
	ds_read_b128 v[8:11], v99 offset:8192
	ds_read_b128 v[12:15], v99 offset:16384
	ds_read_b128 v[16:19], v99 offset:24576
	v_add_u32_e32 v20, 0xc400, v100
	v_add_u32_e32 v21, 0xc408, v100
	s_waitcnt lgkmcnt(2)
	v_pk_add_f32 v[4:5], v[4:5], v[8:9]
	v_pk_add_f32 v[6:7], v[6:7], v[10:11]
	s_waitcnt lgkmcnt(1)
	v_pk_add_f32 v[4:5], v[12:13], v[4:5]
	v_pk_add_f32 v[6:7], v[14:15], v[6:7]
	s_waitcnt lgkmcnt(0)
	v_pk_add_f32 v[4:5], v[16:17], v[4:5]
	v_pk_add_f32 v[6:7], v[18:19], v[6:7]
	s_waitcnt vmcnt(0)
	v_pk_add_f32 v[0:1], v[0:1], v[4:5]
	v_pk_add_f32 v[2:3], v[6:7], v[2:3]
	ds_write2_b32 v20, v0, v1 offset1:1
	ds_write2_b32 v21, v2, v3 offset1:1
	s_waitcnt lgkmcnt(0)
	s_barrier
	s_and_saveexec_b64 s[36:37], s[6:7]
	s_cbranch_execz .LBB0_1510
	v_add_u32_e32 v0, 0xc400, v108
	v_add_u32_e32 v1, 0xc408, v108
	v_add_u32_e32 v2, 0xc410, v108
	v_add_u32_e32 v3, 0xc418, v108
	ds_read2_b32 v[34:35], v0 offset1:1
	ds_read2_b32 v[30:31], v1 offset1:1
	ds_read2_b32 v[22:23], v2 offset1:1
	ds_read2_b32 v[10:11], v3 offset1:1
	s_mov_b32 s16, 0xff61b1e6
	s_waitcnt lgkmcnt(3)
	v_max_f32_e32 v0, v34, v34
	v_max_f32_e32 v0, 0xff61b1e6, v0
	v_cmp_lt_f32_e32 vcc, s16, v34
	v_cmp_gt_f32_e64 s[16:17], v35, v0
	v_add_u32_e32 v2, 0xc420, v108
	ds_read2_b32 v[24:25], v2 offset1:1
	v_cndmask_b32_e64 v0, v0, v35, s[16:17]
	v_cndmask_b32_e64 v1, 0, 1, s[16:17]
	s_waitcnt lgkmcnt(3)
	v_cmp_gt_f32_e64 s[16:17], v30, v0
	v_add_u32_e32 v2, 0xc428, v108
	v_add_u32_e32 v3, 0xc430, v108
	v_cndmask_b32_e64 v0, v0, v30, s[16:17]
	v_cndmask_b32_e64 v1, v1, 2, s[16:17]
	v_cmp_gt_f32_e64 s[16:17], v31, v0
	v_add_u32_e32 v4, 0xc438, v108
	ds_read2_b32 v[32:33], v2 offset1:1
	ds_read2_b32 v[20:21], v3 offset1:1
	ds_read2_b32 v[6:7], v4 offset1:1
	v_cndmask_b32_e64 v0, v0, v31, s[16:17]
	v_cndmask_b32_e64 v1, v1, 3, s[16:17]
	s_waitcnt lgkmcnt(5)
	v_cmp_gt_f32_e64 s[16:17], v22, v0
	v_add_u32_e32 v2, 0xc440, v108
	ds_read2_b32 v[18:19], v2 offset1:1
	v_cndmask_b32_e64 v0, v0, v22, s[16:17]
	v_cndmask_b32_e64 v1, v1, 4, s[16:17]
	v_cmp_gt_f32_e64 s[16:17], v23, v0
	v_add_u32_e32 v2, 0xc448, v108
	v_add_u32_e32 v4, 0xc458, v108
	v_cndmask_b32_e64 v0, v0, v23, s[16:17]
	v_cndmask_b32_e64 v1, v1, 5, s[16:17]
	s_waitcnt lgkmcnt(5)
	v_cmp_gt_f32_e64 s[16:17], v10, v0
	v_add_u32_e32 v3, 0xc450, v108
	ds_read2_b32 v[28:29], v2 offset1:1
	ds_read2_b32 v[12:13], v3 offset1:1
	ds_read2_b32 v[4:5], v4 offset1:1
	v_cndmask_b32_e64 v0, v0, v10, s[16:17]
	v_cndmask_b32_e64 v1, v1, 6, s[16:17]
	v_cmp_gt_f32_e64 s[16:17], v11, v0
	v_add_u32_e32 v2, 0xc460, v108
	ds_read2_b32 v[14:15], v2 offset1:1
	v_cndmask_b32_e64 v0, v0, v11, s[16:17]
	v_cndmask_b32_e64 v1, v1, 7, s[16:17]
	s_waitcnt lgkmcnt(8)
	v_cmp_gt_f32_e64 s[16:17], v24, v0
	v_add_u32_e32 v2, 0xc468, v108
	v_add_u32_e32 v8, 0xc478, v108
	v_cndmask_b32_e64 v0, v0, v24, s[16:17]
	v_cndmask_b32_e64 v1, v1, 8, s[16:17]
	v_cmp_gt_f32_e64 s[16:17], v25, v0
	v_add_u32_e32 v3, 0xc470, v108
	ds_read2_b32 v[26:27], v2 offset1:1
	ds_read2_b32 v[16:17], v3 offset1:1
	ds_read2_b32 v[8:9], v8 offset1:1
	v_cndmask_b32_e64 v0, v0, v25, s[16:17]
	v_cndmask_b32_e64 v1, v1, 9, s[16:17]
	s_waitcnt lgkmcnt(10)
	v_cmp_gt_f32_e64 s[16:17], v32, v0
	s_nop 1
	v_cndmask_b32_e64 v0, v0, v32, s[16:17]
	v_cndmask_b32_e64 v1, v1, 10, s[16:17]
	v_cmp_gt_f32_e64 s[16:17], v33, v0
	s_nop 1
	v_cndmask_b32_e64 v0, v0, v33, s[16:17]
	v_cndmask_b32_e64 v1, v1, 11, s[16:17]
	s_waitcnt lgkmcnt(9)
	v_cmp_gt_f32_e64 s[16:17], v20, v0
	s_nop 1
	v_cndmask_b32_e64 v0, v0, v20, s[16:17]
	v_cndmask_b32_e64 v1, v1, 12, s[16:17]
	v_cmp_gt_f32_e64 s[16:17], v21, v0
	s_nop 1
	v_cndmask_b32_e64 v0, v0, v21, s[16:17]
	v_cndmask_b32_e64 v1, v1, 13, s[16:17]
	s_waitcnt lgkmcnt(8)
	v_cmp_gt_f32_e64 s[16:17], v6, v0
	s_nop 1
	v_cndmask_b32_e64 v0, v0, v6, s[16:17]
	v_cndmask_b32_e64 v1, v1, 14, s[16:17]
	v_cmp_gt_f32_e64 s[16:17], v7, v0
	s_nop 1
	v_cndmask_b32_e64 v0, v0, v7, s[16:17]
	v_cndmask_b32_e64 v1, v1, 15, s[16:17]
	s_waitcnt lgkmcnt(7)
	v_cmp_gt_f32_e64 s[16:17], v18, v0
	s_nop 1
	v_cndmask_b32_e64 v0, v0, v18, s[16:17]
	v_cndmask_b32_e64 v1, v1, 16, s[16:17]
	v_cmp_gt_f32_e64 s[16:17], v19, v0
	s_nop 1
	v_cndmask_b32_e64 v0, v0, v19, s[16:17]
	v_cndmask_b32_e64 v1, v1, 17, s[16:17]
	s_waitcnt lgkmcnt(6)
	v_cmp_gt_f32_e64 s[16:17], v28, v0
	s_nop 1
	v_cndmask_b32_e64 v0, v0, v28, s[16:17]
	v_cndmask_b32_e64 v1, v1, 18, s[16:17]
	v_cmp_gt_f32_e64 s[16:17], v29, v0
	s_nop 1
	v_cndmask_b32_e64 v0, v0, v29, s[16:17]
	v_cndmask_b32_e64 v1, v1, 19, s[16:17]
	s_waitcnt lgkmcnt(5)
	v_cmp_gt_f32_e64 s[16:17], v12, v0
	s_nop 1
	v_cndmask_b32_e64 v0, v0, v12, s[16:17]
	v_cndmask_b32_e64 v1, v1, 20, s[16:17]
	v_cmp_gt_f32_e64 s[16:17], v13, v0
	s_nop 1
	v_cndmask_b32_e64 v0, v0, v13, s[16:17]
	v_cndmask_b32_e64 v1, v1, 21, s[16:17]
	s_waitcnt lgkmcnt(4)
	v_cmp_gt_f32_e64 s[16:17], v4, v0
	s_nop 1
	v_cndmask_b32_e64 v0, v0, v4, s[16:17]
	v_cndmask_b32_e64 v1, v1, 22, s[16:17]
	v_cmp_gt_f32_e64 s[16:17], v5, v0
	s_nop 1
	v_cndmask_b32_e64 v0, v0, v5, s[16:17]
	v_cndmask_b32_e64 v1, v1, 23, s[16:17]
	s_waitcnt lgkmcnt(3)
	v_cmp_gt_f32_e64 s[16:17], v14, v0
	s_nop 1
	v_cndmask_b32_e64 v0, v0, v14, s[16:17]
	v_cndmask_b32_e64 v1, v1, 24, s[16:17]
	v_cmp_gt_f32_e64 s[16:17], v15, v0
	s_nop 1
	v_cndmask_b32_e64 v0, v0, v15, s[16:17]
	v_cndmask_b32_e64 v1, v1, 25, s[16:17]
	s_waitcnt lgkmcnt(2)
	v_cmp_gt_f32_e64 s[16:17], v26, v0
	s_nop 1
	v_cndmask_b32_e64 v0, v0, v26, s[16:17]
	v_cndmask_b32_e64 v1, v1, 26, s[16:17]
	v_cmp_gt_f32_e64 s[16:17], v27, v0
	s_nop 1
	v_cndmask_b32_e64 v0, v0, v27, s[16:17]
	v_cndmask_b32_e64 v1, v1, 27, s[16:17]
	s_waitcnt lgkmcnt(1)
	v_cmp_gt_f32_e64 s[16:17], v16, v0
	s_nop 1
	v_cndmask_b32_e64 v0, v0, v16, s[16:17]
	v_cndmask_b32_e64 v1, v1, 28, s[16:17]
	v_cmp_gt_f32_e64 s[16:17], v17, v0
	s_nop 1
	v_cndmask_b32_e64 v0, v0, v17, s[16:17]
	v_cndmask_b32_e64 v1, v1, 29, s[16:17]
	s_waitcnt lgkmcnt(0)
	v_cmp_gt_f32_e64 s[16:17], v8, v0
	s_nop 1
	v_cndmask_b32_e64 v0, v0, v8, s[16:17]
	v_cndmask_b32_e64 v1, v1, 30, s[16:17]
	v_cmp_gt_f32_e64 s[16:17], v9, v0
	s_nop 1
	v_cndmask_b32_e64 v36, v0, v9, s[16:17]
	v_cndmask_b32_e64 v0, v1, 31, s[16:17]
	v_cmp_ne_u32_e64 s[16:17], 0, v0
	v_lshlrev_b32_e64 v2, v0, 1
	s_and_b64 s[16:17], s[16:17], vcc
	v_cndmask_b32_e64 v1, v112, v34, s[16:17]
	v_and_b32_e32 v3, 2, v2
	v_cmp_eq_u32_e64 s[16:17], 0, v3
	v_cmp_gt_f32_e64 s[18:19], v35, v1
	s_and_b64 s[16:17], s[16:17], s[18:19]
	v_cndmask_b32_e64 v1, v1, v35, s[16:17]
	v_and_b32_e32 v37, 4, v2
	v_cndmask_b32_e64 v3, 0, 1, s[16:17]
	v_cmp_eq_u32_e64 s[16:17], 0, v37
	v_cmp_gt_f32_e64 s[18:19], v30, v1
	s_and_b64 s[16:17], s[16:17], s[18:19]
	v_cndmask_b32_e64 v1, v1, v30, s[16:17]
	v_and_b32_e32 v37, 8, v2
	v_cndmask_b32_e64 v3, v3, 2, s[16:17]
	v_cmp_eq_u32_e64 s[16:17], 0, v37
	v_cmp_gt_f32_e64 s[18:19], v31, v1
	s_and_b64 s[16:17], s[16:17], s[18:19]
	v_cndmask_b32_e64 v1, v1, v31, s[16:17]
	v_and_b32_e32 v37, 16, v2
	v_cndmask_b32_e64 v3, v3, 3, s[16:17]
	v_cmp_eq_u32_e64 s[16:17], 0, v37
	v_cmp_gt_f32_e64 s[18:19], v22, v1
	s_and_b64 s[16:17], s[16:17], s[18:19]
	v_cndmask_b32_e64 v1, v1, v22, s[16:17]
	v_and_b32_e32 v37, 32, v2
	v_cndmask_b32_e64 v3, v3, 4, s[16:17]
	v_cmp_eq_u32_e64 s[16:17], 0, v37
	v_cmp_gt_f32_e64 s[18:19], v23, v1
	s_and_b64 s[16:17], s[16:17], s[18:19]
	v_cndmask_b32_e64 v1, v1, v23, s[16:17]
	v_and_b32_e32 v37, 64, v2
	v_cndmask_b32_e64 v3, v3, 5, s[16:17]
	v_cmp_eq_u32_e64 s[16:17], 0, v37
	v_cmp_gt_f32_e64 s[18:19], v10, v1
	s_and_b64 s[16:17], s[16:17], s[18:19]
	v_cndmask_b32_e64 v1, v1, v10, s[16:17]
	v_and_b32_e32 v37, 0x80, v2
	v_cndmask_b32_e64 v3, v3, 6, s[16:17]
	v_cmp_eq_u32_e64 s[16:17], 0, v37
	v_cmp_gt_f32_e64 s[18:19], v11, v1
	s_and_b64 s[16:17], s[16:17], s[18:19]
	v_cndmask_b32_e64 v1, v1, v11, s[16:17]
	v_and_b32_e32 v37, 0x100, v2
	v_cndmask_b32_e64 v3, v3, 7, s[16:17]
	v_cmp_eq_u32_e64 s[16:17], 0, v37
	v_cmp_gt_f32_e64 s[18:19], v24, v1
	s_and_b64 s[16:17], s[16:17], s[18:19]
	v_cndmask_b32_e64 v1, v1, v24, s[16:17]
	v_and_b32_e32 v37, 0x200, v2
	v_cndmask_b32_e64 v3, v3, 8, s[16:17]
	v_cmp_eq_u32_e64 s[16:17], 0, v37
	v_cmp_gt_f32_e64 s[18:19], v25, v1
	s_and_b64 s[16:17], s[16:17], s[18:19]
	v_cndmask_b32_e64 v1, v1, v25, s[16:17]
	v_and_b32_e32 v37, 0x400, v2
	v_cndmask_b32_e64 v3, v3, 9, s[16:17]
	v_cmp_eq_u32_e64 s[16:17], 0, v37
	v_cmp_gt_f32_e64 s[18:19], v32, v1
	s_and_b64 s[16:17], s[16:17], s[18:19]
	v_cndmask_b32_e64 v1, v1, v32, s[16:17]
	v_and_b32_e32 v37, 0x800, v2
	v_cndmask_b32_e64 v3, v3, 10, s[16:17]
	v_cmp_eq_u32_e64 s[16:17], 0, v37
	v_cmp_gt_f32_e64 s[18:19], v33, v1
	s_and_b64 s[16:17], s[16:17], s[18:19]
	v_cndmask_b32_e64 v1, v1, v33, s[16:17]
	v_and_b32_e32 v37, 0x1000, v2
	v_cndmask_b32_e64 v3, v3, 11, s[16:17]
	v_cmp_eq_u32_e64 s[16:17], 0, v37
	v_cmp_gt_f32_e64 s[18:19], v20, v1
	s_and_b64 s[16:17], s[16:17], s[18:19]
	v_cndmask_b32_e64 v1, v1, v20, s[16:17]
	v_and_b32_e32 v37, 0x2000, v2
	v_cndmask_b32_e64 v3, v3, 12, s[16:17]
	v_cmp_eq_u32_e64 s[16:17], 0, v37
	v_cmp_gt_f32_e64 s[18:19], v21, v1
	s_and_b64 s[16:17], s[16:17], s[18:19]
	v_cndmask_b32_e64 v1, v1, v21, s[16:17]
	v_and_b32_e32 v37, 0x4000, v2
	v_cndmask_b32_e64 v3, v3, 13, s[16:17]
	v_cmp_eq_u32_e64 s[16:17], 0, v37
	v_cmp_gt_f32_e64 s[18:19], v6, v1
	s_and_b64 s[16:17], s[16:17], s[18:19]
	v_cndmask_b32_e64 v1, v1, v6, s[16:17]
	v_and_b32_e32 v37, 0x8000, v2
	v_cndmask_b32_e64 v3, v3, 14, s[16:17]
	v_cmp_eq_u32_e64 s[16:17], 0, v37
	v_cmp_gt_f32_e64 s[18:19], v7, v1
	s_and_b64 s[16:17], s[16:17], s[18:19]
	v_cndmask_b32_e64 v1, v1, v7, s[16:17]
	v_and_b32_e32 v37, 0x10000, v2
	v_cndmask_b32_e64 v3, v3, 15, s[16:17]
	v_cmp_eq_u32_e64 s[16:17], 0, v37
	v_cmp_gt_f32_e64 s[18:19], v18, v1
	s_and_b64 s[16:17], s[16:17], s[18:19]
	v_cndmask_b32_e64 v1, v1, v18, s[16:17]
	v_and_b32_e32 v37, 0x20000, v2
	v_cndmask_b32_e64 v3, v3, 16, s[16:17]
	v_cmp_eq_u32_e64 s[16:17], 0, v37
	v_cmp_gt_f32_e64 s[18:19], v19, v1
	s_and_b64 s[16:17], s[16:17], s[18:19]
	v_cndmask_b32_e64 v1, v1, v19, s[16:17]
	v_and_b32_e32 v37, 0x40000, v2
	v_cndmask_b32_e64 v3, v3, 17, s[16:17]
	v_cmp_eq_u32_e64 s[16:17], 0, v37
	v_cmp_gt_f32_e64 s[18:19], v28, v1
	s_and_b64 s[16:17], s[16:17], s[18:19]
	v_cndmask_b32_e64 v1, v1, v28, s[16:17]
	v_and_b32_e32 v37, 0x80000, v2
	v_cndmask_b32_e64 v3, v3, 18, s[16:17]
	v_cmp_eq_u32_e64 s[16:17], 0, v37
	v_cmp_gt_f32_e64 s[18:19], v29, v1
	s_and_b64 s[16:17], s[16:17], s[18:19]
	v_cndmask_b32_e64 v1, v1, v29, s[16:17]
	v_and_b32_e32 v37, 0x100000, v2
	v_cndmask_b32_e64 v3, v3, 19, s[16:17]
	v_cmp_eq_u32_e64 s[16:17], 0, v37
	v_cmp_gt_f32_e64 s[18:19], v12, v1
	s_and_b64 s[16:17], s[16:17], s[18:19]
	v_cndmask_b32_e64 v1, v1, v12, s[16:17]
	v_and_b32_e32 v37, 0x200000, v2
	v_cndmask_b32_e64 v3, v3, 20, s[16:17]
	v_cmp_eq_u32_e64 s[16:17], 0, v37
	v_cmp_gt_f32_e64 s[18:19], v13, v1
	s_and_b64 s[16:17], s[16:17], s[18:19]
	v_cndmask_b32_e64 v1, v1, v13, s[16:17]
	v_and_b32_e32 v37, 0x400000, v2
	v_cndmask_b32_e64 v3, v3, 21, s[16:17]
	v_cmp_eq_u32_e64 s[16:17], 0, v37
	v_cmp_gt_f32_e64 s[18:19], v4, v1
	s_and_b64 s[16:17], s[16:17], s[18:19]
	v_cndmask_b32_e64 v1, v1, v4, s[16:17]
	v_and_b32_e32 v37, 0x800000, v2
	v_cndmask_b32_e64 v3, v3, 22, s[16:17]
	v_cmp_eq_u32_e64 s[16:17], 0, v37
	v_cmp_gt_f32_e64 s[18:19], v5, v1
	s_and_b64 s[16:17], s[16:17], s[18:19]
	v_cndmask_b32_e64 v1, v1, v5, s[16:17]
	v_and_b32_e32 v37, 0x1000000, v2
	v_cndmask_b32_e64 v3, v3, 23, s[16:17]
	v_cmp_eq_u32_e64 s[16:17], 0, v37
	v_cmp_gt_f32_e64 s[18:19], v14, v1
	s_and_b64 s[16:17], s[16:17], s[18:19]
	v_cndmask_b32_e64 v1, v1, v14, s[16:17]
	v_and_b32_e32 v37, 0x2000000, v2
	v_cndmask_b32_e64 v3, v3, 24, s[16:17]
	v_cmp_eq_u32_e64 s[16:17], 0, v37
	v_cmp_gt_f32_e64 s[18:19], v15, v1
	s_and_b64 s[16:17], s[16:17], s[18:19]
	v_cndmask_b32_e64 v1, v1, v15, s[16:17]
	v_and_b32_e32 v37, 0x4000000, v2
	v_cndmask_b32_e64 v3, v3, 25, s[16:17]
	v_cmp_eq_u32_e64 s[16:17], 0, v37
	v_cmp_gt_f32_e64 s[18:19], v26, v1
	s_and_b64 s[16:17], s[16:17], s[18:19]
	v_cndmask_b32_e64 v1, v1, v26, s[16:17]
	v_and_b32_e32 v37, 0x8000000, v2
	v_cndmask_b32_e64 v3, v3, 26, s[16:17]
	v_cmp_eq_u32_e64 s[16:17], 0, v37
	v_cmp_gt_f32_e64 s[18:19], v27, v1
	s_and_b64 s[16:17], s[16:17], s[18:19]
	v_cndmask_b32_e64 v1, v1, v27, s[16:17]
	v_and_b32_e32 v37, 0x10000000, v2
	v_cndmask_b32_e64 v3, v3, 27, s[16:17]
	v_cmp_eq_u32_e64 s[16:17], 0, v37
	v_cmp_gt_f32_e64 s[18:19], v16, v1
	s_and_b64 s[16:17], s[16:17], s[18:19]
	v_cndmask_b32_e64 v1, v1, v16, s[16:17]
	v_and_b32_e32 v37, 0x20000000, v2
	v_cndmask_b32_e64 v3, v3, 28, s[16:17]
	v_cmp_eq_u32_e64 s[16:17], 0, v37
	v_cmp_gt_f32_e64 s[18:19], v17, v1
	s_and_b64 s[16:17], s[16:17], s[18:19]
	v_cndmask_b32_e64 v1, v1, v17, s[16:17]
	v_and_b32_e32 v37, 2.0, v2
	v_cndmask_b32_e64 v3, v3, 29, s[16:17]
	v_cmp_eq_u32_e64 s[16:17], 0, v37
	v_cmp_gt_f32_e64 s[18:19], v8, v1
	s_and_b64 s[16:17], s[16:17], s[18:19]
	v_cndmask_b32_e64 v1, v1, v8, s[16:17]
	v_cndmask_b32_e64 v3, v3, 30, s[16:17]
	v_cmp_ne_u32_e64 s[16:17], 31, v0
	v_cmp_gt_f32_e64 s[18:19], v9, v1
	s_and_b64 s[16:17], s[16:17], s[18:19]
	v_cndmask_b32_e64 v37, v1, v9, s[16:17]
	v_cndmask_b32_e64 v1, v3, 31, s[16:17]
	v_lshl_or_b32 v3, 1, v1, v2
	v_and_b32_e32 v2, 1, v3
	v_cmp_eq_u32_e64 s[16:17], 0, v2
	s_and_b64 s[16:17], s[16:17], vcc
	v_and_b32_e32 v38, 2, v3
	v_cndmask_b32_e64 v2, v112, v34, s[16:17]
	v_cmp_eq_u32_e64 s[16:17], 0, v38
	v_cmp_gt_f32_e64 s[18:19], v35, v2
	s_and_b64 s[16:17], s[16:17], s[18:19]
	v_cndmask_b32_e64 v2, v2, v35, s[16:17]
	v_and_b32_e32 v39, 4, v3
	v_cndmask_b32_e64 v38, 0, 1, s[16:17]
	v_cmp_eq_u32_e64 s[16:17], 0, v39
	v_cmp_gt_f32_e64 s[18:19], v30, v2
	s_and_b64 s[16:17], s[16:17], s[18:19]
	v_cndmask_b32_e64 v2, v2, v30, s[16:17]
	v_and_b32_e32 v39, 8, v3
	v_cndmask_b32_e64 v38, v38, 2, s[16:17]
	v_cmp_eq_u32_e64 s[16:17], 0, v39
	v_cmp_gt_f32_e64 s[18:19], v31, v2
	s_and_b64 s[16:17], s[16:17], s[18:19]
	v_cndmask_b32_e64 v2, v2, v31, s[16:17]
	v_and_b32_e32 v39, 16, v3
	v_cndmask_b32_e64 v38, v38, 3, s[16:17]
	v_cmp_eq_u32_e64 s[16:17], 0, v39
	v_cmp_gt_f32_e64 s[18:19], v22, v2
	s_and_b64 s[16:17], s[16:17], s[18:19]
	v_cndmask_b32_e64 v2, v2, v22, s[16:17]
	v_and_b32_e32 v39, 32, v3
	v_cndmask_b32_e64 v38, v38, 4, s[16:17]
	v_cmp_eq_u32_e64 s[16:17], 0, v39
	v_cmp_gt_f32_e64 s[18:19], v23, v2
	s_and_b64 s[16:17], s[16:17], s[18:19]
	v_cndmask_b32_e64 v2, v2, v23, s[16:17]
	v_and_b32_e32 v39, 64, v3
	v_cndmask_b32_e64 v38, v38, 5, s[16:17]
	v_cmp_eq_u32_e64 s[16:17], 0, v39
	v_cmp_gt_f32_e64 s[18:19], v10, v2
	s_and_b64 s[16:17], s[16:17], s[18:19]
	v_cndmask_b32_e64 v2, v2, v10, s[16:17]
	v_and_b32_e32 v39, 0x80, v3
	v_cndmask_b32_e64 v38, v38, 6, s[16:17]
	v_cmp_eq_u32_e64 s[16:17], 0, v39
	v_cmp_gt_f32_e64 s[18:19], v11, v2
	s_and_b64 s[16:17], s[16:17], s[18:19]
	v_cndmask_b32_e64 v2, v2, v11, s[16:17]
	v_and_b32_e32 v39, 0x100, v3
	v_cndmask_b32_e64 v38, v38, 7, s[16:17]
	v_cmp_eq_u32_e64 s[16:17], 0, v39
	v_cmp_gt_f32_e64 s[18:19], v24, v2
	s_and_b64 s[16:17], s[16:17], s[18:19]
	v_cndmask_b32_e64 v2, v2, v24, s[16:17]
	v_and_b32_e32 v39, 0x200, v3
	v_cndmask_b32_e64 v38, v38, 8, s[16:17]
	v_cmp_eq_u32_e64 s[16:17], 0, v39
	v_cmp_gt_f32_e64 s[18:19], v25, v2
	s_and_b64 s[16:17], s[16:17], s[18:19]
	v_cndmask_b32_e64 v2, v2, v25, s[16:17]
	v_and_b32_e32 v39, 0x400, v3
	v_cndmask_b32_e64 v38, v38, 9, s[16:17]
	v_cmp_eq_u32_e64 s[16:17], 0, v39
	v_cmp_gt_f32_e64 s[18:19], v32, v2
	s_and_b64 s[16:17], s[16:17], s[18:19]
	v_cndmask_b32_e64 v2, v2, v32, s[16:17]
	v_and_b32_e32 v39, 0x800, v3
	v_cndmask_b32_e64 v38, v38, 10, s[16:17]
	v_cmp_eq_u32_e64 s[16:17], 0, v39
	v_cmp_gt_f32_e64 s[18:19], v33, v2
	s_and_b64 s[16:17], s[16:17], s[18:19]
	v_cndmask_b32_e64 v2, v2, v33, s[16:17]
	v_and_b32_e32 v39, 0x1000, v3
	v_cndmask_b32_e64 v38, v38, 11, s[16:17]
	v_cmp_eq_u32_e64 s[16:17], 0, v39
	v_cmp_gt_f32_e64 s[18:19], v20, v2
	s_and_b64 s[16:17], s[16:17], s[18:19]
	v_cndmask_b32_e64 v2, v2, v20, s[16:17]
	v_and_b32_e32 v39, 0x2000, v3
	v_cndmask_b32_e64 v38, v38, 12, s[16:17]
	v_cmp_eq_u32_e64 s[16:17], 0, v39
	v_cmp_gt_f32_e64 s[18:19], v21, v2
	s_and_b64 s[16:17], s[16:17], s[18:19]
	v_cndmask_b32_e64 v2, v2, v21, s[16:17]
	v_and_b32_e32 v39, 0x4000, v3
	v_cndmask_b32_e64 v38, v38, 13, s[16:17]
	v_cmp_eq_u32_e64 s[16:17], 0, v39
	v_cmp_gt_f32_e64 s[18:19], v6, v2
	s_and_b64 s[16:17], s[16:17], s[18:19]
	v_cndmask_b32_e64 v2, v2, v6, s[16:17]
	v_and_b32_e32 v39, 0x8000, v3
	v_cndmask_b32_e64 v38, v38, 14, s[16:17]
	v_cmp_eq_u32_e64 s[16:17], 0, v39
	v_cmp_gt_f32_e64 s[18:19], v7, v2
	s_and_b64 s[16:17], s[16:17], s[18:19]
	v_cndmask_b32_e64 v2, v2, v7, s[16:17]
	v_and_b32_e32 v39, 0x10000, v3
	v_cndmask_b32_e64 v38, v38, 15, s[16:17]
	v_cmp_eq_u32_e64 s[16:17], 0, v39
	v_cmp_gt_f32_e64 s[18:19], v18, v2
	s_and_b64 s[16:17], s[16:17], s[18:19]
	v_cndmask_b32_e64 v2, v2, v18, s[16:17]
	v_and_b32_e32 v39, 0x20000, v3
	v_cndmask_b32_e64 v38, v38, 16, s[16:17]
	v_cmp_eq_u32_e64 s[16:17], 0, v39
	v_cmp_gt_f32_e64 s[18:19], v19, v2
	s_and_b64 s[16:17], s[16:17], s[18:19]
	v_cndmask_b32_e64 v2, v2, v19, s[16:17]
	v_and_b32_e32 v39, 0x40000, v3
	v_cndmask_b32_e64 v38, v38, 17, s[16:17]
	v_cmp_eq_u32_e64 s[16:17], 0, v39
	v_cmp_gt_f32_e64 s[18:19], v28, v2
	s_and_b64 s[16:17], s[16:17], s[18:19]
	v_cndmask_b32_e64 v2, v2, v28, s[16:17]
	v_and_b32_e32 v39, 0x80000, v3
	v_cndmask_b32_e64 v38, v38, 18, s[16:17]
	v_cmp_eq_u32_e64 s[16:17], 0, v39
	v_cmp_gt_f32_e64 s[18:19], v29, v2
	s_and_b64 s[16:17], s[16:17], s[18:19]
	v_cndmask_b32_e64 v2, v2, v29, s[16:17]
	v_and_b32_e32 v39, 0x100000, v3
	v_cndmask_b32_e64 v38, v38, 19, s[16:17]
	v_cmp_eq_u32_e64 s[16:17], 0, v39
	v_cmp_gt_f32_e64 s[18:19], v12, v2
	s_and_b64 s[16:17], s[16:17], s[18:19]
	v_cndmask_b32_e64 v2, v2, v12, s[16:17]
	v_and_b32_e32 v39, 0x200000, v3
	v_cndmask_b32_e64 v38, v38, 20, s[16:17]
	v_cmp_eq_u32_e64 s[16:17], 0, v39
	v_cmp_gt_f32_e64 s[18:19], v13, v2
	s_and_b64 s[16:17], s[16:17], s[18:19]
	v_cndmask_b32_e64 v2, v2, v13, s[16:17]
	v_and_b32_e32 v39, 0x400000, v3
	v_cndmask_b32_e64 v38, v38, 21, s[16:17]
	v_cmp_eq_u32_e64 s[16:17], 0, v39
	v_cmp_gt_f32_e64 s[18:19], v4, v2
	s_and_b64 s[16:17], s[16:17], s[18:19]
	v_cndmask_b32_e64 v2, v2, v4, s[16:17]
	v_and_b32_e32 v39, 0x800000, v3
	v_cndmask_b32_e64 v38, v38, 22, s[16:17]
	v_cmp_eq_u32_e64 s[16:17], 0, v39
	v_cmp_gt_f32_e64 s[18:19], v5, v2
	s_and_b64 s[16:17], s[16:17], s[18:19]
	v_cndmask_b32_e64 v2, v2, v5, s[16:17]
	v_and_b32_e32 v39, 0x1000000, v3
	v_cndmask_b32_e64 v38, v38, 23, s[16:17]
	v_cmp_eq_u32_e64 s[16:17], 0, v39
	v_cmp_gt_f32_e64 s[18:19], v14, v2
	s_and_b64 s[16:17], s[16:17], s[18:19]
	v_cndmask_b32_e64 v2, v2, v14, s[16:17]
	v_and_b32_e32 v39, 0x2000000, v3
	v_cndmask_b32_e64 v38, v38, 24, s[16:17]
	v_cmp_eq_u32_e64 s[16:17], 0, v39
	v_cmp_gt_f32_e64 s[18:19], v15, v2
	s_and_b64 s[16:17], s[16:17], s[18:19]
	v_cndmask_b32_e64 v2, v2, v15, s[16:17]
	v_and_b32_e32 v39, 0x4000000, v3
	v_cndmask_b32_e64 v38, v38, 25, s[16:17]
	v_cmp_eq_u32_e64 s[16:17], 0, v39
	v_cmp_gt_f32_e64 s[18:19], v26, v2
	s_and_b64 s[16:17], s[16:17], s[18:19]
	v_cndmask_b32_e64 v2, v2, v26, s[16:17]
	v_and_b32_e32 v39, 0x8000000, v3
	v_cndmask_b32_e64 v38, v38, 26, s[16:17]
	v_cmp_eq_u32_e64 s[16:17], 0, v39
	v_cmp_gt_f32_e64 s[18:19], v27, v2
	s_and_b64 s[16:17], s[16:17], s[18:19]
	v_cndmask_b32_e64 v2, v2, v27, s[16:17]
	v_and_b32_e32 v39, 0x10000000, v3
	v_cndmask_b32_e64 v38, v38, 27, s[16:17]
	v_cmp_eq_u32_e64 s[16:17], 0, v39
	v_cmp_gt_f32_e64 s[18:19], v16, v2
	s_and_b64 s[16:17], s[16:17], s[18:19]
	v_cndmask_b32_e64 v2, v2, v16, s[16:17]
	v_and_b32_e32 v39, 0x20000000, v3
	v_cndmask_b32_e64 v38, v38, 28, s[16:17]
	v_cmp_eq_u32_e64 s[16:17], 0, v39
	v_cmp_gt_f32_e64 s[18:19], v17, v2
	s_and_b64 s[16:17], s[16:17], s[18:19]
	v_cndmask_b32_e64 v2, v2, v17, s[16:17]
	v_and_b32_e32 v39, 2.0, v3
	v_cndmask_b32_e64 v38, v38, 29, s[16:17]
	v_cmp_eq_u32_e64 s[16:17], 0, v39
	v_cmp_gt_f32_e64 s[18:19], v8, v2
	s_and_b64 s[16:17], s[16:17], s[18:19]
	v_cndmask_b32_e64 v2, v2, v8, s[16:17]
	v_cndmask_b32_e64 v38, v38, 30, s[16:17]
	v_cmp_lt_i32_e64 s[16:17], -1, v3
	v_cmp_gt_f32_e64 s[18:19], v9, v2
	s_and_b64 s[16:17], s[16:17], s[18:19]
	v_cndmask_b32_e64 v39, v2, v9, s[16:17]
	v_cndmask_b32_e64 v2, v38, 31, s[16:17]
	v_lshlrev_b32_e64 v38, v2, 1
	v_bitop3_b32 v89, v38, 1, v3 bitop3:0xc8
	v_cmp_eq_u32_e64 s[16:17], 0, v89
	s_and_b64 vcc, s[16:17], vcc
	v_cndmask_b32_e32 v34, v112, v34, vcc
	v_bitop3_b32 v89, v38, 2, v3 bitop3:0xc8
	v_cmp_eq_u32_e32 vcc, 0, v89
	v_cmp_gt_f32_e64 s[16:17], v35, v34
	s_and_b64 vcc, vcc, s[16:17]
	v_cndmask_b32_e32 v34, v34, v35, vcc
	v_bitop3_b32 v89, v38, 4, v3 bitop3:0xc8
	v_cndmask_b32_e64 v35, 0, 1, vcc
	v_cmp_eq_u32_e32 vcc, 0, v89
	v_cmp_gt_f32_e64 s[16:17], v30, v34
	s_and_b64 vcc, vcc, s[16:17]
	v_cndmask_b32_e32 v30, v34, v30, vcc
	v_cndmask_b32_e64 v34, v35, 2, vcc
	v_bitop3_b32 v35, v38, 8, v3 bitop3:0xc8
	v_cmp_eq_u32_e32 vcc, 0, v35
	v_cmp_gt_f32_e64 s[16:17], v31, v30
	s_and_b64 vcc, vcc, s[16:17]
	v_cndmask_b32_e32 v30, v30, v31, vcc
	v_cndmask_b32_e64 v31, v34, 3, vcc
	v_bitop3_b32 v34, v38, 16, v3 bitop3:0xc8
	v_cmp_eq_u32_e32 vcc, 0, v34
	v_cmp_gt_f32_e64 s[16:17], v22, v30
	s_and_b64 vcc, vcc, s[16:17]
	v_cndmask_b32_e32 v22, v30, v22, vcc
	v_cndmask_b32_e64 v30, v31, 4, vcc
	v_bitop3_b32 v31, v38, 32, v3 bitop3:0xc8
	v_cmp_eq_u32_e32 vcc, 0, v31
	v_cmp_gt_f32_e64 s[16:17], v23, v22
	s_and_b64 vcc, vcc, s[16:17]
	v_cndmask_b32_e32 v22, v22, v23, vcc
	v_cndmask_b32_e64 v23, v30, 5, vcc
	v_bitop3_b32 v30, v38, 64, v3 bitop3:0xc8
	v_cmp_eq_u32_e32 vcc, 0, v30
	v_cmp_gt_f32_e64 s[16:17], v10, v22
	s_and_b64 vcc, vcc, s[16:17]
	s_movk_i32 s16, 0x80
	v_cndmask_b32_e32 v10, v22, v10, vcc
	v_cndmask_b32_e64 v22, v23, 6, vcc
	v_bitop3_b32 v23, v38, s16, v3 bitop3:0xc8
	v_cmp_eq_u32_e32 vcc, 0, v23
	v_cmp_gt_f32_e64 s[16:17], v11, v10
	s_and_b64 vcc, vcc, s[16:17]
	s_movk_i32 s16, 0x100
	v_cndmask_b32_e32 v10, v10, v11, vcc
	v_cndmask_b32_e64 v11, v22, 7, vcc
	v_bitop3_b32 v22, v38, s16, v3 bitop3:0xc8
	v_cmp_eq_u32_e32 vcc, 0, v22
	v_cmp_gt_f32_e64 s[16:17], v24, v10
	s_and_b64 vcc, vcc, s[16:17]
	s_movk_i32 s16, 0x200
	v_cndmask_b32_e32 v10, v10, v24, vcc
	v_bitop3_b32 v22, v38, s16, v3 bitop3:0xc8
	v_cndmask_b32_e64 v11, v11, 8, vcc
	v_cmp_eq_u32_e32 vcc, 0, v22
	v_cmp_gt_f32_e64 s[16:17], v25, v10
	s_and_b64 vcc, vcc, s[16:17]
	v_cndmask_b32_e32 v10, v10, v25, vcc
	v_bitop3_b32 v22, v38, s52, v3 bitop3:0xc8
	v_cndmask_b32_e64 v11, v11, 9, vcc
	v_cmp_eq_u32_e32 vcc, 0, v22
	v_cmp_gt_f32_e64 s[16:17], v32, v10
	s_and_b64 vcc, vcc, s[16:17]
	s_movk_i32 s16, 0x800
	v_cndmask_b32_e32 v10, v10, v32, vcc
	v_bitop3_b32 v22, v38, s16, v3 bitop3:0xc8
	v_cndmask_b32_e64 v11, v11, 10, vcc
	v_cmp_eq_u32_e32 vcc, 0, v22
	v_cmp_gt_f32_e64 s[16:17], v33, v10
	s_and_b64 vcc, vcc, s[16:17]
	s_movk_i32 s16, 0x1000
	v_cndmask_b32_e32 v10, v10, v33, vcc
	v_bitop3_b32 v22, v38, s16, v3 bitop3:0xc8
	v_cndmask_b32_e64 v11, v11, 11, vcc
	v_cmp_eq_u32_e32 vcc, 0, v22
	v_cmp_gt_f32_e64 s[16:17], v20, v10
	s_and_b64 vcc, vcc, s[16:17]
	s_movk_i32 s16, 0x2000
	v_cndmask_b32_e32 v10, v10, v20, vcc
	v_bitop3_b32 v20, v38, s16, v3 bitop3:0xc8
	v_cndmask_b32_e64 v11, v11, 12, vcc
	v_cmp_eq_u32_e32 vcc, 0, v20
	v_cmp_gt_f32_e64 s[16:17], v21, v10
	s_and_b64 vcc, vcc, s[16:17]
	s_movk_i32 s16, 0x4000
	v_cndmask_b32_e32 v10, v10, v21, vcc
	v_bitop3_b32 v20, v38, s16, v3 bitop3:0xc8
	v_cndmask_b32_e64 v11, v11, 13, vcc
	v_cmp_eq_u32_e32 vcc, 0, v20
	v_cmp_gt_f32_e64 s[16:17], v6, v10
	s_and_b64 vcc, vcc, s[16:17]
	s_mov_b32 s16, 0x8000
	v_cndmask_b32_e32 v6, v10, v6, vcc
	v_cndmask_b32_e64 v10, v11, 14, vcc
	v_bitop3_b32 v11, v38, s16, v3 bitop3:0xc8
	v_cmp_eq_u32_e32 vcc, 0, v11
	v_cmp_gt_f32_e64 s[16:17], v7, v6
	s_and_b64 vcc, vcc, s[16:17]
	s_mov_b32 s16, 0x10000
	v_cndmask_b32_e32 v6, v6, v7, vcc
	v_cndmask_b32_e64 v7, v10, 15, vcc
	v_bitop3_b32 v10, v38, s16, v3 bitop3:0xc8
	v_cmp_eq_u32_e32 vcc, 0, v10
	v_cmp_gt_f32_e64 s[16:17], v18, v6
	s_and_b64 vcc, vcc, s[16:17]
	s_mov_b32 s16, 0x20000
	v_cndmask_b32_e32 v6, v6, v18, vcc
	v_bitop3_b32 v10, v38, s16, v3 bitop3:0xc8
	v_cndmask_b32_e64 v7, v7, 16, vcc
	v_cmp_eq_u32_e32 vcc, 0, v10
	v_cmp_gt_f32_e64 s[16:17], v19, v6
	s_and_b64 vcc, vcc, s[16:17]
	s_mov_b32 s16, 0x40000
	v_cndmask_b32_e32 v6, v6, v19, vcc
	v_bitop3_b32 v10, v38, s16, v3 bitop3:0xc8
	v_cndmask_b32_e64 v7, v7, 17, vcc
	v_cmp_eq_u32_e32 vcc, 0, v10
	v_cmp_gt_f32_e64 s[16:17], v28, v6
	s_and_b64 vcc, vcc, s[16:17]
	s_mov_b32 s16, 0x80000
	v_cndmask_b32_e32 v6, v6, v28, vcc
	v_bitop3_b32 v10, v38, s16, v3 bitop3:0xc8
	v_cndmask_b32_e64 v7, v7, 18, vcc
	v_cmp_eq_u32_e32 vcc, 0, v10
	v_cmp_gt_f32_e64 s[16:17], v29, v6
	s_and_b64 vcc, vcc, s[16:17]
	s_mov_b32 s16, 0x100000
	v_cndmask_b32_e32 v6, v6, v29, vcc
	v_bitop3_b32 v10, v38, s16, v3 bitop3:0xc8
	v_cndmask_b32_e64 v7, v7, 19, vcc
	v_cmp_eq_u32_e32 vcc, 0, v10
	v_cmp_gt_f32_e64 s[16:17], v12, v6
	s_and_b64 vcc, vcc, s[16:17]
	s_mov_b32 s16, 0x200000
	v_cndmask_b32_e32 v6, v6, v12, vcc
	v_bitop3_b32 v10, v38, s16, v3 bitop3:0xc8
	v_cndmask_b32_e64 v7, v7, 20, vcc
	v_cmp_eq_u32_e32 vcc, 0, v10
	v_cmp_gt_f32_e64 s[16:17], v13, v6
	s_and_b64 vcc, vcc, s[16:17]
	s_mov_b32 s16, 0x400000
	v_cndmask_b32_e32 v6, v6, v13, vcc
	v_bitop3_b32 v10, v38, s16, v3 bitop3:0xc8
	v_cndmask_b32_e64 v7, v7, 21, vcc
	v_cmp_eq_u32_e32 vcc, 0, v10
	v_cmp_gt_f32_e64 s[16:17], v4, v6
	s_and_b64 vcc, vcc, s[16:17]
	s_mov_b32 s16, 0x800000
	v_cndmask_b32_e32 v4, v6, v4, vcc
	v_cndmask_b32_e64 v6, v7, 22, vcc
	v_bitop3_b32 v7, v38, s16, v3 bitop3:0xc8
	v_cmp_eq_u32_e32 vcc, 0, v7
	v_cmp_gt_f32_e64 s[16:17], v5, v4
	s_and_b64 vcc, vcc, s[16:17]
	s_mov_b32 s16, 0x1000000
	v_cndmask_b32_e32 v4, v4, v5, vcc
	v_cndmask_b32_e64 v5, v6, 23, vcc
	v_bitop3_b32 v6, v38, s16, v3 bitop3:0xc8
	v_cmp_eq_u32_e32 vcc, 0, v6
	v_cmp_gt_f32_e64 s[16:17], v14, v4
	s_and_b64 vcc, vcc, s[16:17]
	v_cndmask_b32_e32 v4, v4, v14, vcc
	v_bitop3_b32 v6, v38, s61, v3 bitop3:0xc8
	v_cndmask_b32_e64 v5, v5, 24, vcc
	v_cmp_eq_u32_e32 vcc, 0, v6
	v_cmp_gt_f32_e64 s[16:17], v15, v4
	s_and_b64 vcc, vcc, s[16:17]
	v_cndmask_b32_e32 v4, v4, v15, vcc
	v_bitop3_b32 v6, v38, s62, v3 bitop3:0xc8
	v_cndmask_b32_e64 v5, v5, 25, vcc
	v_cmp_eq_u32_e32 vcc, 0, v6
	v_cmp_gt_f32_e64 s[16:17], v26, v4
	s_and_b64 vcc, vcc, s[16:17]
	v_cndmask_b32_e32 v4, v4, v26, vcc
	v_bitop3_b32 v6, v38, s63, v3 bitop3:0xc8
	v_cndmask_b32_e64 v5, v5, 26, vcc
	v_cmp_eq_u32_e32 vcc, 0, v6
	v_cmp_gt_f32_e64 s[16:17], v27, v4
	s_and_b64 vcc, vcc, s[16:17]
	v_cndmask_b32_e32 v4, v4, v27, vcc
	v_bitop3_b32 v6, v38, s64, v3 bitop3:0xc8
	v_cndmask_b32_e64 v5, v5, 27, vcc
	v_cmp_eq_u32_e32 vcc, 0, v6
	v_cmp_gt_f32_e64 s[16:17], v16, v4
	s_and_b64 vcc, vcc, s[16:17]
	v_cndmask_b32_e32 v4, v4, v16, vcc
	v_bitop3_b32 v6, v38, s65, v3 bitop3:0xc8
	v_cndmask_b32_e64 v5, v5, 28, vcc
	v_cmp_eq_u32_e32 vcc, 0, v6
	v_cmp_gt_f32_e64 s[16:17], v17, v4
	s_and_b64 vcc, vcc, s[16:17]
	v_or_b32_e32 v88, v38, v3
	v_cndmask_b32_e32 v4, v4, v17, vcc
	v_bitop3_b32 v3, v38, 2.0, v3 bitop3:0xc8
	v_cndmask_b32_e64 v5, v5, 29, vcc
	v_cmp_eq_u32_e32 vcc, 0, v3
	v_cmp_gt_f32_e64 s[16:17], v8, v4
	s_and_b64 vcc, vcc, s[16:17]
	v_cndmask_b32_e32 v3, v4, v8, vcc
	v_cndmask_b32_e64 v4, v5, 30, vcc
	v_cmp_lt_i32_e32 vcc, -1, v88
	v_cmp_gt_f32_e64 s[16:17], v9, v3
	s_and_b64 vcc, vcc, s[16:17]
	v_cndmask_b32_e32 v5, v3, v9, vcc
	v_cndmask_b32_e64 v3, v4, 31, vcc
	v_sub_f32_e32 v4, v36, v36
	v_mul_f32_e32 v4, 0x3fb8aa3b, v4
	v_exp_f32_e32 v10, v4
	v_sub_f32_e32 v4, v37, v36
	v_mul_f32_e32 v4, 0x3fb8aa3b, v4
	v_exp_f32_e32 v11, v4
	v_sub_f32_e32 v4, v39, v36
	v_mul_f32_e32 v4, 0x3fb8aa3b, v4
	v_exp_f32_e32 v12, v4
	v_sub_f32_e32 v4, v5, v36
	v_mul_f32_e32 v4, 0x3fb8aa3b, v4
	v_exp_f32_e32 v13, v4
	v_add_f32_e32 v4, 0, v10
	v_add_f32_e32 v4, v4, v11
	v_add_f32_e32 v4, v4, v12
	v_add_f32_e32 v14, v4, v13
	v_div_scale_f32 v15, s[16:17], v14, v14, v10
	v_rcp_f32_e32 v16, v15
	v_lshl_add_u32 v4, s66, 8, v94
	v_ashrrev_i32_e32 v5, 31, v4
	v_lshlrev_b64 v[6:7], 2, v[4:5]
	v_fma_f32 v5, -v15, v16, 1.0
	v_fmac_f32_e32 v16, v5, v16
	v_div_scale_f32 v5, vcc, v10, v14, v10
	v_mul_f32_e32 v17, v5, v16
	v_fma_f32 v18, -v15, v17, v5
	v_fmac_f32_e32 v17, v18, v16
	v_fma_f32 v5, -v15, v17, v5
	v_div_fmas_f32 v5, v5, v16, v17
	v_div_fixup_f32 v5, v5, v14, v10
	v_div_scale_f32 v10, s[16:17], v14, v14, v11
	v_rcp_f32_e32 v15, v10
	v_lshl_add_u64 v[8:9], s[20:21], 0, v[6:7]
	v_lshl_add_u64 v[6:7], s[22:23], 0, v[6:7]
	global_store_dword v[6:7], v5, off
	v_or_b32_e32 v6, 1, v4
	v_fma_f32 v4, -v10, v15, 1.0
	v_lshl_add_u32 v5, v0, 2, 0
	v_fmac_f32_e32 v15, v4, v15
	v_div_scale_f32 v4, vcc, v11, v14, v11
	ds_add_u32 v5, v109 offset:58624
	v_mul_f32_e32 v5, v4, v15
	v_fma_f32 v16, -v10, v5, v4
	v_fmac_f32_e32 v5, v16, v15
	v_fma_f32 v4, -v10, v5, v4
	v_div_fmas_f32 v4, v4, v15, v5
	v_div_scale_f32 v5, s[16:17], v14, v14, v12
	v_rcp_f32_e32 v15, v5
	v_ashrrev_i32_e32 v7, 31, v6
	v_div_fixup_f32 v4, v4, v14, v11
	v_lshl_add_u64 v[10:11], v[6:7], 2, s[22:23]
	v_lshl_add_u32 v6, v1, 2, 0
	ds_add_u32 v6, v109 offset:58624
	v_fma_f32 v6, -v5, v15, 1.0
	v_fmac_f32_e32 v15, v6, v15
	v_div_scale_f32 v6, vcc, v12, v14, v12
	v_mul_f32_e32 v7, v6, v15
	v_fma_f32 v16, -v5, v7, v6
	v_fmac_f32_e32 v7, v16, v15
	v_fma_f32 v5, -v5, v7, v6
	v_div_scale_f32 v6, s[16:17], v14, v14, v13
	v_div_fmas_f32 v5, v5, v15, v7
	v_rcp_f32_e32 v7, v6
	v_div_fixup_f32 v5, v5, v14, v12
	v_lshl_add_u32 v12, v2, 2, 0
	ds_add_u32 v12, v109 offset:58624
	global_store_dwordx4 v[8:9], v[0:3], off
	s_nop 1
	v_fma_f32 v0, -v6, v7, 1.0
	v_fmac_f32_e32 v7, v0, v7
	v_div_scale_f32 v0, vcc, v13, v14, v13
	v_mul_f32_e32 v1, v0, v7
	v_fma_f32 v2, -v6, v1, v0
	v_fmac_f32_e32 v1, v2, v7
	v_fma_f32 v0, -v6, v1, v0
	v_div_fmas_f32 v0, v0, v7, v1
	v_div_fixup_f32 v6, v0, v14, v13
	global_store_dwordx3 v[10:11], v[4:6], off
	v_lshl_add_u32 v0, v3, 2, 0
	ds_add_u32 v0, v109 offset:58624

.LBB0_2382:
	s_waitcnt vmcnt(0)
	s_barrier
	s_waitcnt vmcnt(0)
	buffer_inv sc1
	s_waitcnt vmcnt(0)
	v_readlane_b32 s98, v253, 20
	v_mbcnt_lo_u32_b32 v216, -1, 0
	v_mbcnt_hi_u32_b32 v216, -1, v216
	s_lshr_b32 s99, s98, 1
	s_and_b32 s100, s98, 1
	v_lshrrev_b32_e32 v217, 5, v216
	v_and_b32_e32 v216, 31, v216
	s_lshl_b32 s101, s99, 4
	v_add_u32_e32 v218, s101, v217
	v_lshlrev_b32_e32 v219, 7, v218
	v_lshl_add_u32 v219, v216, 2, v219
	v_add_u32_e32 v219, 0xa400, v219
	v_mul_u32_u24_e32 v218, 0x110, v218
	s_lshl_b32 s101, s100, 7
	v_add_u32_e32 v218, s101, v218
	v_lshl_add_u32 v218, v216, 2, v218
	v_add_u32_e32 v218, 0x6000, v218
	s_lshl_b32 s101, s99, 13
	s_lshl_b32 s100, s100, 12
	s_add_i32 s101, s101, s100
	v_lshlrev_b32_e32 v217, 9, v217
	v_add_u32_e32 v217, s101, v217
	v_lshl_add_u32 v217, v216, 2, v217
	s_and_saveexec_b64 s[16:17], s[4:5]
	ds_write_b32 v95, v45 offset:58624
	s_or_b64 exec, exec, s[16:17]
	v_add_u32_e32 v0, s67, v42
	v_ashrrev_i32_e32 v1, 31, v0
	v_lshlrev_b64 v[0:1], 11, v[0:1]
	v_lshl_add_u64 v[92:93], v[46:47], 0, v[0:1]
	global_load_dwordx4 v[30:33], v[92:93], off
	global_load_dwordx4 v[34:37], v[48:49], off
	global_load_dwordx4 v[20:23], v[52:53], off
	global_load_dwordx4 v[24:27], v[92:93], off offset:128
	ds_read_b64 v[38:39], v106 offset:20480
	ds_read_b128 v[116:119], v43 offset:12288
	ds_read_b128 v[120:123], v43 offset:12304
	ds_read_b128 v[124:127], v43 offset:16384
	ds_read_b128 v[128:131], v43 offset:16400
	v_add_u32_e32 v114, 0x6000, v97
	v_mov_b32_e32 v4, 0
	s_waitcnt lgkmcnt(4)
	v_mov_b32_e32 v0, v38
	v_mov_b32_e32 v1, v38
	v_mov_b32_e32 v2, v38
	v_mov_b32_e32 v3, v38
	v_mov_b32_e32 v88, v39
	v_mov_b32_e32 v89, v39
	v_mov_b32_e32 v90, v39
	v_mov_b32_e32 v91, v39
	v_add_u32_e32 v113, 0x6400, v97
	s_mov_b32 s16, 0
	v_mov_b32_e32 v28, v103
	v_mov_b32_e32 v5, v4
	v_mov_b32_e32 v6, v4
	v_mov_b32_e32 v7, v4
	v_mov_b32_e32 v8, v4
	v_mov_b32_e32 v9, v4
	v_mov_b32_e32 v10, v4
	v_mov_b32_e32 v11, v4
	v_mov_b32_e32 v12, v4
	v_mov_b32_e32 v13, v4
	v_mov_b32_e32 v14, v4
	v_mov_b32_e32 v15, v4
	v_mov_b32_e32 v16, v4
	v_mov_b32_e32 v17, v4
	v_mov_b32_e32 v18, v4
	s_waitcnt vmcnt(3)
	v_cvt_f32_f16_sdwa v19, v31 dst_sel:DWORD dst_unused:UNUSED_PAD src0_sel:WORD_1
	v_cvt_f32_f16_e32 v29, v31
	v_cvt_f32_f16_sdwa v31, v30 dst_sel:DWORD dst_unused:UNUSED_PAD src0_sel:WORD_1
	v_cvt_f32_f16_e32 v30, v30
	v_cvt_f32_f16_sdwa v115, v33 dst_sel:DWORD dst_unused:UNUSED_PAD src0_sel:WORD_1
	v_cvt_f32_f16_e32 v134, v33
	v_cvt_f32_f16_sdwa v133, v32 dst_sel:DWORD dst_unused:UNUSED_PAD src0_sel:WORD_1
	v_cvt_f32_f16_e32 v132, v32
	v_sub_f32_e32 v30, v30, v38
	v_sub_f32_e32 v31, v31, v38
	v_sub_f32_e32 v32, v29, v38
	v_sub_f32_e32 v33, v19, v38
	v_sub_f32_e32 v132, v132, v38
	v_sub_f32_e32 v133, v133, v38
	v_sub_f32_e32 v134, v134, v38
	v_sub_f32_e32 v135, v115, v38
	v_pk_mul_f32 v[30:31], v[38:39], v[30:31] op_sel:[1,0]
	v_pk_mul_f32 v[32:33], v[38:39], v[32:33] op_sel:[1,0]
	v_pk_mul_f32 v[134:135], v[38:39], v[134:135] op_sel:[1,0]
	v_pk_mul_f32 v[38:39], v[38:39], v[132:133] op_sel:[1,0]
	s_waitcnt lgkmcnt(1)
	v_fma_f32 v19, v116, v30, v124
	v_fma_f32 v30, v117, v31, v125
	s_waitcnt lgkmcnt(0)
	v_fma_f32 v29, v120, v38, v128
	v_fma_f32 v31, v121, v39, v129
	v_fma_f32 v32, v118, v32, v126
	v_fma_f32 v38, v122, v134, v130
	v_fmac_f32_e32 v127, v119, v33
	v_fmac_f32_e32 v131, v123, v135
	ds_write2_b32 v114, v19, v30 offset1:68
	ds_write2_b32 v113, v29, v31 offset0:16 offset1:84
	ds_write2_b32 v114, v32, v127 offset0:136 offset1:204
	ds_write2_b32 v113, v38, v131 offset0:152 offset1:220
	s_waitcnt vmcnt(2)
	ds_write_b128 v96, v[34:37] offset:41984
	v_mov_b32_e32 v19, v4
	s_waitcnt lgkmcnt(0)
	s_barrier
	ds_read_b32 v200, v218
	ds_read_b32 v208, v219
	ds_read_b32 v201, v218 offset:544
	ds_read_b32 v209, v219 offset:256
	ds_read_b32 v202, v218 offset:1088
	ds_read_b32 v210, v219 offset:512
	ds_read_b32 v203, v218 offset:1632
	ds_read_b32 v211, v219 offset:768
	ds_read_b32 v204, v218 offset:2176
	ds_read_b32 v212, v219 offset:1024
	ds_read_b32 v205, v218 offset:2720
	ds_read_b32 v213, v219 offset:1280
	ds_read_b32 v206, v218 offset:3264
	ds_read_b32 v214, v219 offset:1536
	s_waitcnt lgkmcnt(12)
	v_mfma_f32_32x32x2_f32 v[4:19], v200, v208, v[4:19]
	ds_read_b32 v207, v218 offset:3808
	ds_read_b32 v215, v219 offset:1792
	s_waitcnt lgkmcnt(12)
	v_mfma_f32_32x32x2_f32 v[4:19], v201, v209, v[4:19]
	s_waitcnt lgkmcnt(10)
	v_mfma_f32_32x32x2_f32 v[4:19], v202, v210, v[4:19]
	s_waitcnt lgkmcnt(8)
	v_mfma_f32_32x32x2_f32 v[4:19], v203, v211, v[4:19]
	s_waitcnt lgkmcnt(6)
	v_mfma_f32_32x32x2_f32 v[4:19], v204, v212, v[4:19]
	s_waitcnt lgkmcnt(4)
	v_mfma_f32_32x32x2_f32 v[4:19], v205, v213, v[4:19]
	s_waitcnt lgkmcnt(2)
	v_mfma_f32_32x32x2_f32 v[4:19], v206, v214, v[4:19]
	s_waitcnt lgkmcnt(0)
	v_mfma_f32_32x32x2_f32 v[4:19], v207, v215, v[4:19]
	s_barrier
	global_load_dwordx4 v[32:35], v[92:93], off offset:256
	global_load_dwordx4 v[28:31], v[54:55], off
	s_waitcnt vmcnt(2)
	v_cvt_f32_f16_sdwa v128, v24 dst_sel:DWORD dst_unused:UNUSED_PAD src0_sel:WORD_1
	v_cvt_f32_f16_e32 v24, v24
	v_cvt_f32_f16_e32 v129, v25
	v_cvt_f32_f16_sdwa v130, v26 dst_sel:DWORD dst_unused:UNUSED_PAD src0_sel:WORD_1
	v_cvt_f32_f16_e32 v133, v26
	ds_read_b128 v[36:39], v43 offset:12544
	ds_read_b128 v[116:119], v43 offset:12560
	ds_read_b128 v[120:123], v43 offset:16640
	ds_read_b128 v[124:127], v43 offset:16656
	v_cvt_f32_f16_sdwa v115, v25 dst_sel:DWORD dst_unused:UNUSED_PAD src0_sel:WORD_1
	v_cvt_f32_f16_sdwa v131, v27 dst_sel:DWORD dst_unused:UNUSED_PAD src0_sel:WORD_1
	v_cvt_f32_f16_e32 v132, v27
	v_sub_f32_e32 v24, v24, v0
	v_sub_f32_e32 v25, v128, v1
	v_sub_f32_e32 v26, v129, v2
	v_pk_mul_f32 v[24:25], v[88:89], v[24:25]
	v_sub_f32_e32 v128, v133, v0
	v_sub_f32_e32 v129, v130, v1
	v_sub_f32_e32 v27, v115, v3
	v_sub_f32_e32 v130, v132, v2
	v_sub_f32_e32 v131, v131, v3
	v_pk_mul_f32 v[128:129], v[88:89], v[128:129]
	s_waitcnt lgkmcnt(1)
	v_fma_f32 v24, v36, v24, v120
	v_fma_f32 v25, v37, v25, v121
	v_pk_mul_f32 v[26:27], v[90:91], v[26:27]
	v_pk_mul_f32 v[130:131], v[90:91], v[130:131]
	s_waitcnt lgkmcnt(0)
	v_fma_f32 v36, v116, v128, v124
	ds_write2_b32 v114, v24, v25 offset1:68
	v_fma_f32 v24, v117, v129, v125
	ds_write2_b32 v113, v36, v24 offset0:16 offset1:84
	v_fma_f32 v24, v38, v26, v122
	v_fma_f32 v25, v118, v130, v126
	v_fmac_f32_e32 v123, v39, v27
	v_fmac_f32_e32 v127, v119, v131
	ds_write2_b32 v114, v24, v123 offset0:136 offset1:204
	ds_write2_b32 v113, v25, v127 offset0:152 offset1:220
	ds_write_b128 v96, v[20:23] offset:41984
	s_mov_b32 s16, 0
	v_mov_b32_e32 v20, v103
	s_waitcnt lgkmcnt(0)
	s_barrier
	ds_read_b32 v200, v218
	ds_read_b32 v208, v219
	ds_read_b32 v201, v218 offset:544
	ds_read_b32 v209, v219 offset:256
	ds_read_b32 v202, v218 offset:1088
	ds_read_b32 v210, v219 offset:512
	ds_read_b32 v203, v218 offset:1632
	ds_read_b32 v211, v219 offset:768
	ds_read_b32 v204, v218 offset:2176
	ds_read_b32 v212, v219 offset:1024
	ds_read_b32 v205, v218 offset:2720
	ds_read_b32 v213, v219 offset:1280
	ds_read_b32 v206, v218 offset:3264
	ds_read_b32 v214, v219 offset:1536
	s_waitcnt lgkmcnt(12)
	v_mfma_f32_32x32x2_f32 v[4:19], v200, v208, v[4:19]
	ds_read_b32 v207, v218 offset:3808
	ds_read_b32 v215, v219 offset:1792
	s_waitcnt lgkmcnt(12)
	v_mfma_f32_32x32x2_f32 v[4:19], v201, v209, v[4:19]
	s_waitcnt lgkmcnt(10)
	v_mfma_f32_32x32x2_f32 v[4:19], v202, v210, v[4:19]
	s_waitcnt lgkmcnt(8)
	v_mfma_f32_32x32x2_f32 v[4:19], v203, v211, v[4:19]
	s_waitcnt lgkmcnt(6)
	v_mfma_f32_32x32x2_f32 v[4:19], v204, v212, v[4:19]
	s_waitcnt lgkmcnt(4)
	v_mfma_f32_32x32x2_f32 v[4:19], v205, v213, v[4:19]
	s_waitcnt lgkmcnt(2)
	v_mfma_f32_32x32x2_f32 v[4:19], v206, v214, v[4:19]
	s_waitcnt lgkmcnt(0)
	v_mfma_f32_32x32x2_f32 v[4:19], v207, v215, v[4:19]
	s_barrier
	global_load_dwordx4 v[36:39], v[92:93], off offset:384
	global_load_dwordx4 v[20:23], v[56:57], off
	s_waitcnt vmcnt(3)
	v_cvt_f32_f16_sdwa v128, v32 dst_sel:DWORD dst_unused:UNUSED_PAD src0_sel:WORD_1
	v_cvt_f32_f16_e32 v32, v32
	v_cvt_f32_f16_e32 v129, v33
	v_cvt_f32_f16_sdwa v130, v34 dst_sel:DWORD dst_unused:UNUSED_PAD src0_sel:WORD_1
	v_cvt_f32_f16_e32 v133, v34
	ds_read_b128 v[24:27], v43 offset:12800
	ds_read_b128 v[116:119], v43 offset:12816
	ds_read_b128 v[120:123], v43 offset:16896
	ds_read_b128 v[124:127], v43 offset:16912
	v_cvt_f32_f16_sdwa v115, v33 dst_sel:DWORD dst_unused:UNUSED_PAD src0_sel:WORD_1
	v_cvt_f32_f16_sdwa v131, v35 dst_sel:DWORD dst_unused:UNUSED_PAD src0_sel:WORD_1
	v_cvt_f32_f16_e32 v132, v35
	v_sub_f32_e32 v32, v32, v0
	v_sub_f32_e32 v33, v128, v1
	v_sub_f32_e32 v34, v129, v2
	v_pk_mul_f32 v[32:33], v[88:89], v[32:33]
	v_sub_f32_e32 v128, v133, v0
	v_sub_f32_e32 v129, v130, v1
	v_sub_f32_e32 v35, v115, v3
	v_pk_mul_f32 v[128:129], v[88:89], v[128:129]
	s_waitcnt lgkmcnt(1)
	v_fma_f32 v24, v24, v32, v120
	v_fma_f32 v25, v25, v33, v121
	v_pk_mul_f32 v[34:35], v[90:91], v[34:35]
	v_sub_f32_e32 v130, v132, v2
	v_sub_f32_e32 v131, v131, v3
	s_waitcnt lgkmcnt(0)
	v_fma_f32 v32, v116, v128, v124
	ds_write2_b32 v114, v24, v25 offset1:68
	v_fma_f32 v24, v117, v129, v125
	v_pk_mul_f32 v[130:131], v[90:91], v[130:131]
	ds_write2_b32 v113, v32, v24 offset0:16 offset1:84
	v_fma_f32 v24, v26, v34, v122
	v_fmac_f32_e32 v123, v27, v35
	v_fma_f32 v25, v118, v130, v126
	ds_write2_b32 v114, v24, v123 offset0:136 offset1:204
	v_fmac_f32_e32 v127, v119, v131
	s_mov_b32 s16, 0
	v_mov_b32_e32 v24, v103
	ds_write2_b32 v113, v25, v127 offset0:152 offset1:220
	s_waitcnt vmcnt(2)
	ds_write_b128 v96, v[28:31] offset:41984
	s_waitcnt lgkmcnt(0)
	s_barrier
	ds_read_b32 v200, v218
	ds_read_b32 v208, v219
	ds_read_b32 v201, v218 offset:544
	ds_read_b32 v209, v219 offset:256
	ds_read_b32 v202, v218 offset:1088
	ds_read_b32 v210, v219 offset:512
	ds_read_b32 v203, v218 offset:1632
	ds_read_b32 v211, v219 offset:768
	ds_read_b32 v204, v218 offset:2176
	ds_read_b32 v212, v219 offset:1024
	ds_read_b32 v205, v218 offset:2720
	ds_read_b32 v213, v219 offset:1280
	ds_read_b32 v206, v218 offset:3264
	ds_read_b32 v214, v219 offset:1536
	s_waitcnt lgkmcnt(12)
	v_mfma_f32_32x32x2_f32 v[4:19], v200, v208, v[4:19]
	ds_read_b32 v207, v218 offset:3808
	ds_read_b32 v215, v219 offset:1792
	s_waitcnt lgkmcnt(12)
	v_mfma_f32_32x32x2_f32 v[4:19], v201, v209, v[4:19]
	s_waitcnt lgkmcnt(10)
	v_mfma_f32_32x32x2_f32 v[4:19], v202, v210, v[4:19]
	s_waitcnt lgkmcnt(8)
	v_mfma_f32_32x32x2_f32 v[4:19], v203, v211, v[4:19]
	s_waitcnt lgkmcnt(6)
	v_mfma_f32_32x32x2_f32 v[4:19], v204, v212, v[4:19]
	s_waitcnt lgkmcnt(4)
	v_mfma_f32_32x32x2_f32 v[4:19], v205, v213, v[4:19]
	s_waitcnt lgkmcnt(2)
	v_mfma_f32_32x32x2_f32 v[4:19], v206, v214, v[4:19]
	s_waitcnt lgkmcnt(0)
	v_mfma_f32_32x32x2_f32 v[4:19], v207, v215, v[4:19]
	s_barrier
	global_load_dwordx4 v[28:31], v[92:93], off offset:512
	global_load_dwordx4 v[24:27], v[58:59], off
	s_waitcnt vmcnt(3)
	v_cvt_f32_f16_sdwa v128, v36 dst_sel:DWORD dst_unused:UNUSED_PAD src0_sel:WORD_1
	v_cvt_f32_f16_e32 v36, v36
	v_cvt_f32_f16_e32 v129, v37
	v_cvt_f32_f16_sdwa v130, v38 dst_sel:DWORD dst_unused:UNUSED_PAD src0_sel:WORD_1
	v_cvt_f32_f16_e32 v133, v38
	ds_read_b128 v[32:35], v43 offset:13056
	ds_read_b128 v[116:119], v43 offset:13072
	ds_read_b128 v[120:123], v43 offset:17152
	ds_read_b128 v[124:127], v43 offset:17168
	v_cvt_f32_f16_sdwa v115, v37 dst_sel:DWORD dst_unused:UNUSED_PAD src0_sel:WORD_1
	v_cvt_f32_f16_sdwa v131, v39 dst_sel:DWORD dst_unused:UNUSED_PAD src0_sel:WORD_1
	v_cvt_f32_f16_e32 v132, v39
	v_sub_f32_e32 v36, v36, v0
	v_sub_f32_e32 v37, v128, v1
	v_sub_f32_e32 v38, v129, v2
	v_pk_mul_f32 v[36:37], v[88:89], v[36:37]
	v_sub_f32_e32 v128, v133, v0
	v_sub_f32_e32 v129, v130, v1
	v_sub_f32_e32 v39, v115, v3
	v_sub_f32_e32 v130, v132, v2
	v_sub_f32_e32 v131, v131, v3
	v_pk_mul_f32 v[128:129], v[88:89], v[128:129]
	s_waitcnt lgkmcnt(1)
	v_fma_f32 v32, v32, v36, v120
	v_fma_f32 v33, v33, v37, v121
	v_pk_mul_f32 v[38:39], v[90:91], v[38:39]
	v_pk_mul_f32 v[130:131], v[90:91], v[130:131]
	s_waitcnt lgkmcnt(0)
	v_fma_f32 v36, v116, v128, v124
	ds_write2_b32 v114, v32, v33 offset1:68
	v_fma_f32 v32, v117, v129, v125
	ds_write2_b32 v113, v36, v32 offset0:16 offset1:84
	v_fma_f32 v32, v34, v38, v122
	v_fma_f32 v33, v118, v130, v126
	v_fmac_f32_e32 v123, v35, v39
	v_fmac_f32_e32 v127, v119, v131
	ds_write2_b32 v114, v32, v123 offset0:136 offset1:204
	ds_write2_b32 v113, v33, v127 offset0:152 offset1:220
	s_waitcnt vmcnt(2)
	ds_write_b128 v96, v[20:23] offset:41984
	s_mov_b32 s16, 0
	v_mov_b32_e32 v20, v103
	s_waitcnt lgkmcnt(0)
	s_barrier
	ds_read_b32 v200, v218
	ds_read_b32 v208, v219
	ds_read_b32 v201, v218 offset:544
	ds_read_b32 v209, v219 offset:256
	ds_read_b32 v202, v218 offset:1088
	ds_read_b32 v210, v219 offset:512
	ds_read_b32 v203, v218 offset:1632
	ds_read_b32 v211, v219 offset:768
	ds_read_b32 v204, v218 offset:2176
	ds_read_b32 v212, v219 offset:1024
	ds_read_b32 v205, v218 offset:2720
	ds_read_b32 v213, v219 offset:1280
	ds_read_b32 v206, v218 offset:3264
	ds_read_b32 v214, v219 offset:1536
	s_waitcnt lgkmcnt(12)
	v_mfma_f32_32x32x2_f32 v[4:19], v200, v208, v[4:19]
	ds_read_b32 v207, v218 offset:3808
	ds_read_b32 v215, v219 offset:1792
	s_waitcnt lgkmcnt(12)
	v_mfma_f32_32x32x2_f32 v[4:19], v201, v209, v[4:19]
	s_waitcnt lgkmcnt(10)
	v_mfma_f32_32x32x2_f32 v[4:19], v202, v210, v[4:19]
	s_waitcnt lgkmcnt(8)
	v_mfma_f32_32x32x2_f32 v[4:19], v203, v211, v[4:19]
	s_waitcnt lgkmcnt(6)
	v_mfma_f32_32x32x2_f32 v[4:19], v204, v212, v[4:19]
	s_waitcnt lgkmcnt(4)
	v_mfma_f32_32x32x2_f32 v[4:19], v205, v213, v[4:19]
	s_waitcnt lgkmcnt(2)
	v_mfma_f32_32x32x2_f32 v[4:19], v206, v214, v[4:19]
	s_waitcnt lgkmcnt(0)
	v_mfma_f32_32x32x2_f32 v[4:19], v207, v215, v[4:19]
	s_barrier
	global_load_dwordx4 v[32:35], v[92:93], off offset:640
	global_load_dwordx4 v[20:23], v[60:61], off
	s_waitcnt vmcnt(3)
	v_cvt_f32_f16_sdwa v128, v28 dst_sel:DWORD dst_unused:UNUSED_PAD src0_sel:WORD_1
	v_cvt_f32_f16_e32 v28, v28
	v_cvt_f32_f16_e32 v129, v29
	v_cvt_f32_f16_sdwa v130, v30 dst_sel:DWORD dst_unused:UNUSED_PAD src0_sel:WORD_1
	v_cvt_f32_f16_e32 v133, v30
	ds_read_b128 v[36:39], v43 offset:13312
	ds_read_b128 v[116:119], v43 offset:13328
	ds_read_b128 v[120:123], v43 offset:17408
	ds_read_b128 v[124:127], v43 offset:17424
	v_cvt_f32_f16_sdwa v115, v29 dst_sel:DWORD dst_unused:UNUSED_PAD src0_sel:WORD_1
	v_cvt_f32_f16_sdwa v131, v31 dst_sel:DWORD dst_unused:UNUSED_PAD src0_sel:WORD_1
	v_cvt_f32_f16_e32 v132, v31
	v_sub_f32_e32 v28, v28, v0
	v_sub_f32_e32 v29, v128, v1
	v_sub_f32_e32 v30, v129, v2
	v_pk_mul_f32 v[28:29], v[88:89], v[28:29]
	v_sub_f32_e32 v128, v133, v0
	v_sub_f32_e32 v129, v130, v1
	v_sub_f32_e32 v31, v115, v3
	v_sub_f32_e32 v130, v132, v2
	v_sub_f32_e32 v131, v131, v3
	v_pk_mul_f32 v[128:129], v[88:89], v[128:129]
	s_waitcnt lgkmcnt(1)
	v_fma_f32 v28, v36, v28, v120
	v_fma_f32 v29, v37, v29, v121
	v_pk_mul_f32 v[30:31], v[90:91], v[30:31]
	v_pk_mul_f32 v[130:131], v[90:91], v[130:131]
	s_waitcnt lgkmcnt(0)
	v_fma_f32 v36, v116, v128, v124
	ds_write2_b32 v114, v28, v29 offset1:68
	v_fma_f32 v28, v117, v129, v125
	ds_write2_b32 v113, v36, v28 offset0:16 offset1:84
	v_fma_f32 v28, v38, v30, v122
	v_fma_f32 v29, v118, v130, v126
	v_fmac_f32_e32 v123, v39, v31
	v_fmac_f32_e32 v127, v119, v131
	ds_write2_b32 v114, v28, v123 offset0:136 offset1:204
	ds_write2_b32 v113, v29, v127 offset0:152 offset1:220
	s_waitcnt vmcnt(2)
	ds_write_b128 v96, v[24:27] offset:41984
	s_mov_b32 s16, 0
	v_mov_b32_e32 v24, v103
	s_waitcnt lgkmcnt(0)
	s_barrier
	ds_read_b32 v200, v218
	ds_read_b32 v208, v219
	ds_read_b32 v201, v218 offset:544
	ds_read_b32 v209, v219 offset:256
	ds_read_b32 v202, v218 offset:1088
	ds_read_b32 v210, v219 offset:512
	ds_read_b32 v203, v218 offset:1632
	ds_read_b32 v211, v219 offset:768
	ds_read_b32 v204, v218 offset:2176
	ds_read_b32 v212, v219 offset:1024
	ds_read_b32 v205, v218 offset:2720
	ds_read_b32 v213, v219 offset:1280
	ds_read_b32 v206, v218 offset:3264
	ds_read_b32 v214, v219 offset:1536
	s_waitcnt lgkmcnt(12)
	v_mfma_f32_32x32x2_f32 v[4:19], v200, v208, v[4:19]
	ds_read_b32 v207, v218 offset:3808
	ds_read_b32 v215, v219 offset:1792
	s_waitcnt lgkmcnt(12)
	v_mfma_f32_32x32x2_f32 v[4:19], v201, v209, v[4:19]
	s_waitcnt lgkmcnt(10)
	v_mfma_f32_32x32x2_f32 v[4:19], v202, v210, v[4:19]
	s_waitcnt lgkmcnt(8)
	v_mfma_f32_32x32x2_f32 v[4:19], v203, v211, v[4:19]
	s_waitcnt lgkmcnt(6)
	v_mfma_f32_32x32x2_f32 v[4:19], v204, v212, v[4:19]
	s_waitcnt lgkmcnt(4)
	v_mfma_f32_32x32x2_f32 v[4:19], v205, v213, v[4:19]
	s_waitcnt lgkmcnt(2)
	v_mfma_f32_32x32x2_f32 v[4:19], v206, v214, v[4:19]
	s_waitcnt lgkmcnt(0)
	v_mfma_f32_32x32x2_f32 v[4:19], v207, v215, v[4:19]
	s_barrier
	global_load_dwordx4 v[28:31], v[92:93], off offset:768
	global_load_dwordx4 v[24:27], v[62:63], off
	s_waitcnt vmcnt(3)
	v_cvt_f32_f16_sdwa v128, v32 dst_sel:DWORD dst_unused:UNUSED_PAD src0_sel:WORD_1
	v_cvt_f32_f16_e32 v32, v32
	v_cvt_f32_f16_e32 v129, v33
	v_cvt_f32_f16_sdwa v130, v34 dst_sel:DWORD dst_unused:UNUSED_PAD src0_sel:WORD_1
	v_cvt_f32_f16_e32 v133, v34
	ds_read_b128 v[36:39], v43 offset:13568
	ds_read_b128 v[116:119], v43 offset:13584
	ds_read_b128 v[120:123], v43 offset:17664
	ds_read_b128 v[124:127], v43 offset:17680
	v_cvt_f32_f16_sdwa v115, v33 dst_sel:DWORD dst_unused:UNUSED_PAD src0_sel:WORD_1
	v_cvt_f32_f16_sdwa v131, v35 dst_sel:DWORD dst_unused:UNUSED_PAD src0_sel:WORD_1
	v_cvt_f32_f16_e32 v132, v35
	v_sub_f32_e32 v32, v32, v0
	v_sub_f32_e32 v33, v128, v1
	v_sub_f32_e32 v34, v129, v2
	v_pk_mul_f32 v[32:33], v[88:89], v[32:33]
	v_sub_f32_e32 v128, v133, v0
	v_sub_f32_e32 v129, v130, v1
	v_sub_f32_e32 v35, v115, v3
	v_sub_f32_e32 v130, v132, v2
	v_sub_f32_e32 v131, v131, v3
	v_pk_mul_f32 v[128:129], v[88:89], v[128:129]
	s_waitcnt lgkmcnt(1)
	v_fma_f32 v32, v36, v32, v120
	v_fma_f32 v33, v37, v33, v121
	v_pk_mul_f32 v[34:35], v[90:91], v[34:35]
	v_pk_mul_f32 v[130:131], v[90:91], v[130:131]
	s_waitcnt lgkmcnt(0)
	v_fma_f32 v36, v116, v128, v124
	ds_write2_b32 v114, v32, v33 offset1:68
	v_fma_f32 v32, v117, v129, v125
	ds_write2_b32 v113, v36, v32 offset0:16 offset1:84
	v_fma_f32 v32, v38, v34, v122
	v_fma_f32 v33, v118, v130, v126
	v_fmac_f32_e32 v123, v39, v35
	v_fmac_f32_e32 v127, v119, v131
	ds_write2_b32 v114, v32, v123 offset0:136 offset1:204
	ds_write2_b32 v113, v33, v127 offset0:152 offset1:220
	s_waitcnt vmcnt(2)
	ds_write_b128 v96, v[20:23] offset:41984
	s_mov_b32 s16, 0
	v_mov_b32_e32 v20, v103
	s_waitcnt lgkmcnt(0)
	s_barrier
	ds_read_b32 v200, v218
	ds_read_b32 v208, v219
	ds_read_b32 v201, v218 offset:544
	ds_read_b32 v209, v219 offset:256
	ds_read_b32 v202, v218 offset:1088
	ds_read_b32 v210, v219 offset:512
	ds_read_b32 v203, v218 offset:1632
	ds_read_b32 v211, v219 offset:768
	ds_read_b32 v204, v218 offset:2176
	ds_read_b32 v212, v219 offset:1024
	ds_read_b32 v205, v218 offset:2720
	ds_read_b32 v213, v219 offset:1280
	ds_read_b32 v206, v218 offset:3264
	ds_read_b32 v214, v219 offset:1536
	s_waitcnt lgkmcnt(12)
	v_mfma_f32_32x32x2_f32 v[4:19], v200, v208, v[4:19]
	ds_read_b32 v207, v218 offset:3808
	ds_read_b32 v215, v219 offset:1792
	s_waitcnt lgkmcnt(12)
	v_mfma_f32_32x32x2_f32 v[4:19], v201, v209, v[4:19]
	s_waitcnt lgkmcnt(10)
	v_mfma_f32_32x32x2_f32 v[4:19], v202, v210, v[4:19]
	s_waitcnt lgkmcnt(8)
	v_mfma_f32_32x32x2_f32 v[4:19], v203, v211, v[4:19]
	s_waitcnt lgkmcnt(6)
	v_mfma_f32_32x32x2_f32 v[4:19], v204, v212, v[4:19]
	s_waitcnt lgkmcnt(4)
	v_mfma_f32_32x32x2_f32 v[4:19], v205, v213, v[4:19]
	s_waitcnt lgkmcnt(2)
	v_mfma_f32_32x32x2_f32 v[4:19], v206, v214, v[4:19]
	s_waitcnt lgkmcnt(0)
	v_mfma_f32_32x32x2_f32 v[4:19], v207, v215, v[4:19]
	s_barrier
	global_load_dwordx4 v[32:35], v[92:93], off offset:896
	global_load_dwordx4 v[20:23], v[64:65], off
	s_waitcnt vmcnt(3)
	v_cvt_f32_f16_sdwa v128, v28 dst_sel:DWORD dst_unused:UNUSED_PAD src0_sel:WORD_1
	v_cvt_f32_f16_e32 v28, v28
	v_cvt_f32_f16_e32 v129, v29
	v_cvt_f32_f16_sdwa v130, v30 dst_sel:DWORD dst_unused:UNUSED_PAD src0_sel:WORD_1
	v_cvt_f32_f16_e32 v133, v30
	ds_read_b128 v[36:39], v43 offset:13824
	ds_read_b128 v[116:119], v43 offset:13840
	ds_read_b128 v[120:123], v43 offset:17920
	ds_read_b128 v[124:127], v43 offset:17936
	v_cvt_f32_f16_sdwa v115, v29 dst_sel:DWORD dst_unused:UNUSED_PAD src0_sel:WORD_1
	v_cvt_f32_f16_sdwa v131, v31 dst_sel:DWORD dst_unused:UNUSED_PAD src0_sel:WORD_1
	v_cvt_f32_f16_e32 v132, v31
	v_sub_f32_e32 v28, v28, v0
	v_sub_f32_e32 v29, v128, v1
	v_sub_f32_e32 v30, v129, v2
	v_pk_mul_f32 v[28:29], v[88:89], v[28:29]
	v_sub_f32_e32 v128, v133, v0
	v_sub_f32_e32 v129, v130, v1
	v_sub_f32_e32 v31, v115, v3
	v_sub_f32_e32 v130, v132, v2
	v_sub_f32_e32 v131, v131, v3
	v_pk_mul_f32 v[128:129], v[88:89], v[128:129]
	s_waitcnt lgkmcnt(1)
	v_fma_f32 v28, v36, v28, v120
	v_fma_f32 v29, v37, v29, v121
	v_pk_mul_f32 v[30:31], v[90:91], v[30:31]
	v_pk_mul_f32 v[130:131], v[90:91], v[130:131]
	s_waitcnt lgkmcnt(0)
	v_fma_f32 v36, v116, v128, v124
	ds_write2_b32 v114, v28, v29 offset1:68
	v_fma_f32 v28, v117, v129, v125
	ds_write2_b32 v113, v36, v28 offset0:16 offset1:84
	v_fma_f32 v28, v38, v30, v122
	v_fma_f32 v29, v118, v130, v126
	v_fmac_f32_e32 v123, v39, v31
	v_fmac_f32_e32 v127, v119, v131
	ds_write2_b32 v114, v28, v123 offset0:136 offset1:204
	ds_write2_b32 v113, v29, v127 offset0:152 offset1:220
	s_waitcnt vmcnt(2)
	ds_write_b128 v96, v[24:27] offset:41984
	s_mov_b32 s16, 0
	v_mov_b32_e32 v24, v103
	s_waitcnt lgkmcnt(0)
	s_barrier
	ds_read_b32 v200, v218
	ds_read_b32 v208, v219
	ds_read_b32 v201, v218 offset:544
	ds_read_b32 v209, v219 offset:256
	ds_read_b32 v202, v218 offset:1088
	ds_read_b32 v210, v219 offset:512
	ds_read_b32 v203, v218 offset:1632
	ds_read_b32 v211, v219 offset:768
	ds_read_b32 v204, v218 offset:2176
	ds_read_b32 v212, v219 offset:1024
	ds_read_b32 v205, v218 offset:2720
	ds_read_b32 v213, v219 offset:1280
	ds_read_b32 v206, v218 offset:3264
	ds_read_b32 v214, v219 offset:1536
	s_waitcnt lgkmcnt(12)
	v_mfma_f32_32x32x2_f32 v[4:19], v200, v208, v[4:19]
	ds_read_b32 v207, v218 offset:3808
	ds_read_b32 v215, v219 offset:1792
	s_waitcnt lgkmcnt(12)
	v_mfma_f32_32x32x2_f32 v[4:19], v201, v209, v[4:19]
	s_waitcnt lgkmcnt(10)
	v_mfma_f32_32x32x2_f32 v[4:19], v202, v210, v[4:19]
	s_waitcnt lgkmcnt(8)
	v_mfma_f32_32x32x2_f32 v[4:19], v203, v211, v[4:19]
	s_waitcnt lgkmcnt(6)
	v_mfma_f32_32x32x2_f32 v[4:19], v204, v212, v[4:19]
	s_waitcnt lgkmcnt(4)
	v_mfma_f32_32x32x2_f32 v[4:19], v205, v213, v[4:19]
	s_waitcnt lgkmcnt(2)
	v_mfma_f32_32x32x2_f32 v[4:19], v206, v214, v[4:19]
	s_waitcnt lgkmcnt(0)
	v_mfma_f32_32x32x2_f32 v[4:19], v207, v215, v[4:19]
	s_barrier
	global_load_dwordx4 v[28:31], v[92:93], off offset:1024
	global_load_dwordx4 v[24:27], v[66:67], off
	s_waitcnt vmcnt(3)
	v_cvt_f32_f16_sdwa v128, v32 dst_sel:DWORD dst_unused:UNUSED_PAD src0_sel:WORD_1
	v_cvt_f32_f16_e32 v32, v32
	v_cvt_f32_f16_e32 v129, v33
	v_cvt_f32_f16_sdwa v130, v34 dst_sel:DWORD dst_unused:UNUSED_PAD src0_sel:WORD_1
	v_cvt_f32_f16_e32 v133, v34
	ds_read_b128 v[36:39], v43 offset:14080
	ds_read_b128 v[116:119], v43 offset:14096
	ds_read_b128 v[120:123], v43 offset:18176
	ds_read_b128 v[124:127], v43 offset:18192
	v_cvt_f32_f16_sdwa v115, v33 dst_sel:DWORD dst_unused:UNUSED_PAD src0_sel:WORD_1
	v_cvt_f32_f16_sdwa v131, v35 dst_sel:DWORD dst_unused:UNUSED_PAD src0_sel:WORD_1
	v_cvt_f32_f16_e32 v132, v35
	v_sub_f32_e32 v32, v32, v0
	v_sub_f32_e32 v33, v128, v1
	v_sub_f32_e32 v34, v129, v2
	v_pk_mul_f32 v[32:33], v[88:89], v[32:33]
	v_sub_f32_e32 v128, v133, v0
	v_sub_f32_e32 v129, v130, v1
	v_sub_f32_e32 v35, v115, v3
	v_sub_f32_e32 v130, v132, v2
	v_sub_f32_e32 v131, v131, v3
	v_pk_mul_f32 v[128:129], v[88:89], v[128:129]
	s_waitcnt lgkmcnt(1)
	v_fma_f32 v32, v36, v32, v120
	v_fma_f32 v33, v37, v33, v121
	v_pk_mul_f32 v[34:35], v[90:91], v[34:35]
	v_pk_mul_f32 v[130:131], v[90:91], v[130:131]
	s_waitcnt lgkmcnt(0)
	v_fma_f32 v36, v116, v128, v124
	ds_write2_b32 v114, v32, v33 offset1:68
	v_fma_f32 v32, v117, v129, v125
	ds_write2_b32 v113, v36, v32 offset0:16 offset1:84
	v_fma_f32 v32, v38, v34, v122
	v_fma_f32 v33, v118, v130, v126
	v_fmac_f32_e32 v123, v39, v35
	v_fmac_f32_e32 v127, v119, v131
	ds_write2_b32 v114, v32, v123 offset0:136 offset1:204
	ds_write2_b32 v113, v33, v127 offset0:152 offset1:220
	s_waitcnt vmcnt(2)
	ds_write_b128 v96, v[20:23] offset:41984
	s_mov_b32 s16, 0
	v_mov_b32_e32 v20, v103
	s_waitcnt lgkmcnt(0)
	s_barrier
	ds_read_b32 v200, v218
	ds_read_b32 v208, v219
	ds_read_b32 v201, v218 offset:544
	ds_read_b32 v209, v219 offset:256
	ds_read_b32 v202, v218 offset:1088
	ds_read_b32 v210, v219 offset:512
	ds_read_b32 v203, v218 offset:1632
	ds_read_b32 v211, v219 offset:768
	ds_read_b32 v204, v218 offset:2176
	ds_read_b32 v212, v219 offset:1024
	ds_read_b32 v205, v218 offset:2720
	ds_read_b32 v213, v219 offset:1280
	ds_read_b32 v206, v218 offset:3264
	ds_read_b32 v214, v219 offset:1536
	s_waitcnt lgkmcnt(12)
	v_mfma_f32_32x32x2_f32 v[4:19], v200, v208, v[4:19]
	ds_read_b32 v207, v218 offset:3808
	ds_read_b32 v215, v219 offset:1792
	s_waitcnt lgkmcnt(12)
	v_mfma_f32_32x32x2_f32 v[4:19], v201, v209, v[4:19]
	s_waitcnt lgkmcnt(10)
	v_mfma_f32_32x32x2_f32 v[4:19], v202, v210, v[4:19]
	s_waitcnt lgkmcnt(8)
	v_mfma_f32_32x32x2_f32 v[4:19], v203, v211, v[4:19]
	s_waitcnt lgkmcnt(6)
	v_mfma_f32_32x32x2_f32 v[4:19], v204, v212, v[4:19]
	s_waitcnt lgkmcnt(4)
	v_mfma_f32_32x32x2_f32 v[4:19], v205, v213, v[4:19]
	s_waitcnt lgkmcnt(2)
	v_mfma_f32_32x32x2_f32 v[4:19], v206, v214, v[4:19]
	s_waitcnt lgkmcnt(0)
	v_mfma_f32_32x32x2_f32 v[4:19], v207, v215, v[4:19]
	s_barrier
	global_load_dwordx4 v[32:35], v[92:93], off offset:1152
	global_load_dwordx4 v[20:23], v[68:69], off
	s_waitcnt vmcnt(3)
	v_cvt_f32_f16_sdwa v128, v28 dst_sel:DWORD dst_unused:UNUSED_PAD src0_sel:WORD_1
	v_cvt_f32_f16_e32 v28, v28
	v_cvt_f32_f16_e32 v129, v29
	v_cvt_f32_f16_sdwa v130, v30 dst_sel:DWORD dst_unused:UNUSED_PAD src0_sel:WORD_1
	v_cvt_f32_f16_e32 v133, v30
	ds_read_b128 v[36:39], v43 offset:14336
	ds_read_b128 v[116:119], v43 offset:14352
	ds_read_b128 v[120:123], v43 offset:18432
	ds_read_b128 v[124:127], v43 offset:18448
	v_cvt_f32_f16_sdwa v115, v29 dst_sel:DWORD dst_unused:UNUSED_PAD src0_sel:WORD_1
	v_cvt_f32_f16_sdwa v131, v31 dst_sel:DWORD dst_unused:UNUSED_PAD src0_sel:WORD_1
	v_cvt_f32_f16_e32 v132, v31
	v_sub_f32_e32 v28, v28, v0
	v_sub_f32_e32 v29, v128, v1
	v_sub_f32_e32 v30, v129, v2
	v_pk_mul_f32 v[28:29], v[88:89], v[28:29]
	v_sub_f32_e32 v128, v133, v0
	v_sub_f32_e32 v129, v130, v1
	v_sub_f32_e32 v31, v115, v3
	v_sub_f32_e32 v130, v132, v2
	v_sub_f32_e32 v131, v131, v3
	v_pk_mul_f32 v[128:129], v[88:89], v[128:129]
	s_waitcnt lgkmcnt(1)
	v_fma_f32 v28, v36, v28, v120
	v_fma_f32 v29, v37, v29, v121
	v_pk_mul_f32 v[30:31], v[90:91], v[30:31]
	v_pk_mul_f32 v[130:131], v[90:91], v[130:131]
	s_waitcnt lgkmcnt(0)
	v_fma_f32 v36, v116, v128, v124
	ds_write2_b32 v114, v28, v29 offset1:68
	v_fma_f32 v28, v117, v129, v125
	ds_write2_b32 v113, v36, v28 offset0:16 offset1:84
	v_fma_f32 v28, v38, v30, v122
	v_fma_f32 v29, v118, v130, v126
	v_fmac_f32_e32 v123, v39, v31
	v_fmac_f32_e32 v127, v119, v131
	ds_write2_b32 v114, v28, v123 offset0:136 offset1:204
	ds_write2_b32 v113, v29, v127 offset0:152 offset1:220
	s_waitcnt vmcnt(2)
	ds_write_b128 v96, v[24:27] offset:41984
	s_mov_b32 s16, 0
	v_mov_b32_e32 v24, v103
	s_waitcnt lgkmcnt(0)
	s_barrier
	ds_read_b32 v200, v218
	ds_read_b32 v208, v219
	ds_read_b32 v201, v218 offset:544
	ds_read_b32 v209, v219 offset:256
	ds_read_b32 v202, v218 offset:1088
	ds_read_b32 v210, v219 offset:512
	ds_read_b32 v203, v218 offset:1632
	ds_read_b32 v211, v219 offset:768
	ds_read_b32 v204, v218 offset:2176
	ds_read_b32 v212, v219 offset:1024
	ds_read_b32 v205, v218 offset:2720
	ds_read_b32 v213, v219 offset:1280
	ds_read_b32 v206, v218 offset:3264
	ds_read_b32 v214, v219 offset:1536
	s_waitcnt lgkmcnt(12)
	v_mfma_f32_32x32x2_f32 v[4:19], v200, v208, v[4:19]
	ds_read_b32 v207, v218 offset:3808
	ds_read_b32 v215, v219 offset:1792
	s_waitcnt lgkmcnt(12)
	v_mfma_f32_32x32x2_f32 v[4:19], v201, v209, v[4:19]
	s_waitcnt lgkmcnt(10)
	v_mfma_f32_32x32x2_f32 v[4:19], v202, v210, v[4:19]
	s_waitcnt lgkmcnt(8)
	v_mfma_f32_32x32x2_f32 v[4:19], v203, v211, v[4:19]
	s_waitcnt lgkmcnt(6)
	v_mfma_f32_32x32x2_f32 v[4:19], v204, v212, v[4:19]
	s_waitcnt lgkmcnt(4)
	v_mfma_f32_32x32x2_f32 v[4:19], v205, v213, v[4:19]
	s_waitcnt lgkmcnt(2)
	v_mfma_f32_32x32x2_f32 v[4:19], v206, v214, v[4:19]
	s_waitcnt lgkmcnt(0)
	v_mfma_f32_32x32x2_f32 v[4:19], v207, v215, v[4:19]
	s_barrier
	global_load_dwordx4 v[28:31], v[92:93], off offset:1280
	global_load_dwordx4 v[24:27], v[70:71], off
	s_waitcnt vmcnt(3)
	v_cvt_f32_f16_sdwa v128, v32 dst_sel:DWORD dst_unused:UNUSED_PAD src0_sel:WORD_1
	v_cvt_f32_f16_e32 v32, v32
	v_cvt_f32_f16_e32 v129, v33
	v_cvt_f32_f16_sdwa v130, v34 dst_sel:DWORD dst_unused:UNUSED_PAD src0_sel:WORD_1
	v_cvt_f32_f16_e32 v133, v34
	ds_read_b128 v[36:39], v43 offset:14592
	ds_read_b128 v[116:119], v43 offset:14608
	ds_read_b128 v[120:123], v43 offset:18688
	ds_read_b128 v[124:127], v43 offset:18704
	v_cvt_f32_f16_sdwa v115, v33 dst_sel:DWORD dst_unused:UNUSED_PAD src0_sel:WORD_1
	v_cvt_f32_f16_sdwa v131, v35 dst_sel:DWORD dst_unused:UNUSED_PAD src0_sel:WORD_1
	v_cvt_f32_f16_e32 v132, v35
	v_sub_f32_e32 v32, v32, v0
	v_sub_f32_e32 v33, v128, v1
	v_sub_f32_e32 v34, v129, v2
	v_pk_mul_f32 v[32:33], v[88:89], v[32:33]
	v_sub_f32_e32 v128, v133, v0
	v_sub_f32_e32 v129, v130, v1
	v_sub_f32_e32 v35, v115, v3
	v_sub_f32_e32 v130, v132, v2
	v_sub_f32_e32 v131, v131, v3
	v_pk_mul_f32 v[128:129], v[88:89], v[128:129]
	s_waitcnt lgkmcnt(1)
	v_fma_f32 v32, v36, v32, v120
	v_fma_f32 v33, v37, v33, v121
	v_pk_mul_f32 v[34:35], v[90:91], v[34:35]
	v_pk_mul_f32 v[130:131], v[90:91], v[130:131]
	s_waitcnt lgkmcnt(0)
	v_fma_f32 v36, v116, v128, v124
	ds_write2_b32 v114, v32, v33 offset1:68
	v_fma_f32 v32, v117, v129, v125
	ds_write2_b32 v113, v36, v32 offset0:16 offset1:84
	v_fma_f32 v32, v38, v34, v122
	v_fma_f32 v33, v118, v130, v126
	v_fmac_f32_e32 v123, v39, v35
	v_fmac_f32_e32 v127, v119, v131
	ds_write2_b32 v114, v32, v123 offset0:136 offset1:204
	ds_write2_b32 v113, v33, v127 offset0:152 offset1:220
	s_waitcnt vmcnt(2)
	ds_write_b128 v96, v[20:23] offset:41984
	s_mov_b32 s16, 0
	v_mov_b32_e32 v20, v103
	s_waitcnt lgkmcnt(0)
	s_barrier
	ds_read_b32 v200, v218
	ds_read_b32 v208, v219
	ds_read_b32 v201, v218 offset:544
	ds_read_b32 v209, v219 offset:256
	ds_read_b32 v202, v218 offset:1088
	ds_read_b32 v210, v219 offset:512
	ds_read_b32 v203, v218 offset:1632
	ds_read_b32 v211, v219 offset:768
	ds_read_b32 v204, v218 offset:2176
	ds_read_b32 v212, v219 offset:1024
	ds_read_b32 v205, v218 offset:2720
	ds_read_b32 v213, v219 offset:1280
	ds_read_b32 v206, v218 offset:3264
	ds_read_b32 v214, v219 offset:1536
	s_waitcnt lgkmcnt(12)
	v_mfma_f32_32x32x2_f32 v[4:19], v200, v208, v[4:19]
	ds_read_b32 v207, v218 offset:3808
	ds_read_b32 v215, v219 offset:1792
	s_waitcnt lgkmcnt(12)
	v_mfma_f32_32x32x2_f32 v[4:19], v201, v209, v[4:19]
	s_waitcnt lgkmcnt(10)
	v_mfma_f32_32x32x2_f32 v[4:19], v202, v210, v[4:19]
	s_waitcnt lgkmcnt(8)
	v_mfma_f32_32x32x2_f32 v[4:19], v203, v211, v[4:19]
	s_waitcnt lgkmcnt(6)
	v_mfma_f32_32x32x2_f32 v[4:19], v204, v212, v[4:19]
	s_waitcnt lgkmcnt(4)
	v_mfma_f32_32x32x2_f32 v[4:19], v205, v213, v[4:19]
	s_waitcnt lgkmcnt(2)
	v_mfma_f32_32x32x2_f32 v[4:19], v206, v214, v[4:19]
	s_waitcnt lgkmcnt(0)
	v_mfma_f32_32x32x2_f32 v[4:19], v207, v215, v[4:19]
	s_barrier
	global_load_dwordx4 v[32:35], v[92:93], off offset:1408
	global_load_dwordx4 v[20:23], v[72:73], off
	s_waitcnt vmcnt(3)
	v_cvt_f32_f16_sdwa v128, v28 dst_sel:DWORD dst_unused:UNUSED_PAD src0_sel:WORD_1
	v_cvt_f32_f16_e32 v28, v28
	v_cvt_f32_f16_e32 v129, v29
	v_cvt_f32_f16_sdwa v130, v30 dst_sel:DWORD dst_unused:UNUSED_PAD src0_sel:WORD_1
	v_cvt_f32_f16_e32 v133, v30
	ds_read_b128 v[36:39], v43 offset:14848
	ds_read_b128 v[116:119], v43 offset:14864
	ds_read_b128 v[120:123], v43 offset:18944
	ds_read_b128 v[124:127], v43 offset:18960
	v_cvt_f32_f16_sdwa v115, v29 dst_sel:DWORD dst_unused:UNUSED_PAD src0_sel:WORD_1
	v_cvt_f32_f16_sdwa v131, v31 dst_sel:DWORD dst_unused:UNUSED_PAD src0_sel:WORD_1
	v_cvt_f32_f16_e32 v132, v31
	v_sub_f32_e32 v28, v28, v0
	v_sub_f32_e32 v29, v128, v1
	v_sub_f32_e32 v30, v129, v2
	v_pk_mul_f32 v[28:29], v[88:89], v[28:29]
	v_sub_f32_e32 v128, v133, v0
	v_sub_f32_e32 v129, v130, v1
	v_sub_f32_e32 v31, v115, v3
	v_sub_f32_e32 v130, v132, v2
	v_sub_f32_e32 v131, v131, v3
	v_pk_mul_f32 v[128:129], v[88:89], v[128:129]
	s_waitcnt lgkmcnt(1)
	v_fma_f32 v28, v36, v28, v120
	v_fma_f32 v29, v37, v29, v121
	v_pk_mul_f32 v[30:31], v[90:91], v[30:31]
	v_pk_mul_f32 v[130:131], v[90:91], v[130:131]
	s_waitcnt lgkmcnt(0)
	v_fma_f32 v36, v116, v128, v124
	ds_write2_b32 v114, v28, v29 offset1:68
	v_fma_f32 v28, v117, v129, v125
	ds_write2_b32 v113, v36, v28 offset0:16 offset1:84
	v_fma_f32 v28, v38, v30, v122
	v_fma_f32 v29, v118, v130, v126
	v_fmac_f32_e32 v123, v39, v31
	v_fmac_f32_e32 v127, v119, v131
	ds_write2_b32 v114, v28, v123 offset0:136 offset1:204
	ds_write2_b32 v113, v29, v127 offset0:152 offset1:220
	s_waitcnt vmcnt(2)
	ds_write_b128 v96, v[24:27] offset:41984
	s_mov_b32 s16, 0
	v_mov_b32_e32 v24, v103
	s_waitcnt lgkmcnt(0)
	s_barrier
	ds_read_b32 v200, v218
	ds_read_b32 v208, v219
	ds_read_b32 v201, v218 offset:544
	ds_read_b32 v209, v219 offset:256
	ds_read_b32 v202, v218 offset:1088
	ds_read_b32 v210, v219 offset:512
	ds_read_b32 v203, v218 offset:1632
	ds_read_b32 v211, v219 offset:768
	ds_read_b32 v204, v218 offset:2176
	ds_read_b32 v212, v219 offset:1024
	ds_read_b32 v205, v218 offset:2720
	ds_read_b32 v213, v219 offset:1280
	ds_read_b32 v206, v218 offset:3264
	ds_read_b32 v214, v219 offset:1536
	s_waitcnt lgkmcnt(12)
	v_mfma_f32_32x32x2_f32 v[4:19], v200, v208, v[4:19]
	ds_read_b32 v207, v218 offset:3808
	ds_read_b32 v215, v219 offset:1792
	s_waitcnt lgkmcnt(12)
	v_mfma_f32_32x32x2_f32 v[4:19], v201, v209, v[4:19]
	s_waitcnt lgkmcnt(10)
	v_mfma_f32_32x32x2_f32 v[4:19], v202, v210, v[4:19]
	s_waitcnt lgkmcnt(8)
	v_mfma_f32_32x32x2_f32 v[4:19], v203, v211, v[4:19]
	s_waitcnt lgkmcnt(6)
	v_mfma_f32_32x32x2_f32 v[4:19], v204, v212, v[4:19]
	s_waitcnt lgkmcnt(4)
	v_mfma_f32_32x32x2_f32 v[4:19], v205, v213, v[4:19]
	s_waitcnt lgkmcnt(2)
	v_mfma_f32_32x32x2_f32 v[4:19], v206, v214, v[4:19]
	s_waitcnt lgkmcnt(0)
	v_mfma_f32_32x32x2_f32 v[4:19], v207, v215, v[4:19]
	s_barrier
	global_load_dwordx4 v[28:31], v[92:93], off offset:1536
	global_load_dwordx4 v[24:27], v[74:75], off
	s_waitcnt vmcnt(3)
	v_cvt_f32_f16_sdwa v128, v32 dst_sel:DWORD dst_unused:UNUSED_PAD src0_sel:WORD_1
	v_cvt_f32_f16_e32 v32, v32
	v_cvt_f32_f16_e32 v129, v33
	v_cvt_f32_f16_sdwa v130, v34 dst_sel:DWORD dst_unused:UNUSED_PAD src0_sel:WORD_1
	v_cvt_f32_f16_e32 v133, v34
	ds_read_b128 v[36:39], v43 offset:15104
	ds_read_b128 v[116:119], v43 offset:15120
	ds_read_b128 v[120:123], v43 offset:19200
	ds_read_b128 v[124:127], v43 offset:19216
	v_cvt_f32_f16_sdwa v115, v33 dst_sel:DWORD dst_unused:UNUSED_PAD src0_sel:WORD_1
	v_cvt_f32_f16_sdwa v131, v35 dst_sel:DWORD dst_unused:UNUSED_PAD src0_sel:WORD_1
	v_cvt_f32_f16_e32 v132, v35
	v_sub_f32_e32 v32, v32, v0
	v_sub_f32_e32 v33, v128, v1
	v_sub_f32_e32 v34, v129, v2
	v_pk_mul_f32 v[32:33], v[88:89], v[32:33]
	v_sub_f32_e32 v128, v133, v0
	v_sub_f32_e32 v129, v130, v1
	v_sub_f32_e32 v35, v115, v3
	v_sub_f32_e32 v130, v132, v2
	v_sub_f32_e32 v131, v131, v3
	v_pk_mul_f32 v[128:129], v[88:89], v[128:129]
	s_waitcnt lgkmcnt(1)
	v_fma_f32 v32, v36, v32, v120
	v_fma_f32 v33, v37, v33, v121
	v_pk_mul_f32 v[34:35], v[90:91], v[34:35]
	v_pk_mul_f32 v[130:131], v[90:91], v[130:131]
	s_waitcnt lgkmcnt(0)
	v_fma_f32 v36, v116, v128, v124
	ds_write2_b32 v114, v32, v33 offset1:68
	v_fma_f32 v32, v117, v129, v125
	ds_write2_b32 v113, v36, v32 offset0:16 offset1:84
	v_fma_f32 v32, v38, v34, v122
	v_fma_f32 v33, v118, v130, v126
	v_fmac_f32_e32 v123, v39, v35
	v_fmac_f32_e32 v127, v119, v131
	ds_write2_b32 v114, v32, v123 offset0:136 offset1:204
	ds_write2_b32 v113, v33, v127 offset0:152 offset1:220
	s_waitcnt vmcnt(2)
	ds_write_b128 v96, v[20:23] offset:41984
	s_mov_b32 s16, 0
	v_mov_b32_e32 v20, v103
	s_waitcnt lgkmcnt(0)
	s_barrier
	ds_read_b32 v200, v218
	ds_read_b32 v208, v219
	ds_read_b32 v201, v218 offset:544
	ds_read_b32 v209, v219 offset:256
	ds_read_b32 v202, v218 offset:1088
	ds_read_b32 v210, v219 offset:512
	ds_read_b32 v203, v218 offset:1632
	ds_read_b32 v211, v219 offset:768
	ds_read_b32 v204, v218 offset:2176
	ds_read_b32 v212, v219 offset:1024
	ds_read_b32 v205, v218 offset:2720
	ds_read_b32 v213, v219 offset:1280
	ds_read_b32 v206, v218 offset:3264
	ds_read_b32 v214, v219 offset:1536
	s_waitcnt lgkmcnt(12)
	v_mfma_f32_32x32x2_f32 v[4:19], v200, v208, v[4:19]
	ds_read_b32 v207, v218 offset:3808
	ds_read_b32 v215, v219 offset:1792
	s_waitcnt lgkmcnt(12)
	v_mfma_f32_32x32x2_f32 v[4:19], v201, v209, v[4:19]
	s_waitcnt lgkmcnt(10)
	v_mfma_f32_32x32x2_f32 v[4:19], v202, v210, v[4:19]
	s_waitcnt lgkmcnt(8)
	v_mfma_f32_32x32x2_f32 v[4:19], v203, v211, v[4:19]
	s_waitcnt lgkmcnt(6)
	v_mfma_f32_32x32x2_f32 v[4:19], v204, v212, v[4:19]
	s_waitcnt lgkmcnt(4)
	v_mfma_f32_32x32x2_f32 v[4:19], v205, v213, v[4:19]
	s_waitcnt lgkmcnt(2)
	v_mfma_f32_32x32x2_f32 v[4:19], v206, v214, v[4:19]
	s_waitcnt lgkmcnt(0)
	v_mfma_f32_32x32x2_f32 v[4:19], v207, v215, v[4:19]
	s_barrier
	global_load_dwordx4 v[32:35], v[92:93], off offset:1664
	global_load_dwordx4 v[20:23], v[76:77], off
	s_waitcnt vmcnt(3)
	v_cvt_f32_f16_sdwa v128, v28 dst_sel:DWORD dst_unused:UNUSED_PAD src0_sel:WORD_1
	v_cvt_f32_f16_e32 v28, v28
	v_cvt_f32_f16_e32 v129, v29
	v_cvt_f32_f16_sdwa v130, v30 dst_sel:DWORD dst_unused:UNUSED_PAD src0_sel:WORD_1
	v_cvt_f32_f16_e32 v133, v30
	ds_read_b128 v[36:39], v43 offset:15360
	ds_read_b128 v[116:119], v43 offset:15376
	ds_read_b128 v[120:123], v43 offset:19456
	ds_read_b128 v[124:127], v43 offset:19472
	v_cvt_f32_f16_sdwa v115, v29 dst_sel:DWORD dst_unused:UNUSED_PAD src0_sel:WORD_1
	v_cvt_f32_f16_sdwa v131, v31 dst_sel:DWORD dst_unused:UNUSED_PAD src0_sel:WORD_1
	v_cvt_f32_f16_e32 v132, v31
	v_sub_f32_e32 v28, v28, v0
	v_sub_f32_e32 v29, v128, v1
	v_sub_f32_e32 v30, v129, v2
	v_pk_mul_f32 v[28:29], v[88:89], v[28:29]
	v_sub_f32_e32 v128, v133, v0
	v_sub_f32_e32 v129, v130, v1
	v_sub_f32_e32 v31, v115, v3
	v_sub_f32_e32 v130, v132, v2
	v_sub_f32_e32 v131, v131, v3
	v_pk_mul_f32 v[128:129], v[88:89], v[128:129]
	s_waitcnt lgkmcnt(1)
	v_fma_f32 v28, v36, v28, v120
	v_fma_f32 v29, v37, v29, v121
	v_pk_mul_f32 v[30:31], v[90:91], v[30:31]
	v_pk_mul_f32 v[130:131], v[90:91], v[130:131]
	s_waitcnt lgkmcnt(0)
	v_fma_f32 v36, v116, v128, v124
	ds_write2_b32 v114, v28, v29 offset1:68
	v_fma_f32 v28, v117, v129, v125
	ds_write2_b32 v113, v36, v28 offset0:16 offset1:84
	v_fma_f32 v28, v38, v30, v122
	v_fma_f32 v29, v118, v130, v126
	v_fmac_f32_e32 v123, v39, v31
	v_fmac_f32_e32 v127, v119, v131
	ds_write2_b32 v114, v28, v123 offset0:136 offset1:204
	ds_write2_b32 v113, v29, v127 offset0:152 offset1:220
	s_waitcnt vmcnt(2)
	ds_write_b128 v96, v[24:27] offset:41984
	s_mov_b32 s16, 0
	v_mov_b32_e32 v24, v103
	s_waitcnt lgkmcnt(0)
	s_barrier
	ds_read_b32 v200, v218
	ds_read_b32 v208, v219
	ds_read_b32 v201, v218 offset:544
	ds_read_b32 v209, v219 offset:256
	ds_read_b32 v202, v218 offset:1088
	ds_read_b32 v210, v219 offset:512
	ds_read_b32 v203, v218 offset:1632
	ds_read_b32 v211, v219 offset:768
	ds_read_b32 v204, v218 offset:2176
	ds_read_b32 v212, v219 offset:1024
	ds_read_b32 v205, v218 offset:2720
	ds_read_b32 v213, v219 offset:1280
	ds_read_b32 v206, v218 offset:3264
	ds_read_b32 v214, v219 offset:1536
	s_waitcnt lgkmcnt(12)
	v_mfma_f32_32x32x2_f32 v[4:19], v200, v208, v[4:19]
	ds_read_b32 v207, v218 offset:3808
	ds_read_b32 v215, v219 offset:1792
	s_waitcnt lgkmcnt(12)
	v_mfma_f32_32x32x2_f32 v[4:19], v201, v209, v[4:19]
	s_waitcnt lgkmcnt(10)
	v_mfma_f32_32x32x2_f32 v[4:19], v202, v210, v[4:19]
	s_waitcnt lgkmcnt(8)
	v_mfma_f32_32x32x2_f32 v[4:19], v203, v211, v[4:19]
	s_waitcnt lgkmcnt(6)
	v_mfma_f32_32x32x2_f32 v[4:19], v204, v212, v[4:19]
	s_waitcnt lgkmcnt(4)
	v_mfma_f32_32x32x2_f32 v[4:19], v205, v213, v[4:19]
	s_waitcnt lgkmcnt(2)
	v_mfma_f32_32x32x2_f32 v[4:19], v206, v214, v[4:19]
	s_waitcnt lgkmcnt(0)
	v_mfma_f32_32x32x2_f32 v[4:19], v207, v215, v[4:19]
	s_barrier
	global_load_dwordx4 v[28:31], v[92:93], off offset:1792
	global_load_dwordx4 v[24:27], v[78:79], off
	s_waitcnt vmcnt(3)
	v_cvt_f32_f16_sdwa v128, v32 dst_sel:DWORD dst_unused:UNUSED_PAD src0_sel:WORD_1
	v_cvt_f32_f16_e32 v32, v32
	v_cvt_f32_f16_e32 v129, v33
	v_cvt_f32_f16_sdwa v130, v34 dst_sel:DWORD dst_unused:UNUSED_PAD src0_sel:WORD_1
	v_cvt_f32_f16_e32 v133, v34
	ds_read_b128 v[36:39], v43 offset:15616
	ds_read_b128 v[116:119], v43 offset:15632
	ds_read_b128 v[120:123], v43 offset:19712
	ds_read_b128 v[124:127], v43 offset:19728
	v_cvt_f32_f16_sdwa v115, v33 dst_sel:DWORD dst_unused:UNUSED_PAD src0_sel:WORD_1
	v_cvt_f32_f16_sdwa v131, v35 dst_sel:DWORD dst_unused:UNUSED_PAD src0_sel:WORD_1
	v_cvt_f32_f16_e32 v132, v35
	v_sub_f32_e32 v32, v32, v0
	v_sub_f32_e32 v33, v128, v1
	v_sub_f32_e32 v34, v129, v2
	v_pk_mul_f32 v[32:33], v[88:89], v[32:33]
	v_sub_f32_e32 v128, v133, v0
	v_sub_f32_e32 v129, v130, v1
	v_sub_f32_e32 v35, v115, v3
	v_sub_f32_e32 v130, v132, v2
	v_sub_f32_e32 v131, v131, v3
	v_pk_mul_f32 v[128:129], v[88:89], v[128:129]
	s_waitcnt lgkmcnt(1)
	v_fma_f32 v32, v36, v32, v120
	v_fma_f32 v33, v37, v33, v121
	v_pk_mul_f32 v[34:35], v[90:91], v[34:35]
	v_pk_mul_f32 v[130:131], v[90:91], v[130:131]
	s_waitcnt lgkmcnt(0)
	v_fma_f32 v36, v116, v128, v124
	ds_write2_b32 v114, v32, v33 offset1:68
	v_fma_f32 v32, v117, v129, v125
	ds_write2_b32 v113, v36, v32 offset0:16 offset1:84
	v_fma_f32 v32, v38, v34, v122
	v_fma_f32 v33, v118, v130, v126
	v_fmac_f32_e32 v123, v39, v35
	v_fmac_f32_e32 v127, v119, v131
	ds_write2_b32 v114, v32, v123 offset0:136 offset1:204
	ds_write2_b32 v113, v33, v127 offset0:152 offset1:220
	s_waitcnt vmcnt(2)
	ds_write_b128 v96, v[20:23] offset:41984
	s_mov_b32 s16, 0
	v_mov_b32_e32 v20, v103
	s_waitcnt lgkmcnt(0)
	s_barrier
	ds_read_b32 v200, v218
	ds_read_b32 v208, v219
	ds_read_b32 v201, v218 offset:544
	ds_read_b32 v209, v219 offset:256
	ds_read_b32 v202, v218 offset:1088
	ds_read_b32 v210, v219 offset:512
	ds_read_b32 v203, v218 offset:1632
	ds_read_b32 v211, v219 offset:768
	ds_read_b32 v204, v218 offset:2176
	ds_read_b32 v212, v219 offset:1024
	ds_read_b32 v205, v218 offset:2720
	ds_read_b32 v213, v219 offset:1280
	ds_read_b32 v206, v218 offset:3264
	ds_read_b32 v214, v219 offset:1536
	s_waitcnt lgkmcnt(12)
	v_mfma_f32_32x32x2_f32 v[4:19], v200, v208, v[4:19]
	ds_read_b32 v207, v218 offset:3808
	ds_read_b32 v215, v219 offset:1792
	s_waitcnt lgkmcnt(12)
	v_mfma_f32_32x32x2_f32 v[4:19], v201, v209, v[4:19]
	s_waitcnt lgkmcnt(10)
	v_mfma_f32_32x32x2_f32 v[4:19], v202, v210, v[4:19]
	s_waitcnt lgkmcnt(8)
	v_mfma_f32_32x32x2_f32 v[4:19], v203, v211, v[4:19]
	s_waitcnt lgkmcnt(6)
	v_mfma_f32_32x32x2_f32 v[4:19], v204, v212, v[4:19]
	s_waitcnt lgkmcnt(4)
	v_mfma_f32_32x32x2_f32 v[4:19], v205, v213, v[4:19]
	s_waitcnt lgkmcnt(2)
	v_mfma_f32_32x32x2_f32 v[4:19], v206, v214, v[4:19]
	s_waitcnt lgkmcnt(0)
	v_mfma_f32_32x32x2_f32 v[4:19], v207, v215, v[4:19]
	s_barrier
	global_load_dwordx4 v[32:35], v[92:93], off offset:1920
	global_load_dwordx4 v[20:23], v[80:81], off
	s_waitcnt vmcnt(3)
	v_cvt_f32_f16_sdwa v93, v28 dst_sel:DWORD dst_unused:UNUSED_PAD src0_sel:WORD_1
	v_cvt_f32_f16_e32 v28, v28
	v_cvt_f32_f16_sdwa v92, v29 dst_sel:DWORD dst_unused:UNUSED_PAD src0_sel:WORD_1
	v_cvt_f32_f16_sdwa v128, v30 dst_sel:DWORD dst_unused:UNUSED_PAD src0_sel:WORD_1
	v_cvt_f32_f16_e32 v131, v30
	ds_read_b128 v[36:39], v43 offset:15872
	ds_read_b128 v[116:119], v43 offset:15888
	ds_read_b128 v[120:123], v43 offset:19968
	ds_read_b128 v[124:127], v43 offset:19984
	v_cvt_f32_f16_e32 v115, v29
	v_cvt_f32_f16_sdwa v129, v31 dst_sel:DWORD dst_unused:UNUSED_PAD src0_sel:WORD_1
	v_cvt_f32_f16_e32 v130, v31
	v_sub_f32_e32 v28, v28, v0
	v_sub_f32_e32 v29, v93, v1
	v_sub_f32_e32 v31, v92, v3
	v_pk_mul_f32 v[28:29], v[88:89], v[28:29]
	v_sub_f32_e32 v92, v131, v0
	v_sub_f32_e32 v93, v128, v1
	v_sub_f32_e32 v30, v115, v2
	v_sub_f32_e32 v128, v130, v2
	v_sub_f32_e32 v129, v129, v3
	v_pk_mul_f32 v[92:93], v[88:89], v[92:93]
	s_waitcnt lgkmcnt(1)
	v_fma_f32 v28, v36, v28, v120
	v_fma_f32 v29, v37, v29, v121
	v_pk_mul_f32 v[30:31], v[90:91], v[30:31]
	v_pk_mul_f32 v[128:129], v[90:91], v[128:129]
	s_waitcnt lgkmcnt(0)
	v_fma_f32 v36, v116, v92, v124
	ds_write2_b32 v114, v28, v29 offset1:68
	v_fma_f32 v28, v117, v93, v125
	ds_write2_b32 v113, v36, v28 offset0:16 offset1:84
	v_fma_f32 v28, v38, v30, v122
	v_fma_f32 v29, v118, v128, v126
	v_fmac_f32_e32 v123, v39, v31
	v_fmac_f32_e32 v127, v119, v129
	ds_write2_b32 v114, v28, v123 offset0:136 offset1:204
	ds_write2_b32 v113, v29, v127 offset0:152 offset1:220
	s_waitcnt vmcnt(2)
	ds_write_b128 v96, v[24:27] offset:41984
	s_mov_b32 s16, 0
	v_mov_b32_e32 v24, v103
	s_waitcnt lgkmcnt(0)
	s_barrier
	ds_read_b32 v200, v218
	ds_read_b32 v208, v219
	ds_read_b32 v201, v218 offset:544
	ds_read_b32 v209, v219 offset:256
	ds_read_b32 v202, v218 offset:1088
	ds_read_b32 v210, v219 offset:512
	ds_read_b32 v203, v218 offset:1632
	ds_read_b32 v211, v219 offset:768
	ds_read_b32 v204, v218 offset:2176
	ds_read_b32 v212, v219 offset:1024
	ds_read_b32 v205, v218 offset:2720
	ds_read_b32 v213, v219 offset:1280
	ds_read_b32 v206, v218 offset:3264
	ds_read_b32 v214, v219 offset:1536
	s_waitcnt lgkmcnt(12)
	v_mfma_f32_32x32x2_f32 v[4:19], v200, v208, v[4:19]
	ds_read_b32 v207, v218 offset:3808
	ds_read_b32 v215, v219 offset:1792
	s_waitcnt lgkmcnt(12)
	v_mfma_f32_32x32x2_f32 v[4:19], v201, v209, v[4:19]
	s_waitcnt lgkmcnt(10)
	v_mfma_f32_32x32x2_f32 v[4:19], v202, v210, v[4:19]
	s_waitcnt lgkmcnt(8)
	v_mfma_f32_32x32x2_f32 v[4:19], v203, v211, v[4:19]
	s_waitcnt lgkmcnt(6)
	v_mfma_f32_32x32x2_f32 v[4:19], v204, v212, v[4:19]
	s_waitcnt lgkmcnt(4)
	v_mfma_f32_32x32x2_f32 v[4:19], v205, v213, v[4:19]
	s_waitcnt lgkmcnt(2)
	v_mfma_f32_32x32x2_f32 v[4:19], v206, v214, v[4:19]
	s_waitcnt lgkmcnt(0)
	v_mfma_f32_32x32x2_f32 v[4:19], v207, v215, v[4:19]
	s_waitcnt vmcnt(1)
	v_cvt_f32_f16_sdwa v93, v32 dst_sel:DWORD dst_unused:UNUSED_PAD src0_sel:WORD_1
	v_cvt_f32_f16_e32 v32, v32
	v_cvt_f32_f16_sdwa v121, v34 dst_sel:DWORD dst_unused:UNUSED_PAD src0_sel:WORD_1
	v_cvt_f32_f16_e32 v123, v34
	s_barrier
	ds_read_b128 v[24:27], v43 offset:16128
	ds_read_b128 v[28:31], v43 offset:16144
	ds_read_b128 v[36:39], v43 offset:20224
	ds_read_b128 v[116:119], v43 offset:20240
	v_cvt_f32_f16_sdwa v92, v33 dst_sel:DWORD dst_unused:UNUSED_PAD src0_sel:WORD_1
	v_cvt_f32_f16_e32 v115, v33
	v_cvt_f32_f16_sdwa v120, v35 dst_sel:DWORD dst_unused:UNUSED_PAD src0_sel:WORD_1
	v_cvt_f32_f16_e32 v122, v35
	v_sub_f32_e32 v32, v32, v0
	v_sub_f32_e32 v33, v93, v1
	v_sub_f32_e32 v0, v123, v0
	v_sub_f32_e32 v1, v121, v1
	v_sub_f32_e32 v34, v115, v2
	v_sub_f32_e32 v35, v92, v3
	v_pk_mul_f32 v[0:1], v[88:89], v[0:1]
	v_pk_mul_f32 v[34:35], v[90:91], v[34:35]
	v_sub_f32_e32 v2, v122, v2
	v_sub_f32_e32 v3, v120, v3
	s_waitcnt lgkmcnt(0)
	v_fma_f32 v0, v28, v0, v116
	v_fma_f32 v1, v29, v1, v117
	v_pk_mul_f32 v[32:33], v[88:89], v[32:33]
	v_pk_mul_f32 v[2:3], v[90:91], v[2:3]
	ds_write2_b32 v113, v0, v1 offset0:16 offset1:84
	v_fma_f32 v0, v26, v34, v38
	v_fmac_f32_e32 v39, v27, v35
	v_fma_f32 v24, v24, v32, v36
	v_fma_f32 v25, v25, v33, v37
	v_fma_f32 v1, v30, v2, v118
	ds_write2_b32 v114, v0, v39 offset0:136 offset1:204
	v_fmac_f32_e32 v119, v31, v3
	s_mov_b32 s16, 0
	v_mov_b32_e32 v0, v103
	ds_write2_b32 v114, v24, v25 offset1:68
	ds_write2_b32 v113, v1, v119 offset0:152 offset1:220
	s_waitcnt vmcnt(0)
	ds_write_b128 v96, v[20:23] offset:41984
	s_waitcnt lgkmcnt(0)
	s_barrier
	ds_read_b32 v200, v218
	ds_read_b32 v208, v219
	ds_read_b32 v201, v218 offset:544
	ds_read_b32 v209, v219 offset:256
	ds_read_b32 v202, v218 offset:1088
	ds_read_b32 v210, v219 offset:512
	ds_read_b32 v203, v218 offset:1632
	ds_read_b32 v211, v219 offset:768
	ds_read_b32 v204, v218 offset:2176
	ds_read_b32 v212, v219 offset:1024
	ds_read_b32 v205, v218 offset:2720
	ds_read_b32 v213, v219 offset:1280
	ds_read_b32 v206, v218 offset:3264
	ds_read_b32 v214, v219 offset:1536
	s_waitcnt lgkmcnt(12)
	v_mfma_f32_32x32x2_f32 v[4:19], v200, v208, v[4:19]
	ds_read_b32 v207, v218 offset:3808
	ds_read_b32 v215, v219 offset:1792
	s_waitcnt lgkmcnt(12)
	v_mfma_f32_32x32x2_f32 v[4:19], v201, v209, v[4:19]
	s_waitcnt lgkmcnt(10)
	v_mfma_f32_32x32x2_f32 v[4:19], v202, v210, v[4:19]
	s_waitcnt lgkmcnt(8)
	v_mfma_f32_32x32x2_f32 v[4:19], v203, v211, v[4:19]
	s_waitcnt lgkmcnt(6)
	v_mfma_f32_32x32x2_f32 v[4:19], v204, v212, v[4:19]
	s_waitcnt lgkmcnt(4)
	v_mfma_f32_32x32x2_f32 v[4:19], v205, v213, v[4:19]
	s_waitcnt lgkmcnt(2)
	v_mfma_f32_32x32x2_f32 v[4:19], v206, v214, v[4:19]
	s_waitcnt lgkmcnt(0)
	v_mfma_f32_32x32x2_f32 v[4:19], v207, v215, v[4:19]
	s_barrier
	s_nop 15
	s_nop 3
	ds_write_b32 v217, v4 offset:58752
	ds_write_b32 v217, v5 offset:58880
	ds_write_b32 v217, v6 offset:59008
	ds_write_b32 v217, v7 offset:59136
	ds_write_b32 v217, v8 offset:59776
	ds_write_b32 v217, v9 offset:59904
	ds_write_b32 v217, v10 offset:60032
	ds_write_b32 v217, v11 offset:60160
	ds_write_b32 v217, v12 offset:60800
	ds_write_b32 v217, v13 offset:60928
	ds_write_b32 v217, v14 offset:61056
	ds_write_b32 v217, v15 offset:61184
	ds_write_b32 v217, v16 offset:61824
	ds_write_b32 v217, v17 offset:61952
	ds_write_b32 v217, v18 offset:62080
	ds_write_b32 v217, v19 offset:62208
	s_waitcnt lgkmcnt(0)
	s_barrier
	global_load_dwordx4 v[0:3], v[50:51], off offset:256
	ds_read_b128 v[4:7], v98 offset:58752
	ds_read_b128 v[8:11], v99 offset:8192
	ds_read_b128 v[12:15], v99 offset:16384
	ds_read_b128 v[16:19], v99 offset:24576
	v_add_u32_e32 v20, 0xc400, v100
	v_add_u32_e32 v21, 0xc408, v100
	s_waitcnt lgkmcnt(2)
	v_pk_add_f32 v[4:5], v[4:5], v[8:9]
	v_pk_add_f32 v[6:7], v[6:7], v[10:11]
	s_waitcnt lgkmcnt(1)
	v_pk_add_f32 v[4:5], v[12:13], v[4:5]
	v_pk_add_f32 v[6:7], v[14:15], v[6:7]
	s_waitcnt lgkmcnt(0)
	v_pk_add_f32 v[4:5], v[16:17], v[4:5]
	v_pk_add_f32 v[6:7], v[18:19], v[6:7]
	s_waitcnt vmcnt(0)
	v_pk_add_f32 v[0:1], v[0:1], v[4:5]
	v_pk_add_f32 v[2:3], v[6:7], v[2:3]
	ds_write2_b32 v20, v0, v1 offset1:1
	ds_write2_b32 v21, v2, v3 offset1:1
	s_waitcnt lgkmcnt(0)
	s_barrier
	s_and_saveexec_b64 s[36:37], s[6:7]
	s_cbranch_execz .LBB0_2418
	v_add_u32_e32 v0, 0xc400, v108
	v_add_u32_e32 v1, 0xc408, v108
	v_add_u32_e32 v2, 0xc410, v108
	v_add_u32_e32 v3, 0xc418, v108
	ds_read2_b32 v[34:35], v0 offset1:1
	ds_read2_b32 v[30:31], v1 offset1:1
	ds_read2_b32 v[22:23], v2 offset1:1
	ds_read2_b32 v[10:11], v3 offset1:1
	s_mov_b32 s16, 0xff61b1e6
	s_waitcnt lgkmcnt(3)
	v_max_f32_e32 v0, v34, v34
	v_max_f32_e32 v0, 0xff61b1e6, v0
	v_cmp_lt_f32_e32 vcc, s16, v34
	v_cmp_gt_f32_e64 s[16:17], v35, v0
	v_add_u32_e32 v2, 0xc420, v108
	ds_read2_b32 v[24:25], v2 offset1:1
	v_cndmask_b32_e64 v0, v0, v35, s[16:17]
	v_cndmask_b32_e64 v1, 0, 1, s[16:17]
	s_waitcnt lgkmcnt(3)
	v_cmp_gt_f32_e64 s[16:17], v30, v0
	v_add_u32_e32 v2, 0xc428, v108
	v_add_u32_e32 v3, 0xc430, v108
	v_cndmask_b32_e64 v0, v0, v30, s[16:17]
	v_cndmask_b32_e64 v1, v1, 2, s[16:17]
	v_cmp_gt_f32_e64 s[16:17], v31, v0
	v_add_u32_e32 v4, 0xc438, v108
	ds_read2_b32 v[32:33], v2 offset1:1
	ds_read2_b32 v[20:21], v3 offset1:1
	ds_read2_b32 v[6:7], v4 offset1:1
	v_cndmask_b32_e64 v0, v0, v31, s[16:17]
	v_cndmask_b32_e64 v1, v1, 3, s[16:17]
	s_waitcnt lgkmcnt(5)
	v_cmp_gt_f32_e64 s[16:17], v22, v0
	v_add_u32_e32 v2, 0xc440, v108
	ds_read2_b32 v[18:19], v2 offset1:1
	v_cndmask_b32_e64 v0, v0, v22, s[16:17]
	v_cndmask_b32_e64 v1, v1, 4, s[16:17]
	v_cmp_gt_f32_e64 s[16:17], v23, v0
	v_add_u32_e32 v2, 0xc448, v108
	v_add_u32_e32 v4, 0xc458, v108
	v_cndmask_b32_e64 v0, v0, v23, s[16:17]
	v_cndmask_b32_e64 v1, v1, 5, s[16:17]
	s_waitcnt lgkmcnt(5)
	v_cmp_gt_f32_e64 s[16:17], v10, v0
	v_add_u32_e32 v3, 0xc450, v108
	ds_read2_b32 v[28:29], v2 offset1:1
	ds_read2_b32 v[12:13], v3 offset1:1
	ds_read2_b32 v[4:5], v4 offset1:1
	v_cndmask_b32_e64 v0, v0, v10, s[16:17]
	v_cndmask_b32_e64 v1, v1, 6, s[16:17]
	v_cmp_gt_f32_e64 s[16:17], v11, v0
	v_add_u32_e32 v2, 0xc460, v108
	ds_read2_b32 v[14:15], v2 offset1:1
	v_cndmask_b32_e64 v0, v0, v11, s[16:17]
	v_cndmask_b32_e64 v1, v1, 7, s[16:17]
	s_waitcnt lgkmcnt(8)
	v_cmp_gt_f32_e64 s[16:17], v24, v0
	v_add_u32_e32 v2, 0xc468, v108
	v_add_u32_e32 v8, 0xc478, v108
	v_cndmask_b32_e64 v0, v0, v24, s[16:17]
	v_cndmask_b32_e64 v1, v1, 8, s[16:17]
	v_cmp_gt_f32_e64 s[16:17], v25, v0
	v_add_u32_e32 v3, 0xc470, v108
	ds_read2_b32 v[26:27], v2 offset1:1
	ds_read2_b32 v[16:17], v3 offset1:1
	ds_read2_b32 v[8:9], v8 offset1:1
	v_cndmask_b32_e64 v0, v0, v25, s[16:17]
	v_cndmask_b32_e64 v1, v1, 9, s[16:17]
	s_waitcnt lgkmcnt(10)
	v_cmp_gt_f32_e64 s[16:17], v32, v0
	s_nop 1
	v_cndmask_b32_e64 v0, v0, v32, s[16:17]
	v_cndmask_b32_e64 v1, v1, 10, s[16:17]
	v_cmp_gt_f32_e64 s[16:17], v33, v0
	s_nop 1
	v_cndmask_b32_e64 v0, v0, v33, s[16:17]
	v_cndmask_b32_e64 v1, v1, 11, s[16:17]
	s_waitcnt lgkmcnt(9)
	v_cmp_gt_f32_e64 s[16:17], v20, v0
	s_nop 1
	v_cndmask_b32_e64 v0, v0, v20, s[16:17]
	v_cndmask_b32_e64 v1, v1, 12, s[16:17]
	v_cmp_gt_f32_e64 s[16:17], v21, v0
	s_nop 1
	v_cndmask_b32_e64 v0, v0, v21, s[16:17]
	v_cndmask_b32_e64 v1, v1, 13, s[16:17]
	s_waitcnt lgkmcnt(8)
	v_cmp_gt_f32_e64 s[16:17], v6, v0
	s_nop 1
	v_cndmask_b32_e64 v0, v0, v6, s[16:17]
	v_cndmask_b32_e64 v1, v1, 14, s[16:17]
	v_cmp_gt_f32_e64 s[16:17], v7, v0
	s_nop 1
	v_cndmask_b32_e64 v0, v0, v7, s[16:17]
	v_cndmask_b32_e64 v1, v1, 15, s[16:17]
	s_waitcnt lgkmcnt(7)
	v_cmp_gt_f32_e64 s[16:17], v18, v0
	s_nop 1
	v_cndmask_b32_e64 v0, v0, v18, s[16:17]
	v_cndmask_b32_e64 v1, v1, 16, s[16:17]
	v_cmp_gt_f32_e64 s[16:17], v19, v0
	s_nop 1
	v_cndmask_b32_e64 v0, v0, v19, s[16:17]
	v_cndmask_b32_e64 v1, v1, 17, s[16:17]
	s_waitcnt lgkmcnt(6)
	v_cmp_gt_f32_e64 s[16:17], v28, v0
	s_nop 1
	v_cndmask_b32_e64 v0, v0, v28, s[16:17]
	v_cndmask_b32_e64 v1, v1, 18, s[16:17]
	v_cmp_gt_f32_e64 s[16:17], v29, v0
	s_nop 1
	v_cndmask_b32_e64 v0, v0, v29, s[16:17]
	v_cndmask_b32_e64 v1, v1, 19, s[16:17]
	s_waitcnt lgkmcnt(5)
	v_cmp_gt_f32_e64 s[16:17], v12, v0
	s_nop 1
	v_cndmask_b32_e64 v0, v0, v12, s[16:17]
	v_cndmask_b32_e64 v1, v1, 20, s[16:17]
	v_cmp_gt_f32_e64 s[16:17], v13, v0
	s_nop 1
	v_cndmask_b32_e64 v0, v0, v13, s[16:17]
	v_cndmask_b32_e64 v1, v1, 21, s[16:17]
	s_waitcnt lgkmcnt(4)
	v_cmp_gt_f32_e64 s[16:17], v4, v0
	s_nop 1
	v_cndmask_b32_e64 v0, v0, v4, s[16:17]
	v_cndmask_b32_e64 v1, v1, 22, s[16:17]
	v_cmp_gt_f32_e64 s[16:17], v5, v0
	s_nop 1
	v_cndmask_b32_e64 v0, v0, v5, s[16:17]
	v_cndmask_b32_e64 v1, v1, 23, s[16:17]
	s_waitcnt lgkmcnt(3)
	v_cmp_gt_f32_e64 s[16:17], v14, v0
	s_nop 1
	v_cndmask_b32_e64 v0, v0, v14, s[16:17]
	v_cndmask_b32_e64 v1, v1, 24, s[16:17]
	v_cmp_gt_f32_e64 s[16:17], v15, v0
	s_nop 1
	v_cndmask_b32_e64 v0, v0, v15, s[16:17]
	v_cndmask_b32_e64 v1, v1, 25, s[16:17]
	s_waitcnt lgkmcnt(2)
	v_cmp_gt_f32_e64 s[16:17], v26, v0
	s_nop 1
	v_cndmask_b32_e64 v0, v0, v26, s[16:17]
	v_cndmask_b32_e64 v1, v1, 26, s[16:17]
	v_cmp_gt_f32_e64 s[16:17], v27, v0
	s_nop 1
	v_cndmask_b32_e64 v0, v0, v27, s[16:17]
	v_cndmask_b32_e64 v1, v1, 27, s[16:17]
	s_waitcnt lgkmcnt(1)
	v_cmp_gt_f32_e64 s[16:17], v16, v0
	s_nop 1
	v_cndmask_b32_e64 v0, v0, v16, s[16:17]
	v_cndmask_b32_e64 v1, v1, 28, s[16:17]
	v_cmp_gt_f32_e64 s[16:17], v17, v0
	s_nop 1
	v_cndmask_b32_e64 v0, v0, v17, s[16:17]
	v_cndmask_b32_e64 v1, v1, 29, s[16:17]
	s_waitcnt lgkmcnt(0)
	v_cmp_gt_f32_e64 s[16:17], v8, v0
	s_nop 1
	v_cndmask_b32_e64 v0, v0, v8, s[16:17]
	v_cndmask_b32_e64 v1, v1, 30, s[16:17]
	v_cmp_gt_f32_e64 s[16:17], v9, v0
	s_nop 1
	v_cndmask_b32_e64 v36, v0, v9, s[16:17]
	v_cndmask_b32_e64 v0, v1, 31, s[16:17]
	v_cmp_ne_u32_e64 s[16:17], 0, v0
	v_lshlrev_b32_e64 v2, v0, 1
	s_and_b64 s[16:17], s[16:17], vcc
	v_cndmask_b32_e64 v1, v112, v34, s[16:17]
	v_and_b32_e32 v3, 2, v2
	v_cmp_eq_u32_e64 s[16:17], 0, v3
	v_cmp_gt_f32_e64 s[18:19], v35, v1
	s_and_b64 s[16:17], s[16:17], s[18:19]
	v_cndmask_b32_e64 v1, v1, v35, s[16:17]
	v_and_b32_e32 v37, 4, v2
	v_cndmask_b32_e64 v3, 0, 1, s[16:17]
	v_cmp_eq_u32_e64 s[16:17], 0, v37
	v_cmp_gt_f32_e64 s[18:19], v30, v1
	s_and_b64 s[16:17], s[16:17], s[18:19]
	v_cndmask_b32_e64 v1, v1, v30, s[16:17]
	v_and_b32_e32 v37, 8, v2
	v_cndmask_b32_e64 v3, v3, 2, s[16:17]
	v_cmp_eq_u32_e64 s[16:17], 0, v37
	v_cmp_gt_f32_e64 s[18:19], v31, v1
	s_and_b64 s[16:17], s[16:17], s[18:19]
	v_cndmask_b32_e64 v1, v1, v31, s[16:17]
	v_and_b32_e32 v37, 16, v2
	v_cndmask_b32_e64 v3, v3, 3, s[16:17]
	v_cmp_eq_u32_e64 s[16:17], 0, v37
	v_cmp_gt_f32_e64 s[18:19], v22, v1
	s_and_b64 s[16:17], s[16:17], s[18:19]
	v_cndmask_b32_e64 v1, v1, v22, s[16:17]
	v_and_b32_e32 v37, 32, v2
	v_cndmask_b32_e64 v3, v3, 4, s[16:17]
	v_cmp_eq_u32_e64 s[16:17], 0, v37
	v_cmp_gt_f32_e64 s[18:19], v23, v1
	s_and_b64 s[16:17], s[16:17], s[18:19]
	v_cndmask_b32_e64 v1, v1, v23, s[16:17]
	v_and_b32_e32 v37, 64, v2
	v_cndmask_b32_e64 v3, v3, 5, s[16:17]
	v_cmp_eq_u32_e64 s[16:17], 0, v37
	v_cmp_gt_f32_e64 s[18:19], v10, v1
	s_and_b64 s[16:17], s[16:17], s[18:19]
	v_cndmask_b32_e64 v1, v1, v10, s[16:17]
	v_and_b32_e32 v37, 0x80, v2
	v_cndmask_b32_e64 v3, v3, 6, s[16:17]
	v_cmp_eq_u32_e64 s[16:17], 0, v37
	v_cmp_gt_f32_e64 s[18:19], v11, v1
	s_and_b64 s[16:17], s[16:17], s[18:19]
	v_cndmask_b32_e64 v1, v1, v11, s[16:17]
	v_and_b32_e32 v37, 0x100, v2
	v_cndmask_b32_e64 v3, v3, 7, s[16:17]
	v_cmp_eq_u32_e64 s[16:17], 0, v37
	v_cmp_gt_f32_e64 s[18:19], v24, v1
	s_and_b64 s[16:17], s[16:17], s[18:19]
	v_cndmask_b32_e64 v1, v1, v24, s[16:17]
	v_and_b32_e32 v37, 0x200, v2
	v_cndmask_b32_e64 v3, v3, 8, s[16:17]
	v_cmp_eq_u32_e64 s[16:17], 0, v37
	v_cmp_gt_f32_e64 s[18:19], v25, v1
	s_and_b64 s[16:17], s[16:17], s[18:19]
	v_cndmask_b32_e64 v1, v1, v25, s[16:17]
	v_and_b32_e32 v37, 0x400, v2
	v_cndmask_b32_e64 v3, v3, 9, s[16:17]
	v_cmp_eq_u32_e64 s[16:17], 0, v37
	v_cmp_gt_f32_e64 s[18:19], v32, v1
	s_and_b64 s[16:17], s[16:17], s[18:19]
	v_cndmask_b32_e64 v1, v1, v32, s[16:17]
	v_and_b32_e32 v37, 0x800, v2
	v_cndmask_b32_e64 v3, v3, 10, s[16:17]
	v_cmp_eq_u32_e64 s[16:17], 0, v37
	v_cmp_gt_f32_e64 s[18:19], v33, v1
	s_and_b64 s[16:17], s[16:17], s[18:19]
	v_cndmask_b32_e64 v1, v1, v33, s[16:17]
	v_and_b32_e32 v37, 0x1000, v2
	v_cndmask_b32_e64 v3, v3, 11, s[16:17]
	v_cmp_eq_u32_e64 s[16:17], 0, v37
	v_cmp_gt_f32_e64 s[18:19], v20, v1
	s_and_b64 s[16:17], s[16:17], s[18:19]
	v_cndmask_b32_e64 v1, v1, v20, s[16:17]
	v_and_b32_e32 v37, 0x2000, v2
	v_cndmask_b32_e64 v3, v3, 12, s[16:17]
	v_cmp_eq_u32_e64 s[16:17], 0, v37
	v_cmp_gt_f32_e64 s[18:19], v21, v1
	s_and_b64 s[16:17], s[16:17], s[18:19]
	v_cndmask_b32_e64 v1, v1, v21, s[16:17]
	v_and_b32_e32 v37, 0x4000, v2
	v_cndmask_b32_e64 v3, v3, 13, s[16:17]
	v_cmp_eq_u32_e64 s[16:17], 0, v37
	v_cmp_gt_f32_e64 s[18:19], v6, v1
	s_and_b64 s[16:17], s[16:17], s[18:19]
	v_cndmask_b32_e64 v1, v1, v6, s[16:17]
	v_and_b32_e32 v37, 0x8000, v2
	v_cndmask_b32_e64 v3, v3, 14, s[16:17]
	v_cmp_eq_u32_e64 s[16:17], 0, v37
	v_cmp_gt_f32_e64 s[18:19], v7, v1
	s_and_b64 s[16:17], s[16:17], s[18:19]
	v_cndmask_b32_e64 v1, v1, v7, s[16:17]
	v_and_b32_e32 v37, 0x10000, v2
	v_cndmask_b32_e64 v3, v3, 15, s[16:17]
	v_cmp_eq_u32_e64 s[16:17], 0, v37
	v_cmp_gt_f32_e64 s[18:19], v18, v1
	s_and_b64 s[16:17], s[16:17], s[18:19]
	v_cndmask_b32_e64 v1, v1, v18, s[16:17]
	v_and_b32_e32 v37, 0x20000, v2
	v_cndmask_b32_e64 v3, v3, 16, s[16:17]
	v_cmp_eq_u32_e64 s[16:17], 0, v37
	v_cmp_gt_f32_e64 s[18:19], v19, v1
	s_and_b64 s[16:17], s[16:17], s[18:19]
	v_cndmask_b32_e64 v1, v1, v19, s[16:17]
	v_and_b32_e32 v37, 0x40000, v2
	v_cndmask_b32_e64 v3, v3, 17, s[16:17]
	v_cmp_eq_u32_e64 s[16:17], 0, v37
	v_cmp_gt_f32_e64 s[18:19], v28, v1
	s_and_b64 s[16:17], s[16:17], s[18:19]
	v_cndmask_b32_e64 v1, v1, v28, s[16:17]
	v_and_b32_e32 v37, 0x80000, v2
	v_cndmask_b32_e64 v3, v3, 18, s[16:17]
	v_cmp_eq_u32_e64 s[16:17], 0, v37
	v_cmp_gt_f32_e64 s[18:19], v29, v1
	s_and_b64 s[16:17], s[16:17], s[18:19]
	v_cndmask_b32_e64 v1, v1, v29, s[16:17]
	v_and_b32_e32 v37, 0x100000, v2
	v_cndmask_b32_e64 v3, v3, 19, s[16:17]
	v_cmp_eq_u32_e64 s[16:17], 0, v37
	v_cmp_gt_f32_e64 s[18:19], v12, v1
	s_and_b64 s[16:17], s[16:17], s[18:19]
	v_cndmask_b32_e64 v1, v1, v12, s[16:17]
	v_and_b32_e32 v37, 0x200000, v2
	v_cndmask_b32_e64 v3, v3, 20, s[16:17]
	v_cmp_eq_u32_e64 s[16:17], 0, v37
	v_cmp_gt_f32_e64 s[18:19], v13, v1
	s_and_b64 s[16:17], s[16:17], s[18:19]
	v_cndmask_b32_e64 v1, v1, v13, s[16:17]
	v_and_b32_e32 v37, 0x400000, v2
	v_cndmask_b32_e64 v3, v3, 21, s[16:17]
	v_cmp_eq_u32_e64 s[16:17], 0, v37
	v_cmp_gt_f32_e64 s[18:19], v4, v1
	s_and_b64 s[16:17], s[16:17], s[18:19]
	v_cndmask_b32_e64 v1, v1, v4, s[16:17]
	v_and_b32_e32 v37, 0x800000, v2
	v_cndmask_b32_e64 v3, v3, 22, s[16:17]
	v_cmp_eq_u32_e64 s[16:17], 0, v37
	v_cmp_gt_f32_e64 s[18:19], v5, v1
	s_and_b64 s[16:17], s[16:17], s[18:19]
	v_cndmask_b32_e64 v1, v1, v5, s[16:17]
	v_and_b32_e32 v37, 0x1000000, v2
	v_cndmask_b32_e64 v3, v3, 23, s[16:17]
	v_cmp_eq_u32_e64 s[16:17], 0, v37
	v_cmp_gt_f32_e64 s[18:19], v14, v1
	s_and_b64 s[16:17], s[16:17], s[18:19]
	v_cndmask_b32_e64 v1, v1, v14, s[16:17]
	v_and_b32_e32 v37, 0x2000000, v2
	v_cndmask_b32_e64 v3, v3, 24, s[16:17]
	v_cmp_eq_u32_e64 s[16:17], 0, v37
	v_cmp_gt_f32_e64 s[18:19], v15, v1
	s_and_b64 s[16:17], s[16:17], s[18:19]
	v_cndmask_b32_e64 v1, v1, v15, s[16:17]
	v_and_b32_e32 v37, 0x4000000, v2
	v_cndmask_b32_e64 v3, v3, 25, s[16:17]
	v_cmp_eq_u32_e64 s[16:17], 0, v37
	v_cmp_gt_f32_e64 s[18:19], v26, v1
	s_and_b64 s[16:17], s[16:17], s[18:19]
	v_cndmask_b32_e64 v1, v1, v26, s[16:17]
	v_and_b32_e32 v37, 0x8000000, v2
	v_cndmask_b32_e64 v3, v3, 26, s[16:17]
	v_cmp_eq_u32_e64 s[16:17], 0, v37
	v_cmp_gt_f32_e64 s[18:19], v27, v1
	s_and_b64 s[16:17], s[16:17], s[18:19]
	v_cndmask_b32_e64 v1, v1, v27, s[16:17]
	v_and_b32_e32 v37, 0x10000000, v2
	v_cndmask_b32_e64 v3, v3, 27, s[16:17]
	v_cmp_eq_u32_e64 s[16:17], 0, v37
	v_cmp_gt_f32_e64 s[18:19], v16, v1
	s_and_b64 s[16:17], s[16:17], s[18:19]
	v_cndmask_b32_e64 v1, v1, v16, s[16:17]
	v_and_b32_e32 v37, 0x20000000, v2
	v_cndmask_b32_e64 v3, v3, 28, s[16:17]
	v_cmp_eq_u32_e64 s[16:17], 0, v37
	v_cmp_gt_f32_e64 s[18:19], v17, v1
	s_and_b64 s[16:17], s[16:17], s[18:19]
	v_cndmask_b32_e64 v1, v1, v17, s[16:17]
	v_and_b32_e32 v37, 2.0, v2
	v_cndmask_b32_e64 v3, v3, 29, s[16:17]
	v_cmp_eq_u32_e64 s[16:17], 0, v37
	v_cmp_gt_f32_e64 s[18:19], v8, v1
	s_and_b64 s[16:17], s[16:17], s[18:19]
	v_cndmask_b32_e64 v1, v1, v8, s[16:17]
	v_cndmask_b32_e64 v3, v3, 30, s[16:17]
	v_cmp_ne_u32_e64 s[16:17], 31, v0
	v_cmp_gt_f32_e64 s[18:19], v9, v1
	s_and_b64 s[16:17], s[16:17], s[18:19]
	v_cndmask_b32_e64 v37, v1, v9, s[16:17]
	v_cndmask_b32_e64 v1, v3, 31, s[16:17]
	v_lshl_or_b32 v3, 1, v1, v2
	v_and_b32_e32 v2, 1, v3
	v_cmp_eq_u32_e64 s[16:17], 0, v2
	s_and_b64 s[16:17], s[16:17], vcc
	v_and_b32_e32 v38, 2, v3
	v_cndmask_b32_e64 v2, v112, v34, s[16:17]
	v_cmp_eq_u32_e64 s[16:17], 0, v38
	v_cmp_gt_f32_e64 s[18:19], v35, v2
	s_and_b64 s[16:17], s[16:17], s[18:19]
	v_cndmask_b32_e64 v2, v2, v35, s[16:17]
	v_and_b32_e32 v39, 4, v3
	v_cndmask_b32_e64 v38, 0, 1, s[16:17]
	v_cmp_eq_u32_e64 s[16:17], 0, v39
	v_cmp_gt_f32_e64 s[18:19], v30, v2
	s_and_b64 s[16:17], s[16:17], s[18:19]
	v_cndmask_b32_e64 v2, v2, v30, s[16:17]
	v_and_b32_e32 v39, 8, v3
	v_cndmask_b32_e64 v38, v38, 2, s[16:17]
	v_cmp_eq_u32_e64 s[16:17], 0, v39
	v_cmp_gt_f32_e64 s[18:19], v31, v2
	s_and_b64 s[16:17], s[16:17], s[18:19]
	v_cndmask_b32_e64 v2, v2, v31, s[16:17]
	v_and_b32_e32 v39, 16, v3
	v_cndmask_b32_e64 v38, v38, 3, s[16:17]
	v_cmp_eq_u32_e64 s[16:17], 0, v39
	v_cmp_gt_f32_e64 s[18:19], v22, v2
	s_and_b64 s[16:17], s[16:17], s[18:19]
	v_cndmask_b32_e64 v2, v2, v22, s[16:17]
	v_and_b32_e32 v39, 32, v3
	v_cndmask_b32_e64 v38, v38, 4, s[16:17]
	v_cmp_eq_u32_e64 s[16:17], 0, v39
	v_cmp_gt_f32_e64 s[18:19], v23, v2
	s_and_b64 s[16:17], s[16:17], s[18:19]
	v_cndmask_b32_e64 v2, v2, v23, s[16:17]
	v_and_b32_e32 v39, 64, v3
	v_cndmask_b32_e64 v38, v38, 5, s[16:17]
	v_cmp_eq_u32_e64 s[16:17], 0, v39
	v_cmp_gt_f32_e64 s[18:19], v10, v2
	s_and_b64 s[16:17], s[16:17], s[18:19]
	v_cndmask_b32_e64 v2, v2, v10, s[16:17]
	v_and_b32_e32 v39, 0x80, v3
	v_cndmask_b32_e64 v38, v38, 6, s[16:17]
	v_cmp_eq_u32_e64 s[16:17], 0, v39
	v_cmp_gt_f32_e64 s[18:19], v11, v2
	s_and_b64 s[16:17], s[16:17], s[18:19]
	v_cndmask_b32_e64 v2, v2, v11, s[16:17]
	v_and_b32_e32 v39, 0x100, v3
	v_cndmask_b32_e64 v38, v38, 7, s[16:17]
	v_cmp_eq_u32_e64 s[16:17], 0, v39
	v_cmp_gt_f32_e64 s[18:19], v24, v2
	s_and_b64 s[16:17], s[16:17], s[18:19]
	v_cndmask_b32_e64 v2, v2, v24, s[16:17]
	v_and_b32_e32 v39, 0x200, v3
	v_cndmask_b32_e64 v38, v38, 8, s[16:17]
	v_cmp_eq_u32_e64 s[16:17], 0, v39
	v_cmp_gt_f32_e64 s[18:19], v25, v2
	s_and_b64 s[16:17], s[16:17], s[18:19]
	v_cndmask_b32_e64 v2, v2, v25, s[16:17]
	v_and_b32_e32 v39, 0x400, v3
	v_cndmask_b32_e64 v38, v38, 9, s[16:17]
	v_cmp_eq_u32_e64 s[16:17], 0, v39
	v_cmp_gt_f32_e64 s[18:19], v32, v2
	s_and_b64 s[16:17], s[16:17], s[18:19]
	v_cndmask_b32_e64 v2, v2, v32, s[16:17]
	v_and_b32_e32 v39, 0x800, v3
	v_cndmask_b32_e64 v38, v38, 10, s[16:17]
	v_cmp_eq_u32_e64 s[16:17], 0, v39
	v_cmp_gt_f32_e64 s[18:19], v33, v2
	s_and_b64 s[16:17], s[16:17], s[18:19]
	v_cndmask_b32_e64 v2, v2, v33, s[16:17]
	v_and_b32_e32 v39, 0x1000, v3
	v_cndmask_b32_e64 v38, v38, 11, s[16:17]
	v_cmp_eq_u32_e64 s[16:17], 0, v39
	v_cmp_gt_f32_e64 s[18:19], v20, v2
	s_and_b64 s[16:17], s[16:17], s[18:19]
	v_cndmask_b32_e64 v2, v2, v20, s[16:17]
	v_and_b32_e32 v39, 0x2000, v3
	v_cndmask_b32_e64 v38, v38, 12, s[16:17]
	v_cmp_eq_u32_e64 s[16:17], 0, v39
	v_cmp_gt_f32_e64 s[18:19], v21, v2
	s_and_b64 s[16:17], s[16:17], s[18:19]
	v_cndmask_b32_e64 v2, v2, v21, s[16:17]
	v_and_b32_e32 v39, 0x4000, v3
	v_cndmask_b32_e64 v38, v38, 13, s[16:17]
	v_cmp_eq_u32_e64 s[16:17], 0, v39
	v_cmp_gt_f32_e64 s[18:19], v6, v2
	s_and_b64 s[16:17], s[16:17], s[18:19]
	v_cndmask_b32_e64 v2, v2, v6, s[16:17]
	v_and_b32_e32 v39, 0x8000, v3
	v_cndmask_b32_e64 v38, v38, 14, s[16:17]
	v_cmp_eq_u32_e64 s[16:17], 0, v39
	v_cmp_gt_f32_e64 s[18:19], v7, v2
	s_and_b64 s[16:17], s[16:17], s[18:19]
	v_cndmask_b32_e64 v2, v2, v7, s[16:17]
	v_and_b32_e32 v39, 0x10000, v3
	v_cndmask_b32_e64 v38, v38, 15, s[16:17]
	v_cmp_eq_u32_e64 s[16:17], 0, v39
	v_cmp_gt_f32_e64 s[18:19], v18, v2
	s_and_b64 s[16:17], s[16:17], s[18:19]
	v_cndmask_b32_e64 v2, v2, v18, s[16:17]
	v_and_b32_e32 v39, 0x20000, v3
	v_cndmask_b32_e64 v38, v38, 16, s[16:17]
	v_cmp_eq_u32_e64 s[16:17], 0, v39
	v_cmp_gt_f32_e64 s[18:19], v19, v2
	s_and_b64 s[16:17], s[16:17], s[18:19]
	v_cndmask_b32_e64 v2, v2, v19, s[16:17]
	v_and_b32_e32 v39, 0x40000, v3
	v_cndmask_b32_e64 v38, v38, 17, s[16:17]
	v_cmp_eq_u32_e64 s[16:17], 0, v39
	v_cmp_gt_f32_e64 s[18:19], v28, v2
	s_and_b64 s[16:17], s[16:17], s[18:19]
	v_cndmask_b32_e64 v2, v2, v28, s[16:17]
	v_and_b32_e32 v39, 0x80000, v3
	v_cndmask_b32_e64 v38, v38, 18, s[16:17]
	v_cmp_eq_u32_e64 s[16:17], 0, v39
	v_cmp_gt_f32_e64 s[18:19], v29, v2
	s_and_b64 s[16:17], s[16:17], s[18:19]
	v_cndmask_b32_e64 v2, v2, v29, s[16:17]
	v_and_b32_e32 v39, 0x100000, v3
	v_cndmask_b32_e64 v38, v38, 19, s[16:17]
	v_cmp_eq_u32_e64 s[16:17], 0, v39
	v_cmp_gt_f32_e64 s[18:19], v12, v2
	s_and_b64 s[16:17], s[16:17], s[18:19]
	v_cndmask_b32_e64 v2, v2, v12, s[16:17]
	v_and_b32_e32 v39, 0x200000, v3
	v_cndmask_b32_e64 v38, v38, 20, s[16:17]
	v_cmp_eq_u32_e64 s[16:17], 0, v39
	v_cmp_gt_f32_e64 s[18:19], v13, v2
	s_and_b64 s[16:17], s[16:17], s[18:19]
	v_cndmask_b32_e64 v2, v2, v13, s[16:17]
	v_and_b32_e32 v39, 0x400000, v3
	v_cndmask_b32_e64 v38, v38, 21, s[16:17]
	v_cmp_eq_u32_e64 s[16:17], 0, v39
	v_cmp_gt_f32_e64 s[18:19], v4, v2
	s_and_b64 s[16:17], s[16:17], s[18:19]
	v_cndmask_b32_e64 v2, v2, v4, s[16:17]
	v_and_b32_e32 v39, 0x800000, v3
	v_cndmask_b32_e64 v38, v38, 22, s[16:17]
	v_cmp_eq_u32_e64 s[16:17], 0, v39
	v_cmp_gt_f32_e64 s[18:19], v5, v2
	s_and_b64 s[16:17], s[16:17], s[18:19]
	v_cndmask_b32_e64 v2, v2, v5, s[16:17]
	v_and_b32_e32 v39, 0x1000000, v3
	v_cndmask_b32_e64 v38, v38, 23, s[16:17]
	v_cmp_eq_u32_e64 s[16:17], 0, v39
	v_cmp_gt_f32_e64 s[18:19], v14, v2
	s_and_b64 s[16:17], s[16:17], s[18:19]
	v_cndmask_b32_e64 v2, v2, v14, s[16:17]
	v_and_b32_e32 v39, 0x2000000, v3
	v_cndmask_b32_e64 v38, v38, 24, s[16:17]
	v_cmp_eq_u32_e64 s[16:17], 0, v39
	v_cmp_gt_f32_e64 s[18:19], v15, v2
	s_and_b64 s[16:17], s[16:17], s[18:19]
	v_cndmask_b32_e64 v2, v2, v15, s[16:17]
	v_and_b32_e32 v39, 0x4000000, v3
	v_cndmask_b32_e64 v38, v38, 25, s[16:17]
	v_cmp_eq_u32_e64 s[16:17], 0, v39
	v_cmp_gt_f32_e64 s[18:19], v26, v2
	s_and_b64 s[16:17], s[16:17], s[18:19]
	v_cndmask_b32_e64 v2, v2, v26, s[16:17]
	v_and_b32_e32 v39, 0x8000000, v3
	v_cndmask_b32_e64 v38, v38, 26, s[16:17]
	v_cmp_eq_u32_e64 s[16:17], 0, v39
	v_cmp_gt_f32_e64 s[18:19], v27, v2
	s_and_b64 s[16:17], s[16:17], s[18:19]
	v_cndmask_b32_e64 v2, v2, v27, s[16:17]
	v_and_b32_e32 v39, 0x10000000, v3
	v_cndmask_b32_e64 v38, v38, 27, s[16:17]
	v_cmp_eq_u32_e64 s[16:17], 0, v39
	v_cmp_gt_f32_e64 s[18:19], v16, v2
	s_and_b64 s[16:17], s[16:17], s[18:19]
	v_cndmask_b32_e64 v2, v2, v16, s[16:17]
	v_and_b32_e32 v39, 0x20000000, v3
	v_cndmask_b32_e64 v38, v38, 28, s[16:17]
	v_cmp_eq_u32_e64 s[16:17], 0, v39
	v_cmp_gt_f32_e64 s[18:19], v17, v2
	s_and_b64 s[16:17], s[16:17], s[18:19]
	v_cndmask_b32_e64 v2, v2, v17, s[16:17]
	v_and_b32_e32 v39, 2.0, v3
	v_cndmask_b32_e64 v38, v38, 29, s[16:17]
	v_cmp_eq_u32_e64 s[16:17], 0, v39
	v_cmp_gt_f32_e64 s[18:19], v8, v2
	s_and_b64 s[16:17], s[16:17], s[18:19]
	v_cndmask_b32_e64 v2, v2, v8, s[16:17]
	v_cndmask_b32_e64 v38, v38, 30, s[16:17]
	v_cmp_lt_i32_e64 s[16:17], -1, v3
	v_cmp_gt_f32_e64 s[18:19], v9, v2
	s_and_b64 s[16:17], s[16:17], s[18:19]
	v_cndmask_b32_e64 v39, v2, v9, s[16:17]
	v_cndmask_b32_e64 v2, v38, 31, s[16:17]
	v_lshlrev_b32_e64 v38, v2, 1
	v_bitop3_b32 v89, v38, 1, v3 bitop3:0xc8
	v_cmp_eq_u32_e64 s[16:17], 0, v89
	s_and_b64 vcc, s[16:17], vcc
	v_cndmask_b32_e32 v34, v112, v34, vcc
	v_bitop3_b32 v89, v38, 2, v3 bitop3:0xc8
	v_cmp_eq_u32_e32 vcc, 0, v89
	v_cmp_gt_f32_e64 s[16:17], v35, v34
	s_and_b64 vcc, vcc, s[16:17]
	v_cndmask_b32_e32 v34, v34, v35, vcc
	v_bitop3_b32 v89, v38, 4, v3 bitop3:0xc8
	v_cndmask_b32_e64 v35, 0, 1, vcc
	v_cmp_eq_u32_e32 vcc, 0, v89
	v_cmp_gt_f32_e64 s[16:17], v30, v34
	s_and_b64 vcc, vcc, s[16:17]
	v_cndmask_b32_e32 v30, v34, v30, vcc
	v_cndmask_b32_e64 v34, v35, 2, vcc
	v_bitop3_b32 v35, v38, 8, v3 bitop3:0xc8
	v_cmp_eq_u32_e32 vcc, 0, v35
	v_cmp_gt_f32_e64 s[16:17], v31, v30
	s_and_b64 vcc, vcc, s[16:17]
	v_cndmask_b32_e32 v30, v30, v31, vcc
	v_cndmask_b32_e64 v31, v34, 3, vcc
	v_bitop3_b32 v34, v38, 16, v3 bitop3:0xc8
	v_cmp_eq_u32_e32 vcc, 0, v34
	v_cmp_gt_f32_e64 s[16:17], v22, v30
	s_and_b64 vcc, vcc, s[16:17]
	v_cndmask_b32_e32 v22, v30, v22, vcc
	v_cndmask_b32_e64 v30, v31, 4, vcc
	v_bitop3_b32 v31, v38, 32, v3 bitop3:0xc8
	v_cmp_eq_u32_e32 vcc, 0, v31
	v_cmp_gt_f32_e64 s[16:17], v23, v22
	s_and_b64 vcc, vcc, s[16:17]
	v_cndmask_b32_e32 v22, v22, v23, vcc
	v_cndmask_b32_e64 v23, v30, 5, vcc
	v_bitop3_b32 v30, v38, 64, v3 bitop3:0xc8
	v_cmp_eq_u32_e32 vcc, 0, v30
	v_cmp_gt_f32_e64 s[16:17], v10, v22
	s_and_b64 vcc, vcc, s[16:17]
	s_movk_i32 s16, 0x80
	v_cndmask_b32_e32 v10, v22, v10, vcc
	v_cndmask_b32_e64 v22, v23, 6, vcc
	v_bitop3_b32 v23, v38, s16, v3 bitop3:0xc8
	v_cmp_eq_u32_e32 vcc, 0, v23
	v_cmp_gt_f32_e64 s[16:17], v11, v10
	s_and_b64 vcc, vcc, s[16:17]
	s_movk_i32 s16, 0x100
	v_cndmask_b32_e32 v10, v10, v11, vcc
	v_cndmask_b32_e64 v11, v22, 7, vcc
	v_bitop3_b32 v22, v38, s16, v3 bitop3:0xc8
	v_cmp_eq_u32_e32 vcc, 0, v22
	v_cmp_gt_f32_e64 s[16:17], v24, v10
	s_and_b64 vcc, vcc, s[16:17]
	s_movk_i32 s16, 0x200
	v_cndmask_b32_e32 v10, v10, v24, vcc
	v_bitop3_b32 v22, v38, s16, v3 bitop3:0xc8
	v_cndmask_b32_e64 v11, v11, 8, vcc
	v_cmp_eq_u32_e32 vcc, 0, v22
	v_cmp_gt_f32_e64 s[16:17], v25, v10
	s_and_b64 vcc, vcc, s[16:17]
	v_cndmask_b32_e32 v10, v10, v25, vcc
	v_bitop3_b32 v22, v38, s52, v3 bitop3:0xc8
	v_cndmask_b32_e64 v11, v11, 9, vcc
	v_cmp_eq_u32_e32 vcc, 0, v22
	v_cmp_gt_f32_e64 s[16:17], v32, v10
	s_and_b64 vcc, vcc, s[16:17]
	s_movk_i32 s16, 0x800
	v_cndmask_b32_e32 v10, v10, v32, vcc
	v_bitop3_b32 v22, v38, s16, v3 bitop3:0xc8
	v_cndmask_b32_e64 v11, v11, 10, vcc
	v_cmp_eq_u32_e32 vcc, 0, v22
	v_cmp_gt_f32_e64 s[16:17], v33, v10
	s_and_b64 vcc, vcc, s[16:17]
	s_movk_i32 s16, 0x1000
	v_cndmask_b32_e32 v10, v10, v33, vcc
	v_bitop3_b32 v22, v38, s16, v3 bitop3:0xc8
	v_cndmask_b32_e64 v11, v11, 11, vcc
	v_cmp_eq_u32_e32 vcc, 0, v22
	v_cmp_gt_f32_e64 s[16:17], v20, v10
	s_and_b64 vcc, vcc, s[16:17]
	s_movk_i32 s16, 0x2000
	v_cndmask_b32_e32 v10, v10, v20, vcc
	v_bitop3_b32 v20, v38, s16, v3 bitop3:0xc8
	v_cndmask_b32_e64 v11, v11, 12, vcc
	v_cmp_eq_u32_e32 vcc, 0, v20
	v_cmp_gt_f32_e64 s[16:17], v21, v10
	s_and_b64 vcc, vcc, s[16:17]
	s_movk_i32 s16, 0x4000
	v_cndmask_b32_e32 v10, v10, v21, vcc
	v_bitop3_b32 v20, v38, s16, v3 bitop3:0xc8
	v_cndmask_b32_e64 v11, v11, 13, vcc
	v_cmp_eq_u32_e32 vcc, 0, v20
	v_cmp_gt_f32_e64 s[16:17], v6, v10
	s_and_b64 vcc, vcc, s[16:17]
	s_mov_b32 s16, 0x8000
	v_cndmask_b32_e32 v6, v10, v6, vcc
	v_cndmask_b32_e64 v10, v11, 14, vcc
	v_bitop3_b32 v11, v38, s16, v3 bitop3:0xc8
	v_cmp_eq_u32_e32 vcc, 0, v11
	v_cmp_gt_f32_e64 s[16:17], v7, v6
	s_and_b64 vcc, vcc, s[16:17]
	s_mov_b32 s16, 0x10000
	v_cndmask_b32_e32 v6, v6, v7, vcc
	v_cndmask_b32_e64 v7, v10, 15, vcc
	v_bitop3_b32 v10, v38, s16, v3 bitop3:0xc8
	v_cmp_eq_u32_e32 vcc, 0, v10
	v_cmp_gt_f32_e64 s[16:17], v18, v6
	s_and_b64 vcc, vcc, s[16:17]
	s_mov_b32 s16, 0x20000
	v_cndmask_b32_e32 v6, v6, v18, vcc
	v_bitop3_b32 v10, v38, s16, v3 bitop3:0xc8
	v_cndmask_b32_e64 v7, v7, 16, vcc
	v_cmp_eq_u32_e32 vcc, 0, v10
	v_cmp_gt_f32_e64 s[16:17], v19, v6
	s_and_b64 vcc, vcc, s[16:17]
	s_mov_b32 s16, 0x40000
	v_cndmask_b32_e32 v6, v6, v19, vcc
	v_bitop3_b32 v10, v38, s16, v3 bitop3:0xc8
	v_cndmask_b32_e64 v7, v7, 17, vcc
	v_cmp_eq_u32_e32 vcc, 0, v10
	v_cmp_gt_f32_e64 s[16:17], v28, v6
	s_and_b64 vcc, vcc, s[16:17]
	s_mov_b32 s16, 0x80000
	v_cndmask_b32_e32 v6, v6, v28, vcc
	v_bitop3_b32 v10, v38, s16, v3 bitop3:0xc8
	v_cndmask_b32_e64 v7, v7, 18, vcc
	v_cmp_eq_u32_e32 vcc, 0, v10
	v_cmp_gt_f32_e64 s[16:17], v29, v6
	s_and_b64 vcc, vcc, s[16:17]
	s_mov_b32 s16, 0x100000
	v_cndmask_b32_e32 v6, v6, v29, vcc
	v_bitop3_b32 v10, v38, s16, v3 bitop3:0xc8
	v_cndmask_b32_e64 v7, v7, 19, vcc
	v_cmp_eq_u32_e32 vcc, 0, v10
	v_cmp_gt_f32_e64 s[16:17], v12, v6
	s_and_b64 vcc, vcc, s[16:17]
	s_mov_b32 s16, 0x200000
	v_cndmask_b32_e32 v6, v6, v12, vcc
	v_bitop3_b32 v10, v38, s16, v3 bitop3:0xc8
	v_cndmask_b32_e64 v7, v7, 20, vcc
	v_cmp_eq_u32_e32 vcc, 0, v10
	v_cmp_gt_f32_e64 s[16:17], v13, v6
	s_and_b64 vcc, vcc, s[16:17]
	s_mov_b32 s16, 0x400000
	v_cndmask_b32_e32 v6, v6, v13, vcc
	v_bitop3_b32 v10, v38, s16, v3 bitop3:0xc8
	v_cndmask_b32_e64 v7, v7, 21, vcc
	v_cmp_eq_u32_e32 vcc, 0, v10
	v_cmp_gt_f32_e64 s[16:17], v4, v6
	s_and_b64 vcc, vcc, s[16:17]
	s_mov_b32 s16, 0x800000
	v_cndmask_b32_e32 v4, v6, v4, vcc
	v_cndmask_b32_e64 v6, v7, 22, vcc
	v_bitop3_b32 v7, v38, s16, v3 bitop3:0xc8
	v_cmp_eq_u32_e32 vcc, 0, v7
	v_cmp_gt_f32_e64 s[16:17], v5, v4
	s_and_b64 vcc, vcc, s[16:17]
	s_mov_b32 s16, 0x1000000
	v_cndmask_b32_e32 v4, v4, v5, vcc
	v_cndmask_b32_e64 v5, v6, 23, vcc
	v_bitop3_b32 v6, v38, s16, v3 bitop3:0xc8
	v_cmp_eq_u32_e32 vcc, 0, v6
	v_cmp_gt_f32_e64 s[16:17], v14, v4
	s_and_b64 vcc, vcc, s[16:17]
	v_cndmask_b32_e32 v4, v4, v14, vcc
	v_bitop3_b32 v6, v38, s61, v3 bitop3:0xc8
	v_cndmask_b32_e64 v5, v5, 24, vcc
	v_cmp_eq_u32_e32 vcc, 0, v6
	v_cmp_gt_f32_e64 s[16:17], v15, v4
	s_and_b64 vcc, vcc, s[16:17]
	v_cndmask_b32_e32 v4, v4, v15, vcc
	v_bitop3_b32 v6, v38, s62, v3 bitop3:0xc8
	v_cndmask_b32_e64 v5, v5, 25, vcc
	v_cmp_eq_u32_e32 vcc, 0, v6
	v_cmp_gt_f32_e64 s[16:17], v26, v4
	s_and_b64 vcc, vcc, s[16:17]
	v_cndmask_b32_e32 v4, v4, v26, vcc
	v_bitop3_b32 v6, v38, s63, v3 bitop3:0xc8
	v_cndmask_b32_e64 v5, v5, 26, vcc
	v_cmp_eq_u32_e32 vcc, 0, v6
	v_cmp_gt_f32_e64 s[16:17], v27, v4
	s_and_b64 vcc, vcc, s[16:17]
	v_cndmask_b32_e32 v4, v4, v27, vcc
	v_bitop3_b32 v6, v38, s64, v3 bitop3:0xc8
	v_cndmask_b32_e64 v5, v5, 27, vcc
	v_cmp_eq_u32_e32 vcc, 0, v6
	v_cmp_gt_f32_e64 s[16:17], v16, v4
	s_and_b64 vcc, vcc, s[16:17]
	v_cndmask_b32_e32 v4, v4, v16, vcc
	v_bitop3_b32 v6, v38, s65, v3 bitop3:0xc8
	v_cndmask_b32_e64 v5, v5, 28, vcc
	v_cmp_eq_u32_e32 vcc, 0, v6
	v_cmp_gt_f32_e64 s[16:17], v17, v4
	s_and_b64 vcc, vcc, s[16:17]
	v_or_b32_e32 v88, v38, v3
	v_cndmask_b32_e32 v4, v4, v17, vcc
	v_bitop3_b32 v3, v38, 2.0, v3 bitop3:0xc8
	v_cndmask_b32_e64 v5, v5, 29, vcc
	v_cmp_eq_u32_e32 vcc, 0, v3
	v_cmp_gt_f32_e64 s[16:17], v8, v4
	s_and_b64 vcc, vcc, s[16:17]
	v_cndmask_b32_e32 v3, v4, v8, vcc
	v_cndmask_b32_e64 v4, v5, 30, vcc
	v_cmp_lt_i32_e32 vcc, -1, v88
	v_cmp_gt_f32_e64 s[16:17], v9, v3
	s_and_b64 vcc, vcc, s[16:17]
	v_cndmask_b32_e32 v5, v3, v9, vcc
	v_cndmask_b32_e64 v3, v4, 31, vcc
	v_sub_f32_e32 v4, v36, v36
	v_mul_f32_e32 v4, 0x3fb8aa3b, v4
	v_exp_f32_e32 v10, v4
	v_sub_f32_e32 v4, v37, v36
	v_mul_f32_e32 v4, 0x3fb8aa3b, v4
	v_exp_f32_e32 v11, v4
	v_sub_f32_e32 v4, v39, v36
	v_mul_f32_e32 v4, 0x3fb8aa3b, v4
	v_exp_f32_e32 v12, v4
	v_sub_f32_e32 v4, v5, v36
	v_mul_f32_e32 v4, 0x3fb8aa3b, v4
	v_exp_f32_e32 v13, v4
	v_add_f32_e32 v4, 0, v10
	v_add_f32_e32 v4, v4, v11
	v_add_f32_e32 v4, v4, v12
	v_add_f32_e32 v14, v4, v13
	v_div_scale_f32 v15, s[16:17], v14, v14, v10
	v_rcp_f32_e32 v16, v15
	v_lshl_add_u32 v4, s66, 8, v94
	v_ashrrev_i32_e32 v5, 31, v4
	v_lshlrev_b64 v[6:7], 2, v[4:5]
	v_fma_f32 v5, -v15, v16, 1.0
	v_fmac_f32_e32 v16, v5, v16
	v_div_scale_f32 v5, vcc, v10, v14, v10
	v_mul_f32_e32 v17, v5, v16
	v_fma_f32 v18, -v15, v17, v5
	v_fmac_f32_e32 v17, v18, v16
	v_fma_f32 v5, -v15, v17, v5
	v_div_fmas_f32 v5, v5, v16, v17
	v_div_fixup_f32 v5, v5, v14, v10
	v_div_scale_f32 v10, s[16:17], v14, v14, v11
	v_rcp_f32_e32 v15, v10
	v_lshl_add_u64 v[8:9], s[20:21], 0, v[6:7]
	v_lshl_add_u64 v[6:7], s[22:23], 0, v[6:7]
	global_store_dword v[6:7], v5, off
	v_or_b32_e32 v6, 1, v4
	v_fma_f32 v4, -v10, v15, 1.0
	v_lshl_add_u32 v5, v0, 2, 0
	v_fmac_f32_e32 v15, v4, v15
	v_div_scale_f32 v4, vcc, v11, v14, v11
	ds_add_u32 v5, v109 offset:58624
	v_mul_f32_e32 v5, v4, v15
	v_fma_f32 v16, -v10, v5, v4
	v_fmac_f32_e32 v5, v16, v15
	v_fma_f32 v4, -v10, v5, v4
	v_div_fmas_f32 v4, v4, v15, v5
	v_div_scale_f32 v5, s[16:17], v14, v14, v12
	v_rcp_f32_e32 v15, v5
	v_ashrrev_i32_e32 v7, 31, v6
	v_div_fixup_f32 v4, v4, v14, v11
	v_lshl_add_u64 v[10:11], v[6:7], 2, s[22:23]
	v_lshl_add_u32 v6, v1, 2, 0
	ds_add_u32 v6, v109 offset:58624
	v_fma_f32 v6, -v5, v15, 1.0
	v_fmac_f32_e32 v15, v6, v15
	v_div_scale_f32 v6, vcc, v12, v14, v12
	v_mul_f32_e32 v7, v6, v15
	v_fma_f32 v16, -v5, v7, v6
	v_fmac_f32_e32 v7, v16, v15
	v_fma_f32 v5, -v5, v7, v6
	v_div_scale_f32 v6, s[16:17], v14, v14, v13
	v_div_fmas_f32 v5, v5, v15, v7
	v_rcp_f32_e32 v7, v6
	v_div_fixup_f32 v5, v5, v14, v12
	v_lshl_add_u32 v12, v2, 2, 0
	ds_add_u32 v12, v109 offset:58624
	global_store_dwordx4 v[8:9], v[0:3], off
	s_nop 1
	v_fma_f32 v0, -v6, v7, 1.0
	v_fmac_f32_e32 v7, v0, v7
	v_div_scale_f32 v0, vcc, v13, v14, v13
	v_mul_f32_e32 v1, v0, v7
	v_fma_f32 v2, -v6, v1, v0
	v_fmac_f32_e32 v1, v2, v7
	v_fma_f32 v0, -v6, v1, v0
	v_div_fmas_f32 v0, v0, v7, v1
	v_div_fixup_f32 v6, v0, v14, v13
	global_store_dwordx3 v[10:11], v[4:6], off
	v_lshl_add_u32 v0, v3, 2, 0
	ds_add_u32 v0, v109 offset:58624

.LBB0_3329:
	s_waitcnt vmcnt(0)
	s_barrier
	s_waitcnt vmcnt(0)
	buffer_inv sc1
	s_waitcnt vmcnt(0)
	v_readlane_b32 s98, v253, 20
	v_mbcnt_lo_u32_b32 v216, -1, 0
	v_mbcnt_hi_u32_b32 v216, -1, v216
	s_lshr_b32 s99, s98, 1
	s_and_b32 s100, s98, 1
	v_lshrrev_b32_e32 v217, 5, v216
	v_and_b32_e32 v216, 31, v216
	s_lshl_b32 s101, s99, 4
	v_add_u32_e32 v218, s101, v217
	v_lshlrev_b32_e32 v219, 7, v218
	v_lshl_add_u32 v219, v216, 2, v219
	v_add_u32_e32 v219, 0xa400, v219
	v_mul_u32_u24_e32 v218, 0x110, v218
	s_lshl_b32 s101, s100, 7
	v_add_u32_e32 v218, s101, v218
	v_lshl_add_u32 v218, v216, 2, v218
	v_add_u32_e32 v218, 0x6000, v218
	s_lshl_b32 s101, s99, 13
	s_lshl_b32 s100, s100, 12
	s_add_i32 s101, s101, s100
	v_lshlrev_b32_e32 v217, 9, v217
	v_add_u32_e32 v217, s101, v217
	v_lshl_add_u32 v217, v216, 2, v217
	s_and_saveexec_b64 s[16:17], s[4:5]
	ds_write_b32 v95, v45 offset:58624
	s_or_b64 exec, exec, s[16:17]
	v_add_u32_e32 v0, s96, v42
	v_ashrrev_i32_e32 v1, 31, v0
	v_lshlrev_b64 v[0:1], 11, v[0:1]
	v_lshl_add_u64 v[92:93], v[46:47], 0, v[0:1]
	global_load_dwordx4 v[30:33], v[92:93], off
	global_load_dwordx4 v[34:37], v[48:49], off
	global_load_dwordx4 v[20:23], v[52:53], off
	global_load_dwordx4 v[24:27], v[92:93], off offset:128
	ds_read_b64 v[38:39], v106 offset:20480
	ds_read_b128 v[116:119], v43 offset:12288
	ds_read_b128 v[120:123], v43 offset:12304
	ds_read_b128 v[124:127], v43 offset:16384
	ds_read_b128 v[128:131], v43 offset:16400
	v_add_u32_e32 v114, 0x6000, v97
	v_mov_b32_e32 v4, 0
	s_waitcnt lgkmcnt(4)
	v_mov_b32_e32 v0, v38
	v_mov_b32_e32 v1, v38
	v_mov_b32_e32 v2, v38
	v_mov_b32_e32 v3, v38
	v_mov_b32_e32 v88, v39
	v_mov_b32_e32 v89, v39
	v_mov_b32_e32 v90, v39
	v_mov_b32_e32 v91, v39
	v_add_u32_e32 v113, 0x6400, v97
	s_mov_b32 s16, 0
	v_mov_b32_e32 v28, v103
	v_mov_b32_e32 v5, v4
	v_mov_b32_e32 v6, v4
	v_mov_b32_e32 v7, v4
	v_mov_b32_e32 v8, v4
	v_mov_b32_e32 v9, v4
	v_mov_b32_e32 v10, v4
	v_mov_b32_e32 v11, v4
	v_mov_b32_e32 v12, v4
	v_mov_b32_e32 v13, v4
	v_mov_b32_e32 v14, v4
	v_mov_b32_e32 v15, v4
	v_mov_b32_e32 v16, v4
	v_mov_b32_e32 v17, v4
	v_mov_b32_e32 v18, v4
	s_waitcnt vmcnt(3)
	v_cvt_f32_f16_sdwa v19, v31 dst_sel:DWORD dst_unused:UNUSED_PAD src0_sel:WORD_1
	v_cvt_f32_f16_e32 v29, v31
	v_cvt_f32_f16_sdwa v31, v30 dst_sel:DWORD dst_unused:UNUSED_PAD src0_sel:WORD_1
	v_cvt_f32_f16_e32 v30, v30
	v_cvt_f32_f16_sdwa v115, v33 dst_sel:DWORD dst_unused:UNUSED_PAD src0_sel:WORD_1
	v_cvt_f32_f16_e32 v134, v33
	v_cvt_f32_f16_sdwa v133, v32 dst_sel:DWORD dst_unused:UNUSED_PAD src0_sel:WORD_1
	v_cvt_f32_f16_e32 v132, v32
	v_sub_f32_e32 v30, v30, v38
	v_sub_f32_e32 v31, v31, v38
	v_sub_f32_e32 v32, v29, v38
	v_sub_f32_e32 v33, v19, v38
	v_sub_f32_e32 v132, v132, v38
	v_sub_f32_e32 v133, v133, v38
	v_sub_f32_e32 v134, v134, v38
	v_sub_f32_e32 v135, v115, v38
	v_pk_mul_f32 v[30:31], v[38:39], v[30:31] op_sel:[1,0]
	v_pk_mul_f32 v[32:33], v[38:39], v[32:33] op_sel:[1,0]
	v_pk_mul_f32 v[134:135], v[38:39], v[134:135] op_sel:[1,0]
	v_pk_mul_f32 v[38:39], v[38:39], v[132:133] op_sel:[1,0]
	s_waitcnt lgkmcnt(1)
	v_fma_f32 v19, v116, v30, v124
	v_fma_f32 v30, v117, v31, v125
	s_waitcnt lgkmcnt(0)
	v_fma_f32 v29, v120, v38, v128
	v_fma_f32 v31, v121, v39, v129
	v_fma_f32 v32, v118, v32, v126
	v_fma_f32 v38, v122, v134, v130
	v_fmac_f32_e32 v127, v119, v33
	v_fmac_f32_e32 v131, v123, v135
	ds_write2_b32 v114, v19, v30 offset1:68
	ds_write2_b32 v113, v29, v31 offset0:16 offset1:84
	ds_write2_b32 v114, v32, v127 offset0:136 offset1:204
	ds_write2_b32 v113, v38, v131 offset0:152 offset1:220
	s_waitcnt vmcnt(2)
	ds_write_b128 v96, v[34:37] offset:41984
	v_mov_b32_e32 v19, v4
	s_waitcnt lgkmcnt(0)
	s_barrier
	ds_read_b32 v200, v218
	ds_read_b32 v208, v219
	ds_read_b32 v201, v218 offset:544
	ds_read_b32 v209, v219 offset:256
	ds_read_b32 v202, v218 offset:1088
	ds_read_b32 v210, v219 offset:512
	ds_read_b32 v203, v218 offset:1632
	ds_read_b32 v211, v219 offset:768
	ds_read_b32 v204, v218 offset:2176
	ds_read_b32 v212, v219 offset:1024
	ds_read_b32 v205, v218 offset:2720
	ds_read_b32 v213, v219 offset:1280
	ds_read_b32 v206, v218 offset:3264
	ds_read_b32 v214, v219 offset:1536
	s_waitcnt lgkmcnt(12)
	v_mfma_f32_32x32x2_f32 v[4:19], v200, v208, v[4:19]
	ds_read_b32 v207, v218 offset:3808
	ds_read_b32 v215, v219 offset:1792
	s_waitcnt lgkmcnt(12)
	v_mfma_f32_32x32x2_f32 v[4:19], v201, v209, v[4:19]
	s_waitcnt lgkmcnt(10)
	v_mfma_f32_32x32x2_f32 v[4:19], v202, v210, v[4:19]
	s_waitcnt lgkmcnt(8)
	v_mfma_f32_32x32x2_f32 v[4:19], v203, v211, v[4:19]
	s_waitcnt lgkmcnt(6)
	v_mfma_f32_32x32x2_f32 v[4:19], v204, v212, v[4:19]
	s_waitcnt lgkmcnt(4)
	v_mfma_f32_32x32x2_f32 v[4:19], v205, v213, v[4:19]
	s_waitcnt lgkmcnt(2)
	v_mfma_f32_32x32x2_f32 v[4:19], v206, v214, v[4:19]
	s_waitcnt lgkmcnt(0)
	v_mfma_f32_32x32x2_f32 v[4:19], v207, v215, v[4:19]
	s_barrier
	global_load_dwordx4 v[32:35], v[92:93], off offset:256
	global_load_dwordx4 v[28:31], v[54:55], off
	s_waitcnt vmcnt(2)
	v_cvt_f32_f16_sdwa v128, v24 dst_sel:DWORD dst_unused:UNUSED_PAD src0_sel:WORD_1
	v_cvt_f32_f16_e32 v24, v24
	v_cvt_f32_f16_e32 v129, v25
	v_cvt_f32_f16_sdwa v130, v26 dst_sel:DWORD dst_unused:UNUSED_PAD src0_sel:WORD_1
	v_cvt_f32_f16_e32 v133, v26
	ds_read_b128 v[36:39], v43 offset:12544
	ds_read_b128 v[116:119], v43 offset:12560
	ds_read_b128 v[120:123], v43 offset:16640
	ds_read_b128 v[124:127], v43 offset:16656
	v_cvt_f32_f16_sdwa v115, v25 dst_sel:DWORD dst_unused:UNUSED_PAD src0_sel:WORD_1
	v_cvt_f32_f16_sdwa v131, v27 dst_sel:DWORD dst_unused:UNUSED_PAD src0_sel:WORD_1
	v_cvt_f32_f16_e32 v132, v27
	v_sub_f32_e32 v24, v24, v0
	v_sub_f32_e32 v25, v128, v1
	v_sub_f32_e32 v26, v129, v2
	v_pk_mul_f32 v[24:25], v[88:89], v[24:25]
	v_sub_f32_e32 v128, v133, v0
	v_sub_f32_e32 v129, v130, v1
	v_sub_f32_e32 v27, v115, v3
	v_sub_f32_e32 v130, v132, v2
	v_sub_f32_e32 v131, v131, v3
	v_pk_mul_f32 v[128:129], v[88:89], v[128:129]
	s_waitcnt lgkmcnt(1)
	v_fma_f32 v24, v36, v24, v120
	v_fma_f32 v25, v37, v25, v121
	v_pk_mul_f32 v[26:27], v[90:91], v[26:27]
	v_pk_mul_f32 v[130:131], v[90:91], v[130:131]
	s_waitcnt lgkmcnt(0)
	v_fma_f32 v36, v116, v128, v124
	ds_write2_b32 v114, v24, v25 offset1:68
	v_fma_f32 v24, v117, v129, v125
	ds_write2_b32 v113, v36, v24 offset0:16 offset1:84
	v_fma_f32 v24, v38, v26, v122
	v_fma_f32 v25, v118, v130, v126
	v_fmac_f32_e32 v123, v39, v27
	v_fmac_f32_e32 v127, v119, v131
	ds_write2_b32 v114, v24, v123 offset0:136 offset1:204
	ds_write2_b32 v113, v25, v127 offset0:152 offset1:220
	ds_write_b128 v96, v[20:23] offset:41984
	s_mov_b32 s16, 0
	v_mov_b32_e32 v20, v103
	s_waitcnt lgkmcnt(0)
	s_barrier
	ds_read_b32 v200, v218
	ds_read_b32 v208, v219
	ds_read_b32 v201, v218 offset:544
	ds_read_b32 v209, v219 offset:256
	ds_read_b32 v202, v218 offset:1088
	ds_read_b32 v210, v219 offset:512
	ds_read_b32 v203, v218 offset:1632
	ds_read_b32 v211, v219 offset:768
	ds_read_b32 v204, v218 offset:2176
	ds_read_b32 v212, v219 offset:1024
	ds_read_b32 v205, v218 offset:2720
	ds_read_b32 v213, v219 offset:1280
	ds_read_b32 v206, v218 offset:3264
	ds_read_b32 v214, v219 offset:1536
	s_waitcnt lgkmcnt(12)
	v_mfma_f32_32x32x2_f32 v[4:19], v200, v208, v[4:19]
	ds_read_b32 v207, v218 offset:3808
	ds_read_b32 v215, v219 offset:1792
	s_waitcnt lgkmcnt(12)
	v_mfma_f32_32x32x2_f32 v[4:19], v201, v209, v[4:19]
	s_waitcnt lgkmcnt(10)
	v_mfma_f32_32x32x2_f32 v[4:19], v202, v210, v[4:19]
	s_waitcnt lgkmcnt(8)
	v_mfma_f32_32x32x2_f32 v[4:19], v203, v211, v[4:19]
	s_waitcnt lgkmcnt(6)
	v_mfma_f32_32x32x2_f32 v[4:19], v204, v212, v[4:19]
	s_waitcnt lgkmcnt(4)
	v_mfma_f32_32x32x2_f32 v[4:19], v205, v213, v[4:19]
	s_waitcnt lgkmcnt(2)
	v_mfma_f32_32x32x2_f32 v[4:19], v206, v214, v[4:19]
	s_waitcnt lgkmcnt(0)
	v_mfma_f32_32x32x2_f32 v[4:19], v207, v215, v[4:19]
	s_barrier
	global_load_dwordx4 v[36:39], v[92:93], off offset:384
	global_load_dwordx4 v[20:23], v[56:57], off
	s_waitcnt vmcnt(3)
	v_cvt_f32_f16_sdwa v128, v32 dst_sel:DWORD dst_unused:UNUSED_PAD src0_sel:WORD_1
	v_cvt_f32_f16_e32 v32, v32
	v_cvt_f32_f16_e32 v129, v33
	v_cvt_f32_f16_sdwa v130, v34 dst_sel:DWORD dst_unused:UNUSED_PAD src0_sel:WORD_1
	v_cvt_f32_f16_e32 v133, v34
	ds_read_b128 v[24:27], v43 offset:12800
	ds_read_b128 v[116:119], v43 offset:12816
	ds_read_b128 v[120:123], v43 offset:16896
	ds_read_b128 v[124:127], v43 offset:16912
	v_cvt_f32_f16_sdwa v115, v33 dst_sel:DWORD dst_unused:UNUSED_PAD src0_sel:WORD_1
	v_cvt_f32_f16_sdwa v131, v35 dst_sel:DWORD dst_unused:UNUSED_PAD src0_sel:WORD_1
	v_cvt_f32_f16_e32 v132, v35
	v_sub_f32_e32 v32, v32, v0
	v_sub_f32_e32 v33, v128, v1
	v_sub_f32_e32 v34, v129, v2
	v_pk_mul_f32 v[32:33], v[88:89], v[32:33]
	v_sub_f32_e32 v128, v133, v0
	v_sub_f32_e32 v129, v130, v1
	v_sub_f32_e32 v35, v115, v3
	v_pk_mul_f32 v[128:129], v[88:89], v[128:129]
	s_waitcnt lgkmcnt(1)
	v_fma_f32 v24, v24, v32, v120
	v_fma_f32 v25, v25, v33, v121
	v_pk_mul_f32 v[34:35], v[90:91], v[34:35]
	v_sub_f32_e32 v130, v132, v2
	v_sub_f32_e32 v131, v131, v3
	s_waitcnt lgkmcnt(0)
	v_fma_f32 v32, v116, v128, v124
	ds_write2_b32 v114, v24, v25 offset1:68
	v_fma_f32 v24, v117, v129, v125
	v_pk_mul_f32 v[130:131], v[90:91], v[130:131]
	ds_write2_b32 v113, v32, v24 offset0:16 offset1:84
	v_fma_f32 v24, v26, v34, v122
	v_fmac_f32_e32 v123, v27, v35
	v_fma_f32 v25, v118, v130, v126
	ds_write2_b32 v114, v24, v123 offset0:136 offset1:204
	v_fmac_f32_e32 v127, v119, v131
	s_mov_b32 s16, 0
	v_mov_b32_e32 v24, v103
	ds_write2_b32 v113, v25, v127 offset0:152 offset1:220
	s_waitcnt vmcnt(2)
	ds_write_b128 v96, v[28:31] offset:41984
	s_waitcnt lgkmcnt(0)
	s_barrier
	ds_read_b32 v200, v218
	ds_read_b32 v208, v219
	ds_read_b32 v201, v218 offset:544
	ds_read_b32 v209, v219 offset:256
	ds_read_b32 v202, v218 offset:1088
	ds_read_b32 v210, v219 offset:512
	ds_read_b32 v203, v218 offset:1632
	ds_read_b32 v211, v219 offset:768
	ds_read_b32 v204, v218 offset:2176
	ds_read_b32 v212, v219 offset:1024
	ds_read_b32 v205, v218 offset:2720
	ds_read_b32 v213, v219 offset:1280
	ds_read_b32 v206, v218 offset:3264
	ds_read_b32 v214, v219 offset:1536
	s_waitcnt lgkmcnt(12)
	v_mfma_f32_32x32x2_f32 v[4:19], v200, v208, v[4:19]
	ds_read_b32 v207, v218 offset:3808
	ds_read_b32 v215, v219 offset:1792
	s_waitcnt lgkmcnt(12)
	v_mfma_f32_32x32x2_f32 v[4:19], v201, v209, v[4:19]
	s_waitcnt lgkmcnt(10)
	v_mfma_f32_32x32x2_f32 v[4:19], v202, v210, v[4:19]
	s_waitcnt lgkmcnt(8)
	v_mfma_f32_32x32x2_f32 v[4:19], v203, v211, v[4:19]
	s_waitcnt lgkmcnt(6)
	v_mfma_f32_32x32x2_f32 v[4:19], v204, v212, v[4:19]
	s_waitcnt lgkmcnt(4)
	v_mfma_f32_32x32x2_f32 v[4:19], v205, v213, v[4:19]
	s_waitcnt lgkmcnt(2)
	v_mfma_f32_32x32x2_f32 v[4:19], v206, v214, v[4:19]
	s_waitcnt lgkmcnt(0)
	v_mfma_f32_32x32x2_f32 v[4:19], v207, v215, v[4:19]
	s_barrier
	global_load_dwordx4 v[28:31], v[92:93], off offset:512
	global_load_dwordx4 v[24:27], v[58:59], off
	s_waitcnt vmcnt(3)
	v_cvt_f32_f16_sdwa v128, v36 dst_sel:DWORD dst_unused:UNUSED_PAD src0_sel:WORD_1
	v_cvt_f32_f16_e32 v36, v36
	v_cvt_f32_f16_e32 v129, v37
	v_cvt_f32_f16_sdwa v130, v38 dst_sel:DWORD dst_unused:UNUSED_PAD src0_sel:WORD_1
	v_cvt_f32_f16_e32 v133, v38
	ds_read_b128 v[32:35], v43 offset:13056
	ds_read_b128 v[116:119], v43 offset:13072
	ds_read_b128 v[120:123], v43 offset:17152
	ds_read_b128 v[124:127], v43 offset:17168
	v_cvt_f32_f16_sdwa v115, v37 dst_sel:DWORD dst_unused:UNUSED_PAD src0_sel:WORD_1
	v_cvt_f32_f16_sdwa v131, v39 dst_sel:DWORD dst_unused:UNUSED_PAD src0_sel:WORD_1
	v_cvt_f32_f16_e32 v132, v39
	v_sub_f32_e32 v36, v36, v0
	v_sub_f32_e32 v37, v128, v1
	v_sub_f32_e32 v38, v129, v2
	v_pk_mul_f32 v[36:37], v[88:89], v[36:37]
	v_sub_f32_e32 v128, v133, v0
	v_sub_f32_e32 v129, v130, v1
	v_sub_f32_e32 v39, v115, v3
	v_sub_f32_e32 v130, v132, v2
	v_sub_f32_e32 v131, v131, v3
	v_pk_mul_f32 v[128:129], v[88:89], v[128:129]
	s_waitcnt lgkmcnt(1)
	v_fma_f32 v32, v32, v36, v120
	v_fma_f32 v33, v33, v37, v121
	v_pk_mul_f32 v[38:39], v[90:91], v[38:39]
	v_pk_mul_f32 v[130:131], v[90:91], v[130:131]
	s_waitcnt lgkmcnt(0)
	v_fma_f32 v36, v116, v128, v124
	ds_write2_b32 v114, v32, v33 offset1:68
	v_fma_f32 v32, v117, v129, v125
	ds_write2_b32 v113, v36, v32 offset0:16 offset1:84
	v_fma_f32 v32, v34, v38, v122
	v_fma_f32 v33, v118, v130, v126
	v_fmac_f32_e32 v123, v35, v39
	v_fmac_f32_e32 v127, v119, v131
	ds_write2_b32 v114, v32, v123 offset0:136 offset1:204
	ds_write2_b32 v113, v33, v127 offset0:152 offset1:220
	s_waitcnt vmcnt(2)
	ds_write_b128 v96, v[20:23] offset:41984
	s_mov_b32 s16, 0
	v_mov_b32_e32 v20, v103
	s_waitcnt lgkmcnt(0)
	s_barrier
	ds_read_b32 v200, v218
	ds_read_b32 v208, v219
	ds_read_b32 v201, v218 offset:544
	ds_read_b32 v209, v219 offset:256
	ds_read_b32 v202, v218 offset:1088
	ds_read_b32 v210, v219 offset:512
	ds_read_b32 v203, v218 offset:1632
	ds_read_b32 v211, v219 offset:768
	ds_read_b32 v204, v218 offset:2176
	ds_read_b32 v212, v219 offset:1024
	ds_read_b32 v205, v218 offset:2720
	ds_read_b32 v213, v219 offset:1280
	ds_read_b32 v206, v218 offset:3264
	ds_read_b32 v214, v219 offset:1536
	s_waitcnt lgkmcnt(12)
	v_mfma_f32_32x32x2_f32 v[4:19], v200, v208, v[4:19]
	ds_read_b32 v207, v218 offset:3808
	ds_read_b32 v215, v219 offset:1792
	s_waitcnt lgkmcnt(12)
	v_mfma_f32_32x32x2_f32 v[4:19], v201, v209, v[4:19]
	s_waitcnt lgkmcnt(10)
	v_mfma_f32_32x32x2_f32 v[4:19], v202, v210, v[4:19]
	s_waitcnt lgkmcnt(8)
	v_mfma_f32_32x32x2_f32 v[4:19], v203, v211, v[4:19]
	s_waitcnt lgkmcnt(6)
	v_mfma_f32_32x32x2_f32 v[4:19], v204, v212, v[4:19]
	s_waitcnt lgkmcnt(4)
	v_mfma_f32_32x32x2_f32 v[4:19], v205, v213, v[4:19]
	s_waitcnt lgkmcnt(2)
	v_mfma_f32_32x32x2_f32 v[4:19], v206, v214, v[4:19]
	s_waitcnt lgkmcnt(0)
	v_mfma_f32_32x32x2_f32 v[4:19], v207, v215, v[4:19]
	s_barrier
	global_load_dwordx4 v[32:35], v[92:93], off offset:640
	global_load_dwordx4 v[20:23], v[60:61], off
	s_waitcnt vmcnt(3)
	v_cvt_f32_f16_sdwa v128, v28 dst_sel:DWORD dst_unused:UNUSED_PAD src0_sel:WORD_1
	v_cvt_f32_f16_e32 v28, v28
	v_cvt_f32_f16_e32 v129, v29
	v_cvt_f32_f16_sdwa v130, v30 dst_sel:DWORD dst_unused:UNUSED_PAD src0_sel:WORD_1
	v_cvt_f32_f16_e32 v133, v30
	ds_read_b128 v[36:39], v43 offset:13312
	ds_read_b128 v[116:119], v43 offset:13328
	ds_read_b128 v[120:123], v43 offset:17408
	ds_read_b128 v[124:127], v43 offset:17424
	v_cvt_f32_f16_sdwa v115, v29 dst_sel:DWORD dst_unused:UNUSED_PAD src0_sel:WORD_1
	v_cvt_f32_f16_sdwa v131, v31 dst_sel:DWORD dst_unused:UNUSED_PAD src0_sel:WORD_1
	v_cvt_f32_f16_e32 v132, v31
	v_sub_f32_e32 v28, v28, v0
	v_sub_f32_e32 v29, v128, v1
	v_sub_f32_e32 v30, v129, v2
	v_pk_mul_f32 v[28:29], v[88:89], v[28:29]
	v_sub_f32_e32 v128, v133, v0
	v_sub_f32_e32 v129, v130, v1
	v_sub_f32_e32 v31, v115, v3
	v_sub_f32_e32 v130, v132, v2
	v_sub_f32_e32 v131, v131, v3
	v_pk_mul_f32 v[128:129], v[88:89], v[128:129]
	s_waitcnt lgkmcnt(1)
	v_fma_f32 v28, v36, v28, v120
	v_fma_f32 v29, v37, v29, v121
	v_pk_mul_f32 v[30:31], v[90:91], v[30:31]
	v_pk_mul_f32 v[130:131], v[90:91], v[130:131]
	s_waitcnt lgkmcnt(0)
	v_fma_f32 v36, v116, v128, v124
	ds_write2_b32 v114, v28, v29 offset1:68
	v_fma_f32 v28, v117, v129, v125
	ds_write2_b32 v113, v36, v28 offset0:16 offset1:84
	v_fma_f32 v28, v38, v30, v122
	v_fma_f32 v29, v118, v130, v126
	v_fmac_f32_e32 v123, v39, v31
	v_fmac_f32_e32 v127, v119, v131
	ds_write2_b32 v114, v28, v123 offset0:136 offset1:204
	ds_write2_b32 v113, v29, v127 offset0:152 offset1:220
	s_waitcnt vmcnt(2)
	ds_write_b128 v96, v[24:27] offset:41984
	s_mov_b32 s16, 0
	v_mov_b32_e32 v24, v103
	s_waitcnt lgkmcnt(0)
	s_barrier
	ds_read_b32 v200, v218
	ds_read_b32 v208, v219
	ds_read_b32 v201, v218 offset:544
	ds_read_b32 v209, v219 offset:256
	ds_read_b32 v202, v218 offset:1088
	ds_read_b32 v210, v219 offset:512
	ds_read_b32 v203, v218 offset:1632
	ds_read_b32 v211, v219 offset:768
	ds_read_b32 v204, v218 offset:2176
	ds_read_b32 v212, v219 offset:1024
	ds_read_b32 v205, v218 offset:2720
	ds_read_b32 v213, v219 offset:1280
	ds_read_b32 v206, v218 offset:3264
	ds_read_b32 v214, v219 offset:1536
	s_waitcnt lgkmcnt(12)
	v_mfma_f32_32x32x2_f32 v[4:19], v200, v208, v[4:19]
	ds_read_b32 v207, v218 offset:3808
	ds_read_b32 v215, v219 offset:1792
	s_waitcnt lgkmcnt(12)
	v_mfma_f32_32x32x2_f32 v[4:19], v201, v209, v[4:19]
	s_waitcnt lgkmcnt(10)
	v_mfma_f32_32x32x2_f32 v[4:19], v202, v210, v[4:19]
	s_waitcnt lgkmcnt(8)
	v_mfma_f32_32x32x2_f32 v[4:19], v203, v211, v[4:19]
	s_waitcnt lgkmcnt(6)
	v_mfma_f32_32x32x2_f32 v[4:19], v204, v212, v[4:19]
	s_waitcnt lgkmcnt(4)
	v_mfma_f32_32x32x2_f32 v[4:19], v205, v213, v[4:19]
	s_waitcnt lgkmcnt(2)
	v_mfma_f32_32x32x2_f32 v[4:19], v206, v214, v[4:19]
	s_waitcnt lgkmcnt(0)
	v_mfma_f32_32x32x2_f32 v[4:19], v207, v215, v[4:19]
	s_barrier
	global_load_dwordx4 v[28:31], v[92:93], off offset:768
	global_load_dwordx4 v[24:27], v[62:63], off
	s_waitcnt vmcnt(3)
	v_cvt_f32_f16_sdwa v128, v32 dst_sel:DWORD dst_unused:UNUSED_PAD src0_sel:WORD_1
	v_cvt_f32_f16_e32 v32, v32
	v_cvt_f32_f16_e32 v129, v33
	v_cvt_f32_f16_sdwa v130, v34 dst_sel:DWORD dst_unused:UNUSED_PAD src0_sel:WORD_1
	v_cvt_f32_f16_e32 v133, v34
	ds_read_b128 v[36:39], v43 offset:13568
	ds_read_b128 v[116:119], v43 offset:13584
	ds_read_b128 v[120:123], v43 offset:17664
	ds_read_b128 v[124:127], v43 offset:17680
	v_cvt_f32_f16_sdwa v115, v33 dst_sel:DWORD dst_unused:UNUSED_PAD src0_sel:WORD_1
	v_cvt_f32_f16_sdwa v131, v35 dst_sel:DWORD dst_unused:UNUSED_PAD src0_sel:WORD_1
	v_cvt_f32_f16_e32 v132, v35
	v_sub_f32_e32 v32, v32, v0
	v_sub_f32_e32 v33, v128, v1
	v_sub_f32_e32 v34, v129, v2
	v_pk_mul_f32 v[32:33], v[88:89], v[32:33]
	v_sub_f32_e32 v128, v133, v0
	v_sub_f32_e32 v129, v130, v1
	v_sub_f32_e32 v35, v115, v3
	v_sub_f32_e32 v130, v132, v2
	v_sub_f32_e32 v131, v131, v3
	v_pk_mul_f32 v[128:129], v[88:89], v[128:129]
	s_waitcnt lgkmcnt(1)
	v_fma_f32 v32, v36, v32, v120
	v_fma_f32 v33, v37, v33, v121
	v_pk_mul_f32 v[34:35], v[90:91], v[34:35]
	v_pk_mul_f32 v[130:131], v[90:91], v[130:131]
	s_waitcnt lgkmcnt(0)
	v_fma_f32 v36, v116, v128, v124
	ds_write2_b32 v114, v32, v33 offset1:68
	v_fma_f32 v32, v117, v129, v125
	ds_write2_b32 v113, v36, v32 offset0:16 offset1:84
	v_fma_f32 v32, v38, v34, v122
	v_fma_f32 v33, v118, v130, v126
	v_fmac_f32_e32 v123, v39, v35
	v_fmac_f32_e32 v127, v119, v131
	ds_write2_b32 v114, v32, v123 offset0:136 offset1:204
	ds_write2_b32 v113, v33, v127 offset0:152 offset1:220
	s_waitcnt vmcnt(2)
	ds_write_b128 v96, v[20:23] offset:41984
	s_mov_b32 s16, 0
	v_mov_b32_e32 v20, v103
	s_waitcnt lgkmcnt(0)
	s_barrier
	ds_read_b32 v200, v218
	ds_read_b32 v208, v219
	ds_read_b32 v201, v218 offset:544
	ds_read_b32 v209, v219 offset:256
	ds_read_b32 v202, v218 offset:1088
	ds_read_b32 v210, v219 offset:512
	ds_read_b32 v203, v218 offset:1632
	ds_read_b32 v211, v219 offset:768
	ds_read_b32 v204, v218 offset:2176
	ds_read_b32 v212, v219 offset:1024
	ds_read_b32 v205, v218 offset:2720
	ds_read_b32 v213, v219 offset:1280
	ds_read_b32 v206, v218 offset:3264
	ds_read_b32 v214, v219 offset:1536
	s_waitcnt lgkmcnt(12)
	v_mfma_f32_32x32x2_f32 v[4:19], v200, v208, v[4:19]
	ds_read_b32 v207, v218 offset:3808
	ds_read_b32 v215, v219 offset:1792
	s_waitcnt lgkmcnt(12)
	v_mfma_f32_32x32x2_f32 v[4:19], v201, v209, v[4:19]
	s_waitcnt lgkmcnt(10)
	v_mfma_f32_32x32x2_f32 v[4:19], v202, v210, v[4:19]
	s_waitcnt lgkmcnt(8)
	v_mfma_f32_32x32x2_f32 v[4:19], v203, v211, v[4:19]
	s_waitcnt lgkmcnt(6)
	v_mfma_f32_32x32x2_f32 v[4:19], v204, v212, v[4:19]
	s_waitcnt lgkmcnt(4)
	v_mfma_f32_32x32x2_f32 v[4:19], v205, v213, v[4:19]
	s_waitcnt lgkmcnt(2)
	v_mfma_f32_32x32x2_f32 v[4:19], v206, v214, v[4:19]
	s_waitcnt lgkmcnt(0)
	v_mfma_f32_32x32x2_f32 v[4:19], v207, v215, v[4:19]
	s_barrier
	global_load_dwordx4 v[32:35], v[92:93], off offset:896
	global_load_dwordx4 v[20:23], v[64:65], off
	s_waitcnt vmcnt(3)
	v_cvt_f32_f16_sdwa v128, v28 dst_sel:DWORD dst_unused:UNUSED_PAD src0_sel:WORD_1
	v_cvt_f32_f16_e32 v28, v28
	v_cvt_f32_f16_e32 v129, v29
	v_cvt_f32_f16_sdwa v130, v30 dst_sel:DWORD dst_unused:UNUSED_PAD src0_sel:WORD_1
	v_cvt_f32_f16_e32 v133, v30
	ds_read_b128 v[36:39], v43 offset:13824
	ds_read_b128 v[116:119], v43 offset:13840
	ds_read_b128 v[120:123], v43 offset:17920
	ds_read_b128 v[124:127], v43 offset:17936
	v_cvt_f32_f16_sdwa v115, v29 dst_sel:DWORD dst_unused:UNUSED_PAD src0_sel:WORD_1
	v_cvt_f32_f16_sdwa v131, v31 dst_sel:DWORD dst_unused:UNUSED_PAD src0_sel:WORD_1
	v_cvt_f32_f16_e32 v132, v31
	v_sub_f32_e32 v28, v28, v0
	v_sub_f32_e32 v29, v128, v1
	v_sub_f32_e32 v30, v129, v2
	v_pk_mul_f32 v[28:29], v[88:89], v[28:29]
	v_sub_f32_e32 v128, v133, v0
	v_sub_f32_e32 v129, v130, v1
	v_sub_f32_e32 v31, v115, v3
	v_sub_f32_e32 v130, v132, v2
	v_sub_f32_e32 v131, v131, v3
	v_pk_mul_f32 v[128:129], v[88:89], v[128:129]
	s_waitcnt lgkmcnt(1)
	v_fma_f32 v28, v36, v28, v120
	v_fma_f32 v29, v37, v29, v121
	v_pk_mul_f32 v[30:31], v[90:91], v[30:31]
	v_pk_mul_f32 v[130:131], v[90:91], v[130:131]
	s_waitcnt lgkmcnt(0)
	v_fma_f32 v36, v116, v128, v124
	ds_write2_b32 v114, v28, v29 offset1:68
	v_fma_f32 v28, v117, v129, v125
	ds_write2_b32 v113, v36, v28 offset0:16 offset1:84
	v_fma_f32 v28, v38, v30, v122
	v_fma_f32 v29, v118, v130, v126
	v_fmac_f32_e32 v123, v39, v31
	v_fmac_f32_e32 v127, v119, v131
	ds_write2_b32 v114, v28, v123 offset0:136 offset1:204
	ds_write2_b32 v113, v29, v127 offset0:152 offset1:220
	s_waitcnt vmcnt(2)
	ds_write_b128 v96, v[24:27] offset:41984
	s_mov_b32 s16, 0
	v_mov_b32_e32 v24, v103
	s_waitcnt lgkmcnt(0)
	s_barrier
	ds_read_b32 v200, v218
	ds_read_b32 v208, v219
	ds_read_b32 v201, v218 offset:544
	ds_read_b32 v209, v219 offset:256
	ds_read_b32 v202, v218 offset:1088
	ds_read_b32 v210, v219 offset:512
	ds_read_b32 v203, v218 offset:1632
	ds_read_b32 v211, v219 offset:768
	ds_read_b32 v204, v218 offset:2176
	ds_read_b32 v212, v219 offset:1024
	ds_read_b32 v205, v218 offset:2720
	ds_read_b32 v213, v219 offset:1280
	ds_read_b32 v206, v218 offset:3264
	ds_read_b32 v214, v219 offset:1536
	s_waitcnt lgkmcnt(12)
	v_mfma_f32_32x32x2_f32 v[4:19], v200, v208, v[4:19]
	ds_read_b32 v207, v218 offset:3808
	ds_read_b32 v215, v219 offset:1792
	s_waitcnt lgkmcnt(12)
	v_mfma_f32_32x32x2_f32 v[4:19], v201, v209, v[4:19]
	s_waitcnt lgkmcnt(10)
	v_mfma_f32_32x32x2_f32 v[4:19], v202, v210, v[4:19]
	s_waitcnt lgkmcnt(8)
	v_mfma_f32_32x32x2_f32 v[4:19], v203, v211, v[4:19]
	s_waitcnt lgkmcnt(6)
	v_mfma_f32_32x32x2_f32 v[4:19], v204, v212, v[4:19]
	s_waitcnt lgkmcnt(4)
	v_mfma_f32_32x32x2_f32 v[4:19], v205, v213, v[4:19]
	s_waitcnt lgkmcnt(2)
	v_mfma_f32_32x32x2_f32 v[4:19], v206, v214, v[4:19]
	s_waitcnt lgkmcnt(0)
	v_mfma_f32_32x32x2_f32 v[4:19], v207, v215, v[4:19]
	s_barrier
	global_load_dwordx4 v[28:31], v[92:93], off offset:1024
	global_load_dwordx4 v[24:27], v[66:67], off
	s_waitcnt vmcnt(3)
	v_cvt_f32_f16_sdwa v128, v32 dst_sel:DWORD dst_unused:UNUSED_PAD src0_sel:WORD_1
	v_cvt_f32_f16_e32 v32, v32
	v_cvt_f32_f16_e32 v129, v33
	v_cvt_f32_f16_sdwa v130, v34 dst_sel:DWORD dst_unused:UNUSED_PAD src0_sel:WORD_1
	v_cvt_f32_f16_e32 v133, v34
	ds_read_b128 v[36:39], v43 offset:14080
	ds_read_b128 v[116:119], v43 offset:14096
	ds_read_b128 v[120:123], v43 offset:18176
	ds_read_b128 v[124:127], v43 offset:18192
	v_cvt_f32_f16_sdwa v115, v33 dst_sel:DWORD dst_unused:UNUSED_PAD src0_sel:WORD_1
	v_cvt_f32_f16_sdwa v131, v35 dst_sel:DWORD dst_unused:UNUSED_PAD src0_sel:WORD_1
	v_cvt_f32_f16_e32 v132, v35
	v_sub_f32_e32 v32, v32, v0
	v_sub_f32_e32 v33, v128, v1
	v_sub_f32_e32 v34, v129, v2
	v_pk_mul_f32 v[32:33], v[88:89], v[32:33]
	v_sub_f32_e32 v128, v133, v0
	v_sub_f32_e32 v129, v130, v1
	v_sub_f32_e32 v35, v115, v3
	v_sub_f32_e32 v130, v132, v2
	v_sub_f32_e32 v131, v131, v3
	v_pk_mul_f32 v[128:129], v[88:89], v[128:129]
	s_waitcnt lgkmcnt(1)
	v_fma_f32 v32, v36, v32, v120
	v_fma_f32 v33, v37, v33, v121
	v_pk_mul_f32 v[34:35], v[90:91], v[34:35]
	v_pk_mul_f32 v[130:131], v[90:91], v[130:131]
	s_waitcnt lgkmcnt(0)
	v_fma_f32 v36, v116, v128, v124
	ds_write2_b32 v114, v32, v33 offset1:68
	v_fma_f32 v32, v117, v129, v125
	ds_write2_b32 v113, v36, v32 offset0:16 offset1:84
	v_fma_f32 v32, v38, v34, v122
	v_fma_f32 v33, v118, v130, v126
	v_fmac_f32_e32 v123, v39, v35
	v_fmac_f32_e32 v127, v119, v131
	ds_write2_b32 v114, v32, v123 offset0:136 offset1:204
	ds_write2_b32 v113, v33, v127 offset0:152 offset1:220
	s_waitcnt vmcnt(2)
	ds_write_b128 v96, v[20:23] offset:41984
	s_mov_b32 s16, 0
	v_mov_b32_e32 v20, v103
	s_waitcnt lgkmcnt(0)
	s_barrier
	ds_read_b32 v200, v218
	ds_read_b32 v208, v219
	ds_read_b32 v201, v218 offset:544
	ds_read_b32 v209, v219 offset:256
	ds_read_b32 v202, v218 offset:1088
	ds_read_b32 v210, v219 offset:512
	ds_read_b32 v203, v218 offset:1632
	ds_read_b32 v211, v219 offset:768
	ds_read_b32 v204, v218 offset:2176
	ds_read_b32 v212, v219 offset:1024
	ds_read_b32 v205, v218 offset:2720
	ds_read_b32 v213, v219 offset:1280
	ds_read_b32 v206, v218 offset:3264
	ds_read_b32 v214, v219 offset:1536
	s_waitcnt lgkmcnt(12)
	v_mfma_f32_32x32x2_f32 v[4:19], v200, v208, v[4:19]
	ds_read_b32 v207, v218 offset:3808
	ds_read_b32 v215, v219 offset:1792
	s_waitcnt lgkmcnt(12)
	v_mfma_f32_32x32x2_f32 v[4:19], v201, v209, v[4:19]
	s_waitcnt lgkmcnt(10)
	v_mfma_f32_32x32x2_f32 v[4:19], v202, v210, v[4:19]
	s_waitcnt lgkmcnt(8)
	v_mfma_f32_32x32x2_f32 v[4:19], v203, v211, v[4:19]
	s_waitcnt lgkmcnt(6)
	v_mfma_f32_32x32x2_f32 v[4:19], v204, v212, v[4:19]
	s_waitcnt lgkmcnt(4)
	v_mfma_f32_32x32x2_f32 v[4:19], v205, v213, v[4:19]
	s_waitcnt lgkmcnt(2)
	v_mfma_f32_32x32x2_f32 v[4:19], v206, v214, v[4:19]
	s_waitcnt lgkmcnt(0)
	v_mfma_f32_32x32x2_f32 v[4:19], v207, v215, v[4:19]
	s_barrier
	global_load_dwordx4 v[32:35], v[92:93], off offset:1152
	global_load_dwordx4 v[20:23], v[68:69], off
	s_waitcnt vmcnt(3)
	v_cvt_f32_f16_sdwa v128, v28 dst_sel:DWORD dst_unused:UNUSED_PAD src0_sel:WORD_1
	v_cvt_f32_f16_e32 v28, v28
	v_cvt_f32_f16_e32 v129, v29
	v_cvt_f32_f16_sdwa v130, v30 dst_sel:DWORD dst_unused:UNUSED_PAD src0_sel:WORD_1
	v_cvt_f32_f16_e32 v133, v30
	ds_read_b128 v[36:39], v43 offset:14336
	ds_read_b128 v[116:119], v43 offset:14352
	ds_read_b128 v[120:123], v43 offset:18432
	ds_read_b128 v[124:127], v43 offset:18448
	v_cvt_f32_f16_sdwa v115, v29 dst_sel:DWORD dst_unused:UNUSED_PAD src0_sel:WORD_1
	v_cvt_f32_f16_sdwa v131, v31 dst_sel:DWORD dst_unused:UNUSED_PAD src0_sel:WORD_1
	v_cvt_f32_f16_e32 v132, v31
	v_sub_f32_e32 v28, v28, v0
	v_sub_f32_e32 v29, v128, v1
	v_sub_f32_e32 v30, v129, v2
	v_pk_mul_f32 v[28:29], v[88:89], v[28:29]
	v_sub_f32_e32 v128, v133, v0
	v_sub_f32_e32 v129, v130, v1
	v_sub_f32_e32 v31, v115, v3
	v_sub_f32_e32 v130, v132, v2
	v_sub_f32_e32 v131, v131, v3
	v_pk_mul_f32 v[128:129], v[88:89], v[128:129]
	s_waitcnt lgkmcnt(1)
	v_fma_f32 v28, v36, v28, v120
	v_fma_f32 v29, v37, v29, v121
	v_pk_mul_f32 v[30:31], v[90:91], v[30:31]
	v_pk_mul_f32 v[130:131], v[90:91], v[130:131]
	s_waitcnt lgkmcnt(0)
	v_fma_f32 v36, v116, v128, v124
	ds_write2_b32 v114, v28, v29 offset1:68
	v_fma_f32 v28, v117, v129, v125
	ds_write2_b32 v113, v36, v28 offset0:16 offset1:84
	v_fma_f32 v28, v38, v30, v122
	v_fma_f32 v29, v118, v130, v126
	v_fmac_f32_e32 v123, v39, v31
	v_fmac_f32_e32 v127, v119, v131
	ds_write2_b32 v114, v28, v123 offset0:136 offset1:204
	ds_write2_b32 v113, v29, v127 offset0:152 offset1:220
	s_waitcnt vmcnt(2)
	ds_write_b128 v96, v[24:27] offset:41984
	s_mov_b32 s16, 0
	v_mov_b32_e32 v24, v103
	s_waitcnt lgkmcnt(0)
	s_barrier
	ds_read_b32 v200, v218
	ds_read_b32 v208, v219
	ds_read_b32 v201, v218 offset:544
	ds_read_b32 v209, v219 offset:256
	ds_read_b32 v202, v218 offset:1088
	ds_read_b32 v210, v219 offset:512
	ds_read_b32 v203, v218 offset:1632
	ds_read_b32 v211, v219 offset:768
	ds_read_b32 v204, v218 offset:2176
	ds_read_b32 v212, v219 offset:1024
	ds_read_b32 v205, v218 offset:2720
	ds_read_b32 v213, v219 offset:1280
	ds_read_b32 v206, v218 offset:3264
	ds_read_b32 v214, v219 offset:1536
	s_waitcnt lgkmcnt(12)
	v_mfma_f32_32x32x2_f32 v[4:19], v200, v208, v[4:19]
	ds_read_b32 v207, v218 offset:3808
	ds_read_b32 v215, v219 offset:1792
	s_waitcnt lgkmcnt(12)
	v_mfma_f32_32x32x2_f32 v[4:19], v201, v209, v[4:19]
	s_waitcnt lgkmcnt(10)
	v_mfma_f32_32x32x2_f32 v[4:19], v202, v210, v[4:19]
	s_waitcnt lgkmcnt(8)
	v_mfma_f32_32x32x2_f32 v[4:19], v203, v211, v[4:19]
	s_waitcnt lgkmcnt(6)
	v_mfma_f32_32x32x2_f32 v[4:19], v204, v212, v[4:19]
	s_waitcnt lgkmcnt(4)
	v_mfma_f32_32x32x2_f32 v[4:19], v205, v213, v[4:19]
	s_waitcnt lgkmcnt(2)
	v_mfma_f32_32x32x2_f32 v[4:19], v206, v214, v[4:19]
	s_waitcnt lgkmcnt(0)
	v_mfma_f32_32x32x2_f32 v[4:19], v207, v215, v[4:19]
	s_barrier
	global_load_dwordx4 v[28:31], v[92:93], off offset:1280
	global_load_dwordx4 v[24:27], v[70:71], off
	s_waitcnt vmcnt(3)
	v_cvt_f32_f16_sdwa v128, v32 dst_sel:DWORD dst_unused:UNUSED_PAD src0_sel:WORD_1
	v_cvt_f32_f16_e32 v32, v32
	v_cvt_f32_f16_e32 v129, v33
	v_cvt_f32_f16_sdwa v130, v34 dst_sel:DWORD dst_unused:UNUSED_PAD src0_sel:WORD_1
	v_cvt_f32_f16_e32 v133, v34
	ds_read_b128 v[36:39], v43 offset:14592
	ds_read_b128 v[116:119], v43 offset:14608
	ds_read_b128 v[120:123], v43 offset:18688
	ds_read_b128 v[124:127], v43 offset:18704
	v_cvt_f32_f16_sdwa v115, v33 dst_sel:DWORD dst_unused:UNUSED_PAD src0_sel:WORD_1
	v_cvt_f32_f16_sdwa v131, v35 dst_sel:DWORD dst_unused:UNUSED_PAD src0_sel:WORD_1
	v_cvt_f32_f16_e32 v132, v35
	v_sub_f32_e32 v32, v32, v0
	v_sub_f32_e32 v33, v128, v1
	v_sub_f32_e32 v34, v129, v2
	v_pk_mul_f32 v[32:33], v[88:89], v[32:33]
	v_sub_f32_e32 v128, v133, v0
	v_sub_f32_e32 v129, v130, v1
	v_sub_f32_e32 v35, v115, v3
	v_sub_f32_e32 v130, v132, v2
	v_sub_f32_e32 v131, v131, v3
	v_pk_mul_f32 v[128:129], v[88:89], v[128:129]
	s_waitcnt lgkmcnt(1)
	v_fma_f32 v32, v36, v32, v120
	v_fma_f32 v33, v37, v33, v121
	v_pk_mul_f32 v[34:35], v[90:91], v[34:35]
	v_pk_mul_f32 v[130:131], v[90:91], v[130:131]
	s_waitcnt lgkmcnt(0)
	v_fma_f32 v36, v116, v128, v124
	ds_write2_b32 v114, v32, v33 offset1:68
	v_fma_f32 v32, v117, v129, v125
	ds_write2_b32 v113, v36, v32 offset0:16 offset1:84
	v_fma_f32 v32, v38, v34, v122
	v_fma_f32 v33, v118, v130, v126
	v_fmac_f32_e32 v123, v39, v35
	v_fmac_f32_e32 v127, v119, v131
	ds_write2_b32 v114, v32, v123 offset0:136 offset1:204
	ds_write2_b32 v113, v33, v127 offset0:152 offset1:220
	s_waitcnt vmcnt(2)
	ds_write_b128 v96, v[20:23] offset:41984
	s_mov_b32 s16, 0
	v_mov_b32_e32 v20, v103
	s_waitcnt lgkmcnt(0)
	s_barrier
	ds_read_b32 v200, v218
	ds_read_b32 v208, v219
	ds_read_b32 v201, v218 offset:544
	ds_read_b32 v209, v219 offset:256
	ds_read_b32 v202, v218 offset:1088
	ds_read_b32 v210, v219 offset:512
	ds_read_b32 v203, v218 offset:1632
	ds_read_b32 v211, v219 offset:768
	ds_read_b32 v204, v218 offset:2176
	ds_read_b32 v212, v219 offset:1024
	ds_read_b32 v205, v218 offset:2720
	ds_read_b32 v213, v219 offset:1280
	ds_read_b32 v206, v218 offset:3264
	ds_read_b32 v214, v219 offset:1536
	s_waitcnt lgkmcnt(12)
	v_mfma_f32_32x32x2_f32 v[4:19], v200, v208, v[4:19]
	ds_read_b32 v207, v218 offset:3808
	ds_read_b32 v215, v219 offset:1792
	s_waitcnt lgkmcnt(12)
	v_mfma_f32_32x32x2_f32 v[4:19], v201, v209, v[4:19]
	s_waitcnt lgkmcnt(10)
	v_mfma_f32_32x32x2_f32 v[4:19], v202, v210, v[4:19]
	s_waitcnt lgkmcnt(8)
	v_mfma_f32_32x32x2_f32 v[4:19], v203, v211, v[4:19]
	s_waitcnt lgkmcnt(6)
	v_mfma_f32_32x32x2_f32 v[4:19], v204, v212, v[4:19]
	s_waitcnt lgkmcnt(4)
	v_mfma_f32_32x32x2_f32 v[4:19], v205, v213, v[4:19]
	s_waitcnt lgkmcnt(2)
	v_mfma_f32_32x32x2_f32 v[4:19], v206, v214, v[4:19]
	s_waitcnt lgkmcnt(0)
	v_mfma_f32_32x32x2_f32 v[4:19], v207, v215, v[4:19]
	s_barrier
	global_load_dwordx4 v[32:35], v[92:93], off offset:1408
	global_load_dwordx4 v[20:23], v[72:73], off
	s_waitcnt vmcnt(3)
	v_cvt_f32_f16_sdwa v128, v28 dst_sel:DWORD dst_unused:UNUSED_PAD src0_sel:WORD_1
	v_cvt_f32_f16_e32 v28, v28
	v_cvt_f32_f16_e32 v129, v29
	v_cvt_f32_f16_sdwa v130, v30 dst_sel:DWORD dst_unused:UNUSED_PAD src0_sel:WORD_1
	v_cvt_f32_f16_e32 v133, v30
	ds_read_b128 v[36:39], v43 offset:14848
	ds_read_b128 v[116:119], v43 offset:14864
	ds_read_b128 v[120:123], v43 offset:18944
	ds_read_b128 v[124:127], v43 offset:18960
	v_cvt_f32_f16_sdwa v115, v29 dst_sel:DWORD dst_unused:UNUSED_PAD src0_sel:WORD_1
	v_cvt_f32_f16_sdwa v131, v31 dst_sel:DWORD dst_unused:UNUSED_PAD src0_sel:WORD_1
	v_cvt_f32_f16_e32 v132, v31
	v_sub_f32_e32 v28, v28, v0
	v_sub_f32_e32 v29, v128, v1
	v_sub_f32_e32 v30, v129, v2
	v_pk_mul_f32 v[28:29], v[88:89], v[28:29]
	v_sub_f32_e32 v128, v133, v0
	v_sub_f32_e32 v129, v130, v1
	v_sub_f32_e32 v31, v115, v3
	v_sub_f32_e32 v130, v132, v2
	v_sub_f32_e32 v131, v131, v3
	v_pk_mul_f32 v[128:129], v[88:89], v[128:129]
	s_waitcnt lgkmcnt(1)
	v_fma_f32 v28, v36, v28, v120
	v_fma_f32 v29, v37, v29, v121
	v_pk_mul_f32 v[30:31], v[90:91], v[30:31]
	v_pk_mul_f32 v[130:131], v[90:91], v[130:131]
	s_waitcnt lgkmcnt(0)
	v_fma_f32 v36, v116, v128, v124
	ds_write2_b32 v114, v28, v29 offset1:68
	v_fma_f32 v28, v117, v129, v125
	ds_write2_b32 v113, v36, v28 offset0:16 offset1:84
	v_fma_f32 v28, v38, v30, v122
	v_fma_f32 v29, v118, v130, v126
	v_fmac_f32_e32 v123, v39, v31
	v_fmac_f32_e32 v127, v119, v131
	ds_write2_b32 v114, v28, v123 offset0:136 offset1:204
	ds_write2_b32 v113, v29, v127 offset0:152 offset1:220
	s_waitcnt vmcnt(2)
	ds_write_b128 v96, v[24:27] offset:41984
	s_mov_b32 s16, 0
	v_mov_b32_e32 v24, v103
	s_waitcnt lgkmcnt(0)
	s_barrier
	ds_read_b32 v200, v218
	ds_read_b32 v208, v219
	ds_read_b32 v201, v218 offset:544
	ds_read_b32 v209, v219 offset:256
	ds_read_b32 v202, v218 offset:1088
	ds_read_b32 v210, v219 offset:512
	ds_read_b32 v203, v218 offset:1632
	ds_read_b32 v211, v219 offset:768
	ds_read_b32 v204, v218 offset:2176
	ds_read_b32 v212, v219 offset:1024
	ds_read_b32 v205, v218 offset:2720
	ds_read_b32 v213, v219 offset:1280
	ds_read_b32 v206, v218 offset:3264
	ds_read_b32 v214, v219 offset:1536
	s_waitcnt lgkmcnt(12)
	v_mfma_f32_32x32x2_f32 v[4:19], v200, v208, v[4:19]
	ds_read_b32 v207, v218 offset:3808
	ds_read_b32 v215, v219 offset:1792
	s_waitcnt lgkmcnt(12)
	v_mfma_f32_32x32x2_f32 v[4:19], v201, v209, v[4:19]
	s_waitcnt lgkmcnt(10)
	v_mfma_f32_32x32x2_f32 v[4:19], v202, v210, v[4:19]
	s_waitcnt lgkmcnt(8)
	v_mfma_f32_32x32x2_f32 v[4:19], v203, v211, v[4:19]
	s_waitcnt lgkmcnt(6)
	v_mfma_f32_32x32x2_f32 v[4:19], v204, v212, v[4:19]
	s_waitcnt lgkmcnt(4)
	v_mfma_f32_32x32x2_f32 v[4:19], v205, v213, v[4:19]
	s_waitcnt lgkmcnt(2)
	v_mfma_f32_32x32x2_f32 v[4:19], v206, v214, v[4:19]
	s_waitcnt lgkmcnt(0)
	v_mfma_f32_32x32x2_f32 v[4:19], v207, v215, v[4:19]
	s_barrier
	global_load_dwordx4 v[28:31], v[92:93], off offset:1536
	global_load_dwordx4 v[24:27], v[74:75], off
	s_waitcnt vmcnt(3)
	v_cvt_f32_f16_sdwa v128, v32 dst_sel:DWORD dst_unused:UNUSED_PAD src0_sel:WORD_1
	v_cvt_f32_f16_e32 v32, v32
	v_cvt_f32_f16_e32 v129, v33
	v_cvt_f32_f16_sdwa v130, v34 dst_sel:DWORD dst_unused:UNUSED_PAD src0_sel:WORD_1
	v_cvt_f32_f16_e32 v133, v34
	ds_read_b128 v[36:39], v43 offset:15104
	ds_read_b128 v[116:119], v43 offset:15120
	ds_read_b128 v[120:123], v43 offset:19200
	ds_read_b128 v[124:127], v43 offset:19216
	v_cvt_f32_f16_sdwa v115, v33 dst_sel:DWORD dst_unused:UNUSED_PAD src0_sel:WORD_1
	v_cvt_f32_f16_sdwa v131, v35 dst_sel:DWORD dst_unused:UNUSED_PAD src0_sel:WORD_1
	v_cvt_f32_f16_e32 v132, v35
	v_sub_f32_e32 v32, v32, v0
	v_sub_f32_e32 v33, v128, v1
	v_sub_f32_e32 v34, v129, v2
	v_pk_mul_f32 v[32:33], v[88:89], v[32:33]
	v_sub_f32_e32 v128, v133, v0
	v_sub_f32_e32 v129, v130, v1
	v_sub_f32_e32 v35, v115, v3
	v_sub_f32_e32 v130, v132, v2
	v_sub_f32_e32 v131, v131, v3
	v_pk_mul_f32 v[128:129], v[88:89], v[128:129]
	s_waitcnt lgkmcnt(1)
	v_fma_f32 v32, v36, v32, v120
	v_fma_f32 v33, v37, v33, v121
	v_pk_mul_f32 v[34:35], v[90:91], v[34:35]
	v_pk_mul_f32 v[130:131], v[90:91], v[130:131]
	s_waitcnt lgkmcnt(0)
	v_fma_f32 v36, v116, v128, v124
	ds_write2_b32 v114, v32, v33 offset1:68
	v_fma_f32 v32, v117, v129, v125
	ds_write2_b32 v113, v36, v32 offset0:16 offset1:84
	v_fma_f32 v32, v38, v34, v122
	v_fma_f32 v33, v118, v130, v126
	v_fmac_f32_e32 v123, v39, v35
	v_fmac_f32_e32 v127, v119, v131
	ds_write2_b32 v114, v32, v123 offset0:136 offset1:204
	ds_write2_b32 v113, v33, v127 offset0:152 offset1:220
	s_waitcnt vmcnt(2)
	ds_write_b128 v96, v[20:23] offset:41984
	s_mov_b32 s16, 0
	v_mov_b32_e32 v20, v103
	s_waitcnt lgkmcnt(0)
	s_barrier
	ds_read_b32 v200, v218
	ds_read_b32 v208, v219
	ds_read_b32 v201, v218 offset:544
	ds_read_b32 v209, v219 offset:256
	ds_read_b32 v202, v218 offset:1088
	ds_read_b32 v210, v219 offset:512
	ds_read_b32 v203, v218 offset:1632
	ds_read_b32 v211, v219 offset:768
	ds_read_b32 v204, v218 offset:2176
	ds_read_b32 v212, v219 offset:1024
	ds_read_b32 v205, v218 offset:2720
	ds_read_b32 v213, v219 offset:1280
	ds_read_b32 v206, v218 offset:3264
	ds_read_b32 v214, v219 offset:1536
	s_waitcnt lgkmcnt(12)
	v_mfma_f32_32x32x2_f32 v[4:19], v200, v208, v[4:19]
	ds_read_b32 v207, v218 offset:3808
	ds_read_b32 v215, v219 offset:1792
	s_waitcnt lgkmcnt(12)
	v_mfma_f32_32x32x2_f32 v[4:19], v201, v209, v[4:19]
	s_waitcnt lgkmcnt(10)
	v_mfma_f32_32x32x2_f32 v[4:19], v202, v210, v[4:19]
	s_waitcnt lgkmcnt(8)
	v_mfma_f32_32x32x2_f32 v[4:19], v203, v211, v[4:19]
	s_waitcnt lgkmcnt(6)
	v_mfma_f32_32x32x2_f32 v[4:19], v204, v212, v[4:19]
	s_waitcnt lgkmcnt(4)
	v_mfma_f32_32x32x2_f32 v[4:19], v205, v213, v[4:19]
	s_waitcnt lgkmcnt(2)
	v_mfma_f32_32x32x2_f32 v[4:19], v206, v214, v[4:19]
	s_waitcnt lgkmcnt(0)
	v_mfma_f32_32x32x2_f32 v[4:19], v207, v215, v[4:19]
	s_barrier
	global_load_dwordx4 v[32:35], v[92:93], off offset:1664
	global_load_dwordx4 v[20:23], v[76:77], off
	s_waitcnt vmcnt(3)
	v_cvt_f32_f16_sdwa v128, v28 dst_sel:DWORD dst_unused:UNUSED_PAD src0_sel:WORD_1
	v_cvt_f32_f16_e32 v28, v28
	v_cvt_f32_f16_e32 v129, v29
	v_cvt_f32_f16_sdwa v130, v30 dst_sel:DWORD dst_unused:UNUSED_PAD src0_sel:WORD_1
	v_cvt_f32_f16_e32 v133, v30
	ds_read_b128 v[36:39], v43 offset:15360
	ds_read_b128 v[116:119], v43 offset:15376
	ds_read_b128 v[120:123], v43 offset:19456
	ds_read_b128 v[124:127], v43 offset:19472
	v_cvt_f32_f16_sdwa v115, v29 dst_sel:DWORD dst_unused:UNUSED_PAD src0_sel:WORD_1
	v_cvt_f32_f16_sdwa v131, v31 dst_sel:DWORD dst_unused:UNUSED_PAD src0_sel:WORD_1
	v_cvt_f32_f16_e32 v132, v31
	v_sub_f32_e32 v28, v28, v0
	v_sub_f32_e32 v29, v128, v1
	v_sub_f32_e32 v30, v129, v2
	v_pk_mul_f32 v[28:29], v[88:89], v[28:29]
	v_sub_f32_e32 v128, v133, v0
	v_sub_f32_e32 v129, v130, v1
	v_sub_f32_e32 v31, v115, v3
	v_sub_f32_e32 v130, v132, v2
	v_sub_f32_e32 v131, v131, v3
	v_pk_mul_f32 v[128:129], v[88:89], v[128:129]
	s_waitcnt lgkmcnt(1)
	v_fma_f32 v28, v36, v28, v120
	v_fma_f32 v29, v37, v29, v121
	v_pk_mul_f32 v[30:31], v[90:91], v[30:31]
	v_pk_mul_f32 v[130:131], v[90:91], v[130:131]
	s_waitcnt lgkmcnt(0)
	v_fma_f32 v36, v116, v128, v124
	ds_write2_b32 v114, v28, v29 offset1:68
	v_fma_f32 v28, v117, v129, v125
	ds_write2_b32 v113, v36, v28 offset0:16 offset1:84
	v_fma_f32 v28, v38, v30, v122
	v_fma_f32 v29, v118, v130, v126
	v_fmac_f32_e32 v123, v39, v31
	v_fmac_f32_e32 v127, v119, v131
	ds_write2_b32 v114, v28, v123 offset0:136 offset1:204
	ds_write2_b32 v113, v29, v127 offset0:152 offset1:220
	s_waitcnt vmcnt(2)
	ds_write_b128 v96, v[24:27] offset:41984
	s_mov_b32 s16, 0
	v_mov_b32_e32 v24, v103
	s_waitcnt lgkmcnt(0)
	s_barrier
	ds_read_b32 v200, v218
	ds_read_b32 v208, v219
	ds_read_b32 v201, v218 offset:544
	ds_read_b32 v209, v219 offset:256
	ds_read_b32 v202, v218 offset:1088
	ds_read_b32 v210, v219 offset:512
	ds_read_b32 v203, v218 offset:1632
	ds_read_b32 v211, v219 offset:768
	ds_read_b32 v204, v218 offset:2176
	ds_read_b32 v212, v219 offset:1024
	ds_read_b32 v205, v218 offset:2720
	ds_read_b32 v213, v219 offset:1280
	ds_read_b32 v206, v218 offset:3264
	ds_read_b32 v214, v219 offset:1536
	s_waitcnt lgkmcnt(12)
	v_mfma_f32_32x32x2_f32 v[4:19], v200, v208, v[4:19]
	ds_read_b32 v207, v218 offset:3808
	ds_read_b32 v215, v219 offset:1792
	s_waitcnt lgkmcnt(12)
	v_mfma_f32_32x32x2_f32 v[4:19], v201, v209, v[4:19]
	s_waitcnt lgkmcnt(10)
	v_mfma_f32_32x32x2_f32 v[4:19], v202, v210, v[4:19]
	s_waitcnt lgkmcnt(8)
	v_mfma_f32_32x32x2_f32 v[4:19], v203, v211, v[4:19]
	s_waitcnt lgkmcnt(6)
	v_mfma_f32_32x32x2_f32 v[4:19], v204, v212, v[4:19]
	s_waitcnt lgkmcnt(4)
	v_mfma_f32_32x32x2_f32 v[4:19], v205, v213, v[4:19]
	s_waitcnt lgkmcnt(2)
	v_mfma_f32_32x32x2_f32 v[4:19], v206, v214, v[4:19]
	s_waitcnt lgkmcnt(0)
	v_mfma_f32_32x32x2_f32 v[4:19], v207, v215, v[4:19]
	s_barrier
	global_load_dwordx4 v[28:31], v[92:93], off offset:1792
	global_load_dwordx4 v[24:27], v[78:79], off
	s_waitcnt vmcnt(3)
	v_cvt_f32_f16_sdwa v128, v32 dst_sel:DWORD dst_unused:UNUSED_PAD src0_sel:WORD_1
	v_cvt_f32_f16_e32 v32, v32
	v_cvt_f32_f16_e32 v129, v33
	v_cvt_f32_f16_sdwa v130, v34 dst_sel:DWORD dst_unused:UNUSED_PAD src0_sel:WORD_1
	v_cvt_f32_f16_e32 v133, v34
	ds_read_b128 v[36:39], v43 offset:15616
	ds_read_b128 v[116:119], v43 offset:15632
	ds_read_b128 v[120:123], v43 offset:19712
	ds_read_b128 v[124:127], v43 offset:19728
	v_cvt_f32_f16_sdwa v115, v33 dst_sel:DWORD dst_unused:UNUSED_PAD src0_sel:WORD_1
	v_cvt_f32_f16_sdwa v131, v35 dst_sel:DWORD dst_unused:UNUSED_PAD src0_sel:WORD_1
	v_cvt_f32_f16_e32 v132, v35
	v_sub_f32_e32 v32, v32, v0
	v_sub_f32_e32 v33, v128, v1
	v_sub_f32_e32 v34, v129, v2
	v_pk_mul_f32 v[32:33], v[88:89], v[32:33]
	v_sub_f32_e32 v128, v133, v0
	v_sub_f32_e32 v129, v130, v1
	v_sub_f32_e32 v35, v115, v3
	v_sub_f32_e32 v130, v132, v2
	v_sub_f32_e32 v131, v131, v3
	v_pk_mul_f32 v[128:129], v[88:89], v[128:129]
	s_waitcnt lgkmcnt(1)
	v_fma_f32 v32, v36, v32, v120
	v_fma_f32 v33, v37, v33, v121
	v_pk_mul_f32 v[34:35], v[90:91], v[34:35]
	v_pk_mul_f32 v[130:131], v[90:91], v[130:131]
	s_waitcnt lgkmcnt(0)
	v_fma_f32 v36, v116, v128, v124
	ds_write2_b32 v114, v32, v33 offset1:68
	v_fma_f32 v32, v117, v129, v125
	ds_write2_b32 v113, v36, v32 offset0:16 offset1:84
	v_fma_f32 v32, v38, v34, v122
	v_fma_f32 v33, v118, v130, v126
	v_fmac_f32_e32 v123, v39, v35
	v_fmac_f32_e32 v127, v119, v131
	ds_write2_b32 v114, v32, v123 offset0:136 offset1:204
	ds_write2_b32 v113, v33, v127 offset0:152 offset1:220
	s_waitcnt vmcnt(2)
	ds_write_b128 v96, v[20:23] offset:41984
	s_mov_b32 s16, 0
	v_mov_b32_e32 v20, v103
	s_waitcnt lgkmcnt(0)
	s_barrier
	ds_read_b32 v200, v218
	ds_read_b32 v208, v219
	ds_read_b32 v201, v218 offset:544
	ds_read_b32 v209, v219 offset:256
	ds_read_b32 v202, v218 offset:1088
	ds_read_b32 v210, v219 offset:512
	ds_read_b32 v203, v218 offset:1632
	ds_read_b32 v211, v219 offset:768
	ds_read_b32 v204, v218 offset:2176
	ds_read_b32 v212, v219 offset:1024
	ds_read_b32 v205, v218 offset:2720
	ds_read_b32 v213, v219 offset:1280
	ds_read_b32 v206, v218 offset:3264
	ds_read_b32 v214, v219 offset:1536
	s_waitcnt lgkmcnt(12)
	v_mfma_f32_32x32x2_f32 v[4:19], v200, v208, v[4:19]
	ds_read_b32 v207, v218 offset:3808
	ds_read_b32 v215, v219 offset:1792
	s_waitcnt lgkmcnt(12)
	v_mfma_f32_32x32x2_f32 v[4:19], v201, v209, v[4:19]
	s_waitcnt lgkmcnt(10)
	v_mfma_f32_32x32x2_f32 v[4:19], v202, v210, v[4:19]
	s_waitcnt lgkmcnt(8)
	v_mfma_f32_32x32x2_f32 v[4:19], v203, v211, v[4:19]
	s_waitcnt lgkmcnt(6)
	v_mfma_f32_32x32x2_f32 v[4:19], v204, v212, v[4:19]
	s_waitcnt lgkmcnt(4)
	v_mfma_f32_32x32x2_f32 v[4:19], v205, v213, v[4:19]
	s_waitcnt lgkmcnt(2)
	v_mfma_f32_32x32x2_f32 v[4:19], v206, v214, v[4:19]
	s_waitcnt lgkmcnt(0)
	v_mfma_f32_32x32x2_f32 v[4:19], v207, v215, v[4:19]
	s_barrier
	global_load_dwordx4 v[32:35], v[92:93], off offset:1920
	global_load_dwordx4 v[20:23], v[80:81], off
	s_waitcnt vmcnt(3)
	v_cvt_f32_f16_sdwa v93, v28 dst_sel:DWORD dst_unused:UNUSED_PAD src0_sel:WORD_1
	v_cvt_f32_f16_e32 v28, v28
	v_cvt_f32_f16_sdwa v92, v29 dst_sel:DWORD dst_unused:UNUSED_PAD src0_sel:WORD_1
	v_cvt_f32_f16_sdwa v128, v30 dst_sel:DWORD dst_unused:UNUSED_PAD src0_sel:WORD_1
	v_cvt_f32_f16_e32 v131, v30
	ds_read_b128 v[36:39], v43 offset:15872
	ds_read_b128 v[116:119], v43 offset:15888
	ds_read_b128 v[120:123], v43 offset:19968
	ds_read_b128 v[124:127], v43 offset:19984
	v_cvt_f32_f16_e32 v115, v29
	v_cvt_f32_f16_sdwa v129, v31 dst_sel:DWORD dst_unused:UNUSED_PAD src0_sel:WORD_1
	v_cvt_f32_f16_e32 v130, v31
	v_sub_f32_e32 v28, v28, v0
	v_sub_f32_e32 v29, v93, v1
	v_sub_f32_e32 v31, v92, v3
	v_pk_mul_f32 v[28:29], v[88:89], v[28:29]
	v_sub_f32_e32 v92, v131, v0
	v_sub_f32_e32 v93, v128, v1
	v_sub_f32_e32 v30, v115, v2
	v_sub_f32_e32 v128, v130, v2
	v_sub_f32_e32 v129, v129, v3
	v_pk_mul_f32 v[92:93], v[88:89], v[92:93]
	s_waitcnt lgkmcnt(1)
	v_fma_f32 v28, v36, v28, v120
	v_fma_f32 v29, v37, v29, v121
	v_pk_mul_f32 v[30:31], v[90:91], v[30:31]
	v_pk_mul_f32 v[128:129], v[90:91], v[128:129]
	s_waitcnt lgkmcnt(0)
	v_fma_f32 v36, v116, v92, v124
	ds_write2_b32 v114, v28, v29 offset1:68
	v_fma_f32 v28, v117, v93, v125
	ds_write2_b32 v113, v36, v28 offset0:16 offset1:84
	v_fma_f32 v28, v38, v30, v122
	v_fma_f32 v29, v118, v128, v126
	v_fmac_f32_e32 v123, v39, v31
	v_fmac_f32_e32 v127, v119, v129
	ds_write2_b32 v114, v28, v123 offset0:136 offset1:204
	ds_write2_b32 v113, v29, v127 offset0:152 offset1:220
	s_waitcnt vmcnt(2)
	ds_write_b128 v96, v[24:27] offset:41984
	s_mov_b32 s16, 0
	v_mov_b32_e32 v24, v103
	s_waitcnt lgkmcnt(0)
	s_barrier
	ds_read_b32 v200, v218
	ds_read_b32 v208, v219
	ds_read_b32 v201, v218 offset:544
	ds_read_b32 v209, v219 offset:256
	ds_read_b32 v202, v218 offset:1088
	ds_read_b32 v210, v219 offset:512
	ds_read_b32 v203, v218 offset:1632
	ds_read_b32 v211, v219 offset:768
	ds_read_b32 v204, v218 offset:2176
	ds_read_b32 v212, v219 offset:1024
	ds_read_b32 v205, v218 offset:2720
	ds_read_b32 v213, v219 offset:1280
	ds_read_b32 v206, v218 offset:3264
	ds_read_b32 v214, v219 offset:1536
	s_waitcnt lgkmcnt(12)
	v_mfma_f32_32x32x2_f32 v[4:19], v200, v208, v[4:19]
	ds_read_b32 v207, v218 offset:3808
	ds_read_b32 v215, v219 offset:1792
	s_waitcnt lgkmcnt(12)
	v_mfma_f32_32x32x2_f32 v[4:19], v201, v209, v[4:19]
	s_waitcnt lgkmcnt(10)
	v_mfma_f32_32x32x2_f32 v[4:19], v202, v210, v[4:19]
	s_waitcnt lgkmcnt(8)
	v_mfma_f32_32x32x2_f32 v[4:19], v203, v211, v[4:19]
	s_waitcnt lgkmcnt(6)
	v_mfma_f32_32x32x2_f32 v[4:19], v204, v212, v[4:19]
	s_waitcnt lgkmcnt(4)
	v_mfma_f32_32x32x2_f32 v[4:19], v205, v213, v[4:19]
	s_waitcnt lgkmcnt(2)
	v_mfma_f32_32x32x2_f32 v[4:19], v206, v214, v[4:19]
	s_waitcnt lgkmcnt(0)
	v_mfma_f32_32x32x2_f32 v[4:19], v207, v215, v[4:19]
	s_waitcnt vmcnt(1)
	v_cvt_f32_f16_sdwa v93, v32 dst_sel:DWORD dst_unused:UNUSED_PAD src0_sel:WORD_1
	v_cvt_f32_f16_e32 v32, v32
	v_cvt_f32_f16_sdwa v121, v34 dst_sel:DWORD dst_unused:UNUSED_PAD src0_sel:WORD_1
	v_cvt_f32_f16_e32 v123, v34
	s_barrier
	ds_read_b128 v[24:27], v43 offset:16128
	ds_read_b128 v[28:31], v43 offset:16144
	ds_read_b128 v[36:39], v43 offset:20224
	ds_read_b128 v[116:119], v43 offset:20240
	v_cvt_f32_f16_sdwa v92, v33 dst_sel:DWORD dst_unused:UNUSED_PAD src0_sel:WORD_1
	v_cvt_f32_f16_e32 v115, v33
	v_cvt_f32_f16_sdwa v120, v35 dst_sel:DWORD dst_unused:UNUSED_PAD src0_sel:WORD_1
	v_cvt_f32_f16_e32 v122, v35
	v_sub_f32_e32 v32, v32, v0
	v_sub_f32_e32 v33, v93, v1
	v_sub_f32_e32 v0, v123, v0
	v_sub_f32_e32 v1, v121, v1
	v_sub_f32_e32 v34, v115, v2
	v_sub_f32_e32 v35, v92, v3
	v_pk_mul_f32 v[0:1], v[88:89], v[0:1]
	v_pk_mul_f32 v[34:35], v[90:91], v[34:35]
	v_sub_f32_e32 v2, v122, v2
	v_sub_f32_e32 v3, v120, v3
	s_waitcnt lgkmcnt(0)
	v_fma_f32 v0, v28, v0, v116
	v_fma_f32 v1, v29, v1, v117
	v_pk_mul_f32 v[32:33], v[88:89], v[32:33]
	v_pk_mul_f32 v[2:3], v[90:91], v[2:3]
	ds_write2_b32 v113, v0, v1 offset0:16 offset1:84
	v_fma_f32 v0, v26, v34, v38
	v_fmac_f32_e32 v39, v27, v35
	v_fma_f32 v24, v24, v32, v36
	v_fma_f32 v25, v25, v33, v37
	v_fma_f32 v1, v30, v2, v118
	ds_write2_b32 v114, v0, v39 offset0:136 offset1:204
	v_fmac_f32_e32 v119, v31, v3
	s_mov_b32 s16, 0
	v_mov_b32_e32 v0, v103
	ds_write2_b32 v114, v24, v25 offset1:68
	ds_write2_b32 v113, v1, v119 offset0:152 offset1:220
	s_waitcnt vmcnt(0)
	ds_write_b128 v96, v[20:23] offset:41984
	s_waitcnt lgkmcnt(0)
	s_barrier
	ds_read_b32 v200, v218
	ds_read_b32 v208, v219
	ds_read_b32 v201, v218 offset:544
	ds_read_b32 v209, v219 offset:256
	ds_read_b32 v202, v218 offset:1088
	ds_read_b32 v210, v219 offset:512
	ds_read_b32 v203, v218 offset:1632
	ds_read_b32 v211, v219 offset:768
	ds_read_b32 v204, v218 offset:2176
	ds_read_b32 v212, v219 offset:1024
	ds_read_b32 v205, v218 offset:2720
	ds_read_b32 v213, v219 offset:1280
	ds_read_b32 v206, v218 offset:3264
	ds_read_b32 v214, v219 offset:1536
	s_waitcnt lgkmcnt(12)
	v_mfma_f32_32x32x2_f32 v[4:19], v200, v208, v[4:19]
	ds_read_b32 v207, v218 offset:3808
	ds_read_b32 v215, v219 offset:1792
	s_waitcnt lgkmcnt(12)
	v_mfma_f32_32x32x2_f32 v[4:19], v201, v209, v[4:19]
	s_waitcnt lgkmcnt(10)
	v_mfma_f32_32x32x2_f32 v[4:19], v202, v210, v[4:19]
	s_waitcnt lgkmcnt(8)
	v_mfma_f32_32x32x2_f32 v[4:19], v203, v211, v[4:19]
	s_waitcnt lgkmcnt(6)
	v_mfma_f32_32x32x2_f32 v[4:19], v204, v212, v[4:19]
	s_waitcnt lgkmcnt(4)
	v_mfma_f32_32x32x2_f32 v[4:19], v205, v213, v[4:19]
	s_waitcnt lgkmcnt(2)
	v_mfma_f32_32x32x2_f32 v[4:19], v206, v214, v[4:19]
	s_waitcnt lgkmcnt(0)
	v_mfma_f32_32x32x2_f32 v[4:19], v207, v215, v[4:19]
	s_barrier
	s_nop 15
	s_nop 3
	ds_write_b32 v217, v4 offset:58752
	ds_write_b32 v217, v5 offset:58880
	ds_write_b32 v217, v6 offset:59008
	ds_write_b32 v217, v7 offset:59136
	ds_write_b32 v217, v8 offset:59776
	ds_write_b32 v217, v9 offset:59904
	ds_write_b32 v217, v10 offset:60032
	ds_write_b32 v217, v11 offset:60160
	ds_write_b32 v217, v12 offset:60800
	ds_write_b32 v217, v13 offset:60928
	ds_write_b32 v217, v14 offset:61056
	ds_write_b32 v217, v15 offset:61184
	ds_write_b32 v217, v16 offset:61824
	ds_write_b32 v217, v17 offset:61952
	ds_write_b32 v217, v18 offset:62080
	ds_write_b32 v217, v19 offset:62208
	s_waitcnt lgkmcnt(0)
	s_barrier
	global_load_dwordx4 v[0:3], v[50:51], off offset:384
	ds_read_b128 v[4:7], v98 offset:58752
	ds_read_b128 v[8:11], v99 offset:8192
	ds_read_b128 v[12:15], v99 offset:16384
	ds_read_b128 v[16:19], v99 offset:24576
	v_add_u32_e32 v20, 0xc400, v100
	v_add_u32_e32 v21, 0xc408, v100
	s_waitcnt lgkmcnt(2)
	v_pk_add_f32 v[4:5], v[4:5], v[8:9]
	v_pk_add_f32 v[6:7], v[6:7], v[10:11]
	s_waitcnt lgkmcnt(1)
	v_pk_add_f32 v[4:5], v[12:13], v[4:5]
	v_pk_add_f32 v[6:7], v[14:15], v[6:7]
	s_waitcnt lgkmcnt(0)
	v_pk_add_f32 v[4:5], v[16:17], v[4:5]
	v_pk_add_f32 v[6:7], v[18:19], v[6:7]
	s_waitcnt vmcnt(0)
	v_pk_add_f32 v[0:1], v[0:1], v[4:5]
	v_pk_add_f32 v[2:3], v[6:7], v[2:3]
	ds_write2_b32 v20, v0, v1 offset1:1
	ds_write2_b32 v21, v2, v3 offset1:1
	s_waitcnt lgkmcnt(0)
	s_barrier
	s_and_saveexec_b64 s[36:37], s[6:7]
	s_cbranch_execz .LBB0_3365
	v_add_u32_e32 v0, 0xc400, v108
	v_add_u32_e32 v1, 0xc408, v108
	v_add_u32_e32 v2, 0xc410, v108
	v_add_u32_e32 v3, 0xc418, v108
	ds_read2_b32 v[34:35], v0 offset1:1
	ds_read2_b32 v[28:29], v1 offset1:1
	ds_read2_b32 v[18:19], v2 offset1:1
	ds_read2_b32 v[8:9], v3 offset1:1
	s_mov_b32 s16, 0xff61b1e6
	s_waitcnt lgkmcnt(3)
	v_max_f32_e32 v0, v34, v34
	v_max_f32_e32 v0, 0xff61b1e6, v0
	v_cmp_lt_f32_e32 vcc, s16, v34
	v_cmp_gt_f32_e64 s[16:17], v35, v0
	v_add_u32_e32 v2, 0xc420, v108
	ds_read2_b32 v[20:21], v2 offset1:1
	v_cndmask_b32_e64 v0, v0, v35, s[16:17]
	v_cndmask_b32_e64 v1, 0, 1, s[16:17]
	s_waitcnt lgkmcnt(3)
	v_cmp_gt_f32_e64 s[16:17], v28, v0
	v_add_u32_e32 v2, 0xc428, v108
	v_add_u32_e32 v4, 0xc438, v108
	v_cndmask_b32_e64 v0, v0, v28, s[16:17]
	v_cndmask_b32_e64 v1, v1, 2, s[16:17]
	v_cmp_gt_f32_e64 s[16:17], v29, v0
	v_add_u32_e32 v3, 0xc430, v108
	ds_read2_b32 v[30:31], v2 offset1:1
	ds_read2_b32 v[16:17], v3 offset1:1
	ds_read2_b32 v[4:5], v4 offset1:1
	v_cndmask_b32_e64 v0, v0, v29, s[16:17]
	v_cndmask_b32_e64 v1, v1, 3, s[16:17]
	s_waitcnt lgkmcnt(5)
	v_cmp_gt_f32_e64 s[16:17], v18, v0
	v_add_u32_e32 v2, 0xc440, v108
	ds_read2_b32 v[12:13], v2 offset1:1
	v_cndmask_b32_e64 v0, v0, v18, s[16:17]
	v_cndmask_b32_e64 v1, v1, 4, s[16:17]
	v_cmp_gt_f32_e64 s[16:17], v19, v0
	v_add_u32_e32 v2, 0xc448, v108
	v_add_u32_e32 v6, 0xc458, v108
	v_cndmask_b32_e64 v0, v0, v19, s[16:17]
	v_cndmask_b32_e64 v1, v1, 5, s[16:17]
	s_waitcnt lgkmcnt(5)
	v_cmp_gt_f32_e64 s[16:17], v8, v0
	v_add_u32_e32 v3, 0xc450, v108
	ds_read2_b32 v[26:27], v2 offset1:1
	ds_read2_b32 v[14:15], v3 offset1:1
	ds_read2_b32 v[6:7], v6 offset1:1
	v_cndmask_b32_e64 v0, v0, v8, s[16:17]
	v_cndmask_b32_e64 v1, v1, 6, s[16:17]
	v_cmp_gt_f32_e64 s[16:17], v9, v0
	v_add_u32_e32 v2, 0xc460, v108
	ds_read2_b32 v[22:23], v2 offset1:1
	v_cndmask_b32_e64 v0, v0, v9, s[16:17]
	v_cndmask_b32_e64 v1, v1, 7, s[16:17]
	s_waitcnt lgkmcnt(8)
	v_cmp_gt_f32_e64 s[16:17], v20, v0
	v_add_u32_e32 v2, 0xc468, v108
	v_add_u32_e32 v10, 0xc478, v108
	v_cndmask_b32_e64 v0, v0, v20, s[16:17]
	v_cndmask_b32_e64 v1, v1, 8, s[16:17]
	v_cmp_gt_f32_e64 s[16:17], v21, v0
	v_add_u32_e32 v3, 0xc470, v108
	ds_read2_b32 v[32:33], v2 offset1:1
	ds_read2_b32 v[24:25], v3 offset1:1
	ds_read2_b32 v[10:11], v10 offset1:1
	v_cndmask_b32_e64 v0, v0, v21, s[16:17]
	v_cndmask_b32_e64 v1, v1, 9, s[16:17]
	s_waitcnt lgkmcnt(10)
	v_cmp_gt_f32_e64 s[16:17], v30, v0
	s_nop 1
	v_cndmask_b32_e64 v0, v0, v30, s[16:17]
	v_cndmask_b32_e64 v1, v1, 10, s[16:17]
	v_cmp_gt_f32_e64 s[16:17], v31, v0
	s_nop 1
	v_cndmask_b32_e64 v0, v0, v31, s[16:17]
	v_cndmask_b32_e64 v1, v1, 11, s[16:17]
	s_waitcnt lgkmcnt(9)
	v_cmp_gt_f32_e64 s[16:17], v16, v0
	s_nop 1
	v_cndmask_b32_e64 v0, v0, v16, s[16:17]
	v_cndmask_b32_e64 v1, v1, 12, s[16:17]
	v_cmp_gt_f32_e64 s[16:17], v17, v0
	s_nop 1
	v_cndmask_b32_e64 v0, v0, v17, s[16:17]
	v_cndmask_b32_e64 v1, v1, 13, s[16:17]
	s_waitcnt lgkmcnt(8)
	v_cmp_gt_f32_e64 s[16:17], v4, v0
	s_nop 1
	v_cndmask_b32_e64 v0, v0, v4, s[16:17]
	v_cndmask_b32_e64 v1, v1, 14, s[16:17]
	v_cmp_gt_f32_e64 s[16:17], v5, v0
	s_nop 1
	v_cndmask_b32_e64 v0, v0, v5, s[16:17]
	v_cndmask_b32_e64 v1, v1, 15, s[16:17]
	s_waitcnt lgkmcnt(7)
	v_cmp_gt_f32_e64 s[16:17], v12, v0
	s_nop 1
	v_cndmask_b32_e64 v0, v0, v12, s[16:17]
	v_cndmask_b32_e64 v1, v1, 16, s[16:17]
	v_cmp_gt_f32_e64 s[16:17], v13, v0
	s_nop 1
	v_cndmask_b32_e64 v0, v0, v13, s[16:17]
	v_cndmask_b32_e64 v1, v1, 17, s[16:17]
	s_waitcnt lgkmcnt(6)
	v_cmp_gt_f32_e64 s[16:17], v26, v0
	s_nop 1
	v_cndmask_b32_e64 v0, v0, v26, s[16:17]
	v_cndmask_b32_e64 v1, v1, 18, s[16:17]
	v_cmp_gt_f32_e64 s[16:17], v27, v0
	s_nop 1
	v_cndmask_b32_e64 v0, v0, v27, s[16:17]
	v_cndmask_b32_e64 v1, v1, 19, s[16:17]
	s_waitcnt lgkmcnt(5)
	v_cmp_gt_f32_e64 s[16:17], v14, v0
	s_nop 1
	v_cndmask_b32_e64 v0, v0, v14, s[16:17]
	v_cndmask_b32_e64 v1, v1, 20, s[16:17]
	v_cmp_gt_f32_e64 s[16:17], v15, v0
	s_nop 1
	v_cndmask_b32_e64 v0, v0, v15, s[16:17]
	v_cndmask_b32_e64 v1, v1, 21, s[16:17]
	s_waitcnt lgkmcnt(4)
	v_cmp_gt_f32_e64 s[16:17], v6, v0
	s_nop 1
	v_cndmask_b32_e64 v0, v0, v6, s[16:17]
	v_cndmask_b32_e64 v1, v1, 22, s[16:17]
	v_cmp_gt_f32_e64 s[16:17], v7, v0
	s_nop 1
	v_cndmask_b32_e64 v0, v0, v7, s[16:17]
	v_cndmask_b32_e64 v1, v1, 23, s[16:17]
	s_waitcnt lgkmcnt(3)
	v_cmp_gt_f32_e64 s[16:17], v22, v0
	s_nop 1
	v_cndmask_b32_e64 v0, v0, v22, s[16:17]
	v_cndmask_b32_e64 v1, v1, 24, s[16:17]
	v_cmp_gt_f32_e64 s[16:17], v23, v0
	s_nop 1
	v_cndmask_b32_e64 v0, v0, v23, s[16:17]
	v_cndmask_b32_e64 v1, v1, 25, s[16:17]
	s_waitcnt lgkmcnt(2)
	v_cmp_gt_f32_e64 s[16:17], v32, v0
	s_nop 1
	v_cndmask_b32_e64 v0, v0, v32, s[16:17]
	v_cndmask_b32_e64 v1, v1, 26, s[16:17]
	v_cmp_gt_f32_e64 s[16:17], v33, v0
	s_nop 1
	v_cndmask_b32_e64 v0, v0, v33, s[16:17]
	v_cndmask_b32_e64 v1, v1, 27, s[16:17]
	s_waitcnt lgkmcnt(1)
	v_cmp_gt_f32_e64 s[16:17], v24, v0
	s_nop 1
	v_cndmask_b32_e64 v0, v0, v24, s[16:17]
	v_cndmask_b32_e64 v1, v1, 28, s[16:17]
	v_cmp_gt_f32_e64 s[16:17], v25, v0
	s_nop 1
	v_cndmask_b32_e64 v0, v0, v25, s[16:17]
	v_cndmask_b32_e64 v1, v1, 29, s[16:17]
	s_waitcnt lgkmcnt(0)
	v_cmp_gt_f32_e64 s[16:17], v10, v0
	s_nop 1
	v_cndmask_b32_e64 v0, v0, v10, s[16:17]
	v_cndmask_b32_e64 v1, v1, 30, s[16:17]
	v_cmp_gt_f32_e64 s[16:17], v11, v0
	s_nop 1
	v_cndmask_b32_e64 v36, v0, v11, s[16:17]
	v_cndmask_b32_e64 v0, v1, 31, s[16:17]
	v_cmp_ne_u32_e64 s[16:17], 0, v0
	v_lshlrev_b32_e64 v2, v0, 1
	s_and_b64 s[16:17], s[16:17], vcc
	v_cndmask_b32_e64 v1, v112, v34, s[16:17]
	v_and_b32_e32 v3, 2, v2
	v_cmp_eq_u32_e64 s[16:17], 0, v3
	v_cmp_gt_f32_e64 s[18:19], v35, v1
	s_and_b64 s[16:17], s[16:17], s[18:19]
	v_cndmask_b32_e64 v1, v1, v35, s[16:17]
	v_and_b32_e32 v37, 4, v2
	v_cndmask_b32_e64 v3, 0, 1, s[16:17]
	v_cmp_eq_u32_e64 s[16:17], 0, v37
	v_cmp_gt_f32_e64 s[18:19], v28, v1
	s_and_b64 s[16:17], s[16:17], s[18:19]
	v_cndmask_b32_e64 v1, v1, v28, s[16:17]
	v_and_b32_e32 v37, 8, v2
	v_cndmask_b32_e64 v3, v3, 2, s[16:17]
	v_cmp_eq_u32_e64 s[16:17], 0, v37
	v_cmp_gt_f32_e64 s[18:19], v29, v1
	s_and_b64 s[16:17], s[16:17], s[18:19]
	v_cndmask_b32_e64 v1, v1, v29, s[16:17]
	v_and_b32_e32 v37, 16, v2
	v_cndmask_b32_e64 v3, v3, 3, s[16:17]
	v_cmp_eq_u32_e64 s[16:17], 0, v37
	v_cmp_gt_f32_e64 s[18:19], v18, v1
	s_and_b64 s[16:17], s[16:17], s[18:19]
	v_cndmask_b32_e64 v1, v1, v18, s[16:17]
	v_and_b32_e32 v37, 32, v2
	v_cndmask_b32_e64 v3, v3, 4, s[16:17]
	v_cmp_eq_u32_e64 s[16:17], 0, v37
	v_cmp_gt_f32_e64 s[18:19], v19, v1
	s_and_b64 s[16:17], s[16:17], s[18:19]
	v_cndmask_b32_e64 v1, v1, v19, s[16:17]
	v_and_b32_e32 v37, 64, v2
	v_cndmask_b32_e64 v3, v3, 5, s[16:17]
	v_cmp_eq_u32_e64 s[16:17], 0, v37
	v_cmp_gt_f32_e64 s[18:19], v8, v1
	s_and_b64 s[16:17], s[16:17], s[18:19]
	v_cndmask_b32_e64 v1, v1, v8, s[16:17]
	v_and_b32_e32 v37, 0x80, v2
	v_cndmask_b32_e64 v3, v3, 6, s[16:17]
	v_cmp_eq_u32_e64 s[16:17], 0, v37
	v_cmp_gt_f32_e64 s[18:19], v9, v1
	s_and_b64 s[16:17], s[16:17], s[18:19]
	v_cndmask_b32_e64 v1, v1, v9, s[16:17]
	v_and_b32_e32 v37, 0x100, v2
	v_cndmask_b32_e64 v3, v3, 7, s[16:17]
	v_cmp_eq_u32_e64 s[16:17], 0, v37
	v_cmp_gt_f32_e64 s[18:19], v20, v1
	s_and_b64 s[16:17], s[16:17], s[18:19]
	v_cndmask_b32_e64 v1, v1, v20, s[16:17]
	v_and_b32_e32 v37, 0x200, v2
	v_cndmask_b32_e64 v3, v3, 8, s[16:17]
	v_cmp_eq_u32_e64 s[16:17], 0, v37
	v_cmp_gt_f32_e64 s[18:19], v21, v1
	s_and_b64 s[16:17], s[16:17], s[18:19]
	v_cndmask_b32_e64 v1, v1, v21, s[16:17]
	v_and_b32_e32 v37, 0x400, v2
	v_cndmask_b32_e64 v3, v3, 9, s[16:17]
	v_cmp_eq_u32_e64 s[16:17], 0, v37
	v_cmp_gt_f32_e64 s[18:19], v30, v1
	s_and_b64 s[16:17], s[16:17], s[18:19]
	v_cndmask_b32_e64 v1, v1, v30, s[16:17]
	v_and_b32_e32 v37, 0x800, v2
	v_cndmask_b32_e64 v3, v3, 10, s[16:17]
	v_cmp_eq_u32_e64 s[16:17], 0, v37
	v_cmp_gt_f32_e64 s[18:19], v31, v1
	s_and_b64 s[16:17], s[16:17], s[18:19]
	v_cndmask_b32_e64 v1, v1, v31, s[16:17]
	v_and_b32_e32 v37, 0x1000, v2
	v_cndmask_b32_e64 v3, v3, 11, s[16:17]
	v_cmp_eq_u32_e64 s[16:17], 0, v37
	v_cmp_gt_f32_e64 s[18:19], v16, v1
	s_and_b64 s[16:17], s[16:17], s[18:19]
	v_cndmask_b32_e64 v1, v1, v16, s[16:17]
	v_and_b32_e32 v37, 0x2000, v2
	v_cndmask_b32_e64 v3, v3, 12, s[16:17]
	v_cmp_eq_u32_e64 s[16:17], 0, v37
	v_cmp_gt_f32_e64 s[18:19], v17, v1
	s_and_b64 s[16:17], s[16:17], s[18:19]
	v_cndmask_b32_e64 v1, v1, v17, s[16:17]
	v_and_b32_e32 v37, 0x4000, v2
	v_cndmask_b32_e64 v3, v3, 13, s[16:17]
	v_cmp_eq_u32_e64 s[16:17], 0, v37
	v_cmp_gt_f32_e64 s[18:19], v4, v1
	s_and_b64 s[16:17], s[16:17], s[18:19]
	v_cndmask_b32_e64 v1, v1, v4, s[16:17]
	v_and_b32_e32 v37, 0x8000, v2
	v_cndmask_b32_e64 v3, v3, 14, s[16:17]
	v_cmp_eq_u32_e64 s[16:17], 0, v37
	v_cmp_gt_f32_e64 s[18:19], v5, v1
	s_and_b64 s[16:17], s[16:17], s[18:19]
	v_cndmask_b32_e64 v1, v1, v5, s[16:17]
	v_and_b32_e32 v37, 0x10000, v2
	v_cndmask_b32_e64 v3, v3, 15, s[16:17]
	v_cmp_eq_u32_e64 s[16:17], 0, v37
	v_cmp_gt_f32_e64 s[18:19], v12, v1
	s_and_b64 s[16:17], s[16:17], s[18:19]
	v_cndmask_b32_e64 v1, v1, v12, s[16:17]
	v_and_b32_e32 v37, 0x20000, v2
	v_cndmask_b32_e64 v3, v3, 16, s[16:17]
	v_cmp_eq_u32_e64 s[16:17], 0, v37
	v_cmp_gt_f32_e64 s[18:19], v13, v1
	s_and_b64 s[16:17], s[16:17], s[18:19]
	v_cndmask_b32_e64 v1, v1, v13, s[16:17]
	v_and_b32_e32 v37, 0x40000, v2
	v_cndmask_b32_e64 v3, v3, 17, s[16:17]
	v_cmp_eq_u32_e64 s[16:17], 0, v37
	v_cmp_gt_f32_e64 s[18:19], v26, v1
	s_and_b64 s[16:17], s[16:17], s[18:19]
	v_cndmask_b32_e64 v1, v1, v26, s[16:17]
	v_and_b32_e32 v37, 0x80000, v2
	v_cndmask_b32_e64 v3, v3, 18, s[16:17]
	v_cmp_eq_u32_e64 s[16:17], 0, v37
	v_cmp_gt_f32_e64 s[18:19], v27, v1
	s_and_b64 s[16:17], s[16:17], s[18:19]
	v_cndmask_b32_e64 v1, v1, v27, s[16:17]
	v_and_b32_e32 v37, 0x100000, v2
	v_cndmask_b32_e64 v3, v3, 19, s[16:17]
	v_cmp_eq_u32_e64 s[16:17], 0, v37
	v_cmp_gt_f32_e64 s[18:19], v14, v1
	s_and_b64 s[16:17], s[16:17], s[18:19]
	v_cndmask_b32_e64 v1, v1, v14, s[16:17]
	v_and_b32_e32 v37, 0x200000, v2
	v_cndmask_b32_e64 v3, v3, 20, s[16:17]
	v_cmp_eq_u32_e64 s[16:17], 0, v37
	v_cmp_gt_f32_e64 s[18:19], v15, v1
	s_and_b64 s[16:17], s[16:17], s[18:19]
	v_cndmask_b32_e64 v1, v1, v15, s[16:17]
	v_and_b32_e32 v37, 0x400000, v2
	v_cndmask_b32_e64 v3, v3, 21, s[16:17]
	v_cmp_eq_u32_e64 s[16:17], 0, v37
	v_cmp_gt_f32_e64 s[18:19], v6, v1
	s_and_b64 s[16:17], s[16:17], s[18:19]
	v_cndmask_b32_e64 v1, v1, v6, s[16:17]
	v_and_b32_e32 v37, 0x800000, v2
	v_cndmask_b32_e64 v3, v3, 22, s[16:17]
	v_cmp_eq_u32_e64 s[16:17], 0, v37
	v_cmp_gt_f32_e64 s[18:19], v7, v1
	s_and_b64 s[16:17], s[16:17], s[18:19]
	v_cndmask_b32_e64 v1, v1, v7, s[16:17]
	v_and_b32_e32 v37, 0x1000000, v2
	v_cndmask_b32_e64 v3, v3, 23, s[16:17]
	v_cmp_eq_u32_e64 s[16:17], 0, v37
	v_cmp_gt_f32_e64 s[18:19], v22, v1
	s_and_b64 s[16:17], s[16:17], s[18:19]
	v_cndmask_b32_e64 v1, v1, v22, s[16:17]
	v_and_b32_e32 v37, 0x2000000, v2
	v_cndmask_b32_e64 v3, v3, 24, s[16:17]
	v_cmp_eq_u32_e64 s[16:17], 0, v37
	v_cmp_gt_f32_e64 s[18:19], v23, v1
	s_and_b64 s[16:17], s[16:17], s[18:19]
	v_cndmask_b32_e64 v1, v1, v23, s[16:17]
	v_and_b32_e32 v37, 0x4000000, v2
	v_cndmask_b32_e64 v3, v3, 25, s[16:17]
	v_cmp_eq_u32_e64 s[16:17], 0, v37
	v_cmp_gt_f32_e64 s[18:19], v32, v1
	s_and_b64 s[16:17], s[16:17], s[18:19]
	v_cndmask_b32_e64 v1, v1, v32, s[16:17]
	v_and_b32_e32 v37, 0x8000000, v2
	v_cndmask_b32_e64 v3, v3, 26, s[16:17]
	v_cmp_eq_u32_e64 s[16:17], 0, v37
	v_cmp_gt_f32_e64 s[18:19], v33, v1
	s_and_b64 s[16:17], s[16:17], s[18:19]
	v_cndmask_b32_e64 v1, v1, v33, s[16:17]
	v_and_b32_e32 v37, 0x10000000, v2
	v_cndmask_b32_e64 v3, v3, 27, s[16:17]
	v_cmp_eq_u32_e64 s[16:17], 0, v37
	v_cmp_gt_f32_e64 s[18:19], v24, v1
	s_and_b64 s[16:17], s[16:17], s[18:19]
	v_cndmask_b32_e64 v1, v1, v24, s[16:17]
	v_and_b32_e32 v37, 0x20000000, v2
	v_cndmask_b32_e64 v3, v3, 28, s[16:17]
	v_cmp_eq_u32_e64 s[16:17], 0, v37
	v_cmp_gt_f32_e64 s[18:19], v25, v1
	s_and_b64 s[16:17], s[16:17], s[18:19]
	v_cndmask_b32_e64 v1, v1, v25, s[16:17]
	v_and_b32_e32 v37, 2.0, v2
	v_cndmask_b32_e64 v3, v3, 29, s[16:17]
	v_cmp_eq_u32_e64 s[16:17], 0, v37
	v_cmp_gt_f32_e64 s[18:19], v10, v1
	s_and_b64 s[16:17], s[16:17], s[18:19]
	v_cndmask_b32_e64 v1, v1, v10, s[16:17]
	v_cndmask_b32_e64 v3, v3, 30, s[16:17]
	v_cmp_ne_u32_e64 s[16:17], 31, v0
	v_cmp_gt_f32_e64 s[18:19], v11, v1
	s_and_b64 s[16:17], s[16:17], s[18:19]
	v_cndmask_b32_e64 v37, v1, v11, s[16:17]
	v_cndmask_b32_e64 v1, v3, 31, s[16:17]
	v_lshl_or_b32 v3, 1, v1, v2
	v_and_b32_e32 v2, 1, v3
	v_cmp_eq_u32_e64 s[16:17], 0, v2
	s_and_b64 s[16:17], s[16:17], vcc
	v_and_b32_e32 v38, 2, v3
	v_cndmask_b32_e64 v2, v112, v34, s[16:17]
	v_cmp_eq_u32_e64 s[16:17], 0, v38
	v_cmp_gt_f32_e64 s[18:19], v35, v2
	s_and_b64 s[16:17], s[16:17], s[18:19]
	v_cndmask_b32_e64 v2, v2, v35, s[16:17]
	v_and_b32_e32 v39, 4, v3
	v_cndmask_b32_e64 v38, 0, 1, s[16:17]
	v_cmp_eq_u32_e64 s[16:17], 0, v39
	v_cmp_gt_f32_e64 s[18:19], v28, v2
	s_and_b64 s[16:17], s[16:17], s[18:19]
	v_cndmask_b32_e64 v2, v2, v28, s[16:17]
	v_and_b32_e32 v39, 8, v3
	v_cndmask_b32_e64 v38, v38, 2, s[16:17]
	v_cmp_eq_u32_e64 s[16:17], 0, v39
	v_cmp_gt_f32_e64 s[18:19], v29, v2
	s_and_b64 s[16:17], s[16:17], s[18:19]
	v_cndmask_b32_e64 v2, v2, v29, s[16:17]
	v_and_b32_e32 v39, 16, v3
	v_cndmask_b32_e64 v38, v38, 3, s[16:17]
	v_cmp_eq_u32_e64 s[16:17], 0, v39
	v_cmp_gt_f32_e64 s[18:19], v18, v2
	s_and_b64 s[16:17], s[16:17], s[18:19]
	v_cndmask_b32_e64 v2, v2, v18, s[16:17]
	v_and_b32_e32 v39, 32, v3
	v_cndmask_b32_e64 v38, v38, 4, s[16:17]
	v_cmp_eq_u32_e64 s[16:17], 0, v39
	v_cmp_gt_f32_e64 s[18:19], v19, v2
	s_and_b64 s[16:17], s[16:17], s[18:19]
	v_cndmask_b32_e64 v2, v2, v19, s[16:17]
	v_and_b32_e32 v39, 64, v3
	v_cndmask_b32_e64 v38, v38, 5, s[16:17]
	v_cmp_eq_u32_e64 s[16:17], 0, v39
	v_cmp_gt_f32_e64 s[18:19], v8, v2
	s_and_b64 s[16:17], s[16:17], s[18:19]
	v_cndmask_b32_e64 v2, v2, v8, s[16:17]
	v_and_b32_e32 v39, 0x80, v3
	v_cndmask_b32_e64 v38, v38, 6, s[16:17]
	v_cmp_eq_u32_e64 s[16:17], 0, v39
	v_cmp_gt_f32_e64 s[18:19], v9, v2
	s_and_b64 s[16:17], s[16:17], s[18:19]
	v_cndmask_b32_e64 v2, v2, v9, s[16:17]
	v_and_b32_e32 v39, 0x100, v3
	v_cndmask_b32_e64 v38, v38, 7, s[16:17]
	v_cmp_eq_u32_e64 s[16:17], 0, v39
	v_cmp_gt_f32_e64 s[18:19], v20, v2
	s_and_b64 s[16:17], s[16:17], s[18:19]
	v_cndmask_b32_e64 v2, v2, v20, s[16:17]
	v_and_b32_e32 v39, 0x200, v3
	v_cndmask_b32_e64 v38, v38, 8, s[16:17]
	v_cmp_eq_u32_e64 s[16:17], 0, v39
	v_cmp_gt_f32_e64 s[18:19], v21, v2
	s_and_b64 s[16:17], s[16:17], s[18:19]
	v_cndmask_b32_e64 v2, v2, v21, s[16:17]
	v_and_b32_e32 v39, 0x400, v3
	v_cndmask_b32_e64 v38, v38, 9, s[16:17]
	v_cmp_eq_u32_e64 s[16:17], 0, v39
	v_cmp_gt_f32_e64 s[18:19], v30, v2
	s_and_b64 s[16:17], s[16:17], s[18:19]
	v_cndmask_b32_e64 v2, v2, v30, s[16:17]
	v_and_b32_e32 v39, 0x800, v3
	v_cndmask_b32_e64 v38, v38, 10, s[16:17]
	v_cmp_eq_u32_e64 s[16:17], 0, v39
	v_cmp_gt_f32_e64 s[18:19], v31, v2
	s_and_b64 s[16:17], s[16:17], s[18:19]
	v_cndmask_b32_e64 v2, v2, v31, s[16:17]
	v_and_b32_e32 v39, 0x1000, v3
	v_cndmask_b32_e64 v38, v38, 11, s[16:17]
	v_cmp_eq_u32_e64 s[16:17], 0, v39
	v_cmp_gt_f32_e64 s[18:19], v16, v2
	s_and_b64 s[16:17], s[16:17], s[18:19]
	v_cndmask_b32_e64 v2, v2, v16, s[16:17]
	v_and_b32_e32 v39, 0x2000, v3
	v_cndmask_b32_e64 v38, v38, 12, s[16:17]
	v_cmp_eq_u32_e64 s[16:17], 0, v39
	v_cmp_gt_f32_e64 s[18:19], v17, v2
	s_and_b64 s[16:17], s[16:17], s[18:19]
	v_cndmask_b32_e64 v2, v2, v17, s[16:17]
	v_and_b32_e32 v39, 0x4000, v3
	v_cndmask_b32_e64 v38, v38, 13, s[16:17]
	v_cmp_eq_u32_e64 s[16:17], 0, v39
	v_cmp_gt_f32_e64 s[18:19], v4, v2
	s_and_b64 s[16:17], s[16:17], s[18:19]
	v_cndmask_b32_e64 v2, v2, v4, s[16:17]
	v_and_b32_e32 v39, 0x8000, v3
	v_cndmask_b32_e64 v38, v38, 14, s[16:17]
	v_cmp_eq_u32_e64 s[16:17], 0, v39
	v_cmp_gt_f32_e64 s[18:19], v5, v2
	s_and_b64 s[16:17], s[16:17], s[18:19]
	v_cndmask_b32_e64 v2, v2, v5, s[16:17]
	v_and_b32_e32 v39, 0x10000, v3
	v_cndmask_b32_e64 v38, v38, 15, s[16:17]
	v_cmp_eq_u32_e64 s[16:17], 0, v39
	v_cmp_gt_f32_e64 s[18:19], v12, v2
	s_and_b64 s[16:17], s[16:17], s[18:19]
	v_cndmask_b32_e64 v2, v2, v12, s[16:17]
	v_and_b32_e32 v39, 0x20000, v3
	v_cndmask_b32_e64 v38, v38, 16, s[16:17]
	v_cmp_eq_u32_e64 s[16:17], 0, v39
	v_cmp_gt_f32_e64 s[18:19], v13, v2
	s_and_b64 s[16:17], s[16:17], s[18:19]
	v_cndmask_b32_e64 v2, v2, v13, s[16:17]
	v_and_b32_e32 v39, 0x40000, v3
	v_cndmask_b32_e64 v38, v38, 17, s[16:17]
	v_cmp_eq_u32_e64 s[16:17], 0, v39
	v_cmp_gt_f32_e64 s[18:19], v26, v2
	s_and_b64 s[16:17], s[16:17], s[18:19]
	v_cndmask_b32_e64 v2, v2, v26, s[16:17]
	v_and_b32_e32 v39, 0x80000, v3
	v_cndmask_b32_e64 v38, v38, 18, s[16:17]
	v_cmp_eq_u32_e64 s[16:17], 0, v39
	v_cmp_gt_f32_e64 s[18:19], v27, v2
	s_and_b64 s[16:17], s[16:17], s[18:19]
	v_cndmask_b32_e64 v2, v2, v27, s[16:17]
	v_and_b32_e32 v39, 0x100000, v3
	v_cndmask_b32_e64 v38, v38, 19, s[16:17]
	v_cmp_eq_u32_e64 s[16:17], 0, v39
	v_cmp_gt_f32_e64 s[18:19], v14, v2
	s_and_b64 s[16:17], s[16:17], s[18:19]
	v_cndmask_b32_e64 v2, v2, v14, s[16:17]
	v_and_b32_e32 v39, 0x200000, v3
	v_cndmask_b32_e64 v38, v38, 20, s[16:17]
	v_cmp_eq_u32_e64 s[16:17], 0, v39
	v_cmp_gt_f32_e64 s[18:19], v15, v2
	s_and_b64 s[16:17], s[16:17], s[18:19]
	v_cndmask_b32_e64 v2, v2, v15, s[16:17]
	v_and_b32_e32 v39, 0x400000, v3
	v_cndmask_b32_e64 v38, v38, 21, s[16:17]
	v_cmp_eq_u32_e64 s[16:17], 0, v39
	v_cmp_gt_f32_e64 s[18:19], v6, v2
	s_and_b64 s[16:17], s[16:17], s[18:19]
	v_cndmask_b32_e64 v2, v2, v6, s[16:17]
	v_and_b32_e32 v39, 0x800000, v3
	v_cndmask_b32_e64 v38, v38, 22, s[16:17]
	v_cmp_eq_u32_e64 s[16:17], 0, v39
	v_cmp_gt_f32_e64 s[18:19], v7, v2
	s_and_b64 s[16:17], s[16:17], s[18:19]
	v_cndmask_b32_e64 v2, v2, v7, s[16:17]
	v_and_b32_e32 v39, 0x1000000, v3
	v_cndmask_b32_e64 v38, v38, 23, s[16:17]
	v_cmp_eq_u32_e64 s[16:17], 0, v39
	v_cmp_gt_f32_e64 s[18:19], v22, v2
	s_and_b64 s[16:17], s[16:17], s[18:19]
	v_cndmask_b32_e64 v2, v2, v22, s[16:17]
	v_and_b32_e32 v39, 0x2000000, v3
	v_cndmask_b32_e64 v38, v38, 24, s[16:17]
	v_cmp_eq_u32_e64 s[16:17], 0, v39
	v_cmp_gt_f32_e64 s[18:19], v23, v2
	s_and_b64 s[16:17], s[16:17], s[18:19]
	v_cndmask_b32_e64 v2, v2, v23, s[16:17]
	v_and_b32_e32 v39, 0x4000000, v3
	v_cndmask_b32_e64 v38, v38, 25, s[16:17]
	v_cmp_eq_u32_e64 s[16:17], 0, v39
	v_cmp_gt_f32_e64 s[18:19], v32, v2
	s_and_b64 s[16:17], s[16:17], s[18:19]
	v_cndmask_b32_e64 v2, v2, v32, s[16:17]
	v_and_b32_e32 v39, 0x8000000, v3
	v_cndmask_b32_e64 v38, v38, 26, s[16:17]
	v_cmp_eq_u32_e64 s[16:17], 0, v39
	v_cmp_gt_f32_e64 s[18:19], v33, v2
	s_and_b64 s[16:17], s[16:17], s[18:19]
	v_cndmask_b32_e64 v2, v2, v33, s[16:17]
	v_and_b32_e32 v39, 0x10000000, v3
	v_cndmask_b32_e64 v38, v38, 27, s[16:17]
	v_cmp_eq_u32_e64 s[16:17], 0, v39
	v_cmp_gt_f32_e64 s[18:19], v24, v2
	s_and_b64 s[16:17], s[16:17], s[18:19]
	v_cndmask_b32_e64 v2, v2, v24, s[16:17]
	v_and_b32_e32 v39, 0x20000000, v3
	v_cndmask_b32_e64 v38, v38, 28, s[16:17]
	v_cmp_eq_u32_e64 s[16:17], 0, v39
	v_cmp_gt_f32_e64 s[18:19], v25, v2
	s_and_b64 s[16:17], s[16:17], s[18:19]
	v_cndmask_b32_e64 v2, v2, v25, s[16:17]
	v_and_b32_e32 v39, 2.0, v3
	v_cndmask_b32_e64 v38, v38, 29, s[16:17]
	v_cmp_eq_u32_e64 s[16:17], 0, v39
	v_cmp_gt_f32_e64 s[18:19], v10, v2
	s_and_b64 s[16:17], s[16:17], s[18:19]
	v_cndmask_b32_e64 v2, v2, v10, s[16:17]
	v_cndmask_b32_e64 v38, v38, 30, s[16:17]
	v_cmp_lt_i32_e64 s[16:17], -1, v3
	v_cmp_gt_f32_e64 s[18:19], v11, v2
	s_and_b64 s[16:17], s[16:17], s[18:19]
	v_cndmask_b32_e64 v39, v2, v11, s[16:17]
	v_cndmask_b32_e64 v2, v38, 31, s[16:17]
	v_lshlrev_b32_e64 v38, v2, 1
	v_bitop3_b32 v89, v38, 1, v3 bitop3:0xc8
	v_cmp_eq_u32_e64 s[16:17], 0, v89
	s_and_b64 vcc, s[16:17], vcc
	v_cndmask_b32_e32 v34, v112, v34, vcc
	v_bitop3_b32 v89, v38, 2, v3 bitop3:0xc8
	v_cmp_eq_u32_e32 vcc, 0, v89
	v_cmp_gt_f32_e64 s[16:17], v35, v34
	s_and_b64 vcc, vcc, s[16:17]
	v_cndmask_b32_e32 v34, v34, v35, vcc
	v_bitop3_b32 v89, v38, 4, v3 bitop3:0xc8
	v_cndmask_b32_e64 v35, 0, 1, vcc
	v_cmp_eq_u32_e32 vcc, 0, v89
	v_cmp_gt_f32_e64 s[16:17], v28, v34
	s_and_b64 vcc, vcc, s[16:17]
	v_cndmask_b32_e32 v28, v34, v28, vcc
	v_cndmask_b32_e64 v34, v35, 2, vcc
	v_bitop3_b32 v35, v38, 8, v3 bitop3:0xc8
	v_cmp_eq_u32_e32 vcc, 0, v35
	v_cmp_gt_f32_e64 s[16:17], v29, v28
	s_and_b64 vcc, vcc, s[16:17]
	v_cndmask_b32_e32 v28, v28, v29, vcc
	v_cndmask_b32_e64 v29, v34, 3, vcc
	v_bitop3_b32 v34, v38, 16, v3 bitop3:0xc8
	v_cmp_eq_u32_e32 vcc, 0, v34
	v_cmp_gt_f32_e64 s[16:17], v18, v28
	s_and_b64 vcc, vcc, s[16:17]
	v_cndmask_b32_e32 v18, v28, v18, vcc
	v_cndmask_b32_e64 v28, v29, 4, vcc
	v_bitop3_b32 v29, v38, 32, v3 bitop3:0xc8
	v_cmp_eq_u32_e32 vcc, 0, v29
	v_cmp_gt_f32_e64 s[16:17], v19, v18
	s_and_b64 vcc, vcc, s[16:17]
	v_cndmask_b32_e32 v18, v18, v19, vcc
	v_cndmask_b32_e64 v19, v28, 5, vcc
	v_bitop3_b32 v28, v38, 64, v3 bitop3:0xc8
	v_cmp_eq_u32_e32 vcc, 0, v28
	v_cmp_gt_f32_e64 s[16:17], v8, v18
	s_and_b64 vcc, vcc, s[16:17]
	s_movk_i32 s16, 0x80
	v_cndmask_b32_e32 v8, v18, v8, vcc
	v_cndmask_b32_e64 v18, v19, 6, vcc
	v_bitop3_b32 v19, v38, s16, v3 bitop3:0xc8
	v_cmp_eq_u32_e32 vcc, 0, v19
	v_cmp_gt_f32_e64 s[16:17], v9, v8
	s_and_b64 vcc, vcc, s[16:17]
	s_movk_i32 s16, 0x100
	v_cndmask_b32_e32 v8, v8, v9, vcc
	v_cndmask_b32_e64 v9, v18, 7, vcc
	v_bitop3_b32 v18, v38, s16, v3 bitop3:0xc8
	v_cmp_eq_u32_e32 vcc, 0, v18
	v_cmp_gt_f32_e64 s[16:17], v20, v8
	s_and_b64 vcc, vcc, s[16:17]
	s_movk_i32 s16, 0x200
	v_cndmask_b32_e32 v8, v8, v20, vcc
	v_bitop3_b32 v18, v38, s16, v3 bitop3:0xc8
	v_cndmask_b32_e64 v9, v9, 8, vcc
	v_cmp_eq_u32_e32 vcc, 0, v18
	v_cmp_gt_f32_e64 s[16:17], v21, v8
	s_and_b64 vcc, vcc, s[16:17]
	v_cndmask_b32_e32 v8, v8, v21, vcc
	v_bitop3_b32 v18, v38, s52, v3 bitop3:0xc8
	v_cndmask_b32_e64 v9, v9, 9, vcc
	v_cmp_eq_u32_e32 vcc, 0, v18
	v_cmp_gt_f32_e64 s[16:17], v30, v8
	s_and_b64 vcc, vcc, s[16:17]
	s_movk_i32 s16, 0x800
	v_cndmask_b32_e32 v8, v8, v30, vcc
	v_bitop3_b32 v18, v38, s16, v3 bitop3:0xc8
	v_cndmask_b32_e64 v9, v9, 10, vcc
	v_cmp_eq_u32_e32 vcc, 0, v18
	v_cmp_gt_f32_e64 s[16:17], v31, v8
	s_and_b64 vcc, vcc, s[16:17]
	s_movk_i32 s16, 0x1000
	v_cndmask_b32_e32 v8, v8, v31, vcc
	v_bitop3_b32 v18, v38, s16, v3 bitop3:0xc8
	v_cndmask_b32_e64 v9, v9, 11, vcc
	v_cmp_eq_u32_e32 vcc, 0, v18
	v_cmp_gt_f32_e64 s[16:17], v16, v8
	s_and_b64 vcc, vcc, s[16:17]
	s_movk_i32 s16, 0x2000
	v_cndmask_b32_e32 v8, v8, v16, vcc
	v_bitop3_b32 v16, v38, s16, v3 bitop3:0xc8
	v_cndmask_b32_e64 v9, v9, 12, vcc
	v_cmp_eq_u32_e32 vcc, 0, v16
	v_cmp_gt_f32_e64 s[16:17], v17, v8
	s_and_b64 vcc, vcc, s[16:17]
	s_movk_i32 s16, 0x4000
	v_cndmask_b32_e32 v8, v8, v17, vcc
	v_bitop3_b32 v16, v38, s16, v3 bitop3:0xc8
	v_cndmask_b32_e64 v9, v9, 13, vcc
	v_cmp_eq_u32_e32 vcc, 0, v16
	v_cmp_gt_f32_e64 s[16:17], v4, v8
	s_and_b64 vcc, vcc, s[16:17]
	s_mov_b32 s16, 0x8000
	v_cndmask_b32_e32 v4, v8, v4, vcc
	v_cndmask_b32_e64 v8, v9, 14, vcc
	v_bitop3_b32 v9, v38, s16, v3 bitop3:0xc8
	v_cmp_eq_u32_e32 vcc, 0, v9
	v_cmp_gt_f32_e64 s[16:17], v5, v4
	s_and_b64 vcc, vcc, s[16:17]
	s_mov_b32 s16, 0x10000
	v_cndmask_b32_e32 v4, v4, v5, vcc
	v_cndmask_b32_e64 v5, v8, 15, vcc
	v_bitop3_b32 v8, v38, s16, v3 bitop3:0xc8
	v_cmp_eq_u32_e32 vcc, 0, v8
	v_cmp_gt_f32_e64 s[16:17], v12, v4
	s_and_b64 vcc, vcc, s[16:17]
	s_mov_b32 s16, 0x20000
	v_cndmask_b32_e32 v4, v4, v12, vcc
	v_bitop3_b32 v8, v38, s16, v3 bitop3:0xc8
	v_cndmask_b32_e64 v5, v5, 16, vcc
	v_cmp_eq_u32_e32 vcc, 0, v8
	v_cmp_gt_f32_e64 s[16:17], v13, v4
	s_and_b64 vcc, vcc, s[16:17]
	s_mov_b32 s16, 0x40000
	v_cndmask_b32_e32 v4, v4, v13, vcc
	v_bitop3_b32 v8, v38, s16, v3 bitop3:0xc8
	v_cndmask_b32_e64 v5, v5, 17, vcc
	v_cmp_eq_u32_e32 vcc, 0, v8
	v_cmp_gt_f32_e64 s[16:17], v26, v4
	s_and_b64 vcc, vcc, s[16:17]
	v_cndmask_b32_e32 v4, v4, v26, vcc
	v_bitop3_b32 v8, v38, s61, v3 bitop3:0xc8
	v_cndmask_b32_e64 v5, v5, 18, vcc
	v_cmp_eq_u32_e32 vcc, 0, v8
	v_cmp_gt_f32_e64 s[16:17], v27, v4
	s_and_b64 vcc, vcc, s[16:17]
	v_cndmask_b32_e32 v4, v4, v27, vcc
	v_bitop3_b32 v8, v38, s62, v3 bitop3:0xc8
	v_cndmask_b32_e64 v5, v5, 19, vcc
	v_cmp_eq_u32_e32 vcc, 0, v8
	v_cmp_gt_f32_e64 s[16:17], v14, v4
	s_and_b64 vcc, vcc, s[16:17]
	v_cndmask_b32_e32 v4, v4, v14, vcc
	v_bitop3_b32 v8, v38, s63, v3 bitop3:0xc8
	v_cndmask_b32_e64 v5, v5, 20, vcc
	v_cmp_eq_u32_e32 vcc, 0, v8
	v_cmp_gt_f32_e64 s[16:17], v15, v4
	s_and_b64 vcc, vcc, s[16:17]
	v_cndmask_b32_e32 v4, v4, v15, vcc
	v_bitop3_b32 v8, v38, s64, v3 bitop3:0xc8
	v_cndmask_b32_e64 v5, v5, 21, vcc
	v_cmp_eq_u32_e32 vcc, 0, v8
	v_cmp_gt_f32_e64 s[16:17], v6, v4
	s_and_b64 vcc, vcc, s[16:17]
	v_cndmask_b32_e32 v4, v4, v6, vcc
	v_bitop3_b32 v6, v38, s65, v3 bitop3:0xc8
	v_cndmask_b32_e64 v5, v5, 22, vcc
	v_cmp_eq_u32_e32 vcc, 0, v6
	v_cmp_gt_f32_e64 s[16:17], v7, v4
	s_and_b64 vcc, vcc, s[16:17]
	v_cndmask_b32_e32 v4, v4, v7, vcc
	v_bitop3_b32 v6, v38, s66, v3 bitop3:0xc8
	v_cndmask_b32_e64 v5, v5, 23, vcc
	v_cmp_eq_u32_e32 vcc, 0, v6
	v_cmp_gt_f32_e64 s[16:17], v22, v4
	s_and_b64 vcc, vcc, s[16:17]
	v_cndmask_b32_e32 v4, v4, v22, vcc
	v_bitop3_b32 v6, v38, s67, v3 bitop3:0xc8
	v_cndmask_b32_e64 v5, v5, 24, vcc
	v_cmp_eq_u32_e32 vcc, 0, v6
	v_cmp_gt_f32_e64 s[16:17], v23, v4
	s_and_b64 vcc, vcc, s[16:17]
	v_cndmask_b32_e32 v4, v4, v23, vcc
	v_bitop3_b32 v6, v38, s84, v3 bitop3:0xc8
	v_cndmask_b32_e64 v5, v5, 25, vcc
	v_cmp_eq_u32_e32 vcc, 0, v6
	v_cmp_gt_f32_e64 s[16:17], v32, v4
	s_and_b64 vcc, vcc, s[16:17]
	v_cndmask_b32_e32 v4, v4, v32, vcc
	v_bitop3_b32 v6, v38, s85, v3 bitop3:0xc8
	v_cndmask_b32_e64 v5, v5, 26, vcc
	v_cmp_eq_u32_e32 vcc, 0, v6
	v_cmp_gt_f32_e64 s[16:17], v33, v4
	s_and_b64 vcc, vcc, s[16:17]
	v_cndmask_b32_e32 v4, v4, v33, vcc
	v_bitop3_b32 v6, v38, s86, v3 bitop3:0xc8
	v_cndmask_b32_e64 v5, v5, 27, vcc
	v_cmp_eq_u32_e32 vcc, 0, v6
	v_cmp_gt_f32_e64 s[16:17], v24, v4
	s_and_b64 vcc, vcc, s[16:17]
	v_cndmask_b32_e32 v4, v4, v24, vcc
	v_bitop3_b32 v6, v38, s87, v3 bitop3:0xc8
	v_cndmask_b32_e64 v5, v5, 28, vcc
	v_cmp_eq_u32_e32 vcc, 0, v6
	v_cmp_gt_f32_e64 s[16:17], v25, v4
	s_and_b64 vcc, vcc, s[16:17]
	v_or_b32_e32 v88, v38, v3
	v_cndmask_b32_e32 v4, v4, v25, vcc
	v_bitop3_b32 v3, v38, 2.0, v3 bitop3:0xc8
	v_cndmask_b32_e64 v5, v5, 29, vcc
	v_cmp_eq_u32_e32 vcc, 0, v3
	v_cmp_gt_f32_e64 s[16:17], v10, v4
	s_and_b64 vcc, vcc, s[16:17]
	v_cndmask_b32_e32 v3, v4, v10, vcc
	v_cndmask_b32_e64 v4, v5, 30, vcc
	v_cmp_lt_i32_e32 vcc, -1, v88
	v_cmp_gt_f32_e64 s[16:17], v11, v3
	s_and_b64 vcc, vcc, s[16:17]
	v_cndmask_b32_e32 v5, v3, v11, vcc
	v_cndmask_b32_e64 v3, v4, 31, vcc
	v_sub_f32_e32 v4, v36, v36
	v_mul_f32_e32 v4, 0x3fb8aa3b, v4
	v_exp_f32_e32 v10, v4
	v_sub_f32_e32 v4, v37, v36
	v_mul_f32_e32 v4, 0x3fb8aa3b, v4
	v_exp_f32_e32 v11, v4
	v_sub_f32_e32 v4, v39, v36
	v_mul_f32_e32 v4, 0x3fb8aa3b, v4
	v_exp_f32_e32 v12, v4
	v_sub_f32_e32 v4, v5, v36
	v_mul_f32_e32 v4, 0x3fb8aa3b, v4
	v_exp_f32_e32 v13, v4
	v_add_f32_e32 v4, 0, v10
	v_add_f32_e32 v4, v4, v11
	v_add_f32_e32 v4, v4, v12
	v_add_f32_e32 v14, v4, v13
	v_div_scale_f32 v15, s[16:17], v14, v14, v10
	v_rcp_f32_e32 v16, v15
	v_lshl_add_u32 v4, s91, 8, v94
	v_ashrrev_i32_e32 v5, 31, v4
	v_lshlrev_b64 v[6:7], 2, v[4:5]
	v_fma_f32 v5, -v15, v16, 1.0
	v_fmac_f32_e32 v16, v5, v16
	v_div_scale_f32 v5, vcc, v10, v14, v10
	v_mul_f32_e32 v17, v5, v16
	v_fma_f32 v18, -v15, v17, v5
	v_fmac_f32_e32 v17, v18, v16
	v_fma_f32 v5, -v15, v17, v5
	v_div_fmas_f32 v5, v5, v16, v17
	v_div_fixup_f32 v5, v5, v14, v10
	v_div_scale_f32 v10, s[16:17], v14, v14, v11
	v_rcp_f32_e32 v15, v10
	v_lshl_add_u64 v[8:9], s[20:21], 0, v[6:7]
	v_lshl_add_u64 v[6:7], s[22:23], 0, v[6:7]
	global_store_dword v[6:7], v5, off
	v_or_b32_e32 v6, 1, v4
	v_fma_f32 v4, -v10, v15, 1.0
	v_lshl_add_u32 v5, v0, 2, 0
	v_fmac_f32_e32 v15, v4, v15
	v_div_scale_f32 v4, vcc, v11, v14, v11
	ds_add_u32 v5, v109 offset:58624
	v_mul_f32_e32 v5, v4, v15
	v_fma_f32 v16, -v10, v5, v4
	v_fmac_f32_e32 v5, v16, v15
	v_fma_f32 v4, -v10, v5, v4
	v_div_fmas_f32 v4, v4, v15, v5
	v_div_scale_f32 v5, s[16:17], v14, v14, v12
	v_rcp_f32_e32 v15, v5
	v_ashrrev_i32_e32 v7, 31, v6
	v_div_fixup_f32 v4, v4, v14, v11
	v_lshl_add_u64 v[10:11], v[6:7], 2, s[22:23]
	v_lshl_add_u32 v6, v1, 2, 0
	ds_add_u32 v6, v109 offset:58624
	v_fma_f32 v6, -v5, v15, 1.0
	v_fmac_f32_e32 v15, v6, v15
	v_div_scale_f32 v6, vcc, v12, v14, v12
	v_mul_f32_e32 v7, v6, v15
	v_fma_f32 v16, -v5, v7, v6
	v_fmac_f32_e32 v7, v16, v15
	v_fma_f32 v5, -v5, v7, v6
	v_div_scale_f32 v6, s[16:17], v14, v14, v13
	v_div_fmas_f32 v5, v5, v15, v7
	v_rcp_f32_e32 v7, v6
	v_div_fixup_f32 v5, v5, v14, v12
	v_lshl_add_u32 v12, v2, 2, 0
	ds_add_u32 v12, v109 offset:58624
	global_store_dwordx4 v[8:9], v[0:3], off
	s_nop 1
	v_fma_f32 v0, -v6, v7, 1.0
	v_fmac_f32_e32 v7, v0, v7
	v_div_scale_f32 v0, vcc, v13, v14, v13
	v_mul_f32_e32 v1, v0, v7
	v_fma_f32 v2, -v6, v1, v0
	v_fmac_f32_e32 v1, v2, v7
	v_fma_f32 v0, -v6, v1, v0
	v_div_fmas_f32 v0, v0, v7, v1
	v_div_fixup_f32 v6, v0, v14, v13
	global_store_dwordx3 v[10:11], v[4:6], off
	v_lshl_add_u32 v0, v3, 2, 0
	ds_add_u32 v0, v109 offset:58624

	.amdhsa_kernel _Z10fwd_kernel4Args
		.amdhsa_group_segment_fixed_size 0
		.amdhsa_private_segment_fixed_size 0
		.amdhsa_kernarg_size 536
		.amdhsa_user_sgpr_count 2
		.amdhsa_user_sgpr_dispatch_ptr 0
		.amdhsa_user_sgpr_queue_ptr 0
		.amdhsa_user_sgpr_kernarg_segment_ptr 1
		.amdhsa_user_sgpr_dispatch_id 0
		.amdhsa_user_sgpr_kernarg_preload_length 0
		.amdhsa_user_sgpr_kernarg_preload_offset 0
		.amdhsa_user_sgpr_private_segment_size 0
		.amdhsa_uses_dynamic_stack 0
		.amdhsa_enable_private_segment 0
		.amdhsa_system_sgpr_workgroup_id_x 1
		.amdhsa_system_sgpr_workgroup_id_y 0
		.amdhsa_system_sgpr_workgroup_id_z 0
		.amdhsa_system_sgpr_workgroup_info 0
		.amdhsa_system_vgpr_workitem_id 0
		.amdhsa_next_free_vgpr 254
		.amdhsa_next_free_sgpr 102
		.amdhsa_accum_offset 256
		.amdhsa_reserve_vcc 1
		.amdhsa_float_round_mode_32 0
		.amdhsa_float_round_mode_16_64 0
		.amdhsa_float_denorm_mode_32 3
		.amdhsa_float_denorm_mode_16_64 3
		.amdhsa_dx10_clamp 1
		.amdhsa_ieee_mode 1
		.amdhsa_fp16_overflow 0
		.amdhsa_tg_split 0
		.amdhsa_exception_fp_ieee_invalid_op 0
		.amdhsa_exception_fp_denorm_src 0
		.amdhsa_exception_fp_ieee_div_zero 0
		.amdhsa_exception_fp_ieee_overflow 0
		.amdhsa_exception_fp_ieee_underflow 0
		.amdhsa_exception_fp_ieee_inexact 0
		.amdhsa_exception_int_div_zero 0
	.end_amdhsa_kernel

amdhsa.kernels:
  - .agpr_count:     0
    .args:
      - .offset:         0
        .size:           280
        .value_kind:     by_value
      - .offset:         280
        .size:           4
        .value_kind:     hidden_block_count_x
      - .offset:         284
        .size:           4
        .value_kind:     hidden_block_count_y
      - .offset:         288
        .size:           4
        .value_kind:     hidden_block_count_z
      - .offset:         292
        .size:           2
        .value_kind:     hidden_group_size_x
      - .offset:         294
        .size:           2
        .value_kind:     hidden_group_size_y
      - .offset:         296
        .size:           2
        .value_kind:     hidden_group_size_z
      - .offset:         298
        .size:           2
        .value_kind:     hidden_remainder_x
      - .offset:         300
        .size:           2
        .value_kind:     hidden_remainder_y
      - .offset:         302
        .size:           2
        .value_kind:     hidden_remainder_z
      - .offset:         320
        .size:           8
        .value_kind:     hidden_global_offset_x
      - .offset:         328
        .size:           8
        .value_kind:     hidden_global_offset_y
      - .offset:         336
        .size:           8
        .value_kind:     hidden_global_offset_z
      - .offset:         344
        .size:           2
        .value_kind:     hidden_grid_dims
      - .offset:         400
        .size:           4
        .value_kind:     hidden_dynamic_lds_size
    .group_segment_fixed_size: 0
    .kernarg_segment_align: 8
    .kernarg_segment_size: 536
    .language:       OpenCL C
    .language_version:
      - 2
      - 0
    .max_flat_workgroup_size: 512
    .name:           _Z10fwd_kernel4Args
    .private_segment_fixed_size: 0
    .sgpr_count:     108
    .sgpr_spill_count: 110
    .symbol:         _Z10fwd_kernel4Args.kd
    .uniform_work_group_size: 1
    .uses_dynamic_stack: false
    .vgpr_count:     254
    .vgpr_spill_count: 0
    .wavefront_size: 64
